# output stores of the barrier-terminated thin phases and the plain-store GEMM epilogues made write-through (sc1)
# speedup vs baseline: 1.0038x; 1.0038x over previous
.LBB0_102:
	s_lshl_b64 s[40:41], s[24:25], 2
	v_mov_b32_e32 v85, v161
	s_add_u32 s42, s49, s40
	v_lshl_add_u64 v[0:1], s[34:35], 0, v[84:85]
	s_addc_u32 s43, s48, s41
	v_add_co_u32_e32 v4, vcc, s58, v0
	v_lshl_add_u64 v[8:9], s[42:43], 0, v[84:85]
	s_nop 0
	v_addc_co_u32_e32 v5, vcc, 0, v1, vcc
	global_load_dwordx4 v[48:51], v84, s[34:35] nt
	global_load_dwordx4 v[60:63], v84, s[34:35] offset:16 nt
	global_load_dwordx4 v[52:55], v84, s[42:43] nt
	global_load_dwordx4 v[56:59], v84, s[42:43] offset:16 nt
	global_load_dwordx4 v[28:31], v84, s[34:35] offset:2048 nt
	global_load_dwordx4 v[32:35], v84, s[34:35] offset:2064 nt
	global_load_dwordx4 v[40:43], v84, s[42:43] offset:2048 nt
	global_load_dwordx4 v[44:47], v84, s[42:43] offset:2064 nt
	v_add_co_u32_e32 v10, vcc, s58, v8
	v_lshl_add_u64 v[2:3], v[0:1], 0, s[56:57]
	global_load_dwordx4 v[16:19], v[4:5], off nt
	global_load_dwordx4 v[20:23], v[2:3], off offset:16 nt
	v_addc_co_u32_e32 v11, vcc, 0, v9, vcc
	s_mov_b64 s[42:43], 0x1800
	v_lshl_add_u64 v[2:3], v[8:9], 0, s[56:57]
	global_load_dwordx4 v[24:27], v[10:11], off nt
	global_load_dwordx4 v[36:39], v[2:3], off offset:16 nt
	v_lshl_add_u64 v[6:7], v[0:1], 0, s[42:43]
	global_load_dwordx4 v[0:3], v[4:5], off offset:2048 nt
	s_nop 0
	global_load_dwordx4 v[4:7], v[6:7], off offset:16 nt
	v_lshl_add_u64 v[8:9], v[8:9], 0, s[42:43]
	global_load_dwordx4 v[12:15], v[10:11], off offset:2048 nt
	s_nop 0
	global_load_dwordx4 v[8:11], v[8:9], off offset:16 nt
	s_lshl_b64 s[40:41], s[24:25], 1
	s_add_u32 s40, s50, s40
	s_addc_u32 s41, s51, s41
	s_waitcnt vmcnt(0)
	v_cvt_pk_f16_f32 v65, v50, v51
	s_waitcnt vmcnt(14)
	v_cvt_pk_f16_f32 v67, v62, v63
	v_cvt_pk_f16_f32 v66, v60, v61
	v_cvt_pk_f16_f32 v64, v48, v49
	global_store_dwordx4 v160, v[64:67], s[28:29] sc1
	v_mov_b32_e32 v68, v51
	v_mov_b32_e32 v69, v63
	s_waitcnt vmcnt(13)
	v_cvt_pk_f16_f32 v67, v58, v59
	v_cvt_pk_f16_f32 v66, v56, v57
	v_cvt_pk_f16_f32 v65, v54, v55
	v_cvt_pk_f16_f32 v64, v52, v53
	global_store_dwordx4 v160, v[64:67], s[40:41] sc1
	v_pk_mul_f32 v[68:69], v[68:69], v[68:69]
	v_mov_b32_e32 v70, v55
	s_waitcnt vmcnt(12)
	v_cvt_pk_f16_f32 v67, v34, v35
	v_cvt_pk_f16_f32 v66, v32, v33
	v_cvt_pk_f16_f32 v65, v30, v31
	v_cvt_pk_f16_f32 v64, v28, v29
	global_store_dwordx4 v160, v[64:67], s[28:29] offset:1024 sc1
	v_mov_b32_e32 v71, v59
	v_pk_mul_f32 v[70:71], v[70:71], v[70:71]
	s_waitcnt vmcnt(11)
	v_cvt_pk_f16_f32 v67, v46, v47
	v_cvt_pk_f16_f32 v66, v44, v45
	v_cvt_pk_f16_f32 v65, v42, v43
	v_cvt_pk_f16_f32 v64, v40, v41
	global_store_dwordx4 v160, v[64:67], s[40:41] offset:1024 sc1
	s_waitcnt vmcnt(11)
	v_mul_f32_e32 v85, v16, v16
	v_cvt_pk_f16_f32 v65, v18, v19
	v_cvt_pk_f16_f32 v64, v16, v17
	s_waitcnt vmcnt(10)
	v_cvt_pk_f16_f32 v67, v22, v23
	v_cvt_pk_f16_f32 v66, v20, v21
	global_store_dwordx4 v160, v[64:67], s[28:29] offset:2048 sc1
	s_waitcnt vmcnt(10)
	s_nop 0
	v_cvt_pk_f16_f32 v65, v26, v27
	v_cvt_pk_f16_f32 v64, v24, v25
	s_waitcnt vmcnt(9)
	v_cvt_pk_f16_f32 v67, v38, v39
	v_cvt_pk_f16_f32 v66, v36, v37
	global_store_dwordx4 v160, v[64:67], s[40:41] offset:2048 sc1
	s_waitcnt vmcnt(9)
	s_nop 0
	v_cvt_pk_f16_f32 v65, v2, v3
	v_cvt_pk_f16_f32 v64, v0, v1
	s_waitcnt vmcnt(8)
	v_cvt_pk_f16_f32 v67, v6, v7
	v_cvt_pk_f16_f32 v66, v4, v5
	global_store_dwordx4 v160, v[64:67], s[28:29] offset:3072 sc1
	s_waitcnt vmcnt(8)
	s_nop 0
	v_cvt_pk_f16_f32 v65, v14, v15
	v_cvt_pk_f16_f32 v64, v12, v13
	s_waitcnt vmcnt(7)
	v_cvt_pk_f16_f32 v67, v10, v11
	v_cvt_pk_f16_f32 v66, v8, v9
	global_store_dwordx4 v160, v[64:67], s[40:41] offset:3072 sc1
	s_nop 1
	v_mov_b32_e32 v66, v49
	v_mov_b32_e32 v67, v61
	v_mov_b32_e32 v64, v48
	v_mov_b32_e32 v65, v60
	v_pk_mul_f32 v[66:67], v[66:67], v[66:67]
	s_nop 0
	v_pk_fma_f32 v[64:65], v[64:65], v[64:65], v[66:67]
	v_mov_b32_e32 v66, v50
	v_mov_b32_e32 v67, v62
	v_pk_fma_f32 v[66:67], v[66:67], v[66:67], v[68:69]
	v_mov_b32_e32 v68, v53
	v_mov_b32_e32 v69, v57
	v_pk_add_f32 v[64:65], v[64:65], v[66:67]
	v_mov_b32_e32 v66, v52
	v_mov_b32_e32 v67, v56
	v_pk_mul_f32 v[68:69], v[68:69], v[68:69]
	v_pk_add_f32 v[64:65], v[64:65], v[64:65] op_sel:[0,1] op_sel_hi:[1,0]
	v_pk_fma_f32 v[66:67], v[66:67], v[66:67], v[68:69]
	v_mov_b32_e32 v68, v54
	v_mov_b32_e32 v69, v58
	v_pk_fma_f32 v[68:69], v[68:69], v[68:69], v[70:71]
	v_pk_mul_f32 v[70:71], v[28:29], v[28:29]
	v_pk_add_f32 v[66:67], v[66:67], v[68:69]
	v_pk_mul_f32 v[68:69], v[30:31], v[30:31]
	v_mov_b32_e32 v65, v85
	v_pk_mov_b32 v[86:87], v[70:71], v[68:69] op_sel:[1,0]
	v_mov_b32_e32 v71, v69
	v_pk_add_f32 v[68:69], v[86:87], v[70:71]
	v_pk_mul_f32 v[70:71], v[42:43], v[42:43]
	v_pk_mul_f32 v[86:87], v[40:41], v[40:41]
	v_pk_add_f32 v[68:69], v[68:69], v[68:69] op_sel:[0,1] op_sel_hi:[1,0]
	v_pk_mov_b32 v[88:89], v[86:87], v[70:71] op_sel:[1,0]
	v_mov_b32_e32 v87, v71
	v_pk_add_f32 v[70:71], v[88:89], v[86:87]
	v_mul_f32_e32 v86, v17, v17
	v_mov_b32_e32 v69, v86
	v_pk_add_f32 v[64:65], v[64:65], v[68:69]
	v_mul_f32_e32 v68, v33, v33
	v_mul_f32_e32 v87, v18, v18
	v_pk_fma_f32 v[68:69], v[32:33], v[32:33], v[68:69] op_sel_hi:[1,1,0]
	v_mul_f32_e32 v86, v35, v35
	v_mul_f32_e32 v88, v19, v19
	v_mov_b32_e32 v69, v87
	v_pk_fma_f32 v[86:87], v[34:35], v[34:35], v[86:87] op_sel_hi:[1,1,0]
	v_pk_add_f32 v[66:67], v[66:67], v[66:67] op_sel:[0,1] op_sel_hi:[1,0]
	v_mov_b32_e32 v87, v88
	v_pk_add_f32 v[68:69], v[68:69], v[86:87]
	v_mul_f32_e32 v85, v25, v25
	v_pk_add_f32 v[64:65], v[64:65], v[68:69]
	v_mul_f32_e32 v68, v24, v24
	v_mov_b32_e32 v67, v68
	v_pk_add_f32 v[68:69], v[70:71], v[70:71] op_sel:[0,1] op_sel_hi:[1,0]
	v_mul_f32_e32 v70, v47, v47
	v_mov_b32_e32 v69, v85
	v_pk_add_f32 v[66:67], v[66:67], v[68:69]
	v_mul_f32_e32 v68, v45, v45
	v_mul_f32_e32 v86, v26, v26
	v_mul_f32_e32 v87, v27, v27
	v_pk_fma_f32 v[68:69], v[44:45], v[44:45], v[68:69] op_sel_hi:[1,1,0]
	v_pk_fma_f32 v[70:71], v[46:47], v[46:47], v[70:71] op_sel_hi:[1,1,0]
	v_mov_b32_e32 v69, v86
	v_mov_b32_e32 v71, v87
	v_pk_add_f32 v[68:69], v[68:69], v[70:71]
	v_pk_mul_f32 v[70:71], v[20:21], v[20:21]
	v_pk_add_f32 v[66:67], v[66:67], v[68:69]
	v_pk_mul_f32 v[68:69], v[22:23], v[22:23]
	v_mul_f32_e32 v85, v4, v4
	v_pk_mov_b32 v[86:87], v[70:71], v[68:69] op_sel:[1,0]
	v_mov_b32_e32 v71, v69
	v_pk_add_f32 v[68:69], v[86:87], v[70:71]
	v_pk_mul_f32 v[70:71], v[38:39], v[38:39]
	v_pk_mul_f32 v[86:87], v[36:37], v[36:37]
	v_pk_add_f32 v[64:65], v[64:65], v[64:65] op_sel:[0,1] op_sel_hi:[1,0]
	v_pk_mov_b32 v[88:89], v[86:87], v[70:71] op_sel:[1,0]
	v_mov_b32_e32 v87, v71
	v_pk_add_f32 v[70:71], v[88:89], v[86:87]
	v_mul_f32_e32 v86, v5, v5
	v_pk_add_f32 v[68:69], v[68:69], v[68:69] op_sel:[0,1] op_sel_hi:[1,0]
	v_mov_b32_e32 v65, v85
	v_mov_b32_e32 v69, v86
	v_pk_add_f32 v[64:65], v[64:65], v[68:69]
	v_mul_f32_e32 v68, v1, v1
	v_mul_f32_e32 v87, v6, v6
	v_pk_fma_f32 v[68:69], v[0:1], v[0:1], v[68:69] op_sel_hi:[1,1,0]
	v_mul_f32_e32 v86, v3, v3
	v_mul_f32_e32 v88, v7, v7
	v_mov_b32_e32 v69, v87
	v_pk_fma_f32 v[86:87], v[2:3], v[2:3], v[86:87] op_sel_hi:[1,1,0]
	s_nop 0
	v_mov_b32_e32 v87, v88
	v_pk_add_f32 v[68:69], v[68:69], v[86:87]
	v_mul_f32_e32 v86, v10, v10
	v_pk_add_f32 v[64:65], v[64:65], v[68:69]
	v_mul_f32_e32 v68, v8, v8
	v_add_f32_e32 v85, v64, v65
	v_mul_f32_e32 v69, v9, v9
	v_pk_add_f32 v[64:65], v[66:67], v[66:67] op_sel:[0,1] op_sel_hi:[1,0]
	v_pk_add_f32 v[66:67], v[70:71], v[70:71] op_sel:[0,1] op_sel_hi:[1,0]
	v_mov_b32_e32 v65, v68
	v_mov_b32_e32 v67, v69
	v_pk_add_f32 v[64:65], v[64:65], v[66:67]
	v_mul_f32_e32 v66, v13, v13
	v_mul_f32_e32 v68, v15, v15
	v_mul_f32_e32 v87, v11, v11
	v_pk_fma_f32 v[66:67], v[12:13], v[12:13], v[66:67] op_sel_hi:[1,1,0]
	v_pk_fma_f32 v[68:69], v[14:15], v[14:15], v[68:69] op_sel_hi:[1,1,0]
	v_mov_b32_e32 v67, v86
	v_mov_b32_e32 v69, v87
	v_pk_add_f32 v[66:67], v[66:67], v[68:69]
	s_nop 0
	v_pk_add_f32 v[64:65], v[64:65], v[66:67]
	s_nop 0
	v_add_f32_e32 v64, v64, v65
	ds_swizzle_b32 v65, v85 offset:swizzle(SWAP,1)
	ds_swizzle_b32 v66, v64 offset:swizzle(SWAP,1)
	s_waitcnt lgkmcnt(0)
	v_add_f32_e32 v65, v85, v65
	s_waitcnt lgkmcnt(0)
	v_add_f32_e32 v64, v64, v66
	ds_swizzle_b32 v66, v65 offset:swizzle(SWAP,2)
	s_waitcnt lgkmcnt(0)
	v_add_f32_e32 v65, v65, v66
	ds_swizzle_b32 v66, v64 offset:swizzle(SWAP,2)
	s_waitcnt lgkmcnt(0)
	v_add_f32_e32 v64, v64, v66
	ds_swizzle_b32 v66, v65 offset:swizzle(SWAP,4)
	s_waitcnt lgkmcnt(0)
	v_add_f32_e32 v65, v65, v66
	ds_swizzle_b32 v66, v64 offset:swizzle(SWAP,4)
	s_waitcnt lgkmcnt(0)
	v_add_f32_e32 v64, v64, v66
	ds_swizzle_b32 v66, v65 offset:swizzle(SWAP,8)
	s_waitcnt lgkmcnt(0)
	v_add_f32_e32 v65, v65, v66
	ds_swizzle_b32 v66, v64 offset:swizzle(SWAP,8)
	s_waitcnt lgkmcnt(0)
	v_add_f32_e32 v64, v64, v66
	ds_swizzle_b32 v66, v65 offset:swizzle(SWAP,16)
	s_waitcnt lgkmcnt(0)
	v_add_f32_e32 v65, v65, v66
	ds_swizzle_b32 v66, v64 offset:swizzle(SWAP,16)
	s_waitcnt lgkmcnt(0)
	v_add_f32_e32 v68, v64, v66
	v_mov_b32_e32 v64, v65
	s_nop 1
	v_permlane32_swap_b32_e32 v65, v64
	v_mov_b32_e32 v70, v68
	v_add_f32_e32 v69, v65, v64
	s_nop 0
	v_permlane32_swap_b32_e32 v68, v70
.LBB0_103:
	v_fmamk_f32 v65, v69, 0x3a000000, v254
	v_cmp_gt_f32_e32 vcc, s76, v65
	v_mul_f32_e32 v66, 0x4f800000, v65
	s_lshl_b64 s[24:25], s[24:25], 1
	v_cndmask_b32_e32 v65, v65, v66, vcc
	v_sqrt_f32_e32 v66, v65
	s_add_u32 s40, s52, s24
	v_add_f32_e32 v64, v68, v70
	s_addc_u32 s41, s53, s25
	v_add_u32_e32 v67, -1, v66
	v_fma_f32 v68, -v67, v66, v65
	v_cmp_ge_f32_e64 s[24:25], 0, v68
	v_add_u32_e32 v68, 1, v66
	v_fmamk_f32 v64, v64, 0x3a000000, v254
	v_cndmask_b32_e64 v67, v66, v67, s[24:25]
	v_fma_f32 v66, -v68, v66, v65
	v_cmp_lt_f32_e64 s[24:25], 0, v66
	v_lshl_add_u64 v[96:97], s[28:29], 0, v[160:161]
	s_nop 0
	v_cndmask_b32_e64 v66, v67, v68, s[24:25]
	v_mul_f32_e32 v67, 0x37800000, v66
	v_cndmask_b32_e32 v66, v66, v67, vcc
	v_cmp_class_f32_e32 vcc, v65, v229
	s_nop 1
	v_cndmask_b32_e32 v65, v66, v65, vcc
	v_div_scale_f32 v66, s[24:25], v65, v65, 1.0
	v_rcp_f32_e32 v67, v66
	s_nop 0
	v_fma_f32 v68, -v66, v67, 1.0
	v_fmac_f32_e32 v67, v68, v67
	v_div_scale_f32 v68, vcc, 1.0, v65, 1.0
	v_mul_f32_e32 v69, v68, v67
	v_fma_f32 v70, -v66, v69, v68
	v_fmac_f32_e32 v69, v70, v67
	v_fma_f32 v66, -v66, v69, v68
	v_div_fmas_f32 v66, v66, v67, v69
	v_div_fixup_f32 v92, v66, v65, 1.0
	v_cmp_gt_f32_e32 vcc, s76, v64
	v_mul_f32_e32 v65, 0x4f800000, v64
	v_pk_mul_f32 v[48:49], v[48:49], v[92:93] op_sel_hi:[1,0]
	v_cndmask_b32_e32 v64, v64, v65, vcc
	v_sqrt_f32_e32 v65, v64
	v_pk_mul_f32 v[50:51], v[50:51], v[92:93] op_sel_hi:[1,0]
	v_pk_mul_f32 v[28:29], v[28:29], v[92:93] op_sel_hi:[1,0]
	v_pk_mul_f32 v[30:31], v[30:31], v[92:93] op_sel_hi:[1,0]
	v_add_u32_e32 v66, -1, v65
	v_fma_f32 v67, -v66, v65, v64
	v_cmp_ge_f32_e64 s[24:25], 0, v67
	v_add_u32_e32 v67, 1, v65
	v_pk_mul_f32 v[16:17], v[16:17], v[92:93] op_sel_hi:[1,0]
	v_cndmask_b32_e64 v66, v65, v66, s[24:25]
	v_fma_f32 v65, -v67, v65, v64
	v_cmp_lt_f32_e64 s[24:25], 0, v65
	v_pk_mul_f32 v[18:19], v[18:19], v[92:93] op_sel_hi:[1,0]
	v_pk_mul_f32 v[0:1], v[0:1], v[92:93] op_sel_hi:[1,0]
	v_cndmask_b32_e64 v65, v66, v67, s[24:25]
	v_mul_f32_e32 v66, 0x37800000, v65
	v_cndmask_b32_e32 v65, v65, v66, vcc
	v_cmp_class_f32_e32 vcc, v64, v229
	v_pk_mul_f32 v[2:3], v[2:3], v[92:93] op_sel_hi:[1,0]
	s_nop 0
	v_cndmask_b32_e32 v64, v65, v64, vcc
	v_div_scale_f32 v65, s[24:25], v64, v64, 1.0
	v_rcp_f32_e32 v66, v65
	s_brev_b32 s24, 47
	s_mov_b32 s25, -1
	v_lshl_add_u64 v[90:91], v[96:97], 0, s[24:25]
	v_fma_f32 v67, -v65, v66, 1.0
	v_fmac_f32_e32 v66, v67, v66
	v_div_scale_f32 v67, vcc, 1.0, v64, 1.0
	v_mul_f32_e32 v68, v67, v66
	v_fma_f32 v69, -v65, v68, v67
	v_fmac_f32_e32 v68, v69, v66
	v_fma_f32 v65, -v65, v68, v67
	v_div_fmas_f32 v65, v65, v66, v68
	v_div_fixup_f32 v94, v65, v64, 1.0
	v_pk_mul_f32 v[54:55], v[54:55], v[94:95] op_sel_hi:[1,0]
	v_pk_mul_f32 v[52:53], v[52:53], v[94:95] op_sel_hi:[1,0]
	s_brev_b32 s24, 47
	v_pk_mul_f32 v[88:89], v[134:135], v[48:49]
	v_pk_mul_f32 v[86:87], v[136:137], v[50:51]
	v_pk_mul_f32 v[50:51], v[60:61], v[92:93] op_sel_hi:[1,0]
	v_pk_mul_f32 v[60:61], v[136:137], v[54:55]
	v_pk_mul_f32 v[54:55], v[56:57], v[94:95] op_sel_hi:[1,0]
	v_bfe_u32 v56, v88, 16, 1
	v_add3_u32 v56, v88, v56, s75
	v_bfe_u32 v57, v89, 16, 1
	v_lshrrev_b32_e32 v56, 16, v56
	v_add3_u32 v57, v89, v57, s75
	v_and_or_b32 v56, v57, s55, v56
	v_bfe_u32 v57, v86, 16, 1
	v_pk_mul_f32 v[48:49], v[62:63], v[92:93] op_sel_hi:[1,0]
	v_pk_mul_f32 v[62:63], v[134:135], v[52:53]
	v_pk_mul_f32 v[52:53], v[58:59], v[94:95] op_sel_hi:[1,0]
	v_add3_u32 v57, v86, v57, s75
	v_bfe_u32 v58, v87, 16, 1
	v_pk_mul_f32 v[50:51], v[130:131], v[50:51]
	v_lshrrev_b32_e32 v57, 16, v57
	v_add3_u32 v58, v87, v58, s75
	v_and_or_b32 v57, v58, s55, v57
	v_bfe_u32 v58, v50, 16, 1
	v_add3_u32 v58, v50, v58, s75
	v_bfe_u32 v59, v51, 16, 1
	v_pk_mul_f32 v[48:49], v[132:133], v[48:49]
	v_lshrrev_b32_e32 v58, 16, v58
	v_add3_u32 v59, v51, v59, s75
	v_and_or_b32 v58, v59, s55, v58
	v_bfe_u32 v59, v48, 16, 1
	v_pk_mul_f32 v[54:55], v[130:131], v[54:55]
	v_add3_u32 v59, v48, v59, s75
	v_bfe_u32 v64, v49, 16, 1
	v_lshrrev_b32_e32 v59, 16, v59
	v_add3_u32 v64, v49, v64, s75
	v_and_or_b32 v59, v64, s55, v59
	v_bfe_u32 v64, v62, 16, 1
	v_add3_u32 v64, v62, v64, s75
	v_bfe_u32 v65, v63, 16, 1
	v_lshrrev_b32_e32 v64, 16, v64
	v_add3_u32 v65, v63, v65, s75
	v_and_or_b32 v64, v65, s55, v64
	v_bfe_u32 v65, v60, 16, 1
	v_pk_mul_f32 v[52:53], v[132:133], v[52:53]
	v_add3_u32 v65, v60, v65, s75
	v_bfe_u32 v66, v61, 16, 1
	v_lshrrev_b32_e32 v65, 16, v65
	v_add3_u32 v66, v61, v66, s75
	v_and_or_b32 v65, v66, s55, v65
	v_bfe_u32 v66, v54, 16, 1
	v_add3_u32 v66, v54, v66, s75
	v_bfe_u32 v67, v55, 16, 1
	v_lshrrev_b32_e32 v66, 16, v66
	v_add3_u32 v67, v55, v67, s75
	v_and_or_b32 v66, v67, s55, v66
	v_bfe_u32 v67, v52, 16, 1
	v_add3_u32 v67, v52, v67, s75
	v_bfe_u32 v68, v53, 16, 1
	v_lshrrev_b32_e32 v67, 16, v67
	v_add3_u32 v68, v53, v68, s75
	v_and_or_b32 v67, v68, s55, v67
	v_add_co_u32_e32 v68, vcc, s24, v96
	s_nop 1
	v_addc_co_u32_e32 v69, vcc, -1, v97, vcc
	global_store_dwordx4 v[68:69], v[56:59], off sc1
	global_store_dwordx4 v160, v[64:67], s[40:41] sc1
	s_nop 0
	v_pk_mul_f32 v[58:59], v[142:143], v[28:29]
	v_pk_mul_f32 v[28:29], v[34:35], v[92:93] op_sel_hi:[1,0]
	v_pk_mul_f32 v[34:35], v[42:43], v[94:95] op_sel_hi:[1,0]
	v_pk_mul_f32 v[56:57], v[144:145], v[30:31]
	v_pk_mul_f32 v[30:31], v[32:33], v[92:93] op_sel_hi:[1,0]
	v_pk_mul_f32 v[32:33], v[40:41], v[94:95] op_sel_hi:[1,0]
	v_pk_mul_f32 v[40:41], v[144:145], v[34:35]
	v_pk_mul_f32 v[34:35], v[44:45], v[94:95] op_sel_hi:[1,0]
	v_bfe_u32 v44, v58, 16, 1
	v_add3_u32 v44, v58, v44, s75
	v_bfe_u32 v45, v59, 16, 1
	v_lshrrev_b32_e32 v44, 16, v44
	v_add3_u32 v45, v59, v45, s75
	v_and_or_b32 v44, v45, s55, v44
	v_bfe_u32 v45, v56, 16, 1
	v_pk_mul_f32 v[42:43], v[142:143], v[32:33]
	v_pk_mul_f32 v[32:33], v[46:47], v[94:95] op_sel_hi:[1,0]
	v_add3_u32 v45, v56, v45, s75
	v_bfe_u32 v46, v57, 16, 1
	v_pk_mul_f32 v[30:31], v[138:139], v[30:31]
	v_lshrrev_b32_e32 v45, 16, v45
	v_add3_u32 v46, v57, v46, s75
	v_and_or_b32 v45, v46, s55, v45
	v_bfe_u32 v46, v30, 16, 1
	v_add3_u32 v46, v30, v46, s75
	v_bfe_u32 v47, v31, 16, 1
	v_pk_mul_f32 v[28:29], v[140:141], v[28:29]
	v_lshrrev_b32_e32 v46, 16, v46
	v_add3_u32 v47, v31, v47, s75
	v_and_or_b32 v46, v47, s55, v46
	v_bfe_u32 v47, v28, 16, 1
	v_pk_mul_f32 v[34:35], v[138:139], v[34:35]
	v_add3_u32 v47, v28, v47, s75
	v_bfe_u32 v64, v29, 16, 1
	v_lshrrev_b32_e32 v47, 16, v47
	v_add3_u32 v64, v29, v64, s75
	v_and_or_b32 v47, v64, s55, v47
	v_bfe_u32 v64, v42, 16, 1
	v_add3_u32 v64, v42, v64, s75
	v_bfe_u32 v65, v43, 16, 1
	v_lshrrev_b32_e32 v64, 16, v64
	v_add3_u32 v65, v43, v65, s75
	v_and_or_b32 v64, v65, s55, v64
	v_bfe_u32 v65, v40, 16, 1
	v_pk_mul_f32 v[32:33], v[140:141], v[32:33]
	v_add3_u32 v65, v40, v65, s75
	v_bfe_u32 v66, v41, 16, 1
	v_lshrrev_b32_e32 v65, 16, v65
	v_add3_u32 v66, v41, v66, s75
	v_and_or_b32 v65, v66, s55, v65
	v_bfe_u32 v66, v34, 16, 1
	v_add3_u32 v66, v34, v66, s75
	v_bfe_u32 v67, v35, 16, 1
	v_lshrrev_b32_e32 v66, 16, v66
	v_add3_u32 v67, v35, v67, s75
	v_and_or_b32 v66, v67, s55, v66
	v_bfe_u32 v67, v32, 16, 1
	v_add3_u32 v67, v32, v67, s75
	v_bfe_u32 v68, v33, 16, 1
	v_lshrrev_b32_e32 v67, 16, v67
	v_add3_u32 v68, v33, v68, s75
	v_and_or_b32 v67, v68, s55, v67
	global_store_dwordx4 v[90:91], v[44:47], off offset:1024 sc1
	global_store_dwordx4 v160, v[64:67], s[40:41] offset:1024 sc1
	s_nop 0
	v_pk_mul_f32 v[46:47], v[150:151], v[16:17]
	v_pk_mul_f32 v[16:17], v[22:23], v[92:93] op_sel_hi:[1,0]
	v_pk_mul_f32 v[22:23], v[26:27], v[94:95] op_sel_hi:[1,0]
	v_pk_mul_f32 v[44:45], v[152:153], v[18:19]
	v_pk_mul_f32 v[18:19], v[20:21], v[92:93] op_sel_hi:[1,0]
	v_pk_mul_f32 v[20:21], v[24:25], v[94:95] op_sel_hi:[1,0]
	v_pk_mul_f32 v[24:25], v[152:153], v[22:23]
	v_pk_mul_f32 v[22:23], v[36:37], v[94:95] op_sel_hi:[1,0]
	v_bfe_u32 v36, v46, 16, 1
	v_add3_u32 v36, v46, v36, s75
	v_bfe_u32 v37, v47, 16, 1
	v_lshrrev_b32_e32 v36, 16, v36
	v_add3_u32 v37, v47, v37, s75
	v_and_or_b32 v36, v37, s55, v36
	v_bfe_u32 v37, v44, 16, 1
	v_pk_mul_f32 v[26:27], v[150:151], v[20:21]
	v_pk_mul_f32 v[20:21], v[38:39], v[94:95] op_sel_hi:[1,0]
	v_add3_u32 v37, v44, v37, s75
	v_bfe_u32 v38, v45, 16, 1
	v_pk_mul_f32 v[18:19], v[18:19], v[146:147]
	v_lshrrev_b32_e32 v37, 16, v37
	v_add3_u32 v38, v45, v38, s75
	v_and_or_b32 v37, v38, s55, v37
	v_bfe_u32 v38, v18, 16, 1
	v_add3_u32 v38, v18, v38, s75
	v_bfe_u32 v39, v19, 16, 1
	v_pk_mul_f32 v[16:17], v[16:17], v[148:149]
	v_lshrrev_b32_e32 v38, 16, v38
	v_add3_u32 v39, v19, v39, s75
	v_and_or_b32 v38, v39, s55, v38
	v_bfe_u32 v39, v16, 16, 1
	v_pk_mul_f32 v[22:23], v[146:147], v[22:23]
	v_add3_u32 v39, v16, v39, s75
	v_bfe_u32 v64, v17, 16, 1
	v_lshrrev_b32_e32 v39, 16, v39
	v_add3_u32 v64, v17, v64, s75
	v_and_or_b32 v39, v64, s55, v39
	v_bfe_u32 v64, v26, 16, 1
	v_add3_u32 v64, v26, v64, s75
	v_bfe_u32 v65, v27, 16, 1
	v_lshrrev_b32_e32 v64, 16, v64
	v_add3_u32 v65, v27, v65, s75
	v_and_or_b32 v64, v65, s55, v64
	v_bfe_u32 v65, v24, 16, 1
	v_pk_mul_f32 v[20:21], v[148:149], v[20:21]
	v_add3_u32 v65, v24, v65, s75
	v_bfe_u32 v66, v25, 16, 1
	v_lshrrev_b32_e32 v65, 16, v65
	v_add3_u32 v66, v25, v66, s75
	v_and_or_b32 v65, v66, s55, v65
	v_bfe_u32 v66, v22, 16, 1
	v_add3_u32 v66, v22, v66, s75
	v_bfe_u32 v67, v23, 16, 1
	v_lshrrev_b32_e32 v66, 16, v66
	v_add3_u32 v67, v23, v67, s75
	v_and_or_b32 v66, v67, s55, v66
	v_bfe_u32 v67, v20, 16, 1
	v_add3_u32 v67, v20, v67, s75
	v_bfe_u32 v68, v21, 16, 1
	v_lshrrev_b32_e32 v67, 16, v67
	v_add3_u32 v68, v21, v68, s75
	v_and_or_b32 v67, v68, s55, v67
	global_store_dwordx4 v[90:91], v[36:39], off offset:2048 sc1
	global_store_dwordx4 v160, v[64:67], s[40:41] offset:2048 sc1
	s_nop 0
	v_pk_mul_f32 v[36:37], v[2:3], v[164:165]
	v_pk_mul_f32 v[38:39], v[0:1], v[162:163]
	v_pk_mul_f32 v[2:3], v[4:5], v[92:93] op_sel_hi:[1,0]
	v_pk_mul_f32 v[0:1], v[6:7], v[92:93] op_sel_hi:[1,0]
	v_pk_mul_f32 v[6:7], v[14:15], v[94:95] op_sel_hi:[1,0]
	v_pk_mul_f32 v[4:5], v[2:3], v[154:155]
	v_pk_mul_f32 v[2:3], v[12:13], v[94:95] op_sel_hi:[1,0]
	v_pk_mul_f32 v[12:13], v[6:7], v[164:165]
	v_pk_mul_f32 v[6:7], v[8:9], v[94:95] op_sel_hi:[1,0]
	v_bfe_u32 v8, v38, 16, 1
	v_add3_u32 v8, v38, v8, s75
	v_bfe_u32 v9, v39, 16, 1
	v_lshrrev_b32_e32 v8, 16, v8
	v_add3_u32 v9, v39, v9, s75
	v_and_or_b32 v8, v9, s55, v8
	v_bfe_u32 v9, v36, 16, 1
	v_pk_mul_f32 v[14:15], v[2:3], v[162:163]
	v_pk_mul_f32 v[2:3], v[10:11], v[94:95] op_sel_hi:[1,0]
	v_add3_u32 v9, v36, v9, s75
	v_bfe_u32 v10, v37, 16, 1
	v_lshrrev_b32_e32 v9, 16, v9
	v_add3_u32 v10, v37, v10, s75
	v_and_or_b32 v9, v10, s55, v9
	v_bfe_u32 v10, v4, 16, 1
	v_add3_u32 v10, v4, v10, s75
	v_bfe_u32 v11, v5, 16, 1
	v_pk_mul_f32 v[0:1], v[0:1], v[156:157]
	v_lshrrev_b32_e32 v10, 16, v10
	v_add3_u32 v11, v5, v11, s75
	v_and_or_b32 v10, v11, s55, v10
	v_bfe_u32 v11, v0, 16, 1
	v_pk_mul_f32 v[6:7], v[6:7], v[154:155]
	v_add3_u32 v11, v0, v11, s75
	v_bfe_u32 v64, v1, 16, 1
	v_lshrrev_b32_e32 v11, 16, v11
	v_add3_u32 v64, v1, v64, s75
	v_and_or_b32 v11, v64, s55, v11
	v_bfe_u32 v64, v14, 16, 1
	v_add3_u32 v64, v14, v64, s75
	v_bfe_u32 v65, v15, 16, 1
	v_lshrrev_b32_e32 v64, 16, v64
	v_add3_u32 v65, v15, v65, s75
	v_and_or_b32 v64, v65, s55, v64
	v_bfe_u32 v65, v12, 16, 1
	v_pk_mul_f32 v[2:3], v[2:3], v[156:157]
	v_add3_u32 v65, v12, v65, s75
	v_bfe_u32 v66, v13, 16, 1
	v_lshrrev_b32_e32 v65, 16, v65
	v_add3_u32 v66, v13, v66, s75
	v_and_or_b32 v65, v66, s55, v65
	v_bfe_u32 v66, v6, 16, 1
	v_add3_u32 v66, v6, v66, s75
	v_bfe_u32 v67, v7, 16, 1
	v_lshrrev_b32_e32 v66, 16, v66
	v_add3_u32 v67, v7, v67, s75
	v_and_or_b32 v66, v67, s55, v66
	v_bfe_u32 v67, v2, 16, 1
	v_add3_u32 v67, v2, v67, s75
	v_bfe_u32 v68, v3, 16, 1
	v_lshrrev_b32_e32 v67, 16, v67
	v_add3_u32 v68, v3, v68, s75
	v_and_or_b32 v67, v68, s55, v67
	global_store_dwordx4 v[90:91], v[8:11], off offset:3072 sc1
	global_store_dwordx4 v160, v[64:67], s[40:41] offset:3072 sc1
	ds_read_b128 v[8:11], v93
	ds_read_b128 v[94:97], v93 offset:24576
	s_waitcnt lgkmcnt(0)
	v_mul_f32_e32 v64, v89, v9
	v_mul_f32_e32 v9, v63, v9
	v_fmac_f32_e32 v64, v88, v8
	v_fmac_f32_e32 v9, v62, v8
	v_mul_f32_e32 v8, v61, v11
	v_mul_f32_e32 v65, v87, v11
	v_fmac_f32_e32 v8, v60, v10
	v_fmac_f32_e32 v65, v86, v10
	v_add_f32_e32 v8, v9, v8
	v_add_f32_e32 v64, v64, v65
	v_add_f32_e32 v65, 0, v8
	ds_read_b128 v[8:11], v93 offset:1024
	v_add_f32_e32 v64, 0, v64
	s_waitcnt lgkmcnt(0)
	v_mul_f32_e32 v66, v51, v9
	v_mul_f32_e32 v9, v55, v9
	v_fmac_f32_e32 v66, v50, v8
	v_fmac_f32_e32 v9, v54, v8
	v_mul_f32_e32 v8, v53, v11
	v_fmac_f32_e32 v8, v52, v10
	v_mul_f32_e32 v67, v49, v11
	v_add_f32_e32 v8, v9, v8
	v_fmac_f32_e32 v67, v48, v10
	v_add_f32_e32 v65, v65, v8
	ds_read_b128 v[8:11], v93 offset:2048
	v_add_f32_e32 v66, v66, v67
	v_add_f32_e32 v64, v64, v66
	s_waitcnt lgkmcnt(0)
	v_mul_f32_e32 v66, v59, v9
	v_mul_f32_e32 v9, v43, v9
	v_fmac_f32_e32 v66, v58, v8
	v_fmac_f32_e32 v9, v42, v8
	v_mul_f32_e32 v8, v41, v11
	v_fmac_f32_e32 v8, v40, v10
	v_mul_f32_e32 v67, v57, v11
	v_add_f32_e32 v8, v9, v8
	v_fmac_f32_e32 v67, v56, v10
	v_add_f32_e32 v65, v65, v8
	ds_read_b128 v[8:11], v93 offset:3072
	v_add_f32_e32 v66, v66, v67
	v_add_f32_e32 v64, v64, v66
	s_waitcnt lgkmcnt(0)
	v_mul_f32_e32 v66, v31, v9
	v_mul_f32_e32 v9, v35, v9
	v_fmac_f32_e32 v66, v30, v8
	v_fmac_f32_e32 v9, v34, v8
	v_mul_f32_e32 v8, v33, v11
	v_fmac_f32_e32 v8, v32, v10
	v_mul_f32_e32 v67, v29, v11
	v_add_f32_e32 v8, v9, v8
	v_fmac_f32_e32 v67, v28, v10
	v_add_f32_e32 v65, v65, v8
	ds_read_b128 v[8:11], v93 offset:4096
	v_add_f32_e32 v66, v66, v67
	v_add_f32_e32 v64, v64, v66
	s_waitcnt lgkmcnt(0)
	v_mul_f32_e32 v66, v47, v9
	v_mul_f32_e32 v9, v27, v9
	v_fmac_f32_e32 v66, v46, v8
	v_fmac_f32_e32 v9, v26, v8
	v_mul_f32_e32 v8, v25, v11
	v_fmac_f32_e32 v8, v24, v10
	v_mul_f32_e32 v67, v45, v11
	v_add_f32_e32 v8, v9, v8
	v_fmac_f32_e32 v67, v44, v10
	v_add_f32_e32 v65, v65, v8
	ds_read_b128 v[8:11], v93 offset:5120
	v_add_f32_e32 v66, v66, v67
	v_add_f32_e32 v64, v64, v66
	s_waitcnt lgkmcnt(0)
	v_mul_f32_e32 v66, v19, v9
	v_mul_f32_e32 v9, v23, v9
	v_fmac_f32_e32 v66, v18, v8
	v_fmac_f32_e32 v9, v22, v8
	v_mul_f32_e32 v8, v21, v11
	v_fmac_f32_e32 v8, v20, v10
	v_mul_f32_e32 v67, v17, v11
	v_add_f32_e32 v8, v9, v8
	v_fmac_f32_e32 v67, v16, v10
	v_add_f32_e32 v65, v65, v8
	ds_read_b128 v[8:11], v93 offset:6144
	v_add_f32_e32 v66, v66, v67
	v_add_f32_e32 v64, v64, v66
	s_waitcnt lgkmcnt(0)
	v_mul_f32_e32 v66, v39, v9
	v_mul_f32_e32 v9, v15, v9
	v_fmac_f32_e32 v66, v38, v8
	v_fmac_f32_e32 v9, v14, v8
	v_mul_f32_e32 v8, v13, v11
	v_fmac_f32_e32 v8, v12, v10
	v_mul_f32_e32 v67, v37, v11
	v_add_f32_e32 v8, v9, v8
	v_fmac_f32_e32 v67, v36, v10
	v_add_f32_e32 v65, v65, v8
	ds_read_b128 v[8:11], v93 offset:7168
	v_add_f32_e32 v66, v66, v67
	v_add_f32_e32 v64, v64, v66
	s_waitcnt lgkmcnt(0)
	v_mul_f32_e32 v66, v5, v9
	v_mul_f32_e32 v67, v1, v11
	v_mul_f32_e32 v9, v7, v9
	v_fmac_f32_e32 v66, v4, v8
	v_fmac_f32_e32 v67, v0, v10
	v_fmac_f32_e32 v9, v6, v8
	v_mul_f32_e32 v8, v3, v11
	v_add_f32_e32 v66, v66, v67
	v_fmac_f32_e32 v8, v2, v10
	v_add_f32_e32 v64, v64, v66
	v_add_f32_e32 v8, v9, v8
	v_add_f32_e32 v10, v65, v8
	ds_swizzle_b32 v8, v64 offset:swizzle(SWAP,1)
	ds_swizzle_b32 v11, v10 offset:swizzle(SWAP,1)
	s_waitcnt lgkmcnt(1)
	v_add_f32_e32 v8, v64, v8
	ds_read_b128 v[64:67], v93 offset:8192
	s_waitcnt lgkmcnt(1)
	v_add_f32_e32 v10, v10, v11
	ds_swizzle_b32 v9, v8 offset:swizzle(SWAP,2)
	ds_swizzle_b32 v11, v10 offset:swizzle(SWAP,2)
	s_waitcnt lgkmcnt(2)
	v_mul_f32_e32 v68, v89, v65
	v_mul_f32_e32 v65, v63, v65
	v_fmac_f32_e32 v68, v88, v64
	v_fmac_f32_e32 v65, v62, v64
	v_mul_f32_e32 v64, v61, v67
	v_mul_f32_e32 v69, v87, v67
	v_fmac_f32_e32 v64, v60, v66
	v_fmac_f32_e32 v69, v86, v66
	v_add_f32_e32 v64, v65, v64
	v_add_f32_e32 v68, v68, v69
	v_add_f32_e32 v69, 0, v64
	ds_read_b128 v[64:67], v93 offset:9216
	v_add_f32_e32 v68, 0, v68
	s_waitcnt lgkmcnt(2)
	v_add_f32_e32 v8, v8, v9
	s_waitcnt lgkmcnt(1)
	v_add_f32_e32 v10, v10, v11
	ds_swizzle_b32 v9, v8 offset:swizzle(SWAP,4)
	s_waitcnt lgkmcnt(1)
	v_mul_f32_e32 v70, v51, v65
	v_mul_f32_e32 v65, v55, v65
	v_fmac_f32_e32 v70, v50, v64
	v_fmac_f32_e32 v65, v54, v64
	v_mul_f32_e32 v64, v53, v67
	v_fmac_f32_e32 v64, v52, v66
	v_mul_f32_e32 v71, v49, v67
	v_add_f32_e32 v64, v65, v64
	v_fmac_f32_e32 v71, v48, v66
	v_add_f32_e32 v69, v69, v64
	ds_read_b128 v[64:67], v93 offset:10240
	v_add_f32_e32 v70, v70, v71
	v_add_f32_e32 v68, v68, v70
	ds_swizzle_b32 v11, v10 offset:swizzle(SWAP,4)
	s_waitcnt lgkmcnt(2)
	v_add_f32_e32 v8, v8, v9
	s_waitcnt lgkmcnt(1)
	v_mul_f32_e32 v70, v59, v65
	v_mul_f32_e32 v65, v43, v65
	v_fmac_f32_e32 v70, v58, v64
	v_fmac_f32_e32 v65, v42, v64
	v_mul_f32_e32 v64, v41, v67
	v_fmac_f32_e32 v64, v40, v66
	v_mul_f32_e32 v71, v57, v67
	v_add_f32_e32 v64, v65, v64
	v_fmac_f32_e32 v71, v56, v66
	v_add_f32_e32 v69, v69, v64
	ds_read_b128 v[64:67], v93 offset:11264
	v_add_f32_e32 v70, v70, v71
	v_add_f32_e32 v68, v68, v70
	s_waitcnt lgkmcnt(1)
	v_add_f32_e32 v10, v10, v11
	ds_swizzle_b32 v9, v8 offset:swizzle(SWAP,8)
	s_waitcnt lgkmcnt(1)
	v_mul_f32_e32 v70, v31, v65
	v_mul_f32_e32 v65, v35, v65
	v_fmac_f32_e32 v70, v30, v64
	v_fmac_f32_e32 v65, v34, v64
	v_mul_f32_e32 v64, v33, v67
	v_fmac_f32_e32 v64, v32, v66
	v_mul_f32_e32 v71, v29, v67
	v_add_f32_e32 v64, v65, v64
	v_fmac_f32_e32 v71, v28, v66
	v_add_f32_e32 v69, v69, v64
	ds_read_b128 v[64:67], v93 offset:12288
	v_add_f32_e32 v70, v70, v71
	v_add_f32_e32 v68, v68, v70
	ds_swizzle_b32 v11, v10 offset:swizzle(SWAP,8)
	s_waitcnt lgkmcnt(2)
	v_add_f32_e32 v8, v8, v9
	s_waitcnt lgkmcnt(1)
	v_mul_f32_e32 v70, v47, v65
	v_mul_f32_e32 v65, v27, v65
	v_fmac_f32_e32 v70, v46, v64
	v_fmac_f32_e32 v65, v26, v64
	v_mul_f32_e32 v64, v25, v67
	v_fmac_f32_e32 v64, v24, v66
	v_mul_f32_e32 v71, v45, v67
	v_add_f32_e32 v64, v65, v64
	v_fmac_f32_e32 v71, v44, v66
	v_add_f32_e32 v69, v69, v64
	ds_read_b128 v[64:67], v93 offset:13312
	v_add_f32_e32 v70, v70, v71
	v_add_f32_e32 v68, v68, v70
	s_waitcnt lgkmcnt(1)
	v_add_f32_e32 v10, v10, v11
	ds_swizzle_b32 v9, v8 offset:swizzle(SWAP,16)
	s_waitcnt lgkmcnt(1)
	v_mul_f32_e32 v70, v19, v65
	v_mul_f32_e32 v65, v23, v65
	v_fmac_f32_e32 v70, v18, v64
	v_fmac_f32_e32 v65, v22, v64
	v_mul_f32_e32 v64, v21, v67
	v_fmac_f32_e32 v64, v20, v66
	v_mul_f32_e32 v71, v17, v67
	v_add_f32_e32 v64, v65, v64
	v_fmac_f32_e32 v71, v16, v66
	v_add_f32_e32 v69, v69, v64
	ds_read_b128 v[64:67], v93 offset:14336
	v_add_f32_e32 v70, v70, v71
	v_add_f32_e32 v68, v68, v70
	ds_swizzle_b32 v11, v10 offset:swizzle(SWAP,16)
	s_waitcnt lgkmcnt(2)
	v_add_f32_e32 v8, v8, v9
	s_waitcnt lgkmcnt(1)
	v_mul_f32_e32 v70, v39, v65
	v_mul_f32_e32 v65, v15, v65
	v_fmac_f32_e32 v70, v38, v64
	v_fmac_f32_e32 v65, v14, v64
	v_mul_f32_e32 v64, v13, v67
	v_fmac_f32_e32 v64, v12, v66
	v_mul_f32_e32 v71, v37, v67
	v_add_f32_e32 v64, v65, v64
	v_fmac_f32_e32 v71, v36, v66
	v_add_f32_e32 v69, v69, v64
	ds_read_b128 v[64:67], v93 offset:15360
	v_add_f32_e32 v70, v70, v71
	v_add_f32_e32 v68, v68, v70
	s_waitcnt lgkmcnt(1)
	v_add_f32_e32 v10, v10, v11
	v_mov_b32_e32 v9, v8
	s_waitcnt lgkmcnt(0)
	v_mul_f32_e32 v70, v5, v65
	v_mul_f32_e32 v71, v1, v67
	v_mul_f32_e32 v65, v7, v65
	v_fmac_f32_e32 v70, v4, v64
	v_fmac_f32_e32 v71, v0, v66
	v_fmac_f32_e32 v65, v6, v64
	v_mul_f32_e32 v64, v3, v67
	v_add_f32_e32 v70, v70, v71
	v_fmac_f32_e32 v64, v2, v66
	v_add_f32_e32 v68, v68, v70
	v_add_f32_e32 v64, v65, v64
	v_add_f32_e32 v66, v69, v64
	ds_swizzle_b32 v64, v68 offset:swizzle(SWAP,1)
	ds_swizzle_b32 v67, v66 offset:swizzle(SWAP,1)
	v_mov_b32_e32 v11, v10
	v_permlane32_swap_b32_e32 v8, v9
	s_waitcnt lgkmcnt(1)
	v_add_f32_e32 v64, v68, v64
	ds_read_b128 v[68:71], v93 offset:16384
	s_waitcnt lgkmcnt(1)
	v_add_f32_e32 v66, v66, v67
	ds_swizzle_b32 v65, v64 offset:swizzle(SWAP,2)
	ds_swizzle_b32 v67, v66 offset:swizzle(SWAP,2)
	v_permlane32_swap_b32_e32 v10, v11
	s_waitcnt lgkmcnt(2)
	v_mul_f32_e32 v85, v89, v69
	v_mul_f32_e32 v69, v63, v69
	v_fmac_f32_e32 v85, v88, v68
	v_fmac_f32_e32 v69, v62, v68
	v_mul_f32_e32 v68, v61, v71
	v_mul_f32_e32 v90, v87, v71
	v_fmac_f32_e32 v68, v60, v70
	v_fmac_f32_e32 v90, v86, v70
	v_add_f32_e32 v68, v69, v68
	v_add_f32_e32 v85, v85, v90
	v_add_f32_e32 v90, 0, v68
	ds_read_b128 v[68:71], v93 offset:17408
	v_add_f32_e32 v85, 0, v85
	s_waitcnt lgkmcnt(2)
	v_add_f32_e32 v64, v64, v65
	s_waitcnt lgkmcnt(1)
	v_add_f32_e32 v66, v66, v67
	ds_swizzle_b32 v65, v64 offset:swizzle(SWAP,4)
	s_waitcnt lgkmcnt(1)
	v_mul_f32_e32 v91, v51, v69
	v_mul_f32_e32 v69, v55, v69
	v_fmac_f32_e32 v91, v50, v68
	v_fmac_f32_e32 v69, v54, v68
	v_mul_f32_e32 v68, v53, v71
	v_fmac_f32_e32 v68, v52, v70
	v_mul_f32_e32 v92, v49, v71
	v_add_f32_e32 v68, v69, v68
	v_fmac_f32_e32 v92, v48, v70
	v_add_f32_e32 v90, v90, v68
	ds_read_b128 v[68:71], v93 offset:18432
	v_add_f32_e32 v91, v91, v92
	v_add_f32_e32 v85, v85, v91
	ds_swizzle_b32 v67, v66 offset:swizzle(SWAP,4)
	s_waitcnt lgkmcnt(2)
	v_add_f32_e32 v64, v64, v65
	s_waitcnt lgkmcnt(1)
	v_mul_f32_e32 v91, v59, v69
	v_mul_f32_e32 v69, v43, v69
	v_fmac_f32_e32 v91, v58, v68
	v_fmac_f32_e32 v69, v42, v68
	v_mul_f32_e32 v68, v41, v71
	v_fmac_f32_e32 v68, v40, v70
	v_mul_f32_e32 v92, v57, v71
	v_add_f32_e32 v68, v69, v68
	v_fmac_f32_e32 v92, v56, v70
	v_add_f32_e32 v90, v90, v68
	ds_read_b128 v[68:71], v93 offset:19456
	v_add_f32_e32 v91, v91, v92
	v_add_f32_e32 v85, v85, v91
	s_waitcnt lgkmcnt(1)
	v_add_f32_e32 v66, v66, v67
	ds_swizzle_b32 v65, v64 offset:swizzle(SWAP,8)
	s_waitcnt lgkmcnt(1)
	v_mul_f32_e32 v91, v31, v69
	v_mul_f32_e32 v69, v35, v69
	v_fmac_f32_e32 v91, v30, v68
	v_fmac_f32_e32 v69, v34, v68
	v_mul_f32_e32 v68, v33, v71
	v_fmac_f32_e32 v68, v32, v70
	v_mul_f32_e32 v92, v29, v71
	v_add_f32_e32 v68, v69, v68
	v_fmac_f32_e32 v92, v28, v70
	v_add_f32_e32 v90, v90, v68
	ds_read_b128 v[68:71], v93 offset:20480
	v_add_f32_e32 v91, v91, v92
	v_add_f32_e32 v85, v85, v91
	ds_swizzle_b32 v67, v66 offset:swizzle(SWAP,8)
	s_waitcnt lgkmcnt(2)
	v_add_f32_e32 v64, v64, v65
	s_waitcnt lgkmcnt(1)
	v_mul_f32_e32 v91, v47, v69
	v_mul_f32_e32 v69, v27, v69
	v_fmac_f32_e32 v91, v46, v68
	v_fmac_f32_e32 v69, v26, v68
	v_mul_f32_e32 v68, v25, v71
	v_fmac_f32_e32 v68, v24, v70
	v_mul_f32_e32 v92, v45, v71
	v_add_f32_e32 v68, v69, v68
	v_fmac_f32_e32 v92, v44, v70
	v_add_f32_e32 v90, v90, v68
	ds_read_b128 v[68:71], v93 offset:21504
	v_add_f32_e32 v91, v91, v92
	v_add_f32_e32 v85, v85, v91
	s_waitcnt lgkmcnt(1)
	v_add_f32_e32 v66, v66, v67
	ds_swizzle_b32 v65, v64 offset:swizzle(SWAP,16)
	s_waitcnt lgkmcnt(1)
	v_mul_f32_e32 v91, v19, v69
	v_mul_f32_e32 v69, v23, v69
	v_fmac_f32_e32 v91, v18, v68
	v_fmac_f32_e32 v69, v22, v68
	v_mul_f32_e32 v68, v21, v71
	v_fmac_f32_e32 v68, v20, v70
	v_mul_f32_e32 v92, v17, v71
	v_add_f32_e32 v68, v69, v68
	v_fmac_f32_e32 v92, v16, v70
	v_add_f32_e32 v90, v90, v68
	ds_read_b128 v[68:71], v93 offset:22528
	v_add_f32_e32 v91, v91, v92
	v_add_f32_e32 v85, v85, v91
	ds_swizzle_b32 v67, v66 offset:swizzle(SWAP,16)
	s_waitcnt lgkmcnt(2)
	v_add_f32_e32 v64, v64, v65
	s_waitcnt lgkmcnt(1)
	v_mul_f32_e32 v91, v39, v69
	v_mul_f32_e32 v69, v15, v69
	v_fmac_f32_e32 v91, v38, v68
	v_fmac_f32_e32 v69, v14, v68
	v_mul_f32_e32 v68, v13, v71
	v_fmac_f32_e32 v68, v12, v70
	v_mul_f32_e32 v92, v37, v71
	v_add_f32_e32 v68, v69, v68
	v_fmac_f32_e32 v92, v36, v70
	v_add_f32_e32 v90, v90, v68
	ds_read_b128 v[68:71], v93 offset:23552
	v_add_f32_e32 v91, v91, v92
	v_add_f32_e32 v85, v85, v91
	s_waitcnt lgkmcnt(1)
	v_add_f32_e32 v66, v66, v67
	v_mov_b32_e32 v65, v64
	s_waitcnt lgkmcnt(0)
	v_mul_f32_e32 v91, v5, v69
	v_mul_f32_e32 v92, v1, v71
	v_mul_f32_e32 v69, v7, v69
	v_fmac_f32_e32 v91, v4, v68
	v_fmac_f32_e32 v92, v0, v70
	v_fmac_f32_e32 v69, v6, v68
	v_mul_f32_e32 v68, v3, v71
	v_add_f32_e32 v91, v91, v92
	v_fmac_f32_e32 v68, v2, v70
	v_add_f32_e32 v85, v85, v91
	v_add_f32_e32 v68, v69, v68
	v_add_f32_e32 v70, v90, v68
	ds_swizzle_b32 v68, v85 offset:swizzle(SWAP,1)
	v_mul_f32_e32 v90, v87, v97
	v_fmac_f32_e32 v90, v86, v96
	v_mul_f32_e32 v91, v61, v97
	v_fmac_f32_e32 v91, v60, v96
	s_waitcnt lgkmcnt(0)
	v_add_f32_e32 v68, v85, v68
	v_mul_f32_e32 v85, v89, v95
	v_fmac_f32_e32 v85, v88, v94
	v_add_f32_e32 v85, v85, v90
	v_mul_f32_e32 v90, v63, v95
	v_fmac_f32_e32 v90, v62, v94
	ds_read_b128 v[94:97], v93 offset:25600
	v_add_f32_e32 v90, v90, v91
	v_add_f32_e32 v85, 0, v85
	v_add_f32_e32 v90, 0, v90
	ds_swizzle_b32 v71, v70 offset:swizzle(SWAP,1)
	s_waitcnt lgkmcnt(1)
	v_mul_f32_e32 v91, v51, v95
	v_mul_f32_e32 v92, v49, v97
	v_fmac_f32_e32 v91, v50, v94
	v_fmac_f32_e32 v92, v48, v96
	v_add_f32_e32 v91, v91, v92
	v_add_f32_e32 v85, v85, v91
	v_mul_f32_e32 v91, v55, v95
	v_mul_f32_e32 v92, v53, v97
	v_fmac_f32_e32 v91, v54, v94
	v_fmac_f32_e32 v92, v52, v96
	ds_read_b128 v[94:97], v93 offset:26624
	v_add_f32_e32 v91, v91, v92
	v_add_f32_e32 v90, v90, v91
	s_waitcnt lgkmcnt(1)
	v_add_f32_e32 v70, v70, v71
	ds_swizzle_b32 v69, v68 offset:swizzle(SWAP,2)
	s_waitcnt lgkmcnt(1)
	v_mul_f32_e32 v91, v59, v95
	v_mul_f32_e32 v92, v57, v97
	v_fmac_f32_e32 v91, v58, v94
	v_fmac_f32_e32 v92, v56, v96
	v_add_f32_e32 v91, v91, v92
	v_add_f32_e32 v85, v85, v91
	v_mul_f32_e32 v91, v43, v95
	v_mul_f32_e32 v92, v41, v97
	v_fmac_f32_e32 v91, v42, v94
	v_fmac_f32_e32 v92, v40, v96
	ds_read_b128 v[94:97], v93 offset:27648
	v_add_f32_e32 v91, v91, v92
	v_add_f32_e32 v90, v90, v91
	ds_swizzle_b32 v71, v70 offset:swizzle(SWAP,2)
	s_waitcnt lgkmcnt(2)
	v_add_f32_e32 v68, v68, v69
	s_waitcnt lgkmcnt(1)
	v_mul_f32_e32 v91, v31, v95
	v_mul_f32_e32 v92, v29, v97
	v_fmac_f32_e32 v91, v30, v94
	v_fmac_f32_e32 v92, v28, v96
	v_add_f32_e32 v91, v91, v92
	v_add_f32_e32 v85, v85, v91
	v_mul_f32_e32 v91, v35, v95
	v_mul_f32_e32 v92, v33, v97
	v_fmac_f32_e32 v91, v34, v94
	v_fmac_f32_e32 v92, v32, v96
	ds_read_b128 v[94:97], v93 offset:28672
	v_add_f32_e32 v91, v91, v92
	v_add_f32_e32 v90, v90, v91
	s_waitcnt lgkmcnt(1)
	v_add_f32_e32 v70, v70, v71
	ds_swizzle_b32 v69, v68 offset:swizzle(SWAP,4)
	s_waitcnt lgkmcnt(1)
	v_mul_f32_e32 v91, v47, v95
	v_mul_f32_e32 v92, v45, v97
	v_fmac_f32_e32 v91, v46, v94
	v_fmac_f32_e32 v92, v44, v96
	v_add_f32_e32 v91, v91, v92
	v_add_f32_e32 v85, v85, v91
	v_mul_f32_e32 v91, v27, v95
	v_mul_f32_e32 v92, v25, v97
	v_fmac_f32_e32 v91, v26, v94
	v_fmac_f32_e32 v92, v24, v96
	ds_read_b128 v[94:97], v93 offset:29696
	v_add_f32_e32 v91, v91, v92
	v_add_f32_e32 v90, v90, v91
	ds_swizzle_b32 v71, v70 offset:swizzle(SWAP,4)
	s_waitcnt lgkmcnt(2)
	v_add_f32_e32 v68, v68, v69
	s_waitcnt lgkmcnt(1)
	v_mul_f32_e32 v91, v19, v95
	v_mul_f32_e32 v92, v17, v97
	v_fmac_f32_e32 v91, v18, v94
	v_fmac_f32_e32 v92, v16, v96
	v_add_f32_e32 v91, v91, v92
	v_add_f32_e32 v85, v85, v91
	v_mul_f32_e32 v91, v23, v95
	v_mul_f32_e32 v92, v21, v97
	v_fmac_f32_e32 v91, v22, v94
	v_fmac_f32_e32 v92, v20, v96
	ds_read_b128 v[94:97], v93 offset:30720
	v_add_f32_e32 v91, v91, v92
	v_add_f32_e32 v90, v90, v91
	s_waitcnt lgkmcnt(1)
	v_add_f32_e32 v70, v70, v71
	ds_swizzle_b32 v69, v68 offset:swizzle(SWAP,8)
	s_waitcnt lgkmcnt(1)
	v_mul_f32_e32 v91, v39, v95
	v_mul_f32_e32 v92, v37, v97
	v_fmac_f32_e32 v91, v38, v94
	v_fmac_f32_e32 v92, v36, v96
	v_add_f32_e32 v91, v91, v92
	v_add_f32_e32 v85, v85, v91
	v_mul_f32_e32 v91, v15, v95
	v_mul_f32_e32 v92, v13, v97
	v_fmac_f32_e32 v91, v14, v94
	v_fmac_f32_e32 v92, v12, v96
	ds_read_b128 v[94:97], v93 offset:31744
	v_add_f32_e32 v91, v91, v92
	v_add_f32_e32 v90, v90, v91
	ds_swizzle_b32 v71, v70 offset:swizzle(SWAP,8)
	s_waitcnt lgkmcnt(2)
	v_add_f32_e32 v68, v68, v69
	s_waitcnt lgkmcnt(1)
	v_mul_f32_e32 v91, v5, v95
	v_mul_f32_e32 v92, v1, v97
	v_fmac_f32_e32 v91, v4, v94
	v_fmac_f32_e32 v92, v0, v96
	v_add_f32_e32 v91, v91, v92
	v_add_f32_e32 v85, v85, v91
	v_mul_f32_e32 v91, v7, v95
	v_mul_f32_e32 v92, v3, v97
	v_fmac_f32_e32 v91, v6, v94
	v_fmac_f32_e32 v92, v2, v96
	ds_read_b128 v[94:97], v93 offset:32768
	v_add_f32_e32 v91, v91, v92
	v_add_f32_e32 v91, v90, v91
	ds_swizzle_b32 v90, v85 offset:swizzle(SWAP,1)
	ds_swizzle_b32 v92, v91 offset:swizzle(SWAP,1)
	s_waitcnt lgkmcnt(2)
	v_mul_f32_e32 v98, v89, v95
	v_mul_f32_e32 v95, v63, v95
	v_fmac_f32_e32 v98, v88, v94
	v_fmac_f32_e32 v95, v62, v94
	v_mul_f32_e32 v94, v61, v97
	v_mul_f32_e32 v99, v87, v97
	v_fmac_f32_e32 v94, v60, v96
	v_fmac_f32_e32 v99, v86, v96
	v_add_f32_e32 v94, v95, v94
	v_add_f32_e32 v98, v98, v99
	v_add_f32_e32 v99, 0, v94
	ds_read_b128 v[94:97], v93 offset:33792
	v_add_f32_e32 v98, 0, v98
	s_waitcnt lgkmcnt(2)
	v_add_f32_e32 v85, v85, v90
	s_waitcnt lgkmcnt(1)
	v_add_f32_e32 v91, v91, v92
	ds_swizzle_b32 v90, v85 offset:swizzle(SWAP,2)
	s_waitcnt lgkmcnt(1)
	v_mul_f32_e32 v100, v51, v95
	v_mul_f32_e32 v95, v55, v95
	v_fmac_f32_e32 v100, v50, v94
	v_fmac_f32_e32 v95, v54, v94
	v_mul_f32_e32 v94, v53, v97
	v_fmac_f32_e32 v94, v52, v96
	v_mul_f32_e32 v101, v49, v97
	v_add_f32_e32 v94, v95, v94
	v_fmac_f32_e32 v101, v48, v96
	v_add_f32_e32 v99, v99, v94
	ds_read_b128 v[94:97], v93 offset:34816
	v_add_f32_e32 v100, v100, v101
	v_add_f32_e32 v98, v98, v100
	ds_swizzle_b32 v92, v91 offset:swizzle(SWAP,2)
	s_waitcnt lgkmcnt(2)
	v_add_f32_e32 v85, v85, v90
	s_waitcnt lgkmcnt(1)
	v_mul_f32_e32 v100, v59, v95
	v_mul_f32_e32 v95, v43, v95
	v_fmac_f32_e32 v100, v58, v94
	v_fmac_f32_e32 v95, v42, v94
	v_mul_f32_e32 v94, v41, v97
	v_fmac_f32_e32 v94, v40, v96
	v_mul_f32_e32 v101, v57, v97
	v_add_f32_e32 v94, v95, v94
	v_fmac_f32_e32 v101, v56, v96
	v_add_f32_e32 v99, v99, v94
	ds_read_b128 v[94:97], v93 offset:35840
	v_add_f32_e32 v100, v100, v101
	v_add_f32_e32 v98, v98, v100
	s_waitcnt lgkmcnt(1)
	v_add_f32_e32 v91, v91, v92
	ds_swizzle_b32 v90, v85 offset:swizzle(SWAP,4)
	s_waitcnt lgkmcnt(1)
	v_mul_f32_e32 v100, v31, v95
	v_mul_f32_e32 v95, v35, v95
	v_fmac_f32_e32 v100, v30, v94
	v_fmac_f32_e32 v95, v34, v94
	v_mul_f32_e32 v94, v33, v97
	v_fmac_f32_e32 v94, v32, v96
	v_mul_f32_e32 v101, v29, v97
	v_add_f32_e32 v94, v95, v94
	v_fmac_f32_e32 v101, v28, v96
	v_add_f32_e32 v99, v99, v94
	ds_read_b128 v[94:97], v93 offset:36864
	v_add_f32_e32 v100, v100, v101
	v_add_f32_e32 v98, v98, v100
	ds_swizzle_b32 v92, v91 offset:swizzle(SWAP,4)
	s_waitcnt lgkmcnt(2)
	v_add_f32_e32 v85, v85, v90
	s_waitcnt lgkmcnt(1)
	v_mul_f32_e32 v100, v47, v95
	v_mul_f32_e32 v95, v27, v95
	v_fmac_f32_e32 v100, v46, v94
	v_fmac_f32_e32 v95, v26, v94
	v_mul_f32_e32 v94, v25, v97
	v_fmac_f32_e32 v94, v24, v96
	v_mul_f32_e32 v101, v45, v97
	v_add_f32_e32 v94, v95, v94
	v_fmac_f32_e32 v101, v44, v96
	v_add_f32_e32 v99, v99, v94
	ds_read_b128 v[94:97], v93 offset:37888
	v_add_f32_e32 v100, v100, v101
	v_add_f32_e32 v98, v98, v100
	s_waitcnt lgkmcnt(1)
	v_add_f32_e32 v91, v91, v92
	ds_swizzle_b32 v90, v85 offset:swizzle(SWAP,8)
	s_waitcnt lgkmcnt(1)
	v_mul_f32_e32 v100, v19, v95
	v_mul_f32_e32 v95, v23, v95
	v_fmac_f32_e32 v100, v18, v94
	v_fmac_f32_e32 v95, v22, v94
	v_mul_f32_e32 v94, v21, v97
	v_fmac_f32_e32 v94, v20, v96
	v_mul_f32_e32 v101, v17, v97
	v_add_f32_e32 v94, v95, v94
	v_fmac_f32_e32 v101, v16, v96
	v_add_f32_e32 v99, v99, v94
	ds_read_b128 v[94:97], v93 offset:38912
	v_add_f32_e32 v100, v100, v101
	v_add_f32_e32 v98, v98, v100
	ds_swizzle_b32 v92, v91 offset:swizzle(SWAP,8)
	v_add_f32_e32 v70, v70, v71
	s_waitcnt lgkmcnt(1)
	v_mul_f32_e32 v100, v39, v95
	v_mul_f32_e32 v95, v15, v95
	v_fmac_f32_e32 v100, v38, v94
	v_fmac_f32_e32 v95, v14, v94
	v_mul_f32_e32 v94, v13, v97
	v_fmac_f32_e32 v94, v12, v96
	v_mul_f32_e32 v101, v37, v97
	v_add_f32_e32 v94, v95, v94
	v_fmac_f32_e32 v101, v36, v96
	v_add_f32_e32 v99, v99, v94
	ds_read_b128 v[94:97], v93 offset:39936
	v_add_f32_e32 v100, v100, v101
	v_add_f32_e32 v98, v98, v100
	v_add_f32_e32 v85, v85, v90
	s_waitcnt lgkmcnt(1)
	v_add_f32_e32 v91, v91, v92
	s_waitcnt lgkmcnt(0)
	v_mul_f32_e32 v100, v5, v95
	v_mul_f32_e32 v101, v1, v97
	v_mul_f32_e32 v95, v7, v95
	v_fmac_f32_e32 v100, v4, v94
	v_fmac_f32_e32 v101, v0, v96
	v_fmac_f32_e32 v95, v6, v94
	v_mul_f32_e32 v94, v3, v97
	v_add_f32_e32 v100, v100, v101
	v_fmac_f32_e32 v94, v2, v96
	v_add_f32_e32 v98, v98, v100
	v_add_f32_e32 v94, v95, v94
	v_add_f32_e32 v96, v99, v94
	ds_swizzle_b32 v94, v98 offset:swizzle(SWAP,1)
	ds_swizzle_b32 v97, v96 offset:swizzle(SWAP,1)
	ds_swizzle_b32 v69, v68 offset:swizzle(SWAP,16)
	ds_swizzle_b32 v71, v70 offset:swizzle(SWAP,16)
	ds_swizzle_b32 v90, v85 offset:swizzle(SWAP,16)
	s_waitcnt lgkmcnt(4)
	v_add_f32_e32 v94, v98, v94
	ds_read_b128 v[98:101], v93 offset:40960
	s_waitcnt lgkmcnt(4)
	v_add_f32_e32 v96, v96, v97
	ds_swizzle_b32 v95, v94 offset:swizzle(SWAP,2)
	ds_swizzle_b32 v97, v96 offset:swizzle(SWAP,2)
	ds_swizzle_b32 v92, v91 offset:swizzle(SWAP,16)
	s_waitcnt lgkmcnt(3)
	v_mul_f32_e32 v102, v89, v99
	v_mul_f32_e32 v99, v63, v99
	v_fmac_f32_e32 v102, v88, v98
	v_fmac_f32_e32 v99, v62, v98
	v_mul_f32_e32 v98, v61, v101
	v_mul_f32_e32 v103, v87, v101
	v_fmac_f32_e32 v98, v60, v100
	v_fmac_f32_e32 v103, v86, v100
	v_add_f32_e32 v98, v99, v98
	v_add_f32_e32 v102, v102, v103
	v_add_f32_e32 v103, 0, v98
	ds_read_b128 v[98:101], v93 offset:41984
	v_add_f32_e32 v102, 0, v102
	s_waitcnt lgkmcnt(3)
	v_add_f32_e32 v94, v94, v95
	s_waitcnt lgkmcnt(2)
	v_add_f32_e32 v96, v96, v97
	ds_swizzle_b32 v95, v94 offset:swizzle(SWAP,4)
	s_waitcnt lgkmcnt(1)
	v_mul_f32_e32 v104, v51, v99
	v_mul_f32_e32 v99, v55, v99
	v_fmac_f32_e32 v104, v50, v98
	v_fmac_f32_e32 v99, v54, v98
	v_mul_f32_e32 v98, v53, v101
	v_fmac_f32_e32 v98, v52, v100
	v_mul_f32_e32 v105, v49, v101
	v_add_f32_e32 v98, v99, v98
	v_fmac_f32_e32 v105, v48, v100
	v_add_f32_e32 v103, v103, v98
	ds_read_b128 v[98:101], v93 offset:43008
	v_add_f32_e32 v104, v104, v105
	v_add_f32_e32 v102, v102, v104
	ds_swizzle_b32 v97, v96 offset:swizzle(SWAP,4)
	s_waitcnt lgkmcnt(2)
	v_add_f32_e32 v94, v94, v95
	s_waitcnt lgkmcnt(1)
	v_mul_f32_e32 v104, v59, v99
	v_mul_f32_e32 v99, v43, v99
	v_fmac_f32_e32 v104, v58, v98
	v_fmac_f32_e32 v99, v42, v98
	v_mul_f32_e32 v98, v41, v101
	v_fmac_f32_e32 v98, v40, v100
	v_mul_f32_e32 v105, v57, v101
	v_add_f32_e32 v98, v99, v98
	v_fmac_f32_e32 v105, v56, v100
	v_add_f32_e32 v103, v103, v98
	ds_read_b128 v[98:101], v93 offset:44032
	v_add_f32_e32 v104, v104, v105
	v_add_f32_e32 v102, v102, v104
	s_waitcnt lgkmcnt(1)
	v_add_f32_e32 v96, v96, v97
	ds_swizzle_b32 v95, v94 offset:swizzle(SWAP,8)
	s_waitcnt lgkmcnt(1)
	v_mul_f32_e32 v104, v31, v99
	v_mul_f32_e32 v99, v35, v99
	v_fmac_f32_e32 v104, v30, v98
	v_fmac_f32_e32 v99, v34, v98
	v_mul_f32_e32 v98, v33, v101
	v_fmac_f32_e32 v98, v32, v100
	v_mul_f32_e32 v105, v29, v101
	v_add_f32_e32 v98, v99, v98
	v_fmac_f32_e32 v105, v28, v100
	v_add_f32_e32 v103, v103, v98
	ds_read_b128 v[98:101], v93 offset:45056
	v_add_f32_e32 v104, v104, v105
	v_add_f32_e32 v102, v102, v104
	ds_swizzle_b32 v97, v96 offset:swizzle(SWAP,8)
	s_waitcnt lgkmcnt(2)
	v_add_f32_e32 v94, v94, v95
	s_waitcnt lgkmcnt(1)
	v_mul_f32_e32 v104, v47, v99
	v_mul_f32_e32 v99, v27, v99
	v_fmac_f32_e32 v104, v46, v98
	v_fmac_f32_e32 v99, v26, v98
	v_mul_f32_e32 v98, v25, v101
	v_fmac_f32_e32 v98, v24, v100
	v_mul_f32_e32 v105, v45, v101
	v_add_f32_e32 v98, v99, v98
	v_fmac_f32_e32 v105, v44, v100
	v_add_f32_e32 v103, v103, v98
	ds_read_b128 v[98:101], v93 offset:46080
	v_add_f32_e32 v104, v104, v105
	v_add_f32_e32 v102, v102, v104
	s_waitcnt lgkmcnt(1)
	v_add_f32_e32 v96, v96, v97
	ds_swizzle_b32 v95, v94 offset:swizzle(SWAP,16)
	s_waitcnt lgkmcnt(1)
	v_mul_f32_e32 v104, v19, v99
	v_mul_f32_e32 v99, v23, v99
	v_fmac_f32_e32 v104, v18, v98
	v_fmac_f32_e32 v99, v22, v98
	v_mul_f32_e32 v98, v21, v101
	v_fmac_f32_e32 v98, v20, v100
	v_mul_f32_e32 v105, v17, v101
	v_add_f32_e32 v98, v99, v98
	v_fmac_f32_e32 v105, v16, v100
	v_add_f32_e32 v103, v103, v98
	ds_read_b128 v[98:101], v93 offset:47104
	v_add_f32_e32 v104, v104, v105
	v_add_f32_e32 v102, v102, v104
	ds_swizzle_b32 v97, v96 offset:swizzle(SWAP,16)
	v_add_f32_e32 v68, v68, v69
	s_waitcnt lgkmcnt(1)
	v_mul_f32_e32 v104, v39, v99
	v_mul_f32_e32 v99, v15, v99
	v_fmac_f32_e32 v104, v38, v98
	v_fmac_f32_e32 v99, v14, v98
	v_mul_f32_e32 v98, v13, v101
	v_fmac_f32_e32 v98, v12, v100
	v_mul_f32_e32 v105, v37, v101
	v_add_f32_e32 v98, v99, v98
	v_fmac_f32_e32 v105, v36, v100
	v_add_f32_e32 v103, v103, v98
	ds_read_b128 v[98:101], v93 offset:48128
	v_add_f32_e32 v104, v104, v105
	v_add_f32_e32 v102, v102, v104
	v_add_f32_e32 v70, v70, v71
	v_add_f32_e32 v85, v85, v90
	s_waitcnt lgkmcnt(0)
	v_mul_f32_e32 v104, v5, v99
	v_mul_f32_e32 v105, v1, v101
	v_mul_f32_e32 v99, v7, v99
	v_fmac_f32_e32 v104, v4, v98
	v_fmac_f32_e32 v105, v0, v100
	v_fmac_f32_e32 v99, v6, v98
	v_mul_f32_e32 v98, v3, v101
	v_add_f32_e32 v104, v104, v105
	v_fmac_f32_e32 v98, v2, v100
	v_add_f32_e32 v102, v102, v104
	v_add_f32_e32 v98, v99, v98
	v_add_f32_e32 v100, v103, v98
	ds_swizzle_b32 v98, v102 offset:swizzle(SWAP,1)
	ds_swizzle_b32 v101, v100 offset:swizzle(SWAP,1)
	v_add_f32_e32 v91, v91, v92
	v_add_f32_e32 v94, v94, v95
	v_add_f32_e32 v96, v96, v97
	s_waitcnt lgkmcnt(1)
	v_add_f32_e32 v98, v102, v98
	ds_read_b128 v[102:105], v93 offset:49152
	s_waitcnt lgkmcnt(1)
	v_add_f32_e32 v100, v100, v101
	ds_swizzle_b32 v99, v98 offset:swizzle(SWAP,2)
	ds_swizzle_b32 v101, v100 offset:swizzle(SWAP,2)
	v_mov_b32_e32 v67, v66
	s_waitcnt lgkmcnt(2)
	v_mul_f32_e32 v106, v89, v103
	v_mul_f32_e32 v103, v63, v103
	v_fmac_f32_e32 v106, v88, v102
	v_fmac_f32_e32 v103, v62, v102
	v_mul_f32_e32 v102, v61, v105
	v_mul_f32_e32 v107, v87, v105
	v_fmac_f32_e32 v102, v60, v104
	v_fmac_f32_e32 v107, v86, v104
	v_add_f32_e32 v102, v103, v102
	v_add_f32_e32 v106, v106, v107
	v_add_f32_e32 v107, 0, v102
	ds_read_b128 v[102:105], v93 offset:50176
	v_add_f32_e32 v106, 0, v106
	s_waitcnt lgkmcnt(2)
	v_add_f32_e32 v98, v98, v99
	s_waitcnt lgkmcnt(1)
	v_add_f32_e32 v100, v100, v101
	ds_swizzle_b32 v99, v98 offset:swizzle(SWAP,4)
	s_waitcnt lgkmcnt(1)
	v_mul_f32_e32 v108, v51, v103
	v_mul_f32_e32 v103, v55, v103
	v_fmac_f32_e32 v108, v50, v102
	v_fmac_f32_e32 v103, v54, v102
	v_mul_f32_e32 v102, v53, v105
	v_fmac_f32_e32 v102, v52, v104
	v_mul_f32_e32 v109, v49, v105
	v_add_f32_e32 v102, v103, v102
	v_fmac_f32_e32 v109, v48, v104
	v_add_f32_e32 v107, v107, v102
	ds_read_b128 v[102:105], v93 offset:51200
	v_add_f32_e32 v108, v108, v109
	v_add_f32_e32 v106, v106, v108
	ds_swizzle_b32 v101, v100 offset:swizzle(SWAP,4)
	s_waitcnt lgkmcnt(2)
	v_add_f32_e32 v98, v98, v99
	s_waitcnt lgkmcnt(1)
	v_mul_f32_e32 v108, v59, v103
	v_mul_f32_e32 v103, v43, v103
	v_fmac_f32_e32 v108, v58, v102
	v_fmac_f32_e32 v103, v42, v102
	v_mul_f32_e32 v102, v41, v105
	v_fmac_f32_e32 v102, v40, v104
	v_mul_f32_e32 v109, v57, v105
	v_add_f32_e32 v102, v103, v102
	v_fmac_f32_e32 v109, v56, v104
	v_add_f32_e32 v107, v107, v102
	ds_read_b128 v[102:105], v93 offset:52224
	v_add_f32_e32 v108, v108, v109
	v_add_f32_e32 v106, v106, v108
	s_waitcnt lgkmcnt(1)
	v_add_f32_e32 v100, v100, v101
	ds_swizzle_b32 v99, v98 offset:swizzle(SWAP,8)
	s_waitcnt lgkmcnt(1)
	v_mul_f32_e32 v108, v31, v103
	v_mul_f32_e32 v103, v35, v103
	v_fmac_f32_e32 v108, v30, v102
	v_fmac_f32_e32 v103, v34, v102
	v_mul_f32_e32 v102, v33, v105
	v_fmac_f32_e32 v102, v32, v104
	v_mul_f32_e32 v109, v29, v105
	v_add_f32_e32 v102, v103, v102
	v_fmac_f32_e32 v109, v28, v104
	v_add_f32_e32 v107, v107, v102
	ds_read_b128 v[102:105], v93 offset:53248
	v_add_f32_e32 v108, v108, v109
	v_add_f32_e32 v106, v106, v108
	ds_swizzle_b32 v101, v100 offset:swizzle(SWAP,8)
	s_waitcnt lgkmcnt(2)
	v_add_f32_e32 v98, v98, v99
	s_waitcnt lgkmcnt(1)
	v_mul_f32_e32 v108, v47, v103
	v_mul_f32_e32 v103, v27, v103
	v_fmac_f32_e32 v108, v46, v102
	v_fmac_f32_e32 v103, v26, v102
	v_mul_f32_e32 v102, v25, v105
	v_fmac_f32_e32 v102, v24, v104
	v_mul_f32_e32 v109, v45, v105
	v_add_f32_e32 v102, v103, v102
	v_fmac_f32_e32 v109, v44, v104
	v_add_f32_e32 v107, v107, v102
	ds_read_b128 v[102:105], v93 offset:54272
	v_add_f32_e32 v108, v108, v109
	v_add_f32_e32 v106, v106, v108
	s_waitcnt lgkmcnt(1)
	v_add_f32_e32 v100, v100, v101
	ds_swizzle_b32 v99, v98 offset:swizzle(SWAP,16)
	s_waitcnt lgkmcnt(1)
	v_mul_f32_e32 v108, v19, v103
	v_mul_f32_e32 v103, v23, v103
	v_fmac_f32_e32 v108, v18, v102
	v_fmac_f32_e32 v103, v22, v102
	v_mul_f32_e32 v102, v21, v105
	v_fmac_f32_e32 v102, v20, v104
	v_mul_f32_e32 v109, v17, v105
	v_add_f32_e32 v102, v103, v102
	v_fmac_f32_e32 v109, v16, v104
	v_add_f32_e32 v107, v107, v102
	ds_read_b128 v[102:105], v93 offset:55296
	v_add_f32_e32 v108, v108, v109
	v_add_f32_e32 v106, v106, v108
	ds_swizzle_b32 v101, v100 offset:swizzle(SWAP,16)
	s_waitcnt lgkmcnt(2)
	v_add_f32_e32 v98, v98, v99
	s_waitcnt lgkmcnt(1)
	v_mul_f32_e32 v108, v39, v103
	v_mul_f32_e32 v103, v15, v103
	v_fmac_f32_e32 v108, v38, v102
	v_fmac_f32_e32 v103, v14, v102
	v_mul_f32_e32 v102, v13, v105
	v_fmac_f32_e32 v102, v12, v104
	v_mul_f32_e32 v109, v37, v105
	v_add_f32_e32 v102, v103, v102
	v_fmac_f32_e32 v109, v36, v104
	v_add_f32_e32 v107, v107, v102
	ds_read_b128 v[102:105], v93 offset:56320
	v_add_f32_e32 v108, v108, v109
	v_add_f32_e32 v106, v106, v108
	s_waitcnt lgkmcnt(1)
	v_add_f32_e32 v100, v100, v101
	v_mov_b32_e32 v69, v68
	s_waitcnt lgkmcnt(0)
	v_mul_f32_e32 v108, v5, v103
	v_mul_f32_e32 v109, v1, v105
	v_mul_f32_e32 v103, v7, v103
	v_fmac_f32_e32 v108, v4, v102
	v_fmac_f32_e32 v109, v0, v104
	v_fmac_f32_e32 v103, v6, v102
	v_mul_f32_e32 v102, v3, v105
	v_add_f32_e32 v108, v108, v109
	v_fmac_f32_e32 v102, v2, v104
	v_add_f32_e32 v106, v106, v108
	v_add_f32_e32 v102, v103, v102
	v_add_f32_e32 v104, v107, v102
	ds_swizzle_b32 v102, v106 offset:swizzle(SWAP,1)
	ds_swizzle_b32 v105, v104 offset:swizzle(SWAP,1)
	v_mov_b32_e32 v71, v70
	v_mov_b32_e32 v90, v85
	v_mov_b32_e32 v92, v91
	s_waitcnt lgkmcnt(1)
	v_add_f32_e32 v102, v106, v102
	ds_read_b128 v[106:109], v93 offset:57344
	s_waitcnt lgkmcnt(1)
	v_add_f32_e32 v104, v104, v105
	ds_swizzle_b32 v103, v102 offset:swizzle(SWAP,2)
	ds_swizzle_b32 v105, v104 offset:swizzle(SWAP,2)
	v_mov_b32_e32 v95, v94
	s_waitcnt lgkmcnt(2)
	v_mul_f32_e32 v63, v63, v107
	v_mul_f32_e32 v61, v61, v109
	v_mul_f32_e32 v89, v89, v107
	v_mul_f32_e32 v87, v87, v109
	v_fmac_f32_e32 v63, v62, v106
	v_fmac_f32_e32 v61, v60, v108
	v_fmac_f32_e32 v89, v88, v106
	v_fmac_f32_e32 v87, v86, v108
	v_add_f32_e32 v60, v63, v61
	v_add_f32_e32 v86, v89, v87
	v_add_f32_e32 v87, 0, v60
	ds_read_b128 v[60:63], v93 offset:58368
	v_add_f32_e32 v86, 0, v86
	s_waitcnt lgkmcnt(2)
	v_add_f32_e32 v102, v102, v103
	s_waitcnt lgkmcnt(1)
	v_add_f32_e32 v104, v104, v105
	ds_swizzle_b32 v103, v102 offset:swizzle(SWAP,4)
	s_waitcnt lgkmcnt(1)
	v_mul_f32_e32 v51, v51, v61
	v_mul_f32_e32 v49, v49, v63
	v_fmac_f32_e32 v51, v50, v60
	v_fmac_f32_e32 v49, v48, v62
	v_add_f32_e32 v48, v51, v49
	v_add_f32_e32 v86, v86, v48
	v_mul_f32_e32 v48, v55, v61
	v_mul_f32_e32 v49, v53, v63
	v_fmac_f32_e32 v48, v54, v60
	v_fmac_f32_e32 v49, v52, v62
	v_add_f32_e32 v48, v48, v49
	v_add_f32_e32 v52, v87, v48
	ds_read_b128 v[48:51], v93 offset:59392
	ds_swizzle_b32 v105, v104 offset:swizzle(SWAP,4)
	s_waitcnt lgkmcnt(2)
	v_add_f32_e32 v102, v102, v103
	ds_swizzle_b32 v103, v102 offset:swizzle(SWAP,8)
	v_mov_b32_e32 v97, v96
	s_waitcnt lgkmcnt(2)
	v_mul_f32_e32 v43, v43, v49
	v_mul_f32_e32 v41, v41, v51
	v_fmac_f32_e32 v43, v42, v48
	v_fmac_f32_e32 v41, v40, v50
	v_mul_f32_e32 v53, v59, v49
	v_add_f32_e32 v40, v43, v41
	v_fmac_f32_e32 v53, v58, v48
	v_add_f32_e32 v48, v52, v40
	ds_read_b128 v[40:43], v93 offset:60416
	v_mul_f32_e32 v54, v57, v51
	v_fmac_f32_e32 v54, v56, v50
	v_add_f32_e32 v53, v53, v54
	v_add_f32_e32 v53, v86, v53
	s_waitcnt lgkmcnt(0)
	v_mul_f32_e32 v31, v31, v41
	v_mul_f32_e32 v29, v29, v43
	v_fmac_f32_e32 v31, v30, v40
	v_fmac_f32_e32 v29, v28, v42
	v_add_f32_e32 v28, v31, v29
	v_add_f32_e32 v49, v53, v28
	v_mul_f32_e32 v28, v35, v41
	v_mul_f32_e32 v29, v33, v43
	v_fmac_f32_e32 v28, v34, v40
	v_fmac_f32_e32 v29, v32, v42
	v_add_f32_e32 v28, v28, v29
	v_add_f32_e32 v32, v48, v28
	ds_read_b128 v[28:31], v93 offset:61440
	v_add_f32_e32 v104, v104, v105
	ds_swizzle_b32 v105, v104 offset:swizzle(SWAP,8)
	v_add_f32_e32 v102, v102, v103
	ds_swizzle_b32 v103, v102 offset:swizzle(SWAP,16)
	s_waitcnt lgkmcnt(2)
	v_mul_f32_e32 v27, v27, v29
	v_mul_f32_e32 v25, v25, v31
	v_fmac_f32_e32 v27, v26, v28
	v_fmac_f32_e32 v25, v24, v30
	v_mul_f32_e32 v33, v47, v29
	v_add_f32_e32 v24, v27, v25
	v_fmac_f32_e32 v33, v46, v28
	v_add_f32_e32 v28, v32, v24
	ds_read_b128 v[24:27], v93 offset:62464
	v_mul_f32_e32 v34, v45, v31
	v_fmac_f32_e32 v34, v44, v30
	v_add_f32_e32 v33, v33, v34
	v_add_f32_e32 v33, v49, v33
	s_waitcnt lgkmcnt(0)
	v_mul_f32_e32 v19, v19, v25
	v_mul_f32_e32 v17, v17, v27
	v_fmac_f32_e32 v19, v18, v24
	v_fmac_f32_e32 v17, v16, v26
	v_add_f32_e32 v16, v19, v17
	v_add_f32_e32 v29, v33, v16
	v_mul_f32_e32 v16, v23, v25
	v_mul_f32_e32 v17, v21, v27
	v_fmac_f32_e32 v16, v22, v24
	v_fmac_f32_e32 v17, v20, v26
	v_add_f32_e32 v16, v16, v17
	v_add_f32_e32 v20, v28, v16
	ds_read_b128 v[16:19], v93 offset:63488
	v_add_f32_e32 v104, v104, v105
	ds_swizzle_b32 v105, v104 offset:swizzle(SWAP,16)
	v_add_f32_e32 v102, v102, v103
	v_mov_b32_e32 v99, v98
	s_waitcnt lgkmcnt(1)
	v_mul_f32_e32 v15, v15, v17
	v_mul_f32_e32 v13, v13, v19
	v_fmac_f32_e32 v15, v14, v16
	v_fmac_f32_e32 v13, v12, v18
	v_mul_f32_e32 v21, v39, v17
	v_add_f32_e32 v12, v15, v13
	v_fmac_f32_e32 v21, v38, v16
	v_add_f32_e32 v16, v20, v12
	ds_read_b128 v[12:15], v93 offset:64512
	v_mul_f32_e32 v22, v37, v19
	v_fmac_f32_e32 v22, v36, v18
	v_add_f32_e32 v21, v21, v22
	v_add_f32_e32 v21, v29, v21
	s_waitcnt lgkmcnt(0)
	v_mul_f32_e32 v5, v5, v13
	v_mul_f32_e32 v1, v1, v15
	v_fmac_f32_e32 v5, v4, v12
	v_fmac_f32_e32 v1, v0, v14
	v_add_f32_e32 v0, v5, v1
	v_mul_f32_e32 v1, v7, v13
	v_mul_f32_e32 v3, v3, v15
	v_fmac_f32_e32 v1, v6, v12
	v_fmac_f32_e32 v3, v2, v14
	v_add_f32_e32 v1, v1, v3
	v_add_f32_e32 v0, v21, v0
	v_add_f32_e32 v2, v16, v1
	ds_swizzle_b32 v1, v0 offset:swizzle(SWAP,1)
	ds_swizzle_b32 v3, v2 offset:swizzle(SWAP,1)
	v_add_f32_e32 v104, v104, v105
	v_mov_b32_e32 v101, v100
	v_mov_b32_e32 v103, v102
	s_waitcnt lgkmcnt(1)
	v_add_f32_e32 v0, v0, v1
	s_waitcnt lgkmcnt(0)
	v_add_f32_e32 v2, v2, v3
	ds_swizzle_b32 v1, v0 offset:swizzle(SWAP,2)
	ds_swizzle_b32 v3, v2 offset:swizzle(SWAP,2)
	v_mov_b32_e32 v105, v104
	v_permlane32_swap_b32_e32 v64, v65
	s_waitcnt lgkmcnt(1)
	v_add_f32_e32 v0, v0, v1
	s_waitcnt lgkmcnt(0)
	v_add_f32_e32 v2, v2, v3
	ds_swizzle_b32 v1, v0 offset:swizzle(SWAP,4)
	ds_swizzle_b32 v3, v2 offset:swizzle(SWAP,4)
	v_permlane32_swap_b32_e32 v66, v67
	v_permlane32_swap_b32_e32 v68, v69
	s_waitcnt lgkmcnt(1)
	v_add_f32_e32 v0, v0, v1
	s_waitcnt lgkmcnt(0)
	v_add_f32_e32 v2, v2, v3
	ds_swizzle_b32 v1, v0 offset:swizzle(SWAP,8)
	ds_swizzle_b32 v3, v2 offset:swizzle(SWAP,8)
	v_permlane32_swap_b32_e32 v70, v71
	v_permlane32_swap_b32_e32 v85, v90
	s_waitcnt lgkmcnt(1)
	v_add_f32_e32 v0, v0, v1
	s_waitcnt lgkmcnt(0)
	v_add_f32_e32 v2, v2, v3
	ds_swizzle_b32 v1, v0 offset:swizzle(SWAP,16)
	ds_swizzle_b32 v3, v2 offset:swizzle(SWAP,16)
	v_permlane32_swap_b32_e32 v91, v92
	v_permlane32_swap_b32_e32 v94, v95
	s_waitcnt lgkmcnt(1)
	v_add_f32_e32 v0, v0, v1
	s_waitcnt lgkmcnt(0)
	v_add_f32_e32 v2, v2, v3
	v_mov_b32_e32 v1, v0
	v_mov_b32_e32 v3, v2
	v_permlane32_swap_b32_e32 v96, v97
	v_permlane32_swap_b32_e32 v98, v99
	v_permlane32_swap_b32_e32 v100, v101
	v_permlane32_swap_b32_e32 v102, v103
	v_permlane32_swap_b32_e32 v104, v105
	v_permlane32_swap_b32_e32 v0, v1
	v_permlane32_swap_b32_e32 v2, v3
	s_and_saveexec_b64 s[40:41], s[2:3]
	s_cbranch_execz .LBB0_99
	v_add_f32_e32 v10, v10, v11
	v_add_f32_e32 v8, v8, v9
	v_add_f32_e32 v16, v66, v67
	v_add_f32_e32 v17, v64, v65
	v_cndmask_b32_e64 v8, v8, v10, s[4:5]
	v_add_f32_e32 v14, v70, v71
	v_add_f32_e32 v15, v68, v69
	v_cndmask_b32_e64 v8, 0, v8, s[8:9]
	v_cndmask_b32_e64 v9, v17, v16, s[4:5]
	v_add_f32_e32 v12, v91, v92
	v_add_f32_e32 v13, v85, v90
	v_cndmask_b32_e64 v8, v8, v9, s[10:11]
	v_cndmask_b32_e64 v9, v15, v14, s[4:5]
	v_add_f32_e32 v6, v96, v97
	v_add_f32_e32 v7, v94, v95
	v_cndmask_b32_e64 v8, v8, v9, s[12:13]
	v_cndmask_b32_e64 v9, v13, v12, s[4:5]
	v_add_f32_e32 v4, v100, v101
	v_add_f32_e32 v5, v98, v99
	v_cndmask_b32_e64 v8, v8, v9, s[14:15]
	v_cndmask_b32_e64 v6, v7, v6, s[4:5]
	v_add_f32_e32 v2, v2, v3
	v_add_f32_e32 v0, v0, v1
	v_add_f32_e32 v1, v104, v105
	v_add_f32_e32 v3, v102, v103
	v_cndmask_b32_e64 v6, v8, v6, s[16:17]
	v_cndmask_b32_e64 v4, v5, v4, s[4:5]
	v_cndmask_b32_e64 v4, v6, v4, s[18:19]
	v_cndmask_b32_e64 v1, v3, v1, s[4:5]
	v_cndmask_b32_e64 v1, v4, v1, s[20:21]
	v_cndmask_b32_e64 v0, v0, v2, s[4:5]
	v_cndmask_b32_e64 v1, v1, v0, s[22:23]
	s_and_saveexec_b64 s[24:25], s[6:7]
	s_xor_b64 s[42:43], exec, s[24:25]
	s_cbranch_execz .LBB0_108
	flat_load_dword v0, v[78:79]
	s_mov_b32 s24, 0xbfb8aa3b
	s_waitcnt vmcnt(0) lgkmcnt(0)
	v_add_f32_e32 v0, v1, v0
	v_mul_f32_e64 v1, |v0|, s24
	v_exp_f32_e32 v1, v1
	s_nop 0
	v_add_f32_e32 v3, 1.0, v1
	v_add_f32_e32 v2, -1.0, v3
	v_cmp_neq_f32_e32 vcc, 0, v2
	s_and_saveexec_b64 s[44:45], vcc
	s_cbranch_execz .LBB0_107
	s_mov_b32 s24, 0x800000
	v_cmp_gt_f32_e32 vcc, s24, v3
	s_nop 1
	v_cndmask_b32_e64 v4, 0, 32, vcc
	v_ldexp_f32 v3, v3, v4
	v_log_f32_e32 v3, v3
	v_div_scale_f32 v4, s[24:25], v2, v2, v1
	s_mov_b32 s24, 0x3f317217
	v_mul_f32_e32 v5, 0x3f317217, v3
	v_fma_f32 v5, v3, s24, -v5
	v_fmac_f32_e32 v5, 0x3377d1cf, v3
	v_rcp_f32_e32 v6, v4
	s_mov_b32 s24, 0x7f800000
	v_fmac_f32_e32 v5, 0x3f317217, v3
	v_cmp_lt_f32_e64 s[24:25], |v3|, s24
	s_nop 1
	v_cndmask_b32_e64 v3, v3, v5, s[24:25]
	v_mov_b32_e32 v5, 0x41b17218
	v_cndmask_b32_e32 v5, 0, v5, vcc
	v_sub_f32_e32 v3, v3, v5
	v_fma_f32 v5, -v4, v6, 1.0
	v_fmac_f32_e32 v6, v5, v6
	v_div_scale_f32 v5, vcc, v1, v2, v1
	v_mul_f32_e32 v7, v5, v6
	v_fma_f32 v8, -v4, v7, v5
	v_fmac_f32_e32 v7, v8, v6
	v_fma_f32 v4, -v4, v7, v5
	v_div_fmas_f32 v4, v4, v6, v7
	v_div_fixup_f32 v1, v4, v2, v1
	v_mul_f32_e32 v1, v3, v1

.LBB0_388:
	global_load_dwordx4 v[28:31], v[118:119], off
	global_load_dwordx4 v[4:7], v[118:119], off offset:16
	global_load_dwordx4 v[44:47], v[126:127], off
	global_load_dwordx4 v[36:39], v[120:121], off
	global_load_dwordx4 v[40:43], v[122:123], off
	global_load_dwordx4 v[32:35], v[124:125], off
	global_load_dwordx4 v[16:19], v[120:121], off offset:16
	global_load_dwordx4 v[12:15], v[122:123], off offset:16
	global_load_dwordx4 v[8:11], v[124:125], off offset:16
	global_load_dwordx4 v[20:23], v[126:127], off offset:16
	s_waitcnt vmcnt(10)
	v_lshlrev_b32_e32 v185, 16, v109
	v_lshlrev_b32_e32 v184, 16, v108
	v_and_b32_e32 v187, 0xffff0000, v109
	v_and_b32_e32 v186, 0xffff0000, v108
	v_lshlrev_b32_e32 v177, 16, v107
	v_lshlrev_b32_e32 v176, 16, v106
	v_and_b32_e32 v179, 0xffff0000, v107
	v_and_b32_e32 v178, 0xffff0000, v106
	v_lshlrev_b32_e32 v174, 16, v112
	v_and_b32_e32 v172, 0xffff0000, v112
	v_lshlrev_b32_e32 v171, 16, v105
	v_lshlrev_b32_e32 v170, 16, v104
	v_lshlrev_b32_e32 v175, 16, v113
	v_and_b32_e32 v173, 0xffff0000, v113
	v_lshlrev_b32_e32 v166, 16, v114
	v_and_b32_e32 v162, 0xffff0000, v114
	v_lshlrev_b32_e32 v183, 16, v111
	v_lshlrev_b32_e32 v182, 16, v110
	v_lshlrev_b32_e32 v167, 16, v115
	v_and_b32_e32 v169, 0xffff0000, v111
	v_and_b32_e32 v168, 0xffff0000, v110
	v_and_b32_e32 v163, 0xffff0000, v115
	v_lshlrev_b32_e32 v113, 16, v101
	v_lshlrev_b32_e32 v112, 16, v100
	v_and_b32_e32 v115, 0xffff0000, v101
	v_and_b32_e32 v114, 0xffff0000, v100
	v_and_b32_e32 v181, 0xffff0000, v105
	v_and_b32_e32 v180, 0xffff0000, v104
	s_ashr_i32 s7, s6, 31
	s_add_i32 s12, s12, s13
	s_waitcnt vmcnt(9)
	v_mov_b32_e32 v106, v28
	v_mov_b32_e32 v107, v30
	s_waitcnt vmcnt(7)
	v_mov_b32_e32 v108, v44
	v_mov_b32_e32 v109, v46
	v_mov_b32_e32 v30, v29
	s_waitcnt vmcnt(6)
	v_mov_b32_e32 v110, v36
	v_mov_b32_e32 v111, v38
	s_waitcnt vmcnt(4)
	v_mov_b32_e32 v100, v32
	v_mov_b32_e32 v101, v34
	v_mov_b32_e32 v46, v45
	v_mov_b32_e32 v34, v33
	v_pk_fma_f32 v[32:33], v[106:107], v[184:185], v[108:109]
	v_mov_b32_e32 v104, v40
	v_mov_b32_e32 v105, v42
	v_mov_b32_e32 v38, v37
	v_pk_fma_f32 v[36:37], v[30:31], v[186:187], v[46:47]
	v_pk_fma_f32 v[32:33], v[110:111], v[170:171], v[32:33]
	v_mov_b32_e32 v42, v41
	v_pk_fma_f32 v[36:37], v[38:39], v[180:181], v[36:37]
	v_pk_fma_f32 v[32:33], v[104:105], v[174:175], v[32:33]
	v_pk_fma_f32 v[36:37], v[42:43], v[172:173], v[36:37]
	v_pk_fma_f32 v[40:41], v[100:101], v[112:113], v[32:33]
	v_mov_b32_e32 v28, v4
	v_pk_fma_f32 v[32:33], v[34:35], v[114:115], v[36:37]
	v_mul_f32_e32 v4, 0xbfb8aa3b, v40
	v_mul_f32_e32 v37, 0xbfb8aa3b, v41
	v_mul_f32_e32 v29, 0xbfb8aa3b, v32
	v_mul_f32_e32 v45, 0xbfb8aa3b, v33
	v_exp_f32_e32 v36, v4
	v_exp_f32_e32 v37, v37
	v_exp_f32_e32 v44, v29
	v_exp_f32_e32 v45, v45
	v_mov_b32_e32 v29, v6
	v_mov_b32_e32 v6, v5
	v_pk_add_f32 v[4:5], v[36:37], 1.0 op_sel_hi:[1,0]
	v_pk_add_f32 v[36:37], v[44:45], 1.0 op_sel_hi:[1,0]
	v_div_scale_f32 v44, s[2:3], v5, v5, 1.0
	v_div_scale_f32 v133, s[2:3], v4, v4, 1.0
	v_rcp_f32_e32 v137, v44
	v_rcp_f32_e32 v139, v133
	v_div_scale_f32 v45, vcc, 1.0, v5, 1.0
	v_fma_f32 v145, -v44, v137, 1.0
	v_fma_f32 v147, -v133, v139, 1.0
	v_fmac_f32_e32 v137, v145, v137
	v_div_scale_f32 v135, s[2:3], 1.0, v4, 1.0
	v_fmac_f32_e32 v139, v147, v139
	v_mul_f32_e32 v145, v45, v137
	v_mul_f32_e32 v147, v135, v139
	v_fma_f32 v149, -v44, v145, v45
	v_fma_f32 v151, -v133, v147, v135
	v_fmac_f32_e32 v145, v149, v137
	v_div_scale_f32 v141, s[8:9], v37, v37, 1.0
	v_fmac_f32_e32 v147, v151, v139
	v_fma_f32 v44, -v44, v145, v45
	v_rcp_f32_e32 v143, v141
	v_fma_f32 v45, -v133, v147, v135
	v_div_fmas_f32 v44, v44, v137, v145
	s_mov_b64 vcc, s[2:3]
	v_div_fixup_f32 v5, v44, v5, 1.0
	v_div_fmas_f32 v44, v45, v139, v147
	v_div_fixup_f32 v4, v44, v4, 1.0
	v_pk_mul_f32 v[4:5], v[40:41], v[4:5]
	v_lshlrev_b32_e32 v45, 16, v103
	v_pk_mul_f32 v[184:185], v[160:161], v[4:5] op_sel_hi:[0,1]
	v_fma_f32 v4, -v141, v143, 1.0
	v_fmac_f32_e32 v143, v4, v143
	v_div_scale_f32 v4, vcc, 1.0, v37, 1.0
	v_mul_f32_e32 v5, v4, v143
	v_fma_f32 v40, -v141, v5, v4
	v_fmac_f32_e32 v5, v40, v143
	v_div_scale_f32 v40, s[2:3], v36, v36, 1.0
	v_rcp_f32_e32 v41, v40
	v_fma_f32 v4, -v141, v5, v4
	v_div_fmas_f32 v4, v4, v143, v5
	v_div_fixup_f32 v5, v4, v37, 1.0
	v_fma_f32 v4, -v40, v41, 1.0
	v_fmac_f32_e32 v41, v4, v41
	v_div_scale_f32 v4, vcc, 1.0, v36, 1.0
	v_mul_f32_e32 v37, v4, v41
	v_fma_f32 v44, -v40, v37, v4
	v_fmac_f32_e32 v37, v44, v41
	v_fma_f32 v4, -v40, v37, v4
	v_div_fmas_f32 v4, v4, v41, v37
	v_div_fixup_f32 v4, v4, v36, 1.0
	v_pk_mul_f32 v[4:5], v[32:33], v[4:5]
	s_waitcnt vmcnt(3)
	v_mov_b32_e32 v32, v16
	v_pk_mul_f32 v[186:187], v[160:161], v[4:5] op_sel_hi:[0,1]
	s_waitcnt vmcnt(0)
	v_mov_b32_e32 v4, v20
	v_mov_b32_e32 v5, v22
	v_pk_fma_f32 v[36:37], v[28:29], v[182:183], v[4:5]
	v_mov_b32_e32 v33, v18
	v_pk_fma_f32 v[40:41], v[32:33], v[176:177], v[36:37]
	v_mov_b32_e32 v36, v12
	v_mov_b32_e32 v37, v14
	v_pk_fma_f32 v[182:183], v[36:37], v[166:167], v[40:41]
	v_lshlrev_b32_e32 v44, 16, v102
	v_mov_b32_e32 v40, v8
	v_mov_b32_e32 v41, v10
	v_pk_fma_f32 v[182:183], v[40:41], v[44:45], v[182:183]
	v_mov_b32_e32 v14, v13
	v_mul_f32_e32 v8, 0xbfb8aa3b, v182
	v_exp_f32_e32 v12, v8
	v_mul_f32_e32 v8, 0xbfb8aa3b, v183
	v_exp_f32_e32 v13, v8
	v_mov_b32_e32 v22, v21
	v_pk_fma_f32 v[20:21], v[6:7], v[168:169], v[22:23]
	v_mov_b32_e32 v18, v17
	v_mov_b32_e32 v10, v9
	v_pk_add_f32 v[8:9], v[12:13], 1.0 op_sel_hi:[1,0]
	v_pk_fma_f32 v[16:17], v[18:19], v[178:179], v[20:21]
	v_div_scale_f32 v20, s[2:3], v9, v9, 1.0
	v_rcp_f32_e32 v21, v20
	v_pk_fma_f32 v[16:17], v[14:15], v[162:163], v[16:17]
	v_and_b32_e32 v169, 0xffff0000, v103
	v_and_b32_e32 v168, 0xffff0000, v102
	v_pk_fma_f32 v[12:13], v[10:11], v[168:169], v[16:17]
	v_fma_f32 v17, -v20, v21, 1.0
	v_fmac_f32_e32 v21, v17, v21
	v_div_scale_f32 v17, vcc, 1.0, v9, 1.0
	v_mul_f32_e32 v102, v17, v21
	v_fma_f32 v103, -v20, v102, v17
	v_fmac_f32_e32 v102, v103, v21
	v_fma_f32 v17, -v20, v102, v17
	v_div_scale_f32 v20, s[2:3], v8, v8, 1.0
	v_rcp_f32_e32 v103, v20
	v_div_fmas_f32 v17, v17, v21, v102
	v_div_fixup_f32 v9, v17, v9, 1.0
	v_div_scale_f32 v21, vcc, 1.0, v8, 1.0
	v_fma_f32 v17, -v20, v103, 1.0
	v_fmac_f32_e32 v103, v17, v103
	v_mul_f32_e32 v102, v21, v103
	v_fma_f32 v17, -v20, v102, v21
	v_mul_f32_e32 v16, 0xbfb8aa3b, v12
	v_fmac_f32_e32 v102, v17, v103
	v_mul_f32_e32 v17, 0xbfb8aa3b, v13
	v_exp_f32_e32 v16, v16
	v_exp_f32_e32 v17, v17
	v_fma_f32 v20, -v20, v102, v21
	v_div_fmas_f32 v20, v20, v103, v102
	v_div_fixup_f32 v8, v20, v8, 1.0
	v_pk_add_f32 v[16:17], v[16:17], 1.0 op_sel_hi:[1,0]
	v_pk_mul_f32 v[8:9], v[182:183], v[8:9]
	v_div_scale_f32 v21, s[2:3], v17, v17, 1.0
	v_rcp_f32_e32 v102, v21
	v_pk_mul_f32 v[8:9], v[160:161], v[8:9] op_sel_hi:[0,1]
	v_fma_f32 v20, -v21, v102, 1.0
	v_fmac_f32_e32 v102, v20, v102
	v_div_scale_f32 v20, vcc, 1.0, v17, 1.0
	v_mul_f32_e32 v103, v20, v102
	v_fma_f32 v133, -v21, v103, v20
	v_fmac_f32_e32 v103, v133, v102
	v_fma_f32 v20, -v21, v103, v20
	v_div_scale_f32 v21, s[2:3], v16, v16, 1.0
	v_rcp_f32_e32 v133, v21
	v_div_fmas_f32 v20, v20, v102, v103
	v_div_fixup_f32 v17, v20, v17, 1.0
	s_lshl_b64 s[2:3], s[6:7], 11
	v_fma_f32 v20, -v21, v133, 1.0
	v_fmac_f32_e32 v133, v20, v133
	v_div_scale_f32 v20, vcc, 1.0, v16, 1.0
	v_mul_f32_e32 v102, v20, v133
	v_fma_f32 v103, -v21, v102, v20
	v_fmac_f32_e32 v102, v103, v133
	v_fma_f32 v20, -v21, v102, v20
	v_div_fmas_f32 v20, v20, v133, v102
	v_div_fixup_f32 v16, v20, v16, 1.0
	v_pk_mul_f32 v[12:13], v[12:13], v[16:17]
	v_bfe_u32 v102, v8, 16, 1
	v_pk_mul_f32 v[12:13], v[160:161], v[12:13] op_sel_hi:[0,1]
	v_bfe_u32 v16, v13, 16, 1
	v_bfe_u32 v17, v12, 16, 1
	v_add3_u32 v12, v12, v17, s75
	v_add3_u32 v13, v13, v16, s75
	v_bfe_u32 v16, v184, 16, 1
	v_bfe_u32 v17, v185, 16, 1
	v_bfe_u32 v103, v9, 16, 1
	v_bfe_u32 v20, v187, 16, 1
	v_bfe_u32 v21, v186, 16, 1
	v_add3_u32 v9, v9, v103, s75
	v_add3_u32 v8, v8, v102, s75
	v_add3_u32 v17, v185, v17, s75
	v_add3_u32 v16, v184, v16, s75
	v_add3_u32 v21, v186, v21, s75
	v_add3_u32 v20, v187, v20, s75
	v_lshrrev_b32_e32 v16, 16, v16
	v_lshrrev_b32_e32 v17, 16, v17
	v_lshrrev_b32_e32 v8, 16, v8
	v_lshrrev_b32_e32 v9, 16, v9
	v_and_or_b32 v185, v13, s16, v9
	v_and_or_b32 v184, v12, s16, v8
	v_and_or_b32 v183, v20, s16, v17
	v_and_or_b32 v182, v21, s16, v16
	v_lshl_add_u64 v[8:9], v[128:129], 0, s[2:3]
	global_store_dwordx4 v[8:9], v[182:185], off sc1
	v_pk_fma_f32 v[8:9], v[106:107], v[170:171], v[108:109]
	v_lshlrev_b32_e32 v103, 16, v97
	v_pk_fma_f32 v[8:9], v[110:111], v[174:175], v[8:9]
	v_lshlrev_b32_e32 v102, 16, v96
	v_pk_fma_f32 v[8:9], v[104:105], v[112:113], v[8:9]
	v_and_b32_e32 v170, 0xffff0000, v96
	v_pk_fma_f32 v[8:9], v[100:101], v[102:103], v[8:9]
	v_and_b32_e32 v171, 0xffff0000, v97
	v_mul_f32_e32 v12, 0xbfb8aa3b, v8
	v_mul_f32_e32 v13, 0xbfb8aa3b, v9
	v_exp_f32_e32 v12, v12
	v_exp_f32_e32 v13, v13
	v_pk_fma_f32 v[16:17], v[30:31], v[180:181], v[46:47]
	v_pk_add_f32 v[12:13], v[12:13], 1.0 op_sel_hi:[1,0]
	s_nop 0
	v_div_scale_f32 v21, s[2:3], v13, v13, 1.0
	v_rcp_f32_e32 v96, v21
	v_pk_fma_f32 v[16:17], v[38:39], v[172:173], v[16:17]
	v_fma_f32 v97, -v21, v96, 1.0
	v_fmac_f32_e32 v96, v97, v96
	v_div_scale_f32 v97, vcc, 1.0, v13, 1.0
	v_mul_f32_e32 v133, v97, v96
	v_fma_f32 v135, -v21, v133, v97
	v_fmac_f32_e32 v133, v135, v96
	v_fma_f32 v21, -v21, v133, v97
	v_div_scale_f32 v97, s[2:3], v12, v12, 1.0
	v_rcp_f32_e32 v135, v97
	v_div_fmas_f32 v21, v21, v96, v133
	v_div_fixup_f32 v13, v21, v13, 1.0
	v_div_scale_f32 v96, vcc, 1.0, v12, 1.0
	v_fma_f32 v21, -v97, v135, 1.0
	v_fmac_f32_e32 v135, v21, v135
	v_pk_fma_f32 v[16:17], v[42:43], v[114:115], v[16:17]
	v_mul_f32_e32 v133, v96, v135
	v_pk_fma_f32 v[16:17], v[34:35], v[170:171], v[16:17]
	v_fma_f32 v21, -v97, v133, v96
	v_mul_f32_e32 v20, 0xbfb8aa3b, v16
	v_fmac_f32_e32 v133, v21, v135
	v_mul_f32_e32 v21, 0xbfb8aa3b, v17
	v_exp_f32_e32 v20, v20
	v_exp_f32_e32 v21, v21
	v_fma_f32 v96, -v97, v133, v96
	v_div_fmas_f32 v96, v96, v135, v133
	v_div_fixup_f32 v12, v96, v12, 1.0
	v_pk_add_f32 v[20:21], v[20:21], 1.0 op_sel_hi:[1,0]
	v_pk_mul_f32 v[8:9], v[8:9], v[12:13]
	v_div_scale_f32 v97, s[2:3], v21, v21, 1.0
	v_rcp_f32_e32 v133, v97
	v_pk_mul_f32 v[8:9], v[158:159], v[8:9] op_sel_hi:[0,1]
	v_fma_f32 v12, -v97, v133, 1.0
	v_fmac_f32_e32 v133, v12, v133
	v_div_scale_f32 v12, vcc, 1.0, v21, 1.0
	v_mul_f32_e32 v13, v12, v133
	v_fma_f32 v96, -v97, v13, v12
	v_fmac_f32_e32 v13, v96, v133
	v_div_scale_f32 v96, s[2:3], v20, v20, 1.0
	v_fma_f32 v12, -v97, v13, v12
	v_rcp_f32_e32 v97, v96
	v_div_fmas_f32 v12, v12, v133, v13
	v_div_fixup_f32 v13, v12, v21, 1.0
	v_fma_f32 v12, -v96, v97, 1.0
	v_fmac_f32_e32 v97, v12, v97
	v_div_scale_f32 v12, vcc, 1.0, v20, 1.0
	v_mul_f32_e32 v21, v12, v97
	v_fma_f32 v133, -v96, v21, v12
	v_fmac_f32_e32 v21, v133, v97
	v_fma_f32 v12, -v96, v21, v12
	v_div_fmas_f32 v12, v12, v97, v21
	v_div_fixup_f32 v12, v12, v20, 1.0
	v_pk_mul_f32 v[12:13], v[16:17], v[12:13]
	v_pk_fma_f32 v[16:17], v[28:29], v[176:177], v[4:5]
	v_lshlrev_b32_e32 v97, 16, v99
	v_pk_fma_f32 v[16:17], v[32:33], v[166:167], v[16:17]
	v_lshlrev_b32_e32 v96, 16, v98
	v_pk_fma_f32 v[16:17], v[36:37], v[44:45], v[16:17]
	v_pk_fma_f32 v[176:177], v[6:7], v[178:179], v[22:23]
	v_pk_fma_f32 v[16:17], v[40:41], v[96:97], v[16:17]
	v_pk_fma_f32 v[176:177], v[18:19], v[162:163], v[176:177]
	v_mul_f32_e32 v20, 0xbfb8aa3b, v16
	v_mul_f32_e32 v21, 0xbfb8aa3b, v17
	v_exp_f32_e32 v20, v20
	v_exp_f32_e32 v21, v21
	v_pk_fma_f32 v[176:177], v[14:15], v[168:169], v[176:177]
	v_and_b32_e32 v99, 0xffff0000, v99
	v_and_b32_e32 v98, 0xffff0000, v98
	v_pk_add_f32 v[20:21], v[20:21], 1.0 op_sel_hi:[1,0]
	v_pk_fma_f32 v[176:177], v[10:11], v[98:99], v[176:177]
	v_div_scale_f32 v133, s[2:3], v21, v21, 1.0
	v_rcp_f32_e32 v135, v133
	v_mul_f32_e32 v137, 0xbfb8aa3b, v176
	v_exp_f32_e32 v178, v137
	v_pk_mul_f32 v[12:13], v[158:159], v[12:13] op_sel_hi:[0,1]
	v_fma_f32 v137, -v133, v135, 1.0
	v_fmac_f32_e32 v135, v137, v135
	v_div_scale_f32 v137, vcc, 1.0, v21, 1.0
	v_mul_f32_e32 v139, v137, v135
	v_fma_f32 v141, -v133, v139, v137
	v_fmac_f32_e32 v139, v141, v135
	v_fma_f32 v133, -v133, v139, v137
	v_div_scale_f32 v137, s[2:3], v20, v20, 1.0
	v_rcp_f32_e32 v141, v137
	v_div_fmas_f32 v133, v133, v135, v139
	v_div_fixup_f32 v21, v133, v21, 1.0
	v_pk_fma_f32 v[162:163], v[6:7], v[162:163], v[22:23]
	v_fma_f32 v133, -v137, v141, 1.0
	v_fmac_f32_e32 v141, v133, v141
	v_div_scale_f32 v133, vcc, 1.0, v20, 1.0
	v_mul_f32_e32 v135, v133, v141
	v_fma_f32 v139, -v137, v135, v133
	v_fmac_f32_e32 v135, v139, v141
	v_mul_f32_e32 v139, 0xbfb8aa3b, v177
	v_exp_f32_e32 v179, v139
	v_fma_f32 v133, -v137, v135, v133
	v_div_fmas_f32 v133, v133, v141, v135
	v_div_fixup_f32 v20, v133, v20, 1.0
	v_pk_add_f32 v[178:179], v[178:179], 1.0 op_sel_hi:[1,0]
	v_pk_mul_f32 v[16:17], v[16:17], v[20:21]
	v_div_scale_f32 v135, s[2:3], v179, v179, 1.0
	v_rcp_f32_e32 v137, v135
	v_pk_mul_f32 v[16:17], v[158:159], v[16:17] op_sel_hi:[0,1]
	v_pk_fma_f32 v[162:163], v[18:19], v[168:169], v[162:163]
	v_fma_f32 v20, -v135, v137, 1.0
	v_fmac_f32_e32 v137, v20, v137
	v_div_scale_f32 v20, vcc, 1.0, v179, 1.0
	v_mul_f32_e32 v21, v20, v137
	v_fma_f32 v133, -v135, v21, v20
	v_fmac_f32_e32 v21, v133, v137
	v_div_scale_f32 v133, s[2:3], v178, v178, 1.0
	v_fma_f32 v20, -v135, v21, v20
	v_rcp_f32_e32 v135, v133
	v_div_fmas_f32 v20, v20, v137, v21
	v_div_fixup_f32 v21, v20, v179, 1.0
	s_or_b32 s2, s6, 1
	v_fma_f32 v20, -v133, v135, 1.0
	v_fmac_f32_e32 v135, v20, v135
	v_div_scale_f32 v20, vcc, 1.0, v178, 1.0
	v_mul_f32_e32 v137, v20, v135
	v_fma_f32 v139, -v133, v137, v20
	v_fmac_f32_e32 v137, v139, v135
	v_fma_f32 v20, -v133, v137, v20
	v_div_fmas_f32 v20, v20, v135, v137
	v_div_fixup_f32 v20, v20, v178, 1.0
	v_pk_mul_f32 v[20:21], v[176:177], v[20:21]
	v_bfe_u32 v137, v13, 16, 1
	v_pk_mul_f32 v[20:21], v[158:159], v[20:21] op_sel_hi:[0,1]
	v_bfe_u32 v133, v21, 16, 1
	v_bfe_u32 v135, v20, 16, 1
	v_bfe_u32 v139, v12, 16, 1
	v_add3_u32 v12, v12, v139, s75
	v_add3_u32 v13, v13, v137, s75
	v_add3_u32 v20, v20, v135, s75
	v_add3_u32 v21, v21, v133, s75
	v_bfe_u32 v133, v8, 16, 1
	v_bfe_u32 v135, v9, 16, 1
	v_bfe_u32 v137, v16, 16, 1
	v_bfe_u32 v139, v17, 16, 1
	v_add3_u32 v17, v17, v139, s75
	v_add3_u32 v16, v16, v137, s75
	v_add3_u32 v9, v9, v135, s75
	v_add3_u32 v8, v8, v133, s75
	s_ashr_i32 s3, s2, 31
	v_lshrrev_b32_e32 v8, 16, v8
	v_lshrrev_b32_e32 v9, 16, v9
	v_lshrrev_b32_e32 v16, 16, v16
	v_lshrrev_b32_e32 v17, 16, v17
	s_lshl_b64 s[2:3], s[2:3], 11
	v_and_or_b32 v179, v21, s16, v17
	v_and_or_b32 v178, v20, s16, v16
	v_and_or_b32 v177, v13, s16, v9
	v_and_or_b32 v176, v12, s16, v8
	v_lshl_add_u64 v[8:9], v[128:129], 0, s[2:3]
	global_store_dwordx4 v[8:9], v[176:179], off sc1
	v_pk_fma_f32 v[8:9], v[106:107], v[174:175], v[108:109]
	v_lshlrev_b32_e32 v21, 16, v93
	v_pk_fma_f32 v[8:9], v[110:111], v[112:113], v[8:9]
	v_lshlrev_b32_e32 v20, 16, v92
	v_pk_fma_f32 v[8:9], v[104:105], v[102:103], v[8:9]
	v_pk_fma_f32 v[16:17], v[30:31], v[172:173], v[46:47]
	v_pk_fma_f32 v[8:9], v[100:101], v[20:21], v[8:9]
	v_pk_fma_f32 v[16:17], v[38:39], v[114:115], v[16:17]
	v_mul_f32_e32 v12, 0xbfb8aa3b, v8
	v_mul_f32_e32 v13, 0xbfb8aa3b, v9
	v_exp_f32_e32 v12, v12
	v_exp_f32_e32 v13, v13
	v_pk_fma_f32 v[16:17], v[42:43], v[170:171], v[16:17]
	v_and_b32_e32 v93, 0xffff0000, v93
	v_and_b32_e32 v92, 0xffff0000, v92
	v_pk_add_f32 v[12:13], v[12:13], 1.0 op_sel_hi:[1,0]
	v_pk_fma_f32 v[16:17], v[34:35], v[92:93], v[16:17]
	v_div_scale_f32 v133, s[2:3], v13, v13, 1.0
	v_rcp_f32_e32 v135, v133
	v_mul_f32_e32 v137, 0xbfb8aa3b, v16
	v_exp_f32_e32 v158, v137
	v_pk_fma_f32 v[162:163], v[14:15], v[98:99], v[162:163]
	v_fma_f32 v137, -v133, v135, 1.0
	v_fmac_f32_e32 v135, v137, v135
	v_div_scale_f32 v137, vcc, 1.0, v13, 1.0
	v_mul_f32_e32 v139, v137, v135
	v_fma_f32 v141, -v133, v139, v137
	v_fmac_f32_e32 v139, v141, v135
	v_fma_f32 v133, -v133, v139, v137
	v_div_scale_f32 v137, s[2:3], v12, v12, 1.0
	v_rcp_f32_e32 v141, v137
	v_div_fmas_f32 v133, v133, v135, v139
	v_div_fixup_f32 v13, v133, v13, 1.0
	v_fma_f32 v133, -v137, v141, 1.0
	v_fmac_f32_e32 v141, v133, v141
	v_div_scale_f32 v133, vcc, 1.0, v12, 1.0
	v_mul_f32_e32 v135, v133, v141
	v_fma_f32 v139, -v137, v135, v133
	v_fmac_f32_e32 v135, v139, v141
	v_mul_f32_e32 v139, 0xbfb8aa3b, v17
	v_exp_f32_e32 v159, v139
	v_fma_f32 v133, -v137, v135, v133
	v_div_fmas_f32 v133, v133, v141, v135
	v_div_fixup_f32 v12, v133, v12, 1.0
	v_pk_add_f32 v[158:159], v[158:159], 1.0 op_sel_hi:[1,0]
	v_pk_mul_f32 v[8:9], v[8:9], v[12:13]
	v_div_scale_f32 v135, s[2:3], v159, v159, 1.0
	v_rcp_f32_e32 v137, v135
	v_pk_mul_f32 v[8:9], v[156:157], v[8:9] op_sel_hi:[0,1]
	v_fma_f32 v12, -v135, v137, 1.0
	v_fmac_f32_e32 v137, v12, v137
	v_div_scale_f32 v12, vcc, 1.0, v159, 1.0
	v_mul_f32_e32 v13, v12, v137
	v_fma_f32 v133, -v135, v13, v12
	v_fmac_f32_e32 v13, v133, v137
	v_div_scale_f32 v133, s[2:3], v158, v158, 1.0
	v_fma_f32 v12, -v135, v13, v12
	v_rcp_f32_e32 v135, v133
	v_div_fmas_f32 v12, v12, v137, v13
	v_div_fixup_f32 v13, v12, v159, 1.0
	v_fma_f32 v12, -v133, v135, 1.0
	v_fmac_f32_e32 v135, v12, v135
	v_div_scale_f32 v12, vcc, 1.0, v158, 1.0
	v_mul_f32_e32 v137, v12, v135
	v_fma_f32 v139, -v133, v137, v12
	v_fmac_f32_e32 v137, v139, v135
	v_fma_f32 v12, -v133, v137, v12
	v_div_fmas_f32 v12, v12, v135, v137
	v_div_fixup_f32 v12, v12, v158, 1.0
	v_pk_mul_f32 v[12:13], v[16:17], v[12:13]
	v_pk_fma_f32 v[16:17], v[28:29], v[166:167], v[4:5]
	v_pk_mul_f32 v[12:13], v[156:157], v[12:13] op_sel_hi:[0,1]
	v_pk_fma_f32 v[16:17], v[32:33], v[44:45], v[16:17]
	s_nop 0
	v_pk_fma_f32 v[158:159], v[36:37], v[96:97], v[16:17]
	v_lshlrev_b32_e32 v17, 16, v95
	v_lshlrev_b32_e32 v16, 16, v94
	v_pk_fma_f32 v[158:159], v[40:41], v[16:17], v[158:159]
	v_and_b32_e32 v95, 0xffff0000, v95
	v_mul_f32_e32 v133, 0xbfb8aa3b, v158
	v_exp_f32_e32 v166, v133
	v_mul_f32_e32 v133, 0xbfb8aa3b, v159
	v_exp_f32_e32 v167, v133
	v_and_b32_e32 v94, 0xffff0000, v94
	v_pk_fma_f32 v[162:163], v[10:11], v[94:95], v[162:163]
	v_pk_add_f32 v[166:167], v[166:167], 1.0 op_sel_hi:[1,0]
	s_nop 0
	v_div_scale_f32 v133, s[2:3], v167, v167, 1.0
	v_rcp_f32_e32 v135, v133
	v_mul_f32_e32 v137, 0xbfb8aa3b, v162
	v_exp_f32_e32 v172, v137
	v_fma_f32 v137, -v133, v135, 1.0
	v_fmac_f32_e32 v135, v137, v135
	v_div_scale_f32 v137, vcc, 1.0, v167, 1.0
	v_mul_f32_e32 v139, v137, v135
	v_fma_f32 v141, -v133, v139, v137
	v_fmac_f32_e32 v139, v141, v135
	v_fma_f32 v133, -v133, v139, v137
	v_div_scale_f32 v137, s[2:3], v166, v166, 1.0
	v_rcp_f32_e32 v141, v137
	v_div_fmas_f32 v133, v133, v135, v139
	v_div_fixup_f32 v167, v133, v167, 1.0
	v_fma_f32 v133, -v137, v141, 1.0
	v_fmac_f32_e32 v141, v133, v141
	v_div_scale_f32 v133, vcc, 1.0, v166, 1.0
	v_mul_f32_e32 v135, v133, v141
	v_fma_f32 v139, -v137, v135, v133
	v_fmac_f32_e32 v135, v139, v141
	v_mul_f32_e32 v139, 0xbfb8aa3b, v163
	v_exp_f32_e32 v173, v139
	v_fma_f32 v133, -v137, v135, v133
	v_div_fmas_f32 v133, v133, v141, v135
	v_div_fixup_f32 v166, v133, v166, 1.0
	v_pk_add_f32 v[172:173], v[172:173], 1.0 op_sel_hi:[1,0]
	v_pk_mul_f32 v[158:159], v[158:159], v[166:167]
	v_div_scale_f32 v135, s[2:3], v173, v173, 1.0
	v_rcp_f32_e32 v137, v135
	v_pk_mul_f32 v[158:159], v[156:157], v[158:159] op_sel_hi:[0,1]
	v_bfe_u32 v143, v159, 16, 1
	v_add3_u32 v143, v159, v143, s75
	v_fma_f32 v133, -v135, v137, 1.0
	v_fmac_f32_e32 v137, v133, v137
	v_div_scale_f32 v133, vcc, 1.0, v173, 1.0
	v_mul_f32_e32 v139, v133, v137
	v_fma_f32 v141, -v135, v139, v133
	v_fmac_f32_e32 v139, v141, v137
	v_fma_f32 v133, -v135, v139, v133
	v_div_scale_f32 v135, s[2:3], v172, v172, 1.0
	v_rcp_f32_e32 v141, v135
	v_div_fmas_f32 v133, v133, v137, v139
	v_div_fixup_f32 v167, v133, v173, 1.0
	s_or_b32 s2, s6, 2
	v_fma_f32 v133, -v135, v141, 1.0
	v_fmac_f32_e32 v141, v133, v141
	v_div_scale_f32 v133, vcc, 1.0, v172, 1.0
	v_mul_f32_e32 v137, v133, v141
	v_fma_f32 v139, -v135, v137, v133
	v_fmac_f32_e32 v137, v139, v141
	v_fma_f32 v133, -v135, v137, v133
	v_div_fmas_f32 v133, v133, v141, v137
	v_div_fixup_f32 v166, v133, v172, 1.0
	v_pk_mul_f32 v[162:163], v[162:163], v[166:167]
	v_bfe_u32 v137, v13, 16, 1
	v_bfe_u32 v139, v12, 16, 1
	v_pk_mul_f32 v[156:157], v[156:157], v[162:163] op_sel_hi:[0,1]
	v_add3_u32 v12, v12, v139, s75
	v_add3_u32 v13, v13, v137, s75
	v_bfe_u32 v137, v8, 16, 1
	v_bfe_u32 v139, v9, 16, 1
	v_bfe_u32 v141, v158, 16, 1
	v_bfe_u32 v133, v157, 16, 1
	v_bfe_u32 v135, v156, 16, 1
	v_add3_u32 v141, v158, v141, s75
	v_add3_u32 v9, v9, v139, s75
	v_add3_u32 v8, v8, v137, s75
	s_ashr_i32 s3, s2, 31
	v_add3_u32 v135, v156, v135, s75
	v_add3_u32 v133, v157, v133, s75
	v_lshrrev_b32_e32 v8, 16, v8
	v_lshrrev_b32_e32 v9, 16, v9
	v_lshrrev_b32_e32 v137, 16, v141
	v_lshrrev_b32_e32 v139, 16, v143
	s_lshl_b64 s[2:3], s[2:3], 11
	v_and_or_b32 v159, v133, s16, v139
	v_and_or_b32 v158, v135, s16, v137
	v_and_or_b32 v157, v13, s16, v9
	v_and_or_b32 v156, v12, s16, v8
	v_lshl_add_u64 v[8:9], v[128:129], 0, s[2:3]
	global_store_dwordx4 v[8:9], v[156:159], off sc1
	v_pk_fma_f32 v[8:9], v[106:107], v[112:113], v[108:109]
	s_nop 0
	v_pk_fma_f32 v[8:9], v[110:111], v[102:103], v[8:9]
	v_pk_fma_f32 v[158:159], v[6:7], v[168:169], v[22:23]
	v_pk_fma_f32 v[12:13], v[104:105], v[20:21], v[8:9]
	v_lshlrev_b32_e32 v9, 16, v89
	v_lshlrev_b32_e32 v8, 16, v88
	v_pk_fma_f32 v[12:13], v[100:101], v[8:9], v[12:13]
	v_pk_fma_f32 v[158:159], v[18:19], v[98:99], v[158:159]
	v_mul_f32_e32 v112, 0xbfb8aa3b, v12
	v_exp_f32_e32 v156, v112
	v_pk_fma_f32 v[112:113], v[30:31], v[114:115], v[46:47]
	v_mul_f32_e32 v114, 0xbfb8aa3b, v13
	v_exp_f32_e32 v157, v114
	v_pk_fma_f32 v[112:113], v[38:39], v[170:171], v[112:113]
	v_pk_fma_f32 v[158:159], v[14:15], v[94:95], v[158:159]
	v_pk_fma_f32 v[114:115], v[42:43], v[92:93], v[112:113]
	v_and_b32_e32 v113, 0xffff0000, v89
	v_and_b32_e32 v112, 0xffff0000, v88
	v_pk_add_f32 v[88:89], v[156:157], 1.0 op_sel_hi:[1,0]
	v_pk_fma_f32 v[114:115], v[34:35], v[112:113], v[114:115]
	v_div_scale_f32 v133, s[2:3], v89, v89, 1.0
	v_rcp_f32_e32 v135, v133
	v_mul_f32_e32 v137, 0xbfb8aa3b, v114
	v_exp_f32_e32 v156, v137
	v_pk_fma_f32 v[98:99], v[6:7], v[98:99], v[22:23]
	v_fma_f32 v137, -v133, v135, 1.0
	v_fmac_f32_e32 v135, v137, v135
	v_div_scale_f32 v137, vcc, 1.0, v89, 1.0
	v_mul_f32_e32 v139, v137, v135
	v_fma_f32 v141, -v133, v139, v137
	v_fmac_f32_e32 v139, v141, v135
	v_fma_f32 v133, -v133, v139, v137
	v_div_scale_f32 v137, s[2:3], v88, v88, 1.0
	v_rcp_f32_e32 v141, v137
	v_div_fmas_f32 v133, v133, v135, v139
	v_div_fixup_f32 v89, v133, v89, 1.0
	v_pk_fma_f32 v[98:99], v[18:19], v[94:95], v[98:99]
	v_fma_f32 v133, -v137, v141, 1.0
	v_fmac_f32_e32 v141, v133, v141
	v_div_scale_f32 v133, vcc, 1.0, v88, 1.0
	v_mul_f32_e32 v135, v133, v141
	v_fma_f32 v139, -v137, v135, v133
	v_fmac_f32_e32 v135, v139, v141
	v_mul_f32_e32 v139, 0xbfb8aa3b, v115
	v_exp_f32_e32 v157, v139
	v_fma_f32 v133, -v137, v135, v133
	v_div_fmas_f32 v133, v133, v141, v135
	v_div_fixup_f32 v88, v133, v88, 1.0
	v_pk_add_f32 v[156:157], v[156:157], 1.0 op_sel_hi:[1,0]
	v_pk_mul_f32 v[12:13], v[12:13], v[88:89]
	v_div_scale_f32 v135, s[2:3], v157, v157, 1.0
	v_rcp_f32_e32 v137, v135
	v_pk_mul_f32 v[88:89], v[154:155], v[12:13] op_sel_hi:[0,1]
	v_pk_fma_f32 v[94:95], v[6:7], v[94:95], v[22:23]
	v_fma_f32 v12, -v135, v137, 1.0
	v_fmac_f32_e32 v137, v12, v137
	v_div_scale_f32 v12, vcc, 1.0, v157, 1.0
	v_mul_f32_e32 v13, v12, v137
	v_fma_f32 v133, -v135, v13, v12
	v_fmac_f32_e32 v13, v133, v137
	v_div_scale_f32 v133, s[2:3], v156, v156, 1.0
	v_fma_f32 v12, -v135, v13, v12
	v_rcp_f32_e32 v135, v133
	v_div_fmas_f32 v12, v12, v137, v13
	v_div_fixup_f32 v13, v12, v157, 1.0
	v_fma_f32 v12, -v133, v135, 1.0
	v_fmac_f32_e32 v135, v12, v135
	v_div_scale_f32 v12, vcc, 1.0, v156, 1.0
	v_mul_f32_e32 v137, v12, v135
	v_fma_f32 v139, -v133, v137, v12
	v_fmac_f32_e32 v137, v139, v135
	v_fma_f32 v12, -v133, v137, v12
	v_div_fmas_f32 v12, v12, v135, v137
	v_div_fixup_f32 v12, v12, v156, 1.0
	v_pk_mul_f32 v[12:13], v[114:115], v[12:13]
	s_nop 0
	v_pk_mul_f32 v[114:115], v[154:155], v[12:13] op_sel_hi:[0,1]
	v_pk_fma_f32 v[12:13], v[28:29], v[44:45], v[4:5]
	s_nop 0
	v_pk_fma_f32 v[12:13], v[32:33], v[96:97], v[12:13]
	s_nop 0
	v_pk_fma_f32 v[44:45], v[36:37], v[16:17], v[12:13]
	v_lshlrev_b32_e32 v13, 16, v91
	v_lshlrev_b32_e32 v12, 16, v90
	v_pk_fma_f32 v[44:45], v[40:41], v[12:13], v[44:45]
	v_and_b32_e32 v91, 0xffff0000, v91
	v_mul_f32_e32 v133, 0xbfb8aa3b, v44
	v_exp_f32_e32 v156, v133
	v_mul_f32_e32 v133, 0xbfb8aa3b, v45
	v_exp_f32_e32 v157, v133
	v_and_b32_e32 v90, 0xffff0000, v90
	v_pk_fma_f32 v[158:159], v[10:11], v[90:91], v[158:159]
	v_pk_fma_f32 v[98:99], v[14:15], v[90:91], v[98:99]
	v_pk_add_f32 v[156:157], v[156:157], 1.0 op_sel_hi:[1,0]
	v_mul_f32_e32 v137, 0xbfb8aa3b, v158
	v_div_scale_f32 v133, s[2:3], v157, v157, 1.0
	v_rcp_f32_e32 v135, v133
	v_exp_f32_e32 v162, v137
	v_pk_fma_f32 v[94:95], v[18:19], v[90:91], v[94:95]
	v_pk_fma_f32 v[90:91], v[6:7], v[90:91], v[22:23]
	v_fma_f32 v137, -v133, v135, 1.0
	v_fmac_f32_e32 v135, v137, v135
	v_div_scale_f32 v137, vcc, 1.0, v157, 1.0
	v_mul_f32_e32 v139, v137, v135
	v_fma_f32 v141, -v133, v139, v137
	v_fmac_f32_e32 v139, v141, v135
	v_fma_f32 v133, -v133, v139, v137
	v_div_scale_f32 v137, s[2:3], v156, v156, 1.0
	v_rcp_f32_e32 v141, v137
	v_div_fmas_f32 v133, v133, v135, v139
	v_div_fixup_f32 v157, v133, v157, 1.0
	v_fma_f32 v133, -v137, v141, 1.0
	v_fmac_f32_e32 v141, v133, v141
	v_div_scale_f32 v133, vcc, 1.0, v156, 1.0
	v_mul_f32_e32 v135, v133, v141
	v_fma_f32 v139, -v137, v135, v133
	v_fmac_f32_e32 v135, v139, v141
	v_mul_f32_e32 v139, 0xbfb8aa3b, v159
	v_exp_f32_e32 v163, v139
	v_fma_f32 v133, -v137, v135, v133
	v_div_fmas_f32 v133, v133, v141, v135
	v_div_fixup_f32 v156, v133, v156, 1.0
	v_pk_add_f32 v[162:163], v[162:163], 1.0 op_sel_hi:[1,0]
	v_pk_mul_f32 v[44:45], v[44:45], v[156:157]
	v_div_scale_f32 v135, s[2:3], v163, v163, 1.0
	v_rcp_f32_e32 v137, v135
	v_pk_mul_f32 v[44:45], v[154:155], v[44:45] op_sel_hi:[0,1]
	v_bfe_u32 v143, v45, 16, 1
	v_add3_u32 v45, v45, v143, s75
	v_fma_f32 v133, -v135, v137, 1.0
	v_fmac_f32_e32 v137, v133, v137
	v_div_scale_f32 v133, vcc, 1.0, v163, 1.0
	v_mul_f32_e32 v139, v133, v137
	v_fma_f32 v141, -v135, v139, v133
	v_fmac_f32_e32 v139, v141, v137
	v_fma_f32 v133, -v135, v139, v133
	v_div_scale_f32 v135, s[2:3], v162, v162, 1.0
	v_rcp_f32_e32 v141, v135
	v_div_fmas_f32 v133, v133, v137, v139
	v_div_fixup_f32 v157, v133, v163, 1.0
	s_or_b32 s2, s6, 3
	v_fma_f32 v133, -v135, v141, 1.0
	v_fmac_f32_e32 v141, v133, v141
	v_div_scale_f32 v133, vcc, 1.0, v162, 1.0
	v_mul_f32_e32 v137, v133, v141
	v_fma_f32 v139, -v135, v137, v133
	v_fmac_f32_e32 v137, v139, v141
	v_fma_f32 v133, -v135, v137, v133
	v_div_fmas_f32 v133, v133, v141, v137
	v_div_fixup_f32 v156, v133, v162, 1.0
	v_pk_mul_f32 v[156:157], v[158:159], v[156:157]
	v_bfe_u32 v137, v115, 16, 1
	v_bfe_u32 v139, v114, 16, 1
	v_pk_mul_f32 v[154:155], v[154:155], v[156:157] op_sel_hi:[0,1]
	v_add3_u32 v114, v114, v139, s75
	v_add3_u32 v115, v115, v137, s75
	v_bfe_u32 v137, v88, 16, 1
	v_bfe_u32 v139, v89, 16, 1
	v_bfe_u32 v141, v44, 16, 1
	v_bfe_u32 v133, v155, 16, 1
	v_bfe_u32 v135, v154, 16, 1
	v_add3_u32 v44, v44, v141, s75
	v_add3_u32 v89, v89, v139, s75
	v_add3_u32 v88, v88, v137, s75
	s_ashr_i32 s3, s2, 31
	v_add3_u32 v135, v154, v135, s75
	v_add3_u32 v133, v155, v133, s75
	v_lshrrev_b32_e32 v88, 16, v88
	v_lshrrev_b32_e32 v89, 16, v89
	v_lshrrev_b32_e32 v44, 16, v44
	v_lshrrev_b32_e32 v45, 16, v45
	s_lshl_b64 s[2:3], s[2:3], 11
	v_and_or_b32 v157, v133, s16, v45
	v_and_or_b32 v156, v135, s16, v44
	v_and_or_b32 v155, v115, s16, v89
	v_and_or_b32 v154, v114, s16, v88
	v_lshl_add_u64 v[44:45], v[128:129], 0, s[2:3]
	global_store_dwordx4 v[44:45], v[154:157], off sc1
	v_pk_fma_f32 v[44:45], v[106:107], v[102:103], v[108:109]
	v_lshlrev_b32_e32 v89, 16, v85
	v_pk_fma_f32 v[44:45], v[110:111], v[20:21], v[44:45]
	v_lshlrev_b32_e32 v88, 16, v84
	v_pk_fma_f32 v[44:45], v[104:105], v[8:9], v[44:45]
	v_pk_fma_f32 v[114:115], v[30:31], v[170:171], v[46:47]
	v_pk_fma_f32 v[44:45], v[100:101], v[88:89], v[44:45]
	v_pk_fma_f32 v[114:115], v[38:39], v[92:93], v[114:115]
	v_mul_f32_e32 v102, 0xbfb8aa3b, v44
	v_mul_f32_e32 v103, 0xbfb8aa3b, v45
	v_exp_f32_e32 v102, v102
	v_exp_f32_e32 v103, v103
	v_pk_fma_f32 v[114:115], v[42:43], v[112:113], v[114:115]
	v_and_b32_e32 v85, 0xffff0000, v85
	v_and_b32_e32 v84, 0xffff0000, v84
	v_pk_add_f32 v[102:103], v[102:103], 1.0 op_sel_hi:[1,0]
	v_pk_fma_f32 v[114:115], v[34:35], v[84:85], v[114:115]
	v_div_scale_f32 v133, s[2:3], v103, v103, 1.0
	v_rcp_f32_e32 v135, v133
	v_mul_f32_e32 v137, 0xbfb8aa3b, v114
	v_exp_f32_e32 v154, v137
	v_pk_fma_f32 v[20:21], v[106:107], v[20:21], v[108:109]
	v_fma_f32 v137, -v133, v135, 1.0
	v_fmac_f32_e32 v135, v137, v135
	v_div_scale_f32 v137, vcc, 1.0, v103, 1.0
	v_mul_f32_e32 v139, v137, v135
	v_fma_f32 v141, -v133, v139, v137
	v_fmac_f32_e32 v139, v141, v135
	v_fma_f32 v133, -v133, v139, v137
	v_div_scale_f32 v137, s[2:3], v102, v102, 1.0
	v_rcp_f32_e32 v141, v137
	v_div_fmas_f32 v133, v133, v135, v139
	v_div_fixup_f32 v103, v133, v103, 1.0
	v_pk_fma_f32 v[20:21], v[110:111], v[8:9], v[20:21]
	v_fma_f32 v133, -v137, v141, 1.0
	v_fmac_f32_e32 v141, v133, v141
	v_div_scale_f32 v133, vcc, 1.0, v102, 1.0
	v_mul_f32_e32 v135, v133, v141
	v_fma_f32 v139, -v137, v135, v133
	v_fmac_f32_e32 v135, v139, v141
	v_mul_f32_e32 v139, 0xbfb8aa3b, v115
	v_exp_f32_e32 v155, v139
	v_fma_f32 v133, -v137, v135, v133
	v_div_fmas_f32 v133, v133, v141, v135
	v_div_fixup_f32 v102, v133, v102, 1.0
	v_pk_add_f32 v[154:155], v[154:155], 1.0 op_sel_hi:[1,0]
	v_pk_mul_f32 v[44:45], v[44:45], v[102:103]
	v_div_scale_f32 v135, s[2:3], v155, v155, 1.0
	v_rcp_f32_e32 v137, v135
	v_pk_mul_f32 v[102:103], v[152:153], v[44:45] op_sel_hi:[0,1]
	v_pk_fma_f32 v[92:93], v[30:31], v[92:93], v[46:47]
	v_pk_fma_f32 v[8:9], v[106:107], v[8:9], v[108:109]
	v_fma_f32 v44, -v135, v137, 1.0
	v_fmac_f32_e32 v137, v44, v137
	v_div_scale_f32 v44, vcc, 1.0, v155, 1.0
	v_mul_f32_e32 v45, v44, v137
	v_fma_f32 v133, -v135, v45, v44
	v_fmac_f32_e32 v45, v133, v137
	v_div_scale_f32 v133, s[2:3], v154, v154, 1.0
	v_fma_f32 v44, -v135, v45, v44
	v_rcp_f32_e32 v135, v133
	v_div_fmas_f32 v44, v44, v137, v45
	v_div_fixup_f32 v45, v44, v155, 1.0
	v_pk_fma_f32 v[92:93], v[38:39], v[112:113], v[92:93]
	v_fma_f32 v44, -v133, v135, 1.0
	v_fmac_f32_e32 v135, v44, v135
	v_div_scale_f32 v44, vcc, 1.0, v154, 1.0
	v_mul_f32_e32 v137, v44, v135
	v_fma_f32 v139, -v133, v137, v44
	v_fmac_f32_e32 v137, v139, v135
	v_fma_f32 v44, -v133, v137, v44
	v_div_fmas_f32 v44, v44, v135, v137
	v_div_fixup_f32 v44, v44, v154, 1.0
	v_pk_mul_f32 v[44:45], v[114:115], v[44:45]
	v_pk_fma_f32 v[92:93], v[42:43], v[84:85], v[92:93]
	v_pk_mul_f32 v[114:115], v[152:153], v[44:45] op_sel_hi:[0,1]
	v_pk_fma_f32 v[44:45], v[28:29], v[96:97], v[4:5]
	v_pk_fma_f32 v[8:9], v[110:111], v[88:89], v[8:9]
	v_pk_fma_f32 v[44:45], v[32:33], v[16:17], v[44:45]
	v_pk_fma_f32 v[16:17], v[28:29], v[16:17], v[4:5]
	v_pk_fma_f32 v[96:97], v[36:37], v[12:13], v[44:45]
	v_lshlrev_b32_e32 v45, 16, v87
	v_lshlrev_b32_e32 v44, 16, v86
	v_pk_fma_f32 v[96:97], v[40:41], v[44:45], v[96:97]
	v_and_b32_e32 v87, 0xffff0000, v87
	v_mul_f32_e32 v133, 0xbfb8aa3b, v96
	v_exp_f32_e32 v154, v133
	v_mul_f32_e32 v133, 0xbfb8aa3b, v97
	v_exp_f32_e32 v155, v133
	v_and_b32_e32 v86, 0xffff0000, v86
	v_pk_fma_f32 v[98:99], v[10:11], v[86:87], v[98:99]
	v_pk_fma_f32 v[16:17], v[32:33], v[12:13], v[16:17]
	v_pk_add_f32 v[154:155], v[154:155], 1.0 op_sel_hi:[1,0]
	v_mul_f32_e32 v137, 0xbfb8aa3b, v98
	v_div_scale_f32 v133, s[2:3], v155, v155, 1.0
	v_rcp_f32_e32 v135, v133
	v_exp_f32_e32 v156, v137
	v_pk_fma_f32 v[94:95], v[14:15], v[86:87], v[94:95]
	v_pk_fma_f32 v[12:13], v[28:29], v[12:13], v[4:5]
	v_fma_f32 v137, -v133, v135, 1.0
	v_fmac_f32_e32 v135, v137, v135
	v_div_scale_f32 v137, vcc, 1.0, v155, 1.0
	v_mul_f32_e32 v139, v137, v135
	v_fma_f32 v141, -v133, v139, v137
	v_fmac_f32_e32 v139, v141, v135
	v_fma_f32 v133, -v133, v139, v137
	v_div_scale_f32 v137, s[2:3], v154, v154, 1.0
	v_rcp_f32_e32 v141, v137
	v_div_fmas_f32 v133, v133, v135, v139
	v_div_fixup_f32 v155, v133, v155, 1.0
	v_pk_fma_f32 v[12:13], v[32:33], v[44:45], v[12:13]
	v_fma_f32 v133, -v137, v141, 1.0
	v_fmac_f32_e32 v141, v133, v141
	v_div_scale_f32 v133, vcc, 1.0, v154, 1.0
	v_mul_f32_e32 v135, v133, v141
	v_fma_f32 v139, -v137, v135, v133
	v_fmac_f32_e32 v135, v139, v141
	v_mul_f32_e32 v139, 0xbfb8aa3b, v99
	v_exp_f32_e32 v157, v139
	v_fma_f32 v133, -v137, v135, v133
	v_div_fmas_f32 v133, v133, v141, v135
	v_div_fixup_f32 v154, v133, v154, 1.0
	v_pk_add_f32 v[156:157], v[156:157], 1.0 op_sel_hi:[1,0]
	v_pk_mul_f32 v[96:97], v[96:97], v[154:155]
	v_div_scale_f32 v135, s[2:3], v157, v157, 1.0
	v_rcp_f32_e32 v137, v135
	v_pk_mul_f32 v[96:97], v[152:153], v[96:97] op_sel_hi:[0,1]
	v_pk_fma_f32 v[90:91], v[18:19], v[86:87], v[90:91]
	v_pk_fma_f32 v[86:87], v[6:7], v[86:87], v[22:23]
	v_fma_f32 v133, -v135, v137, 1.0
	v_fmac_f32_e32 v137, v133, v137
	v_div_scale_f32 v133, vcc, 1.0, v157, 1.0
	v_mul_f32_e32 v139, v133, v137
	v_fma_f32 v141, -v135, v139, v133
	v_fmac_f32_e32 v139, v141, v137
	v_fma_f32 v133, -v135, v139, v133
	v_div_scale_f32 v135, s[2:3], v156, v156, 1.0
	v_rcp_f32_e32 v141, v135
	v_div_fmas_f32 v133, v133, v137, v139
	v_div_fixup_f32 v155, v133, v157, 1.0
	s_or_b32 s2, s6, 4
	v_fma_f32 v133, -v135, v141, 1.0
	v_fmac_f32_e32 v141, v133, v141
	v_div_scale_f32 v133, vcc, 1.0, v156, 1.0
	v_mul_f32_e32 v137, v133, v141
	v_fma_f32 v139, -v135, v137, v133
	v_fmac_f32_e32 v137, v139, v141
	v_fma_f32 v133, -v135, v137, v133
	v_div_fmas_f32 v133, v133, v141, v137
	v_div_fixup_f32 v154, v133, v156, 1.0
	v_pk_mul_f32 v[98:99], v[98:99], v[154:155]
	v_bfe_u32 v137, v115, 16, 1
	v_pk_mul_f32 v[98:99], v[152:153], v[98:99] op_sel_hi:[0,1]
	v_bfe_u32 v133, v99, 16, 1
	v_bfe_u32 v135, v98, 16, 1
	v_bfe_u32 v139, v114, 16, 1
	v_add3_u32 v114, v114, v139, s75
	v_add3_u32 v115, v115, v137, s75
	v_add3_u32 v98, v98, v135, s75
	v_add3_u32 v99, v99, v133, s75
	v_bfe_u32 v133, v102, 16, 1
	v_bfe_u32 v135, v103, 16, 1
	v_bfe_u32 v137, v96, 16, 1
	v_bfe_u32 v139, v97, 16, 1
	v_add3_u32 v97, v97, v139, s75
	v_add3_u32 v96, v96, v137, s75
	v_add3_u32 v103, v103, v135, s75
	v_add3_u32 v102, v102, v133, s75
	s_ashr_i32 s3, s2, 31
	v_lshrrev_b32_e32 v102, 16, v102
	v_lshrrev_b32_e32 v103, 16, v103
	v_lshrrev_b32_e32 v96, 16, v96
	v_lshrrev_b32_e32 v97, 16, v97
	s_lshl_b64 s[2:3], s[2:3], 11
	v_and_or_b32 v99, v99, s16, v97
	v_and_or_b32 v98, v98, s16, v96
	v_and_or_b32 v97, v115, s16, v103
	v_and_or_b32 v96, v114, s16, v102
	v_lshl_add_u64 v[102:103], v[128:129], 0, s[2:3]
	global_store_dwordx4 v[102:103], v[96:99], off sc1
	s_nop 1
	v_pk_fma_f32 v[96:97], v[104:105], v[88:89], v[20:21]
	v_lshlrev_b32_e32 v21, 16, v81
	v_lshlrev_b32_e32 v20, 16, v80
	v_pk_fma_f32 v[96:97], v[100:101], v[20:21], v[96:97]
	v_and_b32_e32 v81, 0xffff0000, v81
	v_mul_f32_e32 v98, 0xbfb8aa3b, v96
	v_mul_f32_e32 v99, 0xbfb8aa3b, v97
	v_exp_f32_e32 v98, v98
	v_exp_f32_e32 v99, v99
	v_and_b32_e32 v80, 0xffff0000, v80
	v_pk_fma_f32 v[102:103], v[34:35], v[80:81], v[92:93]
	v_pk_add_f32 v[98:99], v[98:99], 1.0 op_sel_hi:[1,0]
	s_nop 0
	v_div_scale_f32 v114, s[2:3], v99, v99, 1.0
	v_rcp_f32_e32 v115, v114
	v_mul_f32_e32 v92, 0xbfb8aa3b, v102
	v_exp_f32_e32 v92, v92
	v_fma_f32 v93, -v114, v115, 1.0
	v_fmac_f32_e32 v115, v93, v115
	v_div_scale_f32 v93, vcc, 1.0, v99, 1.0
	v_mul_f32_e32 v133, v93, v115
	v_fma_f32 v135, -v114, v133, v93
	v_fmac_f32_e32 v133, v135, v115
	v_fma_f32 v93, -v114, v133, v93
	v_div_scale_f32 v114, s[2:3], v98, v98, 1.0
	v_rcp_f32_e32 v135, v114
	v_div_fmas_f32 v93, v93, v115, v133
	v_div_fixup_f32 v99, v93, v99, 1.0
	v_div_scale_f32 v115, vcc, 1.0, v98, 1.0
	v_fma_f32 v93, -v114, v135, 1.0
	v_fmac_f32_e32 v135, v93, v135
	v_mul_f32_e32 v133, v115, v135
	v_fma_f32 v93, -v114, v133, v115
	v_fmac_f32_e32 v133, v93, v135
	v_mul_f32_e32 v93, 0xbfb8aa3b, v103
	v_exp_f32_e32 v93, v93
	v_fma_f32 v114, -v114, v133, v115
	v_div_fmas_f32 v133, v114, v135, v133
	v_div_fixup_f32 v98, v133, v98, 1.0
	v_pk_add_f32 v[114:115], v[92:93], 1.0 op_sel_hi:[1,0]
	v_pk_mul_f32 v[92:93], v[96:97], v[98:99]
	v_div_scale_f32 v135, s[2:3], v115, v115, 1.0
	v_rcp_f32_e32 v137, v135
	v_pk_mul_f32 v[92:93], v[150:151], v[92:93] op_sel_hi:[0,1]
	v_fma_f32 v96, -v135, v137, 1.0
	v_fmac_f32_e32 v137, v96, v137
	v_div_scale_f32 v96, vcc, 1.0, v115, 1.0
	v_mul_f32_e32 v97, v96, v137
	v_fma_f32 v98, -v135, v97, v96
	v_fmac_f32_e32 v97, v98, v137
	v_div_scale_f32 v98, s[2:3], v114, v114, 1.0
	v_rcp_f32_e32 v99, v98
	v_fma_f32 v96, -v135, v97, v96
	v_div_fmas_f32 v96, v96, v137, v97
	v_div_fixup_f32 v97, v96, v115, 1.0
	v_fma_f32 v96, -v98, v99, 1.0
	v_fmac_f32_e32 v99, v96, v99
	v_div_scale_f32 v96, vcc, 1.0, v114, 1.0
	v_mul_f32_e32 v115, v96, v99
	v_fma_f32 v133, -v98, v115, v96
	v_fmac_f32_e32 v115, v133, v99
	v_fma_f32 v96, -v98, v115, v96
	v_div_fmas_f32 v96, v96, v99, v115
	v_pk_fma_f32 v[98:99], v[36:37], v[44:45], v[16:17]
	v_lshlrev_b32_e32 v17, 16, v83
	v_lshlrev_b32_e32 v16, 16, v82
	v_div_fixup_f32 v96, v96, v114, 1.0
	v_pk_fma_f32 v[98:99], v[40:41], v[16:17], v[98:99]
	v_pk_mul_f32 v[96:97], v[102:103], v[96:97]
	v_mul_f32_e32 v102, 0xbfb8aa3b, v98
	v_mul_f32_e32 v103, 0xbfb8aa3b, v99
	v_exp_f32_e32 v102, v102
	v_exp_f32_e32 v103, v103
	v_and_b32_e32 v83, 0xffff0000, v83
	v_and_b32_e32 v82, 0xffff0000, v82
	v_pk_fma_f32 v[94:95], v[10:11], v[82:83], v[94:95]
	v_pk_add_f32 v[102:103], v[102:103], 1.0 op_sel_hi:[1,0]
	v_mul_f32_e32 v114, 0xbfb8aa3b, v94
	v_div_scale_f32 v115, s[2:3], v103, v103, 1.0
	v_rcp_f32_e32 v133, v115
	v_exp_f32_e32 v114, v114
	v_pk_mul_f32 v[96:97], v[150:151], v[96:97] op_sel_hi:[0,1]
	v_pk_fma_f32 v[90:91], v[14:15], v[82:83], v[90:91]
	v_fma_f32 v135, -v115, v133, 1.0
	v_fmac_f32_e32 v133, v135, v133
	v_div_scale_f32 v135, vcc, 1.0, v103, 1.0
	v_mul_f32_e32 v137, v135, v133
	v_fma_f32 v139, -v115, v137, v135
	v_fmac_f32_e32 v137, v139, v133
	v_fma_f32 v115, -v115, v137, v135
	v_div_scale_f32 v135, s[2:3], v102, v102, 1.0
	v_rcp_f32_e32 v139, v135
	v_div_fmas_f32 v115, v115, v133, v137
	v_div_fixup_f32 v103, v115, v103, 1.0
	v_div_scale_f32 v133, vcc, 1.0, v102, 1.0
	v_fma_f32 v115, -v135, v139, 1.0
	v_fmac_f32_e32 v139, v115, v139
	v_mul_f32_e32 v137, v133, v139
	v_fma_f32 v115, -v135, v137, v133
	v_fmac_f32_e32 v137, v115, v139
	v_mul_f32_e32 v115, 0xbfb8aa3b, v95
	v_exp_f32_e32 v115, v115
	v_fma_f32 v133, -v135, v137, v133
	v_div_fmas_f32 v133, v133, v139, v137
	v_div_fixup_f32 v102, v133, v102, 1.0
	v_pk_add_f32 v[114:115], v[114:115], 1.0 op_sel_hi:[1,0]
	v_pk_mul_f32 v[98:99], v[98:99], v[102:103]
	v_div_scale_f32 v135, s[2:3], v115, v115, 1.0
	v_rcp_f32_e32 v137, v135
	v_pk_mul_f32 v[98:99], v[150:151], v[98:99] op_sel_hi:[0,1]
	v_pk_fma_f32 v[44:45], v[28:29], v[44:45], v[4:5]
	v_pk_fma_f32 v[86:87], v[18:19], v[82:83], v[86:87]
	v_fma_f32 v102, -v135, v137, 1.0
	v_fmac_f32_e32 v137, v102, v137
	v_div_scale_f32 v102, vcc, 1.0, v115, 1.0
	v_mul_f32_e32 v103, v102, v137
	v_fma_f32 v133, -v135, v103, v102
	v_fmac_f32_e32 v103, v133, v137
	v_div_scale_f32 v133, s[2:3], v114, v114, 1.0
	v_fma_f32 v102, -v135, v103, v102
	v_rcp_f32_e32 v135, v133
	v_div_fmas_f32 v102, v102, v137, v103
	v_div_fixup_f32 v103, v102, v115, 1.0
	s_or_b32 s2, s6, 5
	v_fma_f32 v102, -v133, v135, 1.0
	v_fmac_f32_e32 v135, v102, v135
	v_div_scale_f32 v102, vcc, 1.0, v114, 1.0
	v_mul_f32_e32 v115, v102, v135
	v_fma_f32 v137, -v133, v115, v102
	v_fmac_f32_e32 v115, v137, v135
	v_fma_f32 v102, -v133, v115, v102
	v_div_fmas_f32 v102, v102, v135, v115
	v_div_fixup_f32 v102, v102, v114, 1.0
	v_pk_mul_f32 v[94:95], v[94:95], v[102:103]
	v_bfe_u32 v114, v97, 16, 1
	v_pk_mul_f32 v[94:95], v[150:151], v[94:95] op_sel_hi:[0,1]
	v_bfe_u32 v102, v95, 16, 1
	v_bfe_u32 v103, v94, 16, 1
	v_bfe_u32 v115, v96, 16, 1
	v_add3_u32 v96, v96, v115, s75
	v_add3_u32 v97, v97, v114, s75
	v_add3_u32 v94, v94, v103, s75
	v_add3_u32 v95, v95, v102, s75
	v_bfe_u32 v102, v92, 16, 1
	v_bfe_u32 v103, v93, 16, 1
	v_bfe_u32 v114, v98, 16, 1
	v_bfe_u32 v115, v99, 16, 1
	v_add3_u32 v99, v99, v115, s75
	v_add3_u32 v98, v98, v114, s75
	v_add3_u32 v93, v93, v103, s75
	v_add3_u32 v92, v92, v102, s75
	s_ashr_i32 s3, s2, 31
	v_lshrrev_b32_e32 v92, 16, v92
	v_lshrrev_b32_e32 v93, 16, v93
	v_lshrrev_b32_e32 v98, 16, v98
	v_lshrrev_b32_e32 v99, 16, v99
	s_lshl_b64 s[2:3], s[2:3], 11
	v_and_or_b32 v95, v95, s16, v99
	v_and_or_b32 v94, v94, s16, v98
	v_and_or_b32 v93, v97, s16, v93
	v_and_or_b32 v92, v96, s16, v92
	v_lshl_add_u64 v[96:97], v[128:129], 0, s[2:3]
	global_store_dwordx4 v[96:97], v[92:95], off sc1
	v_pk_fma_f32 v[44:45], v[32:33], v[16:17], v[44:45]
	v_pk_fma_f32 v[82:83], v[6:7], v[82:83], v[22:23]
	v_pk_fma_f32 v[92:93], v[104:105], v[20:21], v[8:9]
	v_lshlrev_b32_e32 v9, 16, v77
	v_lshlrev_b32_e32 v8, 16, v76
	v_pk_fma_f32 v[94:95], v[100:101], v[8:9], v[92:93]
	s_nop 0
	v_mul_f32_e32 v92, 0xbfb8aa3b, v94
	v_mul_f32_e32 v97, 0xbfb8aa3b, v95
	v_exp_f32_e32 v96, v92
	v_exp_f32_e32 v97, v97
	v_pk_fma_f32 v[92:93], v[30:31], v[112:113], v[46:47]
	s_nop 0
	v_pk_fma_f32 v[92:93], v[38:39], v[84:85], v[92:93]
	v_pk_fma_f32 v[84:85], v[30:31], v[84:85], v[46:47]
	v_pk_fma_f32 v[98:99], v[42:43], v[80:81], v[92:93]
	v_and_b32_e32 v93, 0xffff0000, v77
	v_and_b32_e32 v92, 0xffff0000, v76
	v_pk_add_f32 v[76:77], v[96:97], 1.0 op_sel_hi:[1,0]
	v_pk_fma_f32 v[96:97], v[34:35], v[92:93], v[98:99]
	v_div_scale_f32 v102, s[2:3], v77, v77, 1.0
	v_rcp_f32_e32 v103, v102
	v_mul_f32_e32 v98, 0xbfb8aa3b, v96
	v_exp_f32_e32 v98, v98
	v_pk_fma_f32 v[84:85], v[38:39], v[80:81], v[84:85]
	v_fma_f32 v99, -v102, v103, 1.0
	v_fmac_f32_e32 v103, v99, v103
	v_div_scale_f32 v99, vcc, 1.0, v77, 1.0
	v_mul_f32_e32 v112, v99, v103
	v_fma_f32 v113, -v102, v112, v99
	v_fmac_f32_e32 v112, v113, v103
	v_fma_f32 v99, -v102, v112, v99
	v_div_scale_f32 v102, s[2:3], v76, v76, 1.0
	v_rcp_f32_e32 v113, v102
	v_div_fmas_f32 v99, v99, v103, v112
	v_div_fixup_f32 v77, v99, v77, 1.0
	v_div_scale_f32 v103, vcc, 1.0, v76, 1.0
	v_fma_f32 v99, -v102, v113, 1.0
	v_fmac_f32_e32 v113, v99, v113
	v_mul_f32_e32 v112, v103, v113
	v_fma_f32 v99, -v102, v112, v103
	v_fmac_f32_e32 v112, v99, v113
	v_mul_f32_e32 v99, 0xbfb8aa3b, v97
	v_exp_f32_e32 v99, v99
	v_fma_f32 v102, -v102, v112, v103
	v_div_fmas_f32 v102, v102, v113, v112
	v_div_fixup_f32 v76, v102, v76, 1.0
	v_pk_add_f32 v[98:99], v[98:99], 1.0 op_sel_hi:[1,0]
	v_pk_mul_f32 v[76:77], v[94:95], v[76:77]
	v_div_scale_f32 v103, s[2:3], v99, v99, 1.0
	v_rcp_f32_e32 v112, v103
	v_pk_mul_f32 v[76:77], v[148:149], v[76:77] op_sel_hi:[0,1]
	v_pk_fma_f32 v[84:85], v[42:43], v[92:93], v[84:85]
	v_pk_fma_f32 v[80:81], v[30:31], v[80:81], v[46:47]
	v_fma_f32 v94, -v103, v112, 1.0
	v_fmac_f32_e32 v112, v94, v112
	v_div_scale_f32 v94, vcc, 1.0, v99, 1.0
	v_mul_f32_e32 v95, v94, v112
	v_fma_f32 v102, -v103, v95, v94
	v_fmac_f32_e32 v95, v102, v112
	v_div_scale_f32 v102, s[2:3], v98, v98, 1.0
	v_fma_f32 v94, -v103, v95, v94
	v_rcp_f32_e32 v103, v102
	v_div_fmas_f32 v94, v94, v112, v95
	v_div_fixup_f32 v95, v94, v99, 1.0
	v_pk_fma_f32 v[80:81], v[38:39], v[92:93], v[80:81]
	v_fma_f32 v94, -v102, v103, 1.0
	v_fmac_f32_e32 v103, v94, v103
	v_div_scale_f32 v94, vcc, 1.0, v98, 1.0
	v_mul_f32_e32 v99, v94, v103
	v_fma_f32 v112, -v102, v99, v94
	v_fmac_f32_e32 v99, v112, v103
	v_fma_f32 v94, -v102, v99, v94
	v_div_fmas_f32 v94, v94, v103, v99
	v_div_fixup_f32 v94, v94, v98, 1.0
	v_pk_mul_f32 v[94:95], v[96:97], v[94:95]
	v_pk_fma_f32 v[96:97], v[36:37], v[16:17], v[12:13]
	v_lshlrev_b32_e32 v13, 16, v79
	v_lshlrev_b32_e32 v12, 16, v78
	v_pk_fma_f32 v[96:97], v[40:41], v[12:13], v[96:97]
	v_and_b32_e32 v79, 0xffff0000, v79
	v_mul_f32_e32 v98, 0xbfb8aa3b, v96
	v_mul_f32_e32 v99, 0xbfb8aa3b, v97
	v_exp_f32_e32 v98, v98
	v_exp_f32_e32 v99, v99
	v_and_b32_e32 v78, 0xffff0000, v78
	v_pk_fma_f32 v[90:91], v[10:11], v[78:79], v[90:91]
	v_pk_mul_f32 v[94:95], v[148:149], v[94:95] op_sel_hi:[0,1]
	v_pk_add_f32 v[98:99], v[98:99], 1.0 op_sel_hi:[1,0]
	v_mul_f32_e32 v102, 0xbfb8aa3b, v90
	v_div_scale_f32 v103, s[2:3], v99, v99, 1.0
	v_rcp_f32_e32 v112, v103
	v_exp_f32_e32 v102, v102
	v_pk_fma_f32 v[86:87], v[14:15], v[78:79], v[86:87]
	v_pk_fma_f32 v[16:17], v[28:29], v[16:17], v[4:5]
	v_fma_f32 v113, -v103, v112, 1.0
	v_fmac_f32_e32 v112, v113, v112
	v_div_scale_f32 v113, vcc, 1.0, v99, 1.0
	v_mul_f32_e32 v114, v113, v112
	v_fma_f32 v115, -v103, v114, v113
	v_fmac_f32_e32 v114, v115, v112
	v_fma_f32 v103, -v103, v114, v113
	v_div_scale_f32 v113, s[2:3], v98, v98, 1.0
	v_rcp_f32_e32 v115, v113
	v_div_fmas_f32 v103, v103, v112, v114
	v_div_fixup_f32 v99, v103, v99, 1.0
	v_div_scale_f32 v112, vcc, 1.0, v98, 1.0
	v_fma_f32 v103, -v113, v115, 1.0
	v_fmac_f32_e32 v115, v103, v115
	v_mul_f32_e32 v114, v112, v115
	v_fma_f32 v103, -v113, v114, v112
	v_fmac_f32_e32 v114, v103, v115
	v_mul_f32_e32 v103, 0xbfb8aa3b, v91
	v_exp_f32_e32 v103, v103
	v_fma_f32 v112, -v113, v114, v112
	v_div_fmas_f32 v112, v112, v115, v114
	v_div_fixup_f32 v98, v112, v98, 1.0
	v_pk_add_f32 v[102:103], v[102:103], 1.0 op_sel_hi:[1,0]
	v_pk_mul_f32 v[96:97], v[96:97], v[98:99]
	v_div_scale_f32 v113, s[2:3], v103, v103, 1.0
	v_rcp_f32_e32 v114, v113
	v_pk_mul_f32 v[96:97], v[148:149], v[96:97] op_sel_hi:[0,1]
	v_pk_fma_f32 v[16:17], v[32:33], v[12:13], v[16:17]
	v_pk_fma_f32 v[82:83], v[18:19], v[78:79], v[82:83]
	v_fma_f32 v98, -v113, v114, 1.0
	v_fmac_f32_e32 v114, v98, v114
	v_div_scale_f32 v98, vcc, 1.0, v103, 1.0
	v_mul_f32_e32 v99, v98, v114
	v_fma_f32 v112, -v113, v99, v98
	v_fmac_f32_e32 v99, v112, v114
	v_div_scale_f32 v112, s[2:3], v102, v102, 1.0
	v_fma_f32 v98, -v113, v99, v98
	v_rcp_f32_e32 v113, v112
	v_div_fmas_f32 v98, v98, v114, v99
	v_div_fixup_f32 v99, v98, v103, 1.0
	s_or_b32 s2, s6, 6
	v_fma_f32 v98, -v112, v113, 1.0
	v_fmac_f32_e32 v113, v98, v113
	v_div_scale_f32 v98, vcc, 1.0, v102, 1.0
	v_mul_f32_e32 v103, v98, v113
	v_fma_f32 v114, -v112, v103, v98
	v_fmac_f32_e32 v103, v114, v113
	v_fma_f32 v98, -v112, v103, v98
	v_div_fmas_f32 v98, v98, v113, v103
	v_div_fixup_f32 v98, v98, v102, 1.0
	v_pk_mul_f32 v[90:91], v[90:91], v[98:99]
	v_bfe_u32 v102, v95, 16, 1
	v_pk_mul_f32 v[90:91], v[148:149], v[90:91] op_sel_hi:[0,1]
	v_bfe_u32 v98, v91, 16, 1
	v_bfe_u32 v99, v90, 16, 1
	v_bfe_u32 v103, v94, 16, 1
	v_add3_u32 v94, v94, v103, s75
	v_add3_u32 v95, v95, v102, s75
	v_add3_u32 v90, v90, v99, s75
	v_add3_u32 v91, v91, v98, s75
	v_bfe_u32 v98, v76, 16, 1
	v_bfe_u32 v99, v77, 16, 1
	v_bfe_u32 v102, v96, 16, 1
	v_bfe_u32 v103, v97, 16, 1
	v_add3_u32 v97, v97, v103, s75
	v_add3_u32 v96, v96, v102, s75
	v_add3_u32 v77, v77, v99, s75
	v_add3_u32 v76, v76, v98, s75
	s_ashr_i32 s3, s2, 31
	v_lshrrev_b32_e32 v76, 16, v76
	v_lshrrev_b32_e32 v77, 16, v77
	v_lshrrev_b32_e32 v96, 16, v96
	v_lshrrev_b32_e32 v97, 16, v97
	s_lshl_b64 s[2:3], s[2:3], 11
	v_and_or_b32 v97, v91, s16, v97
	v_and_or_b32 v96, v90, s16, v96
	v_and_or_b32 v95, v95, s16, v77
	v_and_or_b32 v94, v94, s16, v76
	v_lshl_add_u64 v[76:77], v[128:129], 0, s[2:3]
	global_store_dwordx4 v[76:77], v[94:97], off sc1
	v_pk_fma_f32 v[76:77], v[106:107], v[88:89], v[108:109]
	v_pk_fma_f32 v[78:79], v[6:7], v[78:79], v[22:23]
	v_pk_fma_f32 v[76:77], v[110:111], v[20:21], v[76:77]
	v_pk_fma_f32 v[20:21], v[106:107], v[20:21], v[108:109]
	v_pk_fma_f32 v[88:89], v[104:105], v[8:9], v[76:77]
	v_lshlrev_b32_e32 v77, 16, v73
	v_lshlrev_b32_e32 v76, 16, v72
	v_pk_fma_f32 v[88:89], v[100:101], v[76:77], v[88:89]
	v_and_b32_e32 v73, 0xffff0000, v73
	v_mul_f32_e32 v90, 0xbfb8aa3b, v88
	v_mul_f32_e32 v91, 0xbfb8aa3b, v89
	v_exp_f32_e32 v90, v90
	v_exp_f32_e32 v91, v91
	v_and_b32_e32 v72, 0xffff0000, v72
	v_pk_fma_f32 v[94:95], v[34:35], v[72:73], v[84:85]
	v_pk_fma_f32 v[20:21], v[110:111], v[8:9], v[20:21]
	v_pk_add_f32 v[90:91], v[90:91], 1.0 op_sel_hi:[1,0]
	v_mul_f32_e32 v84, 0xbfb8aa3b, v94
	v_div_scale_f32 v96, s[2:3], v91, v91, 1.0
	v_rcp_f32_e32 v97, v96
	v_exp_f32_e32 v84, v84
	v_pk_fma_f32 v[80:81], v[42:43], v[72:73], v[80:81]
	v_pk_fma_f32 v[8:9], v[106:107], v[8:9], v[108:109]
	v_fma_f32 v85, -v96, v97, 1.0
	v_fmac_f32_e32 v97, v85, v97
	v_div_scale_f32 v85, vcc, 1.0, v91, 1.0
	v_mul_f32_e32 v98, v85, v97
	v_fma_f32 v99, -v96, v98, v85
	v_fmac_f32_e32 v98, v99, v97
	v_fma_f32 v85, -v96, v98, v85
	v_div_scale_f32 v96, s[2:3], v90, v90, 1.0
	v_rcp_f32_e32 v99, v96
	v_div_fmas_f32 v85, v85, v97, v98
	v_div_fixup_f32 v91, v85, v91, 1.0
	v_div_scale_f32 v97, vcc, 1.0, v90, 1.0
	v_fma_f32 v85, -v96, v99, 1.0
	v_fmac_f32_e32 v99, v85, v99
	v_mul_f32_e32 v98, v97, v99
	v_fma_f32 v85, -v96, v98, v97
	v_fmac_f32_e32 v98, v85, v99
	v_mul_f32_e32 v85, 0xbfb8aa3b, v95
	v_exp_f32_e32 v85, v85
	v_fma_f32 v96, -v96, v98, v97
	v_div_fmas_f32 v98, v96, v99, v98
	v_div_fixup_f32 v90, v98, v90, 1.0
	v_pk_add_f32 v[96:97], v[84:85], 1.0 op_sel_hi:[1,0]
	v_pk_mul_f32 v[84:85], v[88:89], v[90:91]
	v_div_scale_f32 v99, s[2:3], v97, v97, 1.0
	v_rcp_f32_e32 v102, v99
	v_pk_mul_f32 v[84:85], v[146:147], v[84:85] op_sel_hi:[0,1]
	v_pk_fma_f32 v[8:9], v[110:111], v[76:77], v[8:9]
	v_fma_f32 v88, -v99, v102, 1.0
	v_fmac_f32_e32 v102, v88, v102
	v_div_scale_f32 v88, vcc, 1.0, v97, 1.0
	v_mul_f32_e32 v89, v88, v102
	v_fma_f32 v90, -v99, v89, v88
	v_fmac_f32_e32 v89, v90, v102
	v_div_scale_f32 v90, s[2:3], v96, v96, 1.0
	v_rcp_f32_e32 v91, v90
	v_fma_f32 v88, -v99, v89, v88
	v_div_fmas_f32 v88, v88, v102, v89
	v_div_fixup_f32 v89, v88, v97, 1.0
	v_fma_f32 v88, -v90, v91, 1.0
	v_fmac_f32_e32 v91, v88, v91
	v_div_scale_f32 v88, vcc, 1.0, v96, 1.0
	v_mul_f32_e32 v97, v88, v91
	v_fma_f32 v98, -v90, v97, v88
	v_fmac_f32_e32 v97, v98, v91
	v_fma_f32 v88, -v90, v97, v88
	v_div_fmas_f32 v88, v88, v91, v97
	v_pk_fma_f32 v[90:91], v[36:37], v[12:13], v[44:45]
	v_lshlrev_b32_e32 v45, 16, v75
	v_lshlrev_b32_e32 v44, 16, v74
	v_div_fixup_f32 v88, v88, v96, 1.0
	v_pk_fma_f32 v[90:91], v[40:41], v[44:45], v[90:91]
	v_pk_mul_f32 v[88:89], v[94:95], v[88:89]
	v_mul_f32_e32 v94, 0xbfb8aa3b, v90
	v_mul_f32_e32 v95, 0xbfb8aa3b, v91
	v_exp_f32_e32 v94, v94
	v_exp_f32_e32 v95, v95
	v_and_b32_e32 v75, 0xffff0000, v75
	v_and_b32_e32 v74, 0xffff0000, v74
	v_pk_fma_f32 v[86:87], v[10:11], v[74:75], v[86:87]
	v_pk_add_f32 v[94:95], v[94:95], 1.0 op_sel_hi:[1,0]
	v_mul_f32_e32 v96, 0xbfb8aa3b, v86
	v_div_scale_f32 v97, s[2:3], v95, v95, 1.0
	v_rcp_f32_e32 v98, v97
	v_exp_f32_e32 v96, v96
	v_pk_mul_f32 v[88:89], v[146:147], v[88:89] op_sel_hi:[0,1]
	v_pk_fma_f32 v[82:83], v[14:15], v[74:75], v[82:83]
	v_fma_f32 v99, -v97, v98, 1.0
	v_fmac_f32_e32 v98, v99, v98
	v_div_scale_f32 v99, vcc, 1.0, v95, 1.0
	v_mul_f32_e32 v102, v99, v98
	v_fma_f32 v103, -v97, v102, v99
	v_fmac_f32_e32 v102, v103, v98
	v_fma_f32 v97, -v97, v102, v99
	v_div_scale_f32 v99, s[2:3], v94, v94, 1.0
	v_rcp_f32_e32 v103, v99
	v_div_fmas_f32 v97, v97, v98, v102
	v_div_fixup_f32 v95, v97, v95, 1.0
	v_div_scale_f32 v98, vcc, 1.0, v94, 1.0
	v_fma_f32 v97, -v99, v103, 1.0
	v_fmac_f32_e32 v103, v97, v103
	v_mul_f32_e32 v102, v98, v103
	v_fma_f32 v97, -v99, v102, v98
	v_fmac_f32_e32 v102, v97, v103
	v_mul_f32_e32 v97, 0xbfb8aa3b, v87
	v_exp_f32_e32 v97, v97
	v_fma_f32 v98, -v99, v102, v98
	v_div_fmas_f32 v98, v98, v103, v102
	v_div_fixup_f32 v94, v98, v94, 1.0
	v_pk_add_f32 v[96:97], v[96:97], 1.0 op_sel_hi:[1,0]
	v_pk_mul_f32 v[90:91], v[90:91], v[94:95]
	v_div_scale_f32 v99, s[2:3], v97, v97, 1.0
	v_rcp_f32_e32 v102, v99
	v_pk_mul_f32 v[90:91], v[146:147], v[90:91] op_sel_hi:[0,1]
	v_pk_fma_f32 v[12:13], v[28:29], v[12:13], v[4:5]
	v_pk_fma_f32 v[78:79], v[18:19], v[74:75], v[78:79]
	v_fma_f32 v94, -v99, v102, 1.0
	v_fmac_f32_e32 v102, v94, v102
	v_div_scale_f32 v94, vcc, 1.0, v97, 1.0
	v_mul_f32_e32 v95, v94, v102
	v_fma_f32 v98, -v99, v95, v94
	v_fmac_f32_e32 v95, v98, v102
	v_div_scale_f32 v98, s[2:3], v96, v96, 1.0
	v_fma_f32 v94, -v99, v95, v94
	v_rcp_f32_e32 v99, v98
	v_div_fmas_f32 v94, v94, v102, v95
	v_div_fixup_f32 v95, v94, v97, 1.0
	s_or_b32 s2, s6, 7
	v_fma_f32 v94, -v98, v99, 1.0
	v_fmac_f32_e32 v99, v94, v99
	v_div_scale_f32 v94, vcc, 1.0, v96, 1.0
	v_mul_f32_e32 v97, v94, v99
	v_fma_f32 v102, -v98, v97, v94
	v_fmac_f32_e32 v97, v102, v99
	v_fma_f32 v94, -v98, v97, v94
	v_div_fmas_f32 v94, v94, v99, v97
	v_div_fixup_f32 v94, v94, v96, 1.0
	v_pk_mul_f32 v[86:87], v[86:87], v[94:95]
	v_bfe_u32 v96, v89, 16, 1
	v_pk_mul_f32 v[86:87], v[146:147], v[86:87] op_sel_hi:[0,1]
	v_bfe_u32 v94, v87, 16, 1
	v_bfe_u32 v95, v86, 16, 1
	v_bfe_u32 v97, v88, 16, 1
	v_add3_u32 v88, v88, v97, s75
	v_add3_u32 v89, v89, v96, s75
	v_add3_u32 v86, v86, v95, s75
	v_add3_u32 v87, v87, v94, s75
	v_bfe_u32 v94, v84, 16, 1
	v_bfe_u32 v95, v85, 16, 1
	v_bfe_u32 v96, v90, 16, 1
	v_bfe_u32 v97, v91, 16, 1
	v_add3_u32 v91, v91, v97, s75
	v_add3_u32 v90, v90, v96, s75
	v_add3_u32 v85, v85, v95, s75
	v_add3_u32 v84, v84, v94, s75
	s_ashr_i32 s3, s2, 31
	v_lshrrev_b32_e32 v84, 16, v84
	v_lshrrev_b32_e32 v85, 16, v85
	v_lshrrev_b32_e32 v90, 16, v90
	v_lshrrev_b32_e32 v91, 16, v91
	s_lshl_b64 s[2:3], s[2:3], 11
	v_and_or_b32 v87, v87, s16, v91
	v_and_or_b32 v86, v86, s16, v90
	v_and_or_b32 v85, v89, s16, v85
	v_and_or_b32 v84, v88, s16, v84
	v_lshl_add_u64 v[88:89], v[128:129], 0, s[2:3]
	global_store_dwordx4 v[88:89], v[84:87], off sc1
	v_pk_fma_f32 v[12:13], v[32:33], v[44:45], v[12:13]
	v_pk_fma_f32 v[74:75], v[6:7], v[74:75], v[22:23]
	v_pk_fma_f32 v[84:85], v[104:105], v[76:77], v[20:21]
	v_lshlrev_b32_e32 v21, 16, v69
	v_lshlrev_b32_e32 v20, 16, v68
	v_pk_fma_f32 v[84:85], v[100:101], v[20:21], v[84:85]
	v_and_b32_e32 v69, 0xffff0000, v69
	v_mul_f32_e32 v86, 0xbfb8aa3b, v84
	v_mul_f32_e32 v87, 0xbfb8aa3b, v85
	v_exp_f32_e32 v86, v86
	v_exp_f32_e32 v87, v87
	v_and_b32_e32 v68, 0xffff0000, v68
	v_pk_fma_f32 v[88:89], v[34:35], v[68:69], v[80:81]
	v_pk_add_f32 v[86:87], v[86:87], 1.0 op_sel_hi:[1,0]
	s_nop 0
	v_div_scale_f32 v90, s[2:3], v87, v87, 1.0
	v_rcp_f32_e32 v91, v90
	v_mul_f32_e32 v80, 0xbfb8aa3b, v88
	v_exp_f32_e32 v80, v80
	v_fma_f32 v81, -v90, v91, 1.0
	v_fmac_f32_e32 v91, v81, v91
	v_div_scale_f32 v81, vcc, 1.0, v87, 1.0
	v_mul_f32_e32 v94, v81, v91
	v_fma_f32 v95, -v90, v94, v81
	v_fmac_f32_e32 v94, v95, v91
	v_fma_f32 v81, -v90, v94, v81
	v_div_scale_f32 v90, s[2:3], v86, v86, 1.0
	v_rcp_f32_e32 v95, v90
	v_div_fmas_f32 v81, v81, v91, v94
	v_div_fixup_f32 v87, v81, v87, 1.0
	v_div_scale_f32 v91, vcc, 1.0, v86, 1.0
	v_fma_f32 v81, -v90, v95, 1.0
	v_fmac_f32_e32 v95, v81, v95
	v_mul_f32_e32 v94, v91, v95
	v_fma_f32 v81, -v90, v94, v91
	v_fmac_f32_e32 v94, v81, v95
	v_mul_f32_e32 v81, 0xbfb8aa3b, v89
	v_exp_f32_e32 v81, v81
	v_fma_f32 v90, -v90, v94, v91
	v_div_fmas_f32 v94, v90, v95, v94
	v_div_fixup_f32 v86, v94, v86, 1.0
	v_pk_add_f32 v[90:91], v[80:81], 1.0 op_sel_hi:[1,0]
	v_pk_mul_f32 v[80:81], v[84:85], v[86:87]
	v_div_scale_f32 v95, s[2:3], v91, v91, 1.0
	v_rcp_f32_e32 v96, v95
	v_pk_mul_f32 v[80:81], v[144:145], v[80:81] op_sel_hi:[0,1]
	v_fma_f32 v84, -v95, v96, 1.0
	v_fmac_f32_e32 v96, v84, v96
	v_div_scale_f32 v84, vcc, 1.0, v91, 1.0
	v_mul_f32_e32 v85, v84, v96
	v_fma_f32 v86, -v95, v85, v84
	v_fmac_f32_e32 v85, v86, v96
	v_div_scale_f32 v86, s[2:3], v90, v90, 1.0
	v_rcp_f32_e32 v87, v86
	v_fma_f32 v84, -v95, v85, v84
	v_div_fmas_f32 v84, v84, v96, v85
	v_div_fixup_f32 v85, v84, v91, 1.0
	v_fma_f32 v84, -v86, v87, 1.0
	v_fmac_f32_e32 v87, v84, v87
	v_div_scale_f32 v84, vcc, 1.0, v90, 1.0
	v_mul_f32_e32 v91, v84, v87
	v_fma_f32 v94, -v86, v91, v84
	v_fmac_f32_e32 v91, v94, v87
	v_fma_f32 v84, -v86, v91, v84
	v_div_fmas_f32 v84, v84, v87, v91
	v_pk_fma_f32 v[86:87], v[36:37], v[44:45], v[16:17]
	v_lshlrev_b32_e32 v17, 16, v71
	v_lshlrev_b32_e32 v16, 16, v70
	v_div_fixup_f32 v84, v84, v90, 1.0
	v_pk_fma_f32 v[86:87], v[40:41], v[16:17], v[86:87]
	v_pk_mul_f32 v[84:85], v[88:89], v[84:85]
	v_mul_f32_e32 v88, 0xbfb8aa3b, v86
	v_mul_f32_e32 v89, 0xbfb8aa3b, v87
	v_exp_f32_e32 v88, v88
	v_exp_f32_e32 v89, v89
	v_and_b32_e32 v71, 0xffff0000, v71
	v_and_b32_e32 v70, 0xffff0000, v70
	v_pk_fma_f32 v[82:83], v[10:11], v[70:71], v[82:83]
	v_pk_add_f32 v[88:89], v[88:89], 1.0 op_sel_hi:[1,0]
	v_mul_f32_e32 v90, 0xbfb8aa3b, v82
	v_div_scale_f32 v91, s[2:3], v89, v89, 1.0
	v_rcp_f32_e32 v94, v91
	v_exp_f32_e32 v90, v90
	v_pk_mul_f32 v[84:85], v[144:145], v[84:85] op_sel_hi:[0,1]
	v_pk_fma_f32 v[78:79], v[14:15], v[70:71], v[78:79]
	v_fma_f32 v95, -v91, v94, 1.0
	v_fmac_f32_e32 v94, v95, v94
	v_div_scale_f32 v95, vcc, 1.0, v89, 1.0
	v_mul_f32_e32 v96, v95, v94
	v_fma_f32 v97, -v91, v96, v95
	v_fmac_f32_e32 v96, v97, v94
	v_fma_f32 v91, -v91, v96, v95
	v_div_scale_f32 v95, s[2:3], v88, v88, 1.0
	v_rcp_f32_e32 v97, v95
	v_div_fmas_f32 v91, v91, v94, v96
	v_div_fixup_f32 v89, v91, v89, 1.0
	v_div_scale_f32 v94, vcc, 1.0, v88, 1.0
	v_fma_f32 v91, -v95, v97, 1.0
	v_fmac_f32_e32 v97, v91, v97
	v_mul_f32_e32 v96, v94, v97
	v_fma_f32 v91, -v95, v96, v94
	v_fmac_f32_e32 v96, v91, v97
	v_mul_f32_e32 v91, 0xbfb8aa3b, v83
	v_exp_f32_e32 v91, v91
	v_fma_f32 v94, -v95, v96, v94
	v_div_fmas_f32 v94, v94, v97, v96
	v_div_fixup_f32 v88, v94, v88, 1.0
	v_pk_add_f32 v[90:91], v[90:91], 1.0 op_sel_hi:[1,0]
	v_pk_mul_f32 v[86:87], v[86:87], v[88:89]
	v_div_scale_f32 v95, s[2:3], v91, v91, 1.0
	v_rcp_f32_e32 v96, v95
	v_pk_mul_f32 v[86:87], v[144:145], v[86:87] op_sel_hi:[0,1]
	v_pk_fma_f32 v[44:45], v[28:29], v[44:45], v[4:5]
	v_pk_fma_f32 v[74:75], v[18:19], v[70:71], v[74:75]
	v_fma_f32 v88, -v95, v96, 1.0
	v_fmac_f32_e32 v96, v88, v96
	v_div_scale_f32 v88, vcc, 1.0, v91, 1.0
	v_mul_f32_e32 v89, v88, v96
	v_fma_f32 v94, -v95, v89, v88
	v_fmac_f32_e32 v89, v94, v96
	v_div_scale_f32 v94, s[2:3], v90, v90, 1.0
	v_fma_f32 v88, -v95, v89, v88
	v_rcp_f32_e32 v95, v94
	v_div_fmas_f32 v88, v88, v96, v89
	v_div_fixup_f32 v89, v88, v91, 1.0
	s_or_b32 s2, s14, 8
	v_fma_f32 v88, -v94, v95, 1.0
	v_fmac_f32_e32 v95, v88, v95
	v_div_scale_f32 v88, vcc, 1.0, v90, 1.0
	v_mul_f32_e32 v91, v88, v95
	v_fma_f32 v96, -v94, v91, v88
	v_fmac_f32_e32 v91, v96, v95
	v_fma_f32 v88, -v94, v91, v88
	v_div_fmas_f32 v88, v88, v95, v91
	v_div_fixup_f32 v88, v88, v90, 1.0
	v_pk_mul_f32 v[82:83], v[82:83], v[88:89]
	v_bfe_u32 v90, v85, 16, 1
	v_pk_mul_f32 v[82:83], v[144:145], v[82:83] op_sel_hi:[0,1]
	v_bfe_u32 v88, v83, 16, 1
	v_bfe_u32 v89, v82, 16, 1
	v_bfe_u32 v91, v84, 16, 1
	v_add3_u32 v84, v84, v91, s75
	v_add3_u32 v85, v85, v90, s75
	v_add3_u32 v82, v82, v89, s75
	v_add3_u32 v83, v83, v88, s75
	v_bfe_u32 v88, v80, 16, 1
	v_bfe_u32 v89, v81, 16, 1
	v_bfe_u32 v90, v86, 16, 1
	v_bfe_u32 v91, v87, 16, 1
	v_add3_u32 v87, v87, v91, s75
	v_add3_u32 v86, v86, v90, s75
	v_add3_u32 v81, v81, v89, s75
	v_add3_u32 v80, v80, v88, s75
	s_ashr_i32 s3, s2, 31
	v_lshrrev_b32_e32 v80, 16, v80
	v_lshrrev_b32_e32 v81, 16, v81
	v_lshrrev_b32_e32 v86, 16, v86
	v_lshrrev_b32_e32 v87, 16, v87
	s_lshl_b64 s[2:3], s[2:3], 11
	v_and_or_b32 v83, v83, s16, v87
	v_and_or_b32 v82, v82, s16, v86
	v_and_or_b32 v81, v85, s16, v81
	v_and_or_b32 v80, v84, s16, v80
	v_lshl_add_u64 v[84:85], v[128:129], 0, s[2:3]
	global_store_dwordx4 v[84:85], v[80:83], off sc1
	v_pk_fma_f32 v[44:45], v[32:33], v[16:17], v[44:45]
	v_pk_fma_f32 v[70:71], v[6:7], v[70:71], v[22:23]
	v_pk_fma_f32 v[80:81], v[104:105], v[20:21], v[8:9]
	v_lshlrev_b32_e32 v9, 16, v65
	v_lshlrev_b32_e32 v8, 16, v64
	v_pk_fma_f32 v[82:83], v[100:101], v[8:9], v[80:81]
	s_nop 0
	v_mul_f32_e32 v80, 0xbfb8aa3b, v82
	v_mul_f32_e32 v85, 0xbfb8aa3b, v83
	v_exp_f32_e32 v84, v80
	v_exp_f32_e32 v85, v85
	v_pk_fma_f32 v[80:81], v[30:31], v[92:93], v[46:47]
	s_nop 0
	v_pk_fma_f32 v[80:81], v[38:39], v[72:73], v[80:81]
	v_pk_fma_f32 v[72:73], v[30:31], v[72:73], v[46:47]
	v_pk_fma_f32 v[86:87], v[42:43], v[68:69], v[80:81]
	v_and_b32_e32 v81, 0xffff0000, v65
	v_and_b32_e32 v80, 0xffff0000, v64
	v_pk_add_f32 v[64:65], v[84:85], 1.0 op_sel_hi:[1,0]
	v_pk_fma_f32 v[84:85], v[34:35], v[80:81], v[86:87]
	v_div_scale_f32 v88, s[2:3], v65, v65, 1.0
	v_rcp_f32_e32 v89, v88
	v_mul_f32_e32 v86, 0xbfb8aa3b, v84
	v_exp_f32_e32 v86, v86
	v_pk_fma_f32 v[72:73], v[38:39], v[68:69], v[72:73]
	v_fma_f32 v87, -v88, v89, 1.0
	v_fmac_f32_e32 v89, v87, v89
	v_div_scale_f32 v87, vcc, 1.0, v65, 1.0
	v_mul_f32_e32 v90, v87, v89
	v_fma_f32 v91, -v88, v90, v87
	v_fmac_f32_e32 v90, v91, v89
	v_fma_f32 v87, -v88, v90, v87
	v_div_scale_f32 v88, s[2:3], v64, v64, 1.0
	v_rcp_f32_e32 v91, v88
	v_div_fmas_f32 v87, v87, v89, v90
	v_div_fixup_f32 v65, v87, v65, 1.0
	v_div_scale_f32 v89, vcc, 1.0, v64, 1.0
	v_fma_f32 v87, -v88, v91, 1.0
	v_fmac_f32_e32 v91, v87, v91
	v_mul_f32_e32 v90, v89, v91
	v_fma_f32 v87, -v88, v90, v89
	v_fmac_f32_e32 v90, v87, v91
	v_mul_f32_e32 v87, 0xbfb8aa3b, v85
	v_exp_f32_e32 v87, v87
	v_fma_f32 v88, -v88, v90, v89
	v_div_fmas_f32 v88, v88, v91, v90
	v_div_fixup_f32 v64, v88, v64, 1.0
	v_pk_add_f32 v[86:87], v[86:87], 1.0 op_sel_hi:[1,0]
	v_pk_mul_f32 v[64:65], v[82:83], v[64:65]
	v_div_scale_f32 v89, s[2:3], v87, v87, 1.0
	v_rcp_f32_e32 v90, v89
	v_pk_mul_f32 v[64:65], v[142:143], v[64:65] op_sel_hi:[0,1]
	v_pk_fma_f32 v[72:73], v[42:43], v[80:81], v[72:73]
	v_pk_fma_f32 v[68:69], v[30:31], v[68:69], v[46:47]
	v_fma_f32 v82, -v89, v90, 1.0
	v_fmac_f32_e32 v90, v82, v90
	v_div_scale_f32 v82, vcc, 1.0, v87, 1.0
	v_mul_f32_e32 v83, v82, v90
	v_fma_f32 v88, -v89, v83, v82
	v_fmac_f32_e32 v83, v88, v90
	v_div_scale_f32 v88, s[2:3], v86, v86, 1.0
	v_fma_f32 v82, -v89, v83, v82
	v_rcp_f32_e32 v89, v88
	v_div_fmas_f32 v82, v82, v90, v83
	v_div_fixup_f32 v83, v82, v87, 1.0
	v_pk_fma_f32 v[68:69], v[38:39], v[80:81], v[68:69]
	v_fma_f32 v82, -v88, v89, 1.0
	v_fmac_f32_e32 v89, v82, v89
	v_div_scale_f32 v82, vcc, 1.0, v86, 1.0
	v_mul_f32_e32 v87, v82, v89
	v_fma_f32 v90, -v88, v87, v82
	v_fmac_f32_e32 v87, v90, v89
	v_fma_f32 v82, -v88, v87, v82
	v_div_fmas_f32 v82, v82, v89, v87
	v_div_fixup_f32 v82, v82, v86, 1.0
	v_pk_mul_f32 v[82:83], v[84:85], v[82:83]
	v_pk_fma_f32 v[84:85], v[36:37], v[16:17], v[12:13]
	v_lshlrev_b32_e32 v13, 16, v67
	v_lshlrev_b32_e32 v12, 16, v66
	v_pk_fma_f32 v[84:85], v[40:41], v[12:13], v[84:85]
	v_and_b32_e32 v67, 0xffff0000, v67
	v_mul_f32_e32 v86, 0xbfb8aa3b, v84
	v_mul_f32_e32 v87, 0xbfb8aa3b, v85
	v_exp_f32_e32 v86, v86
	v_exp_f32_e32 v87, v87
	v_and_b32_e32 v66, 0xffff0000, v66
	v_pk_fma_f32 v[78:79], v[10:11], v[66:67], v[78:79]
	v_pk_mul_f32 v[82:83], v[142:143], v[82:83] op_sel_hi:[0,1]
	v_pk_add_f32 v[86:87], v[86:87], 1.0 op_sel_hi:[1,0]
	v_mul_f32_e32 v88, 0xbfb8aa3b, v78
	v_div_scale_f32 v89, s[2:3], v87, v87, 1.0
	v_rcp_f32_e32 v90, v89
	v_exp_f32_e32 v88, v88
	v_pk_fma_f32 v[74:75], v[14:15], v[66:67], v[74:75]
	v_pk_fma_f32 v[16:17], v[28:29], v[16:17], v[4:5]
	v_fma_f32 v91, -v89, v90, 1.0
	v_fmac_f32_e32 v90, v91, v90
	v_div_scale_f32 v91, vcc, 1.0, v87, 1.0
	v_mul_f32_e32 v92, v91, v90
	v_fma_f32 v93, -v89, v92, v91
	v_fmac_f32_e32 v92, v93, v90
	v_fma_f32 v89, -v89, v92, v91
	v_div_scale_f32 v91, s[2:3], v86, v86, 1.0
	v_rcp_f32_e32 v93, v91
	v_div_fmas_f32 v89, v89, v90, v92
	v_div_fixup_f32 v87, v89, v87, 1.0
	v_div_scale_f32 v90, vcc, 1.0, v86, 1.0
	v_fma_f32 v89, -v91, v93, 1.0
	v_fmac_f32_e32 v93, v89, v93
	v_mul_f32_e32 v92, v90, v93
	v_fma_f32 v89, -v91, v92, v90
	v_fmac_f32_e32 v92, v89, v93
	v_mul_f32_e32 v89, 0xbfb8aa3b, v79
	v_exp_f32_e32 v89, v89
	v_fma_f32 v90, -v91, v92, v90
	v_div_fmas_f32 v90, v90, v93, v92
	v_div_fixup_f32 v86, v90, v86, 1.0
	v_pk_add_f32 v[88:89], v[88:89], 1.0 op_sel_hi:[1,0]
	v_pk_mul_f32 v[84:85], v[84:85], v[86:87]
	v_div_scale_f32 v91, s[2:3], v89, v89, 1.0
	v_rcp_f32_e32 v92, v91
	v_pk_mul_f32 v[84:85], v[142:143], v[84:85] op_sel_hi:[0,1]
	v_pk_fma_f32 v[16:17], v[32:33], v[12:13], v[16:17]
	v_pk_fma_f32 v[70:71], v[18:19], v[66:67], v[70:71]
	v_fma_f32 v86, -v91, v92, 1.0
	v_fmac_f32_e32 v92, v86, v92
	v_div_scale_f32 v86, vcc, 1.0, v89, 1.0
	v_mul_f32_e32 v87, v86, v92
	v_fma_f32 v90, -v91, v87, v86
	v_fmac_f32_e32 v87, v90, v92
	v_div_scale_f32 v90, s[2:3], v88, v88, 1.0
	v_fma_f32 v86, -v91, v87, v86
	v_rcp_f32_e32 v91, v90
	v_div_fmas_f32 v86, v86, v92, v87
	v_div_fixup_f32 v87, v86, v89, 1.0
	s_or_b32 s2, s14, 9
	v_fma_f32 v86, -v90, v91, 1.0
	v_fmac_f32_e32 v91, v86, v91
	v_div_scale_f32 v86, vcc, 1.0, v88, 1.0
	v_mul_f32_e32 v89, v86, v91
	v_fma_f32 v92, -v90, v89, v86
	v_fmac_f32_e32 v89, v92, v91
	v_fma_f32 v86, -v90, v89, v86
	v_div_fmas_f32 v86, v86, v91, v89
	v_div_fixup_f32 v86, v86, v88, 1.0
	v_pk_mul_f32 v[78:79], v[78:79], v[86:87]
	v_bfe_u32 v88, v83, 16, 1
	v_pk_mul_f32 v[78:79], v[142:143], v[78:79] op_sel_hi:[0,1]
	v_bfe_u32 v86, v79, 16, 1
	v_bfe_u32 v87, v78, 16, 1
	v_bfe_u32 v89, v82, 16, 1
	v_add3_u32 v82, v82, v89, s75
	v_add3_u32 v83, v83, v88, s75
	v_add3_u32 v78, v78, v87, s75
	v_add3_u32 v79, v79, v86, s75
	v_bfe_u32 v86, v64, 16, 1
	v_bfe_u32 v87, v65, 16, 1
	v_bfe_u32 v88, v84, 16, 1
	v_bfe_u32 v89, v85, 16, 1
	v_add3_u32 v85, v85, v89, s75
	v_add3_u32 v84, v84, v88, s75
	v_add3_u32 v65, v65, v87, s75
	v_add3_u32 v64, v64, v86, s75
	s_ashr_i32 s3, s2, 31
	v_lshrrev_b32_e32 v64, 16, v64
	v_lshrrev_b32_e32 v65, 16, v65
	v_lshrrev_b32_e32 v84, 16, v84
	v_lshrrev_b32_e32 v85, 16, v85
	s_lshl_b64 s[2:3], s[2:3], 11
	v_and_or_b32 v85, v79, s16, v85
	v_and_or_b32 v84, v78, s16, v84
	v_and_or_b32 v83, v83, s16, v65
	v_and_or_b32 v82, v82, s16, v64
	v_lshl_add_u64 v[64:65], v[128:129], 0, s[2:3]
	global_store_dwordx4 v[64:65], v[82:85], off sc1
	v_pk_fma_f32 v[64:65], v[106:107], v[76:77], v[108:109]
	s_nop 0
	v_pk_fma_f32 v[64:65], v[110:111], v[20:21], v[64:65]
	v_pk_fma_f32 v[20:21], v[106:107], v[20:21], v[108:109]
	v_pk_fma_f32 v[76:77], v[104:105], v[8:9], v[64:65]
	v_lshlrev_b32_e32 v65, 16, v61
	v_lshlrev_b32_e32 v64, 16, v60
	v_pk_fma_f32 v[76:77], v[100:101], v[64:65], v[76:77]
	v_and_b32_e32 v61, 0xffff0000, v61
	v_mul_f32_e32 v78, 0xbfb8aa3b, v76
	v_mul_f32_e32 v79, 0xbfb8aa3b, v77
	v_exp_f32_e32 v78, v78
	v_exp_f32_e32 v79, v79
	v_and_b32_e32 v60, 0xffff0000, v60
	v_pk_fma_f32 v[82:83], v[34:35], v[60:61], v[72:73]
	v_pk_fma_f32 v[20:21], v[110:111], v[8:9], v[20:21]
	v_pk_add_f32 v[78:79], v[78:79], 1.0 op_sel_hi:[1,0]
	v_mul_f32_e32 v72, 0xbfb8aa3b, v82
	v_div_scale_f32 v84, s[2:3], v79, v79, 1.0
	v_rcp_f32_e32 v85, v84
	v_exp_f32_e32 v72, v72
	v_pk_fma_f32 v[68:69], v[42:43], v[60:61], v[68:69]
	v_pk_fma_f32 v[8:9], v[106:107], v[8:9], v[108:109]
	v_fma_f32 v73, -v84, v85, 1.0
	v_fmac_f32_e32 v85, v73, v85
	v_div_scale_f32 v73, vcc, 1.0, v79, 1.0
	v_mul_f32_e32 v86, v73, v85
	v_fma_f32 v87, -v84, v86, v73
	v_fmac_f32_e32 v86, v87, v85
	v_fma_f32 v73, -v84, v86, v73
	v_div_scale_f32 v84, s[2:3], v78, v78, 1.0
	v_rcp_f32_e32 v87, v84
	v_div_fmas_f32 v73, v73, v85, v86
	v_div_fixup_f32 v79, v73, v79, 1.0
	v_div_scale_f32 v85, vcc, 1.0, v78, 1.0
	v_fma_f32 v73, -v84, v87, 1.0
	v_fmac_f32_e32 v87, v73, v87
	v_mul_f32_e32 v86, v85, v87
	v_fma_f32 v73, -v84, v86, v85
	v_fmac_f32_e32 v86, v73, v87
	v_mul_f32_e32 v73, 0xbfb8aa3b, v83
	v_exp_f32_e32 v73, v73
	v_fma_f32 v84, -v84, v86, v85
	v_div_fmas_f32 v86, v84, v87, v86
	v_div_fixup_f32 v78, v86, v78, 1.0
	v_pk_add_f32 v[84:85], v[72:73], 1.0 op_sel_hi:[1,0]
	v_pk_mul_f32 v[72:73], v[76:77], v[78:79]
	v_div_scale_f32 v87, s[2:3], v85, v85, 1.0
	v_rcp_f32_e32 v88, v87
	v_pk_mul_f32 v[72:73], v[140:141], v[72:73] op_sel_hi:[0,1]
	v_pk_fma_f32 v[8:9], v[110:111], v[64:65], v[8:9]
	v_fma_f32 v76, -v87, v88, 1.0
	v_fmac_f32_e32 v88, v76, v88
	v_div_scale_f32 v76, vcc, 1.0, v85, 1.0
	v_mul_f32_e32 v77, v76, v88
	v_fma_f32 v78, -v87, v77, v76
	v_fmac_f32_e32 v77, v78, v88
	v_div_scale_f32 v78, s[2:3], v84, v84, 1.0
	v_rcp_f32_e32 v79, v78
	v_fma_f32 v76, -v87, v77, v76
	v_div_fmas_f32 v76, v76, v88, v77
	v_div_fixup_f32 v77, v76, v85, 1.0
	v_fma_f32 v76, -v78, v79, 1.0
	v_fmac_f32_e32 v79, v76, v79
	v_div_scale_f32 v76, vcc, 1.0, v84, 1.0
	v_mul_f32_e32 v85, v76, v79
	v_fma_f32 v86, -v78, v85, v76
	v_fmac_f32_e32 v85, v86, v79
	v_fma_f32 v76, -v78, v85, v76
	v_div_fmas_f32 v76, v76, v79, v85
	v_pk_fma_f32 v[78:79], v[36:37], v[12:13], v[44:45]
	v_lshlrev_b32_e32 v45, 16, v63
	v_lshlrev_b32_e32 v44, 16, v62
	v_div_fixup_f32 v76, v76, v84, 1.0
	v_pk_fma_f32 v[78:79], v[40:41], v[44:45], v[78:79]
	v_pk_mul_f32 v[76:77], v[82:83], v[76:77]
	v_mul_f32_e32 v82, 0xbfb8aa3b, v78
	v_mul_f32_e32 v83, 0xbfb8aa3b, v79
	v_exp_f32_e32 v82, v82
	v_exp_f32_e32 v83, v83
	v_and_b32_e32 v63, 0xffff0000, v63
	v_and_b32_e32 v62, 0xffff0000, v62
	v_pk_fma_f32 v[74:75], v[10:11], v[62:63], v[74:75]
	v_pk_add_f32 v[82:83], v[82:83], 1.0 op_sel_hi:[1,0]
	v_mul_f32_e32 v84, 0xbfb8aa3b, v74
	v_div_scale_f32 v85, s[2:3], v83, v83, 1.0
	v_rcp_f32_e32 v86, v85
	v_exp_f32_e32 v84, v84
	v_pk_mul_f32 v[76:77], v[140:141], v[76:77] op_sel_hi:[0,1]
	v_pk_fma_f32 v[70:71], v[14:15], v[62:63], v[70:71]
	v_fma_f32 v87, -v85, v86, 1.0
	v_fmac_f32_e32 v86, v87, v86
	v_div_scale_f32 v87, vcc, 1.0, v83, 1.0
	v_mul_f32_e32 v88, v87, v86
	v_fma_f32 v89, -v85, v88, v87
	v_fmac_f32_e32 v88, v89, v86
	v_fma_f32 v85, -v85, v88, v87
	v_div_scale_f32 v87, s[2:3], v82, v82, 1.0
	v_rcp_f32_e32 v89, v87
	v_div_fmas_f32 v85, v85, v86, v88
	v_div_fixup_f32 v83, v85, v83, 1.0
	v_div_scale_f32 v86, vcc, 1.0, v82, 1.0
	v_fma_f32 v85, -v87, v89, 1.0
	v_fmac_f32_e32 v89, v85, v89
	v_mul_f32_e32 v88, v86, v89
	v_fma_f32 v85, -v87, v88, v86
	v_fmac_f32_e32 v88, v85, v89
	v_mul_f32_e32 v85, 0xbfb8aa3b, v75
	v_exp_f32_e32 v85, v85
	v_fma_f32 v86, -v87, v88, v86
	v_div_fmas_f32 v86, v86, v89, v88
	v_div_fixup_f32 v82, v86, v82, 1.0
	v_pk_add_f32 v[84:85], v[84:85], 1.0 op_sel_hi:[1,0]
	v_pk_mul_f32 v[78:79], v[78:79], v[82:83]
	v_div_scale_f32 v87, s[2:3], v85, v85, 1.0
	v_rcp_f32_e32 v88, v87
	v_pk_mul_f32 v[78:79], v[140:141], v[78:79] op_sel_hi:[0,1]
	v_pk_fma_f32 v[12:13], v[28:29], v[12:13], v[4:5]
	v_fma_f32 v82, -v87, v88, 1.0
	v_fmac_f32_e32 v88, v82, v88
	v_div_scale_f32 v82, vcc, 1.0, v85, 1.0
	v_mul_f32_e32 v83, v82, v88
	v_fma_f32 v86, -v87, v83, v82
	v_fmac_f32_e32 v83, v86, v88
	v_div_scale_f32 v86, s[2:3], v84, v84, 1.0
	v_fma_f32 v82, -v87, v83, v82
	v_rcp_f32_e32 v87, v86
	v_div_fmas_f32 v82, v82, v88, v83
	v_div_fixup_f32 v83, v82, v85, 1.0
	s_or_b32 s2, s14, 10
	v_fma_f32 v82, -v86, v87, 1.0
	v_fmac_f32_e32 v87, v82, v87
	v_div_scale_f32 v82, vcc, 1.0, v84, 1.0
	v_mul_f32_e32 v85, v82, v87
	v_fma_f32 v88, -v86, v85, v82
	v_fmac_f32_e32 v85, v88, v87
	v_fma_f32 v82, -v86, v85, v82
	v_div_fmas_f32 v82, v82, v87, v85
	v_div_fixup_f32 v82, v82, v84, 1.0
	v_pk_mul_f32 v[74:75], v[74:75], v[82:83]
	v_bfe_u32 v84, v77, 16, 1
	v_pk_mul_f32 v[74:75], v[140:141], v[74:75] op_sel_hi:[0,1]
	v_bfe_u32 v82, v75, 16, 1
	v_bfe_u32 v83, v74, 16, 1
	v_bfe_u32 v85, v76, 16, 1
	v_add3_u32 v76, v76, v85, s75
	v_add3_u32 v77, v77, v84, s75
	v_add3_u32 v74, v74, v83, s75
	v_add3_u32 v75, v75, v82, s75
	v_bfe_u32 v82, v72, 16, 1
	v_bfe_u32 v83, v73, 16, 1
	v_bfe_u32 v84, v78, 16, 1
	v_bfe_u32 v85, v79, 16, 1
	v_add3_u32 v79, v79, v85, s75
	v_add3_u32 v78, v78, v84, s75
	v_add3_u32 v73, v73, v83, s75
	v_add3_u32 v72, v72, v82, s75
	s_ashr_i32 s3, s2, 31
	v_lshrrev_b32_e32 v72, 16, v72
	v_lshrrev_b32_e32 v73, 16, v73
	v_lshrrev_b32_e32 v78, 16, v78
	v_lshrrev_b32_e32 v79, 16, v79
	s_lshl_b64 s[2:3], s[2:3], 11
	v_and_or_b32 v75, v75, s16, v79
	v_and_or_b32 v74, v74, s16, v78
	v_and_or_b32 v73, v77, s16, v73
	v_and_or_b32 v72, v76, s16, v72
	v_lshl_add_u64 v[76:77], v[128:129], 0, s[2:3]
	global_store_dwordx4 v[76:77], v[72:75], off sc1
	v_pk_fma_f32 v[12:13], v[32:33], v[44:45], v[12:13]
	s_nop 0
	v_pk_fma_f32 v[72:73], v[104:105], v[64:65], v[20:21]
	v_lshlrev_b32_e32 v21, 16, v57
	v_lshlrev_b32_e32 v20, 16, v56
	v_pk_fma_f32 v[72:73], v[100:101], v[20:21], v[72:73]
	v_and_b32_e32 v57, 0xffff0000, v57
	v_mul_f32_e32 v74, 0xbfb8aa3b, v72
	v_mul_f32_e32 v75, 0xbfb8aa3b, v73
	v_exp_f32_e32 v74, v74
	v_exp_f32_e32 v75, v75
	v_and_b32_e32 v56, 0xffff0000, v56
	v_pk_fma_f32 v[76:77], v[34:35], v[56:57], v[68:69]
	v_pk_add_f32 v[74:75], v[74:75], 1.0 op_sel_hi:[1,0]
	s_nop 0
	v_div_scale_f32 v78, s[2:3], v75, v75, 1.0
	v_rcp_f32_e32 v79, v78
	v_mul_f32_e32 v68, 0xbfb8aa3b, v76
	v_exp_f32_e32 v68, v68
	v_fma_f32 v69, -v78, v79, 1.0
	v_fmac_f32_e32 v79, v69, v79
	v_div_scale_f32 v69, vcc, 1.0, v75, 1.0
	v_mul_f32_e32 v82, v69, v79
	v_fma_f32 v83, -v78, v82, v69
	v_fmac_f32_e32 v82, v83, v79
	v_fma_f32 v69, -v78, v82, v69
	v_div_scale_f32 v78, s[2:3], v74, v74, 1.0
	v_rcp_f32_e32 v83, v78
	v_div_fmas_f32 v69, v69, v79, v82
	v_div_fixup_f32 v75, v69, v75, 1.0
	v_div_scale_f32 v79, vcc, 1.0, v74, 1.0
	v_fma_f32 v69, -v78, v83, 1.0
	v_fmac_f32_e32 v83, v69, v83
	v_mul_f32_e32 v82, v79, v83
	v_fma_f32 v69, -v78, v82, v79
	v_fmac_f32_e32 v82, v69, v83
	v_mul_f32_e32 v69, 0xbfb8aa3b, v77
	v_exp_f32_e32 v69, v69
	v_fma_f32 v78, -v78, v82, v79
	v_div_fmas_f32 v82, v78, v83, v82
	v_div_fixup_f32 v74, v82, v74, 1.0
	v_pk_add_f32 v[78:79], v[68:69], 1.0 op_sel_hi:[1,0]
	v_pk_mul_f32 v[68:69], v[72:73], v[74:75]
	v_div_scale_f32 v83, s[2:3], v79, v79, 1.0
	v_rcp_f32_e32 v84, v83
	v_pk_mul_f32 v[68:69], v[138:139], v[68:69] op_sel_hi:[0,1]
	v_fma_f32 v72, -v83, v84, 1.0
	v_fmac_f32_e32 v84, v72, v84
	v_div_scale_f32 v72, vcc, 1.0, v79, 1.0
	v_mul_f32_e32 v73, v72, v84
	v_fma_f32 v74, -v83, v73, v72
	v_fmac_f32_e32 v73, v74, v84
	v_div_scale_f32 v74, s[2:3], v78, v78, 1.0
	v_rcp_f32_e32 v75, v74
	v_fma_f32 v72, -v83, v73, v72
	v_div_fmas_f32 v72, v72, v84, v73
	v_div_fixup_f32 v73, v72, v79, 1.0
	v_fma_f32 v72, -v74, v75, 1.0
	v_fmac_f32_e32 v75, v72, v75
	v_div_scale_f32 v72, vcc, 1.0, v78, 1.0
	v_mul_f32_e32 v79, v72, v75
	v_fma_f32 v82, -v74, v79, v72
	v_fmac_f32_e32 v79, v82, v75
	v_fma_f32 v72, -v74, v79, v72
	v_div_fmas_f32 v72, v72, v75, v79
	v_pk_fma_f32 v[74:75], v[36:37], v[44:45], v[16:17]
	v_lshlrev_b32_e32 v17, 16, v59
	v_lshlrev_b32_e32 v16, 16, v58
	v_div_fixup_f32 v72, v72, v78, 1.0
	v_pk_fma_f32 v[74:75], v[40:41], v[16:17], v[74:75]
	v_pk_mul_f32 v[72:73], v[76:77], v[72:73]
	v_mul_f32_e32 v76, 0xbfb8aa3b, v74
	v_mul_f32_e32 v77, 0xbfb8aa3b, v75
	v_exp_f32_e32 v76, v76
	v_exp_f32_e32 v77, v77
	v_and_b32_e32 v59, 0xffff0000, v59
	v_and_b32_e32 v58, 0xffff0000, v58
	v_pk_fma_f32 v[70:71], v[10:11], v[58:59], v[70:71]
	v_pk_add_f32 v[76:77], v[76:77], 1.0 op_sel_hi:[1,0]
	v_mul_f32_e32 v78, 0xbfb8aa3b, v70
	v_div_scale_f32 v79, s[2:3], v77, v77, 1.0
	v_rcp_f32_e32 v82, v79
	v_exp_f32_e32 v78, v78
	v_pk_mul_f32 v[72:73], v[138:139], v[72:73] op_sel_hi:[0,1]
	v_pk_fma_f32 v[44:45], v[28:29], v[44:45], v[4:5]
	v_fma_f32 v83, -v79, v82, 1.0
	v_fmac_f32_e32 v82, v83, v82
	v_div_scale_f32 v83, vcc, 1.0, v77, 1.0
	v_mul_f32_e32 v84, v83, v82
	v_fma_f32 v85, -v79, v84, v83
	v_fmac_f32_e32 v84, v85, v82
	v_fma_f32 v79, -v79, v84, v83
	v_div_scale_f32 v83, s[2:3], v76, v76, 1.0
	v_rcp_f32_e32 v85, v83
	v_div_fmas_f32 v79, v79, v82, v84
	v_div_fixup_f32 v77, v79, v77, 1.0
	v_div_scale_f32 v82, vcc, 1.0, v76, 1.0
	v_fma_f32 v79, -v83, v85, 1.0
	v_fmac_f32_e32 v85, v79, v85
	v_mul_f32_e32 v84, v82, v85
	v_fma_f32 v79, -v83, v84, v82
	v_fmac_f32_e32 v84, v79, v85
	v_mul_f32_e32 v79, 0xbfb8aa3b, v71
	v_exp_f32_e32 v79, v79
	v_fma_f32 v82, -v83, v84, v82
	v_div_fmas_f32 v82, v82, v85, v84
	v_div_fixup_f32 v76, v82, v76, 1.0
	v_pk_add_f32 v[78:79], v[78:79], 1.0 op_sel_hi:[1,0]
	v_pk_mul_f32 v[74:75], v[74:75], v[76:77]
	v_div_scale_f32 v83, s[2:3], v79, v79, 1.0
	v_rcp_f32_e32 v84, v83
	v_pk_mul_f32 v[74:75], v[138:139], v[74:75] op_sel_hi:[0,1]
	v_pk_fma_f32 v[44:45], v[32:33], v[16:17], v[44:45]
	v_fma_f32 v76, -v83, v84, 1.0
	v_fmac_f32_e32 v84, v76, v84
	v_div_scale_f32 v76, vcc, 1.0, v79, 1.0
	v_mul_f32_e32 v77, v76, v84
	v_fma_f32 v82, -v83, v77, v76
	v_fmac_f32_e32 v77, v82, v84
	v_div_scale_f32 v82, s[2:3], v78, v78, 1.0
	v_fma_f32 v76, -v83, v77, v76
	v_rcp_f32_e32 v83, v82
	v_div_fmas_f32 v76, v76, v84, v77
	v_div_fixup_f32 v77, v76, v79, 1.0
	s_or_b32 s2, s14, 11
	v_fma_f32 v76, -v82, v83, 1.0
	v_fmac_f32_e32 v83, v76, v83
	v_div_scale_f32 v76, vcc, 1.0, v78, 1.0
	v_mul_f32_e32 v79, v76, v83
	v_fma_f32 v84, -v82, v79, v76
	v_fmac_f32_e32 v79, v84, v83
	v_fma_f32 v76, -v82, v79, v76
	v_div_fmas_f32 v76, v76, v83, v79
	v_div_fixup_f32 v76, v76, v78, 1.0
	v_pk_mul_f32 v[70:71], v[70:71], v[76:77]
	v_bfe_u32 v78, v73, 16, 1
	v_pk_mul_f32 v[70:71], v[138:139], v[70:71] op_sel_hi:[0,1]
	v_bfe_u32 v76, v71, 16, 1
	v_bfe_u32 v77, v70, 16, 1
	v_bfe_u32 v79, v72, 16, 1
	v_add3_u32 v72, v72, v79, s75
	v_add3_u32 v73, v73, v78, s75
	v_add3_u32 v70, v70, v77, s75
	v_add3_u32 v71, v71, v76, s75
	v_bfe_u32 v76, v68, 16, 1
	v_bfe_u32 v77, v69, 16, 1
	v_bfe_u32 v78, v74, 16, 1
	v_bfe_u32 v79, v75, 16, 1
	v_add3_u32 v75, v75, v79, s75
	v_add3_u32 v74, v74, v78, s75
	v_add3_u32 v69, v69, v77, s75
	v_add3_u32 v68, v68, v76, s75
	s_ashr_i32 s3, s2, 31
	v_lshrrev_b32_e32 v68, 16, v68
	v_lshrrev_b32_e32 v69, 16, v69
	v_lshrrev_b32_e32 v74, 16, v74
	v_lshrrev_b32_e32 v75, 16, v75
	s_lshl_b64 s[2:3], s[2:3], 11
	v_and_or_b32 v71, v71, s16, v75
	v_and_or_b32 v70, v70, s16, v74
	v_and_or_b32 v69, v73, s16, v69
	v_and_or_b32 v68, v72, s16, v68
	v_lshl_add_u64 v[72:73], v[128:129], 0, s[2:3]
	global_store_dwordx4 v[72:73], v[68:71], off sc1
	s_nop 1
	v_pk_fma_f32 v[68:69], v[104:105], v[20:21], v[8:9]
	v_lshlrev_b32_e32 v9, 16, v53
	v_lshlrev_b32_e32 v8, 16, v52
	v_pk_fma_f32 v[70:71], v[100:101], v[8:9], v[68:69]
	s_nop 0
	v_mul_f32_e32 v68, 0xbfb8aa3b, v70
	v_mul_f32_e32 v73, 0xbfb8aa3b, v71
	v_exp_f32_e32 v72, v68
	v_exp_f32_e32 v73, v73
	v_pk_fma_f32 v[68:69], v[30:31], v[80:81], v[46:47]
	s_nop 0
	v_pk_fma_f32 v[68:69], v[38:39], v[60:61], v[68:69]
	v_pk_fma_f32 v[60:61], v[30:31], v[60:61], v[46:47]
	v_pk_fma_f32 v[74:75], v[42:43], v[56:57], v[68:69]
	v_and_b32_e32 v69, 0xffff0000, v53
	v_and_b32_e32 v68, 0xffff0000, v52
	v_pk_add_f32 v[52:53], v[72:73], 1.0 op_sel_hi:[1,0]
	v_pk_fma_f32 v[72:73], v[34:35], v[68:69], v[74:75]
	v_div_scale_f32 v76, s[2:3], v53, v53, 1.0
	v_rcp_f32_e32 v77, v76
	v_mul_f32_e32 v74, 0xbfb8aa3b, v72
	v_exp_f32_e32 v74, v74
	v_pk_fma_f32 v[60:61], v[38:39], v[56:57], v[60:61]
	v_fma_f32 v75, -v76, v77, 1.0
	v_fmac_f32_e32 v77, v75, v77
	v_div_scale_f32 v75, vcc, 1.0, v53, 1.0
	v_mul_f32_e32 v78, v75, v77
	v_fma_f32 v79, -v76, v78, v75
	v_fmac_f32_e32 v78, v79, v77
	v_fma_f32 v75, -v76, v78, v75
	v_div_scale_f32 v76, s[2:3], v52, v52, 1.0
	v_rcp_f32_e32 v79, v76
	v_div_fmas_f32 v75, v75, v77, v78
	v_div_fixup_f32 v53, v75, v53, 1.0
	v_div_scale_f32 v77, vcc, 1.0, v52, 1.0
	v_fma_f32 v75, -v76, v79, 1.0
	v_fmac_f32_e32 v79, v75, v79
	v_mul_f32_e32 v78, v77, v79
	v_fma_f32 v75, -v76, v78, v77
	v_fmac_f32_e32 v78, v75, v79
	v_mul_f32_e32 v75, 0xbfb8aa3b, v73
	v_exp_f32_e32 v75, v75
	v_fma_f32 v76, -v76, v78, v77
	v_div_fmas_f32 v76, v76, v79, v78
	v_div_fixup_f32 v52, v76, v52, 1.0
	v_pk_add_f32 v[74:75], v[74:75], 1.0 op_sel_hi:[1,0]
	v_pk_mul_f32 v[52:53], v[70:71], v[52:53]
	v_div_scale_f32 v77, s[2:3], v75, v75, 1.0
	v_rcp_f32_e32 v78, v77
	v_pk_mul_f32 v[70:71], v[136:137], v[52:53] op_sel_hi:[0,1]
	v_fma_f32 v52, -v77, v78, 1.0
	v_fmac_f32_e32 v78, v52, v78
	v_div_scale_f32 v52, vcc, 1.0, v75, 1.0
	v_mul_f32_e32 v53, v52, v78
	v_fma_f32 v76, -v77, v53, v52
	v_fmac_f32_e32 v53, v76, v78
	v_div_scale_f32 v76, s[2:3], v74, v74, 1.0
	v_fma_f32 v52, -v77, v53, v52
	v_rcp_f32_e32 v77, v76
	v_div_fmas_f32 v52, v52, v78, v53
	v_div_fixup_f32 v53, v52, v75, 1.0
	v_fma_f32 v52, -v76, v77, 1.0
	v_fmac_f32_e32 v77, v52, v77
	v_div_scale_f32 v52, vcc, 1.0, v74, 1.0
	v_mul_f32_e32 v75, v52, v77
	v_fma_f32 v78, -v76, v75, v52
	v_fmac_f32_e32 v75, v78, v77
	v_fma_f32 v52, -v76, v75, v52
	v_div_fmas_f32 v52, v52, v77, v75
	v_div_fixup_f32 v52, v52, v74, 1.0
	v_pk_mul_f32 v[52:53], v[72:73], v[52:53]
	s_nop 0
	v_pk_mul_f32 v[72:73], v[136:137], v[52:53] op_sel_hi:[0,1]
	v_pk_fma_f32 v[52:53], v[36:37], v[16:17], v[12:13]
	v_lshlrev_b32_e32 v13, 16, v55
	v_lshlrev_b32_e32 v12, 16, v54
	v_pk_fma_f32 v[74:75], v[40:41], v[12:13], v[52:53]
	v_pk_fma_f32 v[16:17], v[28:29], v[16:17], v[4:5]
	v_mul_f32_e32 v52, 0xbfb8aa3b, v74
	v_exp_f32_e32 v76, v52
	v_pk_fma_f32 v[52:53], v[6:7], v[66:67], v[22:23]
	v_mul_f32_e32 v66, 0xbfb8aa3b, v75
	v_exp_f32_e32 v77, v66
	v_pk_fma_f32 v[52:53], v[18:19], v[62:63], v[52:53]
	v_pk_fma_f32 v[16:17], v[32:33], v[12:13], v[16:17]
	v_pk_fma_f32 v[66:67], v[14:15], v[58:59], v[52:53]
	v_and_b32_e32 v53, 0xffff0000, v55
	v_and_b32_e32 v52, 0xffff0000, v54
	v_pk_add_f32 v[54:55], v[76:77], 1.0 op_sel_hi:[1,0]
	v_pk_fma_f32 v[66:67], v[10:11], v[52:53], v[66:67]
	v_div_scale_f32 v77, s[2:3], v55, v55, 1.0
	v_rcp_f32_e32 v78, v77
	v_mul_f32_e32 v76, 0xbfb8aa3b, v66
	v_exp_f32_e32 v76, v76
	v_pk_fma_f32 v[4:5], v[28:29], v[12:13], v[4:5]
	v_fma_f32 v79, -v77, v78, 1.0
	v_fmac_f32_e32 v78, v79, v78
	v_div_scale_f32 v79, vcc, 1.0, v55, 1.0
	v_mul_f32_e32 v80, v79, v78
	v_fma_f32 v81, -v77, v80, v79
	v_fmac_f32_e32 v80, v81, v78
	v_fma_f32 v77, -v77, v80, v79
	v_div_scale_f32 v79, s[2:3], v54, v54, 1.0
	v_rcp_f32_e32 v81, v79
	v_div_fmas_f32 v77, v77, v78, v80
	v_div_fixup_f32 v55, v77, v55, 1.0
	v_div_scale_f32 v78, vcc, 1.0, v54, 1.0
	v_fma_f32 v77, -v79, v81, 1.0
	v_fmac_f32_e32 v81, v77, v81
	v_mul_f32_e32 v80, v78, v81
	v_fma_f32 v77, -v79, v80, v78
	v_fmac_f32_e32 v80, v77, v81
	v_mul_f32_e32 v77, 0xbfb8aa3b, v67
	v_exp_f32_e32 v77, v77
	v_fma_f32 v78, -v79, v80, v78
	v_div_fmas_f32 v78, v78, v81, v80
	v_div_fixup_f32 v54, v78, v54, 1.0
	v_pk_add_f32 v[76:77], v[76:77], 1.0 op_sel_hi:[1,0]
	v_pk_mul_f32 v[54:55], v[74:75], v[54:55]
	v_div_scale_f32 v79, s[2:3], v77, v77, 1.0
	v_rcp_f32_e32 v80, v79
	v_pk_mul_f32 v[54:55], v[136:137], v[54:55] op_sel_hi:[0,1]
	v_fma_f32 v74, -v79, v80, 1.0
	v_fmac_f32_e32 v80, v74, v80
	v_div_scale_f32 v74, vcc, 1.0, v77, 1.0
	v_mul_f32_e32 v75, v74, v80
	v_fma_f32 v78, -v79, v75, v74
	v_fmac_f32_e32 v75, v78, v80
	v_div_scale_f32 v78, s[2:3], v76, v76, 1.0
	v_fma_f32 v74, -v79, v75, v74
	v_rcp_f32_e32 v79, v78
	v_div_fmas_f32 v74, v74, v80, v75
	v_div_fixup_f32 v75, v74, v77, 1.0
	s_or_b32 s2, s14, 12
	v_fma_f32 v74, -v78, v79, 1.0
	v_fmac_f32_e32 v79, v74, v79
	v_div_scale_f32 v74, vcc, 1.0, v76, 1.0
	v_mul_f32_e32 v77, v74, v79
	v_fma_f32 v80, -v78, v77, v74
	v_fmac_f32_e32 v77, v80, v79
	v_fma_f32 v74, -v78, v77, v74
	v_div_fmas_f32 v74, v74, v79, v77
	v_div_fixup_f32 v74, v74, v76, 1.0
	v_pk_mul_f32 v[66:67], v[66:67], v[74:75]
	v_bfe_u32 v76, v73, 16, 1
	v_pk_mul_f32 v[66:67], v[136:137], v[66:67] op_sel_hi:[0,1]
	v_bfe_u32 v74, v67, 16, 1
	v_bfe_u32 v75, v66, 16, 1
	v_bfe_u32 v77, v72, 16, 1
	v_add3_u32 v77, v72, v77, s75
	v_add3_u32 v76, v73, v76, s75
	v_add3_u32 v66, v66, v75, s75
	v_add3_u32 v67, v67, v74, s75
	v_bfe_u32 v72, v70, 16, 1
	v_bfe_u32 v73, v71, 16, 1
	v_bfe_u32 v74, v54, 16, 1
	v_bfe_u32 v75, v55, 16, 1
	v_add3_u32 v55, v55, v75, s75
	v_add3_u32 v54, v54, v74, s75
	v_add3_u32 v71, v71, v73, s75
	v_add3_u32 v70, v70, v72, s75
	s_ashr_i32 s3, s2, 31
	v_lshrrev_b32_e32 v70, 16, v70
	v_lshrrev_b32_e32 v71, 16, v71
	v_lshrrev_b32_e32 v54, 16, v54
	v_lshrrev_b32_e32 v55, 16, v55
	s_lshl_b64 s[2:3], s[2:3], 11
	v_and_or_b32 v73, v67, s16, v55
	v_and_or_b32 v72, v66, s16, v54
	v_and_or_b32 v71, v76, s16, v71
	v_and_or_b32 v70, v77, s16, v70
	v_lshl_add_u64 v[54:55], v[128:129], 0, s[2:3]
	global_store_dwordx4 v[54:55], v[70:73], off sc1
	v_pk_fma_f32 v[54:55], v[106:107], v[64:65], v[108:109]
	s_nop 0
	v_pk_fma_f32 v[54:55], v[110:111], v[20:21], v[54:55]
	v_pk_fma_f32 v[70:71], v[42:43], v[68:69], v[60:61]
	v_pk_fma_f32 v[64:65], v[104:105], v[8:9], v[54:55]
	v_lshlrev_b32_e32 v55, 16, v49
	v_lshlrev_b32_e32 v54, 16, v48
	v_pk_fma_f32 v[64:65], v[100:101], v[54:55], v[64:65]
	v_and_b32_e32 v61, 0xffff0000, v49
	v_mul_f32_e32 v66, 0xbfb8aa3b, v64
	v_mul_f32_e32 v67, 0xbfb8aa3b, v65
	v_exp_f32_e32 v66, v66
	v_exp_f32_e32 v67, v67
	v_and_b32_e32 v60, 0xffff0000, v48
	v_pk_fma_f32 v[20:21], v[106:107], v[20:21], v[108:109]
	v_pk_add_f32 v[48:49], v[66:67], 1.0 op_sel_hi:[1,0]
	s_nop 0
	v_div_scale_f32 v72, s[2:3], v49, v49, 1.0
	v_rcp_f32_e32 v73, v72
	v_pk_fma_f32 v[66:67], v[34:35], v[60:61], v[70:71]
	v_pk_fma_f32 v[20:21], v[110:111], v[8:9], v[20:21]
	v_mul_f32_e32 v70, 0xbfb8aa3b, v66
	v_fma_f32 v71, -v72, v73, 1.0
	v_fmac_f32_e32 v73, v71, v73
	v_div_scale_f32 v71, vcc, 1.0, v49, 1.0
	v_mul_f32_e32 v74, v71, v73
	v_fma_f32 v75, -v72, v74, v71
	v_fmac_f32_e32 v74, v75, v73
	v_fma_f32 v71, -v72, v74, v71
	v_div_scale_f32 v72, s[2:3], v48, v48, 1.0
	v_rcp_f32_e32 v75, v72
	v_div_fmas_f32 v71, v71, v73, v74
	v_div_fixup_f32 v49, v71, v49, 1.0
	v_div_scale_f32 v73, vcc, 1.0, v48, 1.0
	v_fma_f32 v71, -v72, v75, 1.0
	v_fmac_f32_e32 v75, v71, v75
	v_mul_f32_e32 v74, v73, v75
	v_fma_f32 v71, -v72, v74, v73
	v_fmac_f32_e32 v74, v71, v75
	v_mul_f32_e32 v71, 0xbfb8aa3b, v67
	v_exp_f32_e32 v70, v70
	v_exp_f32_e32 v71, v71
	v_fma_f32 v72, -v72, v74, v73
	v_div_fmas_f32 v72, v72, v75, v74
	v_div_fixup_f32 v48, v72, v48, 1.0
	v_pk_add_f32 v[70:71], v[70:71], 1.0 op_sel_hi:[1,0]
	v_pk_mul_f32 v[48:49], v[64:65], v[48:49]
	v_div_scale_f32 v73, s[2:3], v71, v71, 1.0
	v_rcp_f32_e32 v74, v73
	v_pk_mul_f32 v[64:65], v[134:135], v[48:49] op_sel_hi:[0,1]
	v_pk_fma_f32 v[8:9], v[106:107], v[8:9], v[108:109]
	v_fma_f32 v48, -v73, v74, 1.0
	v_fmac_f32_e32 v74, v48, v74
	v_div_scale_f32 v48, vcc, 1.0, v71, 1.0
	v_mul_f32_e32 v49, v48, v74
	v_fma_f32 v72, -v73, v49, v48
	v_fmac_f32_e32 v49, v72, v74
	v_div_scale_f32 v72, s[2:3], v70, v70, 1.0
	v_fma_f32 v48, -v73, v49, v48
	v_rcp_f32_e32 v73, v72
	v_div_fmas_f32 v48, v48, v74, v49
	v_div_fixup_f32 v49, v48, v71, 1.0
	v_pk_fma_f32 v[8:9], v[110:111], v[54:55], v[8:9]
	v_fma_f32 v48, -v72, v73, 1.0
	v_fmac_f32_e32 v73, v48, v73
	v_div_scale_f32 v48, vcc, 1.0, v70, 1.0
	v_mul_f32_e32 v71, v48, v73
	v_fma_f32 v74, -v72, v71, v48
	v_fmac_f32_e32 v71, v74, v73
	v_fma_f32 v48, -v72, v71, v48
	v_div_fmas_f32 v48, v48, v73, v71
	v_div_fixup_f32 v48, v48, v70, 1.0
	v_pk_mul_f32 v[48:49], v[66:67], v[48:49]
	s_nop 0
	v_pk_mul_f32 v[66:67], v[134:135], v[48:49] op_sel_hi:[0,1]
	v_pk_fma_f32 v[48:49], v[36:37], v[12:13], v[44:45]
	v_lshlrev_b32_e32 v45, 16, v51
	v_lshlrev_b32_e32 v44, 16, v50
	v_pk_fma_f32 v[70:71], v[40:41], v[44:45], v[48:49]
	v_pk_fma_f32 v[16:17], v[36:37], v[44:45], v[16:17]
	v_mul_f32_e32 v48, 0xbfb8aa3b, v70
	v_exp_f32_e32 v72, v48
	v_pk_fma_f32 v[48:49], v[6:7], v[62:63], v[22:23]
	v_mul_f32_e32 v62, 0xbfb8aa3b, v71
	v_exp_f32_e32 v73, v62
	v_pk_fma_f32 v[48:49], v[18:19], v[58:59], v[48:49]
	v_pk_fma_f32 v[4:5], v[32:33], v[44:45], v[4:5]
	v_pk_fma_f32 v[62:63], v[14:15], v[52:53], v[48:49]
	v_and_b32_e32 v49, 0xffff0000, v51
	v_and_b32_e32 v48, 0xffff0000, v50
	v_pk_add_f32 v[50:51], v[72:73], 1.0 op_sel_hi:[1,0]
	v_pk_fma_f32 v[62:63], v[10:11], v[48:49], v[62:63]
	v_div_scale_f32 v73, s[2:3], v51, v51, 1.0
	v_rcp_f32_e32 v74, v73
	v_mul_f32_e32 v72, 0xbfb8aa3b, v62
	v_exp_f32_e32 v72, v72
	v_lshlrev_b32_e32 v13, 16, v3
	v_fma_f32 v75, -v73, v74, 1.0
	v_fmac_f32_e32 v74, v75, v74
	v_div_scale_f32 v75, vcc, 1.0, v51, 1.0
	v_mul_f32_e32 v76, v75, v74
	v_fma_f32 v77, -v73, v76, v75
	v_fmac_f32_e32 v76, v77, v74
	v_fma_f32 v73, -v73, v76, v75
	v_div_scale_f32 v75, s[2:3], v50, v50, 1.0
	v_rcp_f32_e32 v77, v75
	v_div_fmas_f32 v73, v73, v74, v76
	v_div_fixup_f32 v51, v73, v51, 1.0
	v_div_scale_f32 v74, vcc, 1.0, v50, 1.0
	v_fma_f32 v73, -v75, v77, 1.0
	v_fmac_f32_e32 v77, v73, v77
	v_mul_f32_e32 v76, v74, v77
	v_fma_f32 v73, -v75, v76, v74
	v_fmac_f32_e32 v76, v73, v77
	v_mul_f32_e32 v73, 0xbfb8aa3b, v63
	v_exp_f32_e32 v73, v73
	v_fma_f32 v74, -v75, v76, v74
	v_div_fmas_f32 v74, v74, v77, v76
	v_div_fixup_f32 v50, v74, v50, 1.0
	v_pk_add_f32 v[72:73], v[72:73], 1.0 op_sel_hi:[1,0]
	v_pk_mul_f32 v[50:51], v[70:71], v[50:51]
	v_div_scale_f32 v75, s[2:3], v73, v73, 1.0
	v_rcp_f32_e32 v76, v75
	v_pk_mul_f32 v[50:51], v[134:135], v[50:51] op_sel_hi:[0,1]
	v_lshlrev_b32_e32 v12, 16, v2
	v_and_b32_e32 v3, 0xffff0000, v3
	v_fma_f32 v70, -v75, v76, 1.0
	v_fmac_f32_e32 v76, v70, v76
	v_div_scale_f32 v70, vcc, 1.0, v73, 1.0
	v_mul_f32_e32 v71, v70, v76
	v_fma_f32 v74, -v75, v71, v70
	v_fmac_f32_e32 v71, v74, v76
	v_div_scale_f32 v74, s[2:3], v72, v72, 1.0
	v_fma_f32 v70, -v75, v71, v70
	v_rcp_f32_e32 v75, v74
	v_div_fmas_f32 v70, v70, v76, v71
	v_div_fixup_f32 v71, v70, v73, 1.0
	s_or_b32 s2, s14, 13
	v_fma_f32 v70, -v74, v75, 1.0
	v_fmac_f32_e32 v75, v70, v75
	v_div_scale_f32 v70, vcc, 1.0, v72, 1.0
	v_mul_f32_e32 v73, v70, v75
	v_fma_f32 v76, -v74, v73, v70
	v_fmac_f32_e32 v73, v76, v75
	v_fma_f32 v70, -v74, v73, v70
	v_div_fmas_f32 v70, v70, v75, v73
	v_div_fixup_f32 v70, v70, v72, 1.0
	v_pk_mul_f32 v[62:63], v[62:63], v[70:71]
	v_bfe_u32 v72, v67, 16, 1
	v_pk_mul_f32 v[62:63], v[134:135], v[62:63] op_sel_hi:[0,1]
	v_bfe_u32 v70, v63, 16, 1
	v_bfe_u32 v71, v62, 16, 1
	v_bfe_u32 v73, v66, 16, 1
	v_add3_u32 v66, v66, v73, s75
	v_add3_u32 v67, v67, v72, s75
	v_add3_u32 v62, v62, v71, s75
	v_add3_u32 v63, v63, v70, s75
	v_bfe_u32 v70, v64, 16, 1
	v_bfe_u32 v71, v65, 16, 1
	v_bfe_u32 v72, v50, 16, 1
	v_bfe_u32 v73, v51, 16, 1
	v_add3_u32 v51, v51, v73, s75
	v_add3_u32 v50, v50, v72, s75
	v_add3_u32 v65, v65, v71, s75
	v_add3_u32 v64, v64, v70, s75
	s_ashr_i32 s3, s2, 31
	v_lshrrev_b32_e32 v70, 16, v64
	v_lshrrev_b32_e32 v71, 16, v65
	v_lshrrev_b32_e32 v50, 16, v50
	v_lshrrev_b32_e32 v51, 16, v51
	s_lshl_b64 s[2:3], s[2:3], 11
	v_and_or_b32 v65, v63, s16, v51
	v_and_or_b32 v64, v62, s16, v50
	v_and_or_b32 v63, v67, s16, v71
	v_and_or_b32 v62, v66, s16, v70
	v_lshl_add_u64 v[50:51], v[128:129], 0, s[2:3]
	global_store_dwordx4 v[50:51], v[62:65], off sc1
	v_pk_fma_f32 v[50:51], v[104:105], v[54:55], v[20:21]
	v_lshlrev_b32_e32 v21, 16, v25
	v_lshlrev_b32_e32 v20, 16, v24
	v_pk_fma_f32 v[62:63], v[100:101], v[20:21], v[50:51]
	v_pk_fma_f32 v[8:9], v[104:105], v[20:21], v[8:9]
	v_mul_f32_e32 v50, 0xbfb8aa3b, v62
	v_exp_f32_e32 v64, v50
	v_pk_fma_f32 v[50:51], v[30:31], v[56:57], v[46:47]
	v_mul_f32_e32 v56, 0xbfb8aa3b, v63
	v_exp_f32_e32 v65, v56
	v_pk_fma_f32 v[50:51], v[38:39], v[68:69], v[50:51]
	v_and_b32_e32 v2, 0xffff0000, v2
	v_pk_fma_f32 v[56:57], v[42:43], v[60:61], v[50:51]
	v_and_b32_e32 v51, 0xffff0000, v25
	v_and_b32_e32 v50, 0xffff0000, v24
	v_pk_add_f32 v[24:25], v[64:65], 1.0 op_sel_hi:[1,0]
	v_pk_fma_f32 v[64:65], v[34:35], v[50:51], v[56:57]
	v_div_scale_f32 v66, s[2:3], v25, v25, 1.0
	v_rcp_f32_e32 v67, v66
	v_mul_f32_e32 v56, 0xbfb8aa3b, v64
	v_exp_f32_e32 v56, v56
	v_fma_f32 v57, -v66, v67, 1.0
	v_fmac_f32_e32 v67, v57, v67
	v_div_scale_f32 v57, vcc, 1.0, v25, 1.0
	v_mul_f32_e32 v70, v57, v67
	v_fma_f32 v71, -v66, v70, v57
	v_fmac_f32_e32 v70, v71, v67
	v_fma_f32 v57, -v66, v70, v57
	v_div_scale_f32 v66, s[2:3], v24, v24, 1.0
	v_rcp_f32_e32 v71, v66
	v_div_fmas_f32 v57, v57, v67, v70
	v_div_fixup_f32 v25, v57, v25, 1.0
	v_div_scale_f32 v67, vcc, 1.0, v24, 1.0
	v_fma_f32 v57, -v66, v71, 1.0
	v_fmac_f32_e32 v71, v57, v71
	v_mul_f32_e32 v70, v67, v71
	v_fma_f32 v57, -v66, v70, v67
	v_fmac_f32_e32 v70, v57, v71
	v_mul_f32_e32 v57, 0xbfb8aa3b, v65
	v_exp_f32_e32 v57, v57
	v_fma_f32 v66, -v66, v70, v67
	v_div_fmas_f32 v70, v66, v71, v70
	v_div_fixup_f32 v24, v70, v24, 1.0
	v_pk_add_f32 v[66:67], v[56:57], 1.0 op_sel_hi:[1,0]
	v_pk_mul_f32 v[24:25], v[62:63], v[24:25]
	v_div_scale_f32 v71, s[2:3], v67, v67, 1.0
	v_rcp_f32_e32 v72, v71
	v_pk_mul_f32 v[56:57], v[132:133], v[24:25] op_sel_hi:[0,1]
	v_fma_f32 v24, -v71, v72, 1.0
	v_fmac_f32_e32 v72, v24, v72
	v_div_scale_f32 v24, vcc, 1.0, v67, 1.0
	v_mul_f32_e32 v25, v24, v72
	v_fma_f32 v62, -v71, v25, v24
	v_fmac_f32_e32 v25, v62, v72
	v_div_scale_f32 v62, s[2:3], v66, v66, 1.0
	v_rcp_f32_e32 v63, v62
	v_fma_f32 v24, -v71, v25, v24
	v_div_fmas_f32 v24, v24, v72, v25
	v_div_fixup_f32 v25, v24, v67, 1.0
	v_fma_f32 v24, -v62, v63, 1.0
	v_fmac_f32_e32 v63, v24, v63
	v_div_scale_f32 v24, vcc, 1.0, v66, 1.0
	v_mul_f32_e32 v67, v24, v63
	v_fma_f32 v70, -v62, v67, v24
	v_fmac_f32_e32 v67, v70, v63
	v_fma_f32 v24, -v62, v67, v24
	v_div_fmas_f32 v24, v24, v63, v67
	v_div_fixup_f32 v24, v24, v66, 1.0
	v_pk_mul_f32 v[24:25], v[64:65], v[24:25]
	s_nop 0
	v_pk_mul_f32 v[62:63], v[132:133], v[24:25] op_sel_hi:[0,1]
	v_lshlrev_b32_e32 v25, 16, v27
	v_lshlrev_b32_e32 v24, 16, v26
	v_pk_fma_f32 v[64:65], v[40:41], v[24:25], v[16:17]
	v_pk_fma_f32 v[4:5], v[36:37], v[24:25], v[4:5]
	v_mul_f32_e32 v16, 0xbfb8aa3b, v64
	v_exp_f32_e32 v66, v16
	v_pk_fma_f32 v[16:17], v[6:7], v[58:59], v[22:23]
	v_mul_f32_e32 v58, 0xbfb8aa3b, v65
	v_exp_f32_e32 v67, v58
	v_pk_fma_f32 v[16:17], v[18:19], v[52:53], v[16:17]
	v_pk_fma_f32 v[4:5], v[40:41], v[12:13], v[4:5]
	v_pk_fma_f32 v[58:59], v[14:15], v[48:49], v[16:17]
	v_and_b32_e32 v17, 0xffff0000, v27
	v_and_b32_e32 v16, 0xffff0000, v26
	v_pk_add_f32 v[26:27], v[66:67], 1.0 op_sel_hi:[1,0]
	v_pk_fma_f32 v[58:59], v[10:11], v[16:17], v[58:59]
	v_div_scale_f32 v67, s[2:3], v27, v27, 1.0
	v_rcp_f32_e32 v70, v67
	v_mul_f32_e32 v66, 0xbfb8aa3b, v58
	v_exp_f32_e32 v66, v66
	v_mul_f32_e32 v12, 0xbfb8aa3b, v5
	v_fma_f32 v71, -v67, v70, 1.0
	v_fmac_f32_e32 v70, v71, v70
	v_div_scale_f32 v71, vcc, 1.0, v27, 1.0
	v_mul_f32_e32 v72, v71, v70
	v_fma_f32 v73, -v67, v72, v71
	v_fmac_f32_e32 v72, v73, v70
	v_fma_f32 v67, -v67, v72, v71
	v_div_scale_f32 v71, s[2:3], v26, v26, 1.0
	v_rcp_f32_e32 v73, v71
	v_div_fmas_f32 v67, v67, v70, v72
	v_div_fixup_f32 v27, v67, v27, 1.0
	v_div_scale_f32 v70, vcc, 1.0, v26, 1.0
	v_fma_f32 v67, -v71, v73, 1.0
	v_fmac_f32_e32 v73, v67, v73
	v_mul_f32_e32 v72, v70, v73
	v_fma_f32 v67, -v71, v72, v70
	v_fmac_f32_e32 v72, v67, v73
	v_mul_f32_e32 v67, 0xbfb8aa3b, v59
	v_exp_f32_e32 v67, v67
	v_fma_f32 v70, -v71, v72, v70
	v_div_fmas_f32 v70, v70, v73, v72
	v_div_fixup_f32 v26, v70, v26, 1.0
	v_pk_add_f32 v[66:67], v[66:67], 1.0 op_sel_hi:[1,0]
	v_pk_mul_f32 v[26:27], v[64:65], v[26:27]
	v_div_scale_f32 v71, s[2:3], v67, v67, 1.0
	v_rcp_f32_e32 v72, v71
	v_pk_mul_f32 v[26:27], v[132:133], v[26:27] op_sel_hi:[0,1]
	v_exp_f32_e32 v13, v12
	v_mul_f32_e32 v12, 0xbfb8aa3b, v4
	v_fma_f32 v64, -v71, v72, 1.0
	v_fmac_f32_e32 v72, v64, v72
	v_div_scale_f32 v64, vcc, 1.0, v67, 1.0
	v_mul_f32_e32 v65, v64, v72
	v_fma_f32 v70, -v71, v65, v64
	v_fmac_f32_e32 v65, v70, v72
	v_div_scale_f32 v70, s[2:3], v66, v66, 1.0
	v_fma_f32 v64, -v71, v65, v64
	v_rcp_f32_e32 v71, v70
	v_div_fmas_f32 v64, v64, v72, v65
	v_div_fixup_f32 v65, v64, v67, 1.0
	s_or_b32 s2, s14, 14
	v_fma_f32 v64, -v70, v71, 1.0
	v_fmac_f32_e32 v71, v64, v71
	v_div_scale_f32 v64, vcc, 1.0, v66, 1.0
	v_mul_f32_e32 v67, v64, v71
	v_fma_f32 v72, -v70, v67, v64
	v_fmac_f32_e32 v67, v72, v71
	v_fma_f32 v64, -v70, v67, v64
	v_div_fmas_f32 v64, v64, v71, v67
	v_div_fixup_f32 v64, v64, v66, 1.0
	v_pk_mul_f32 v[58:59], v[58:59], v[64:65]
	v_bfe_u32 v66, v63, 16, 1
	v_pk_mul_f32 v[58:59], v[132:133], v[58:59] op_sel_hi:[0,1]
	v_bfe_u32 v64, v59, 16, 1
	v_bfe_u32 v65, v58, 16, 1
	v_bfe_u32 v67, v62, 16, 1
	v_add3_u32 v62, v62, v67, s75
	v_add3_u32 v63, v63, v66, s75
	v_add3_u32 v58, v58, v65, s75
	v_add3_u32 v59, v59, v64, s75
	v_bfe_u32 v64, v56, 16, 1
	v_bfe_u32 v65, v57, 16, 1
	v_bfe_u32 v66, v26, 16, 1
	v_bfe_u32 v67, v27, 16, 1
	v_add3_u32 v27, v27, v67, s75
	v_add3_u32 v26, v26, v66, s75
	v_add3_u32 v57, v57, v65, s75
	v_add3_u32 v56, v56, v64, s75
	s_ashr_i32 s3, s2, 31
	v_lshrrev_b32_e32 v56, 16, v56
	v_lshrrev_b32_e32 v57, 16, v57
	v_lshrrev_b32_e32 v26, 16, v26
	v_lshrrev_b32_e32 v27, 16, v27
	s_lshl_b64 s[2:3], s[2:3], 11
	v_and_or_b32 v59, v59, s16, v27
	v_and_or_b32 v58, v58, s16, v26
	v_and_or_b32 v57, v63, s16, v57
	v_and_or_b32 v56, v62, s16, v56
	v_lshl_add_u64 v[26:27], v[128:129], 0, s[2:3]
	global_store_dwordx4 v[26:27], v[56:59], off sc1
	v_pk_fma_f32 v[26:27], v[30:31], v[68:69], v[46:47]
	v_and_b32_e32 v31, 0xffff0000, v1
	v_pk_fma_f32 v[26:27], v[38:39], v[60:61], v[26:27]
	v_and_b32_e32 v30, 0xffff0000, v0
	v_pk_fma_f32 v[26:27], v[42:43], v[50:51], v[26:27]
	v_lshlrev_b32_e32 v1, 16, v1
	v_pk_fma_f32 v[26:27], v[34:35], v[30:31], v[26:27]
	v_lshlrev_b32_e32 v0, 16, v0
	v_mul_f32_e32 v30, 0xbfb8aa3b, v27
	v_exp_f32_e32 v31, v30
	v_mul_f32_e32 v30, 0xbfb8aa3b, v26
	v_exp_f32_e32 v30, v30
	v_pk_fma_f32 v[8:9], v[100:101], v[0:1], v[8:9]
	v_exp_f32_e32 v12, v12
	v_mul_f32_e32 v0, 0xbfb8aa3b, v9
	v_pk_add_f32 v[20:21], v[30:31], 1.0 op_sel_hi:[1,0]
	v_exp_f32_e32 v1, v0
	v_div_scale_f32 v30, s[2:3], v21, v21, 1.0
	v_rcp_f32_e32 v31, v30
	v_pk_fma_f32 v[6:7], v[6:7], v[52:53], v[22:23]
	v_pk_add_f32 v[12:13], v[12:13], 1.0 op_sel_hi:[1,0]
	v_pk_fma_f32 v[6:7], v[18:19], v[48:49], v[6:7]
	v_fma_f32 v0, -v30, v31, 1.0
	v_fmac_f32_e32 v31, v0, v31
	v_div_scale_f32 v0, vcc, 1.0, v21, 1.0
	v_mul_f32_e32 v34, v0, v31
	v_fma_f32 v35, -v30, v34, v0
	v_fmac_f32_e32 v34, v35, v31
	v_fma_f32 v0, -v30, v34, v0
	v_div_scale_f32 v30, s[2:3], v20, v20, 1.0
	v_rcp_f32_e32 v35, v30
	v_div_fmas_f32 v0, v0, v31, v34
	v_div_fixup_f32 v21, v0, v21, 1.0
	v_div_scale_f32 v31, vcc, 1.0, v20, 1.0
	v_fma_f32 v0, -v30, v35, 1.0
	v_fmac_f32_e32 v35, v0, v35
	v_mul_f32_e32 v34, v31, v35
	v_fma_f32 v0, -v30, v34, v31
	v_fmac_f32_e32 v34, v0, v35
	v_mul_f32_e32 v0, 0xbfb8aa3b, v8
	v_exp_f32_e32 v0, v0
	v_fma_f32 v30, -v30, v34, v31
	v_div_fmas_f32 v34, v30, v35, v34
	v_div_fixup_f32 v20, v34, v20, 1.0
	v_pk_add_f32 v[30:31], v[0:1], 1.0 op_sel_hi:[1,0]
	v_pk_mul_f32 v[0:1], v[26:27], v[20:21]
	v_div_scale_f32 v35, s[2:3], v31, v31, 1.0
	v_rcp_f32_e32 v38, v35
	v_pk_fma_f32 v[6:7], v[14:15], v[16:17], v[6:7]
	v_div_scale_f32 v14, s[2:3], v13, v13, 1.0
	v_fma_f32 v20, -v35, v38, 1.0
	v_fmac_f32_e32 v38, v20, v38
	v_div_scale_f32 v20, vcc, 1.0, v31, 1.0
	v_mul_f32_e32 v21, v20, v38
	v_fma_f32 v26, -v35, v21, v20
	v_fmac_f32_e32 v21, v26, v38
	v_div_scale_f32 v26, s[2:3], v30, v30, 1.0
	v_rcp_f32_e32 v27, v26
	v_fma_f32 v20, -v35, v21, v20
	v_div_fmas_f32 v20, v20, v38, v21
	v_div_fixup_f32 v21, v20, v31, 1.0
	v_fma_f32 v20, -v26, v27, 1.0
	v_fmac_f32_e32 v27, v20, v27
	v_div_scale_f32 v20, vcc, 1.0, v30, 1.0
	v_rcp_f32_e32 v15, v14
	v_mul_f32_e32 v31, v20, v27
	v_fma_f32 v34, -v26, v31, v20
	v_fmac_f32_e32 v31, v34, v27
	v_fma_f32 v20, -v26, v31, v20
	v_pk_fma_f32 v[2:3], v[10:11], v[2:3], v[6:7]
	v_fma_f32 v7, -v14, v15, 1.0
	v_div_fmas_f32 v20, v20, v27, v31
	v_fmac_f32_e32 v15, v7, v15
	v_div_scale_f32 v7, vcc, 1.0, v13, 1.0
	v_mul_f32_e32 v10, v7, v15
	v_fma_f32 v11, -v14, v10, v7
	v_fmac_f32_e32 v10, v11, v15
	v_fma_f32 v7, -v14, v10, v7
	v_div_scale_f32 v14, s[2:3], v12, v12, 1.0
	v_rcp_f32_e32 v16, v14
	v_div_fmas_f32 v7, v7, v15, v10
	v_div_fixup_f32 v11, v7, v13, 1.0
	v_div_scale_f32 v10, vcc, 1.0, v12, 1.0
	v_fma_f32 v7, -v14, v16, 1.0
	v_fmac_f32_e32 v16, v7, v16
	v_mul_f32_e32 v13, v10, v16
	v_fma_f32 v7, -v14, v13, v10
	v_mul_f32_e32 v6, 0xbfb8aa3b, v2
	v_fmac_f32_e32 v13, v7, v16
	v_mul_f32_e32 v7, 0xbfb8aa3b, v3
	v_exp_f32_e32 v6, v6
	v_exp_f32_e32 v7, v7
	v_fma_f32 v10, -v14, v13, v10
	v_div_fmas_f32 v10, v10, v16, v13
	v_div_fixup_f32 v10, v10, v12, 1.0
	v_pk_add_f32 v[6:7], v[6:7], 1.0 op_sel_hi:[1,0]
	v_pk_mul_f32 v[4:5], v[4:5], v[10:11]
	v_div_scale_f32 v13, s[2:3], v7, v7, 1.0
	v_rcp_f32_e32 v14, v13
	v_div_fixup_f32 v20, v20, v30, 1.0
	v_pk_mul_f32 v[0:1], v[130:131], v[0:1] op_sel_hi:[0,1]
	v_pk_mul_f32 v[8:9], v[8:9], v[20:21]
	v_fma_f32 v10, -v13, v14, 1.0
	v_fmac_f32_e32 v14, v10, v14
	v_div_scale_f32 v10, vcc, 1.0, v7, 1.0
	v_mul_f32_e32 v11, v10, v14
	v_fma_f32 v12, -v13, v11, v10
	v_fmac_f32_e32 v11, v12, v14
	v_div_scale_f32 v12, s[2:3], v6, v6, 1.0
	v_fma_f32 v10, -v13, v11, v10
	v_rcp_f32_e32 v13, v12
	v_div_fmas_f32 v10, v10, v14, v11
	v_div_fixup_f32 v7, v10, v7, 1.0
	v_pk_mul_f32 v[8:9], v[130:131], v[8:9] op_sel_hi:[0,1]
	v_fma_f32 v10, -v12, v13, 1.0
	v_fmac_f32_e32 v13, v10, v13
	v_div_scale_f32 v10, vcc, 1.0, v6, 1.0
	v_mul_f32_e32 v11, v10, v13
	v_fma_f32 v14, -v12, v11, v10
	v_fmac_f32_e32 v11, v14, v13
	v_fma_f32 v10, -v12, v11, v10
	v_div_fmas_f32 v10, v10, v13, v11
	v_div_fixup_f32 v6, v10, v6, 1.0
	v_pk_mul_f32 v[2:3], v[2:3], v[6:7]
	v_pk_mul_f32 v[4:5], v[130:131], v[4:5] op_sel_hi:[0,1]
	v_pk_mul_f32 v[2:3], v[130:131], v[2:3] op_sel_hi:[0,1]
	v_bfe_u32 v6, v3, 16, 1
	v_bfe_u32 v7, v2, 16, 1
	v_bfe_u32 v10, v1, 16, 1
	v_bfe_u32 v11, v0, 16, 1
	v_add3_u32 v0, v0, v11, s75
	v_add3_u32 v1, v1, v10, s75
	v_add3_u32 v2, v2, v7, s75
	v_add3_u32 v3, v3, v6, s75
	v_bfe_u32 v6, v8, 16, 1
	v_bfe_u32 v7, v9, 16, 1
	v_bfe_u32 v10, v4, 16, 1
	v_bfe_u32 v11, v5, 16, 1
	s_or_b32 s2, s14, 15
	v_add3_u32 v5, v5, v11, s75
	v_add3_u32 v4, v4, v10, s75
	v_add3_u32 v7, v9, v7, s75
	v_add3_u32 v6, v8, v6, s75
	s_ashr_i32 s3, s2, 31
	v_lshrrev_b32_e32 v6, 16, v6
	v_lshrrev_b32_e32 v7, 16, v7
	v_lshrrev_b32_e32 v4, 16, v4
	v_lshrrev_b32_e32 v5, 16, v5
	s_lshl_b64 s[2:3], s[2:3], 11
	s_add_i32 s14, s14, s15
	v_and_or_b32 v3, v3, s16, v5
	v_and_or_b32 v2, v2, s16, v4
	v_and_or_b32 v1, v1, s16, v7
	v_and_or_b32 v0, v0, s16, v6
	v_lshl_add_u64 v[4:5], v[128:129], 0, s[2:3]
	s_cmpk_gt_i32 s12, 0xfff
	global_store_dwordx4 v[4:5], v[0:3], off sc1
	s_cbranch_scc1 .LBB0_461

.LBB0_687:
	v_mad_i64_i32 v[128:129], s[14:15], v178, s84, v[180:181]
	global_load_dwordx4 v[156:159], v[128:129], off offset:2048
	v_or_b32_e32 v192, 16, v178
	v_mad_i64_i32 v[128:129], s[14:15], v192, s84, v[180:181]
	global_load_dwordx4 v[152:155], v[128:129], off offset:2048
	v_or_b32_e32 v190, 32, v178
	v_mad_i64_i32 v[128:129], s[14:15], v190, s84, v[180:181]
	global_load_dwordx4 v[148:151], v[128:129], off offset:2048
	v_or_b32_e32 v188, 48, v178
	v_mad_i64_i32 v[128:129], s[14:15], v188, s84, v[180:181]
	v_add_u32_e32 v186, 0x80, v178
	global_load_dwordx4 v[144:147], v[128:129], off offset:2048
	v_mad_i64_i32 v[128:129], s[14:15], v186, s84, v[180:181]
	v_add_u32_e32 v184, 0x90, v178
	global_load_dwordx4 v[140:143], v[128:129], off offset:2048
	v_mad_i64_i32 v[128:129], s[14:15], v184, s84, v[180:181]
	v_add_u32_e32 v182, 0xa0, v178
	global_load_dwordx4 v[136:139], v[128:129], off offset:2048
	v_mad_i64_i32 v[128:129], s[14:15], v182, s84, v[180:181]
	v_add_u32_e32 v162, 0xb0, v178
	v_ashrrev_i32_e32 v179, 31, v178
	global_load_dwordx4 v[132:135], v[128:129], off offset:2048
	v_mad_i64_i32 v[128:129], s[14:15], v162, s84, v[180:181]
	v_or_b32_e32 v180, s53, v200
	global_load_dwordx4 v[128:131], v[128:129], off offset:2048
	v_ashrrev_i32_e32 v181, 31, v180
	v_ashrrev_i32_e32 v193, 31, v192
	v_ashrrev_i32_e32 v191, 31, v190
	v_ashrrev_i32_e32 v189, 31, v188
	v_ashrrev_i32_e32 v187, 31, v186
	v_ashrrev_i32_e32 v185, 31, v184
	v_ashrrev_i32_e32 v183, 31, v182
	v_ashrrev_i32_e32 v163, 31, v162
	s_mov_b64 s[14:15], -1
	s_and_b64 vcc, exec, s[2:3]
	s_waitcnt vmcnt(0)
	v_cvt_f32_ubyte0_e32 v160, v156
	v_mul_f32_e32 v160, 0x3b808081, v160
	v_mul_f32_e32 v124, v124, v160
	v_cvt_f32_ubyte0_e32 v160, v157
	v_mul_f32_e32 v160, 0x3b808081, v160
	v_mul_f32_e32 v120, v120, v160
	v_cvt_f32_ubyte1_e32 v160, v156
	v_mul_f32_e32 v160, 0x3b808081, v160
	v_mul_f32_e32 v125, v125, v160
	v_cvt_f32_ubyte1_e32 v160, v157
	v_mul_f32_e32 v160, 0x3b808081, v160
	v_mul_f32_e32 v121, v121, v160
	v_cvt_f32_ubyte2_e32 v160, v156
	v_mul_f32_e32 v160, 0x3b808081, v160
	v_mul_f32_e32 v126, v126, v160
	v_cvt_f32_ubyte2_e32 v160, v157
	v_mul_f32_e32 v160, 0x3b808081, v160
	v_mul_f32_e32 v160, v122, v160
	v_cvt_f32_ubyte3_e32 v122, v156
	v_mul_f32_e32 v122, 0x3b808081, v122
	v_mul_f32_e32 v127, v127, v122
	v_cvt_f32_ubyte3_e32 v122, v157
	v_mul_f32_e32 v122, 0x3b808081, v122
	v_mul_f32_e32 v156, v123, v122
	v_cvt_pk_bf16_f32 v122, v124, v125
	v_cvt_pk_bf16_f32 v123, v126, v127
	v_cvt_pk_bf16_f32 v124, v120, v121
	v_lshlrev_b64 v[120:121], 12, v[178:179]
	v_lshl_add_u64 v[126:127], s[8:9], 0, v[120:121]
	v_lshlrev_b64 v[120:121], 1, v[180:181]
	v_lshl_add_u64 v[126:127], v[126:127], 0, v[120:121]
	v_cvt_pk_bf16_f32 v125, v160, v156
	global_store_dwordx4 v[126:127], v[122:125], off sc1
	s_nop 1
	v_cvt_f32_ubyte0_e32 v122, v158
	v_mul_f32_e32 v122, 0x3b808081, v122
	v_mul_f32_e32 v116, v116, v122
	v_cvt_f32_ubyte0_e32 v122, v159
	v_mul_f32_e32 v122, 0x3b808081, v122
	v_mul_f32_e32 v122, v112, v122
	v_cvt_f32_ubyte1_e32 v112, v158
	v_mul_f32_e32 v112, 0x3b808081, v112
	v_mul_f32_e32 v112, v117, v112
	v_cvt_f32_ubyte1_e32 v117, v159
	v_mul_f32_e32 v117, 0x3b808081, v117
	v_mul_f32_e32 v117, v113, v117
	v_cvt_f32_ubyte2_e32 v113, v158
	v_mul_f32_e32 v113, 0x3b808081, v113
	v_mul_f32_e32 v113, v118, v113
	v_cvt_f32_ubyte2_e32 v118, v159
	v_mul_f32_e32 v118, 0x3b808081, v118
	v_mul_f32_e32 v118, v114, v118
	v_cvt_f32_ubyte3_e32 v114, v158
	v_mul_f32_e32 v114, 0x3b808081, v114
	v_mul_f32_e32 v114, v119, v114
	v_cvt_f32_ubyte3_e32 v119, v159
	v_mul_f32_e32 v119, 0x3b808081, v119
	v_mul_f32_e32 v115, v115, v119
	v_cvt_pk_bf16_f32 v112, v116, v112
	v_cvt_pk_bf16_f32 v113, v113, v114
	v_cvt_pk_bf16_f32 v114, v122, v117
	v_cvt_pk_bf16_f32 v115, v118, v115
	global_store_dwordx4 v[126:127], v[112:115], off offset:256 sc1
	s_nop 1
	v_cvt_f32_ubyte0_e32 v112, v152
	v_mul_f32_e32 v112, 0x3b808081, v112
	v_mul_f32_e32 v108, v108, v112
	v_cvt_f32_ubyte0_e32 v112, v153
	v_mul_f32_e32 v112, 0x3b808081, v112
	v_mul_f32_e32 v112, v104, v112
	v_cvt_f32_ubyte1_e32 v104, v152
	v_mul_f32_e32 v104, 0x3b808081, v104
	v_mul_f32_e32 v104, v109, v104
	v_cvt_f32_ubyte1_e32 v109, v153
	v_mul_f32_e32 v109, 0x3b808081, v109
	v_mul_f32_e32 v109, v105, v109
	v_cvt_f32_ubyte2_e32 v105, v152
	v_mul_f32_e32 v105, 0x3b808081, v105
	v_mul_f32_e32 v105, v110, v105
	v_cvt_f32_ubyte2_e32 v110, v153
	v_mul_f32_e32 v110, 0x3b808081, v110
	v_mul_f32_e32 v110, v106, v110
	v_cvt_f32_ubyte3_e32 v106, v152
	v_mul_f32_e32 v106, 0x3b808081, v106
	v_mul_f32_e32 v106, v111, v106
	v_cvt_f32_ubyte3_e32 v111, v153
	v_cvt_pk_bf16_f32 v104, v108, v104
	v_cvt_pk_bf16_f32 v105, v105, v106
	v_cvt_pk_bf16_f32 v106, v112, v109
	v_lshlrev_b64 v[108:109], 12, v[192:193]
	v_mul_f32_e32 v111, 0x3b808081, v111
	v_lshl_add_u64 v[108:109], s[8:9], 0, v[108:109]
	v_mul_f32_e32 v107, v107, v111
	v_lshl_add_u64 v[108:109], v[108:109], 0, v[120:121]
	v_cvt_pk_bf16_f32 v107, v110, v107
	global_store_dwordx4 v[108:109], v[104:107], off sc1
	s_nop 1
	v_cvt_f32_ubyte0_e32 v104, v154
	v_mul_f32_e32 v104, 0x3b808081, v104
	v_mul_f32_e32 v100, v100, v104
	v_cvt_f32_ubyte0_e32 v104, v155
	v_mul_f32_e32 v104, 0x3b808081, v104
	v_mul_f32_e32 v104, v96, v104
	v_cvt_f32_ubyte1_e32 v96, v154
	v_mul_f32_e32 v96, 0x3b808081, v96
	v_mul_f32_e32 v96, v101, v96
	v_cvt_f32_ubyte1_e32 v101, v155
	v_mul_f32_e32 v101, 0x3b808081, v101
	v_mul_f32_e32 v101, v97, v101
	v_cvt_f32_ubyte2_e32 v97, v154
	v_mul_f32_e32 v97, 0x3b808081, v97
	v_mul_f32_e32 v97, v102, v97
	v_cvt_f32_ubyte2_e32 v102, v155
	v_mul_f32_e32 v102, 0x3b808081, v102
	v_mul_f32_e32 v102, v98, v102
	v_cvt_f32_ubyte3_e32 v98, v154
	v_mul_f32_e32 v98, 0x3b808081, v98
	v_mul_f32_e32 v98, v103, v98
	v_cvt_f32_ubyte3_e32 v103, v155
	v_mul_f32_e32 v103, 0x3b808081, v103
	v_mul_f32_e32 v99, v99, v103
	v_cvt_pk_bf16_f32 v96, v100, v96
	v_cvt_pk_bf16_f32 v97, v97, v98
	v_cvt_pk_bf16_f32 v98, v104, v101
	v_cvt_pk_bf16_f32 v99, v102, v99
	global_store_dwordx4 v[108:109], v[96:99], off offset:256 sc1
	s_nop 1
	v_cvt_f32_ubyte0_e32 v96, v148
	v_mul_f32_e32 v96, 0x3b808081, v96
	v_mul_f32_e32 v92, v92, v96
	v_cvt_f32_ubyte0_e32 v96, v149
	v_mul_f32_e32 v96, 0x3b808081, v96
	v_mul_f32_e32 v96, v88, v96
	v_cvt_f32_ubyte1_e32 v88, v148
	v_mul_f32_e32 v88, 0x3b808081, v88
	v_mul_f32_e32 v88, v93, v88
	v_cvt_f32_ubyte1_e32 v93, v149
	v_mul_f32_e32 v93, 0x3b808081, v93
	v_mul_f32_e32 v93, v89, v93
	v_cvt_f32_ubyte2_e32 v89, v148
	v_mul_f32_e32 v89, 0x3b808081, v89
	v_mul_f32_e32 v89, v94, v89
	v_cvt_f32_ubyte2_e32 v94, v149
	v_mul_f32_e32 v94, 0x3b808081, v94
	v_mul_f32_e32 v94, v90, v94
	v_cvt_f32_ubyte3_e32 v90, v148
	v_mul_f32_e32 v90, 0x3b808081, v90
	v_mul_f32_e32 v90, v95, v90
	v_cvt_f32_ubyte3_e32 v95, v149
	v_cvt_pk_bf16_f32 v88, v92, v88
	v_cvt_pk_bf16_f32 v89, v89, v90
	v_cvt_pk_bf16_f32 v90, v96, v93
	v_lshlrev_b64 v[92:93], 12, v[190:191]
	v_mul_f32_e32 v95, 0x3b808081, v95
	v_lshl_add_u64 v[92:93], s[8:9], 0, v[92:93]
	v_mul_f32_e32 v91, v91, v95
	v_lshl_add_u64 v[92:93], v[92:93], 0, v[120:121]
	v_cvt_pk_bf16_f32 v91, v94, v91
	global_store_dwordx4 v[92:93], v[88:91], off sc1
	s_nop 1
	v_cvt_f32_ubyte0_e32 v88, v150
	v_mul_f32_e32 v88, 0x3b808081, v88
	v_mul_f32_e32 v84, v84, v88
	v_cvt_f32_ubyte0_e32 v88, v151
	v_mul_f32_e32 v88, 0x3b808081, v88
	v_mul_f32_e32 v88, v80, v88
	v_cvt_f32_ubyte1_e32 v80, v150
	v_mul_f32_e32 v80, 0x3b808081, v80
	v_mul_f32_e32 v80, v85, v80
	v_cvt_f32_ubyte1_e32 v85, v151
	v_mul_f32_e32 v85, 0x3b808081, v85
	v_mul_f32_e32 v85, v81, v85
	v_cvt_f32_ubyte2_e32 v81, v150
	v_mul_f32_e32 v81, 0x3b808081, v81
	v_mul_f32_e32 v81, v86, v81
	v_cvt_f32_ubyte2_e32 v86, v151
	v_mul_f32_e32 v86, 0x3b808081, v86
	v_mul_f32_e32 v86, v82, v86
	v_cvt_f32_ubyte3_e32 v82, v150
	v_mul_f32_e32 v82, 0x3b808081, v82
	v_mul_f32_e32 v82, v87, v82
	v_cvt_f32_ubyte3_e32 v87, v151
	v_mul_f32_e32 v87, 0x3b808081, v87
	v_mul_f32_e32 v83, v83, v87
	v_cvt_pk_bf16_f32 v80, v84, v80
	v_cvt_pk_bf16_f32 v81, v81, v82
	v_cvt_pk_bf16_f32 v82, v88, v85
	v_cvt_pk_bf16_f32 v83, v86, v83
	global_store_dwordx4 v[92:93], v[80:83], off offset:256 sc1
	s_nop 1
	v_cvt_f32_ubyte0_e32 v80, v144
	v_mul_f32_e32 v80, 0x3b808081, v80
	v_mul_f32_e32 v76, v76, v80
	v_cvt_f32_ubyte0_e32 v80, v145
	v_mul_f32_e32 v80, 0x3b808081, v80
	v_mul_f32_e32 v80, v72, v80
	v_cvt_f32_ubyte1_e32 v72, v144
	v_mul_f32_e32 v72, 0x3b808081, v72
	v_mul_f32_e32 v72, v77, v72
	v_cvt_f32_ubyte1_e32 v77, v145
	v_mul_f32_e32 v77, 0x3b808081, v77
	v_mul_f32_e32 v77, v73, v77
	v_cvt_f32_ubyte2_e32 v73, v144
	v_mul_f32_e32 v73, 0x3b808081, v73
	v_mul_f32_e32 v73, v78, v73
	v_cvt_f32_ubyte2_e32 v78, v145
	v_mul_f32_e32 v78, 0x3b808081, v78
	v_mul_f32_e32 v78, v74, v78
	v_cvt_f32_ubyte3_e32 v74, v144
	v_mul_f32_e32 v74, 0x3b808081, v74
	v_mul_f32_e32 v74, v79, v74
	v_cvt_f32_ubyte3_e32 v79, v145
	v_cvt_pk_bf16_f32 v72, v76, v72
	v_cvt_pk_bf16_f32 v73, v73, v74
	v_cvt_pk_bf16_f32 v74, v80, v77
	v_lshlrev_b64 v[76:77], 12, v[188:189]
	v_mul_f32_e32 v79, 0x3b808081, v79
	v_lshl_add_u64 v[76:77], s[8:9], 0, v[76:77]
	v_mul_f32_e32 v75, v75, v79
	v_lshl_add_u64 v[76:77], v[76:77], 0, v[120:121]
	v_cvt_pk_bf16_f32 v75, v78, v75
	global_store_dwordx4 v[76:77], v[72:75], off sc1
	s_nop 1
	v_cvt_f32_ubyte0_e32 v72, v146
	v_mul_f32_e32 v72, 0x3b808081, v72
	v_mul_f32_e32 v68, v68, v72
	v_cvt_f32_ubyte0_e32 v72, v147
	v_mul_f32_e32 v72, 0x3b808081, v72
	v_mul_f32_e32 v72, v64, v72
	v_cvt_f32_ubyte1_e32 v64, v146
	v_mul_f32_e32 v64, 0x3b808081, v64
	v_mul_f32_e32 v64, v69, v64
	v_cvt_f32_ubyte1_e32 v69, v147
	v_mul_f32_e32 v69, 0x3b808081, v69
	v_mul_f32_e32 v69, v65, v69
	v_cvt_f32_ubyte2_e32 v65, v146
	v_mul_f32_e32 v65, 0x3b808081, v65
	v_mul_f32_e32 v65, v70, v65
	v_cvt_f32_ubyte2_e32 v70, v147
	v_mul_f32_e32 v70, 0x3b808081, v70
	v_mul_f32_e32 v70, v66, v70
	v_cvt_f32_ubyte3_e32 v66, v146
	v_mul_f32_e32 v66, 0x3b808081, v66
	v_mul_f32_e32 v66, v71, v66
	v_cvt_f32_ubyte3_e32 v71, v147
	v_mul_f32_e32 v71, 0x3b808081, v71
	v_mul_f32_e32 v67, v67, v71
	v_cvt_pk_bf16_f32 v64, v68, v64
	v_cvt_pk_bf16_f32 v65, v65, v66
	v_cvt_pk_bf16_f32 v66, v72, v69
	v_cvt_pk_bf16_f32 v67, v70, v67
	global_store_dwordx4 v[76:77], v[64:67], off offset:256 sc1
	s_nop 1
	v_cvt_f32_ubyte0_e32 v64, v140
	v_mul_f32_e32 v64, 0x3b808081, v64
	v_mul_f32_e32 v60, v60, v64
	v_cvt_f32_ubyte0_e32 v64, v141
	v_mul_f32_e32 v64, 0x3b808081, v64
	v_mul_f32_e32 v64, v56, v64
	v_cvt_f32_ubyte1_e32 v56, v140
	v_mul_f32_e32 v56, 0x3b808081, v56
	v_mul_f32_e32 v56, v61, v56
	v_cvt_f32_ubyte1_e32 v61, v141
	v_mul_f32_e32 v61, 0x3b808081, v61
	v_mul_f32_e32 v61, v57, v61
	v_cvt_f32_ubyte2_e32 v57, v140
	v_mul_f32_e32 v57, 0x3b808081, v57
	v_mul_f32_e32 v57, v62, v57
	v_cvt_f32_ubyte2_e32 v62, v141
	v_mul_f32_e32 v62, 0x3b808081, v62
	v_mul_f32_e32 v62, v58, v62
	v_cvt_f32_ubyte3_e32 v58, v140
	v_mul_f32_e32 v58, 0x3b808081, v58
	v_mul_f32_e32 v58, v63, v58
	v_cvt_f32_ubyte3_e32 v63, v141
	v_cvt_pk_bf16_f32 v56, v60, v56
	v_cvt_pk_bf16_f32 v57, v57, v58
	v_cvt_pk_bf16_f32 v58, v64, v61
	v_lshlrev_b64 v[60:61], 12, v[186:187]
	v_mul_f32_e32 v63, 0x3b808081, v63
	v_lshl_add_u64 v[60:61], s[8:9], 0, v[60:61]
	v_mul_f32_e32 v59, v59, v63
	v_lshl_add_u64 v[60:61], v[60:61], 0, v[120:121]
	v_cvt_pk_bf16_f32 v59, v62, v59
	global_store_dwordx4 v[60:61], v[56:59], off sc1
	s_nop 1
	v_cvt_f32_ubyte0_e32 v56, v142
	v_mul_f32_e32 v56, 0x3b808081, v56
	v_mul_f32_e32 v52, v52, v56
	v_cvt_f32_ubyte0_e32 v56, v143
	v_mul_f32_e32 v56, 0x3b808081, v56
	v_mul_f32_e32 v56, v48, v56
	v_cvt_f32_ubyte1_e32 v48, v142
	v_mul_f32_e32 v48, 0x3b808081, v48
	v_mul_f32_e32 v48, v53, v48
	v_cvt_f32_ubyte1_e32 v53, v143
	v_mul_f32_e32 v53, 0x3b808081, v53
	v_mul_f32_e32 v53, v49, v53
	v_cvt_f32_ubyte2_e32 v49, v142
	v_mul_f32_e32 v49, 0x3b808081, v49
	v_mul_f32_e32 v49, v54, v49
	v_cvt_f32_ubyte2_e32 v54, v143
	v_mul_f32_e32 v54, 0x3b808081, v54
	v_mul_f32_e32 v54, v50, v54
	v_cvt_f32_ubyte3_e32 v50, v142
	v_mul_f32_e32 v50, 0x3b808081, v50
	v_mul_f32_e32 v50, v55, v50
	v_cvt_f32_ubyte3_e32 v55, v143
	v_mul_f32_e32 v55, 0x3b808081, v55
	v_mul_f32_e32 v51, v51, v55
	v_cvt_pk_bf16_f32 v48, v52, v48
	v_cvt_pk_bf16_f32 v49, v49, v50
	v_cvt_pk_bf16_f32 v50, v56, v53
	v_cvt_pk_bf16_f32 v51, v54, v51
	global_store_dwordx4 v[60:61], v[48:51], off offset:256 sc1
	s_nop 1
	v_cvt_f32_ubyte0_e32 v48, v136
	v_mul_f32_e32 v48, 0x3b808081, v48
	v_mul_f32_e32 v44, v44, v48
	v_cvt_f32_ubyte0_e32 v48, v137
	v_mul_f32_e32 v48, 0x3b808081, v48
	v_mul_f32_e32 v48, v40, v48
	v_cvt_f32_ubyte1_e32 v40, v136
	v_mul_f32_e32 v40, 0x3b808081, v40
	v_mul_f32_e32 v40, v45, v40
	v_cvt_f32_ubyte1_e32 v45, v137
	v_mul_f32_e32 v45, 0x3b808081, v45
	v_mul_f32_e32 v45, v41, v45
	v_cvt_f32_ubyte2_e32 v41, v136
	v_mul_f32_e32 v41, 0x3b808081, v41
	v_mul_f32_e32 v41, v46, v41
	v_cvt_f32_ubyte2_e32 v46, v137
	v_mul_f32_e32 v46, 0x3b808081, v46
	v_mul_f32_e32 v46, v42, v46
	v_cvt_f32_ubyte3_e32 v42, v136
	v_mul_f32_e32 v42, 0x3b808081, v42
	v_mul_f32_e32 v42, v47, v42
	v_cvt_f32_ubyte3_e32 v47, v137
	v_cvt_pk_bf16_f32 v40, v44, v40
	v_cvt_pk_bf16_f32 v41, v41, v42
	v_cvt_pk_bf16_f32 v42, v48, v45
	v_lshlrev_b64 v[44:45], 12, v[184:185]
	v_mul_f32_e32 v47, 0x3b808081, v47
	v_lshl_add_u64 v[44:45], s[8:9], 0, v[44:45]
	v_mul_f32_e32 v43, v43, v47
	v_lshl_add_u64 v[44:45], v[44:45], 0, v[120:121]
	v_cvt_pk_bf16_f32 v43, v46, v43
	global_store_dwordx4 v[44:45], v[40:43], off sc1
	s_nop 1
	v_cvt_f32_ubyte0_e32 v40, v138
	v_mul_f32_e32 v40, 0x3b808081, v40
	v_mul_f32_e32 v36, v36, v40
	v_cvt_f32_ubyte0_e32 v40, v139
	v_mul_f32_e32 v40, 0x3b808081, v40
	v_mul_f32_e32 v40, v32, v40
	v_cvt_f32_ubyte1_e32 v32, v138
	v_mul_f32_e32 v32, 0x3b808081, v32
	v_mul_f32_e32 v32, v37, v32
	v_cvt_f32_ubyte1_e32 v37, v139
	v_mul_f32_e32 v37, 0x3b808081, v37
	v_mul_f32_e32 v37, v33, v37
	v_cvt_f32_ubyte2_e32 v33, v138
	v_mul_f32_e32 v33, 0x3b808081, v33
	v_mul_f32_e32 v33, v38, v33
	v_cvt_f32_ubyte2_e32 v38, v139
	v_mul_f32_e32 v38, 0x3b808081, v38
	v_mul_f32_e32 v38, v34, v38
	v_cvt_f32_ubyte3_e32 v34, v138
	v_mul_f32_e32 v34, 0x3b808081, v34
	v_mul_f32_e32 v34, v39, v34
	v_cvt_f32_ubyte3_e32 v39, v139
	v_mul_f32_e32 v39, 0x3b808081, v39
	v_mul_f32_e32 v35, v35, v39
	v_cvt_pk_bf16_f32 v32, v36, v32
	v_cvt_pk_bf16_f32 v33, v33, v34
	v_cvt_pk_bf16_f32 v34, v40, v37
	v_cvt_pk_bf16_f32 v35, v38, v35
	global_store_dwordx4 v[44:45], v[32:35], off offset:256 sc1
	s_nop 1
	v_cvt_f32_ubyte0_e32 v32, v132
	v_mul_f32_e32 v32, 0x3b808081, v32
	v_mul_f32_e32 v28, v28, v32
	v_cvt_f32_ubyte0_e32 v32, v133
	v_mul_f32_e32 v32, 0x3b808081, v32
	v_mul_f32_e32 v32, v24, v32
	v_cvt_f32_ubyte1_e32 v24, v132
	v_mul_f32_e32 v24, 0x3b808081, v24
	v_mul_f32_e32 v24, v29, v24
	v_cvt_f32_ubyte1_e32 v29, v133
	v_mul_f32_e32 v29, 0x3b808081, v29
	v_mul_f32_e32 v29, v25, v29
	v_cvt_f32_ubyte2_e32 v25, v132
	v_mul_f32_e32 v25, 0x3b808081, v25
	v_mul_f32_e32 v25, v30, v25
	v_cvt_f32_ubyte2_e32 v30, v133
	v_mul_f32_e32 v30, 0x3b808081, v30
	v_mul_f32_e32 v30, v26, v30
	v_cvt_f32_ubyte3_e32 v26, v132
	v_mul_f32_e32 v26, 0x3b808081, v26
	v_mul_f32_e32 v26, v31, v26
	v_cvt_f32_ubyte3_e32 v31, v133
	v_cvt_pk_bf16_f32 v24, v28, v24
	v_cvt_pk_bf16_f32 v25, v25, v26
	v_cvt_pk_bf16_f32 v26, v32, v29
	v_lshlrev_b64 v[28:29], 12, v[182:183]
	v_mul_f32_e32 v31, 0x3b808081, v31
	v_lshl_add_u64 v[28:29], s[8:9], 0, v[28:29]
	v_mul_f32_e32 v27, v27, v31
	v_lshl_add_u64 v[28:29], v[28:29], 0, v[120:121]
	v_cvt_pk_bf16_f32 v27, v30, v27
	global_store_dwordx4 v[28:29], v[24:27], off sc1
	s_nop 1
	v_cvt_f32_ubyte0_e32 v24, v134
	v_mul_f32_e32 v24, 0x3b808081, v24
	v_mul_f32_e32 v20, v20, v24
	v_cvt_f32_ubyte0_e32 v24, v135
	v_mul_f32_e32 v24, 0x3b808081, v24
	v_mul_f32_e32 v24, v16, v24
	v_cvt_f32_ubyte1_e32 v16, v134
	v_mul_f32_e32 v16, 0x3b808081, v16
	v_mul_f32_e32 v16, v21, v16
	v_cvt_f32_ubyte1_e32 v21, v135
	v_mul_f32_e32 v21, 0x3b808081, v21
	v_mul_f32_e32 v21, v17, v21
	v_cvt_f32_ubyte2_e32 v17, v134
	v_mul_f32_e32 v17, 0x3b808081, v17
	v_mul_f32_e32 v17, v22, v17
	v_cvt_f32_ubyte2_e32 v22, v135
	v_mul_f32_e32 v22, 0x3b808081, v22
	v_mul_f32_e32 v22, v18, v22
	v_cvt_f32_ubyte3_e32 v18, v134
	v_mul_f32_e32 v18, 0x3b808081, v18
	v_mul_f32_e32 v18, v23, v18
	v_cvt_f32_ubyte3_e32 v23, v135
	v_mul_f32_e32 v23, 0x3b808081, v23
	v_mul_f32_e32 v19, v19, v23
	v_cvt_pk_bf16_f32 v16, v20, v16
	v_cvt_pk_bf16_f32 v17, v17, v18
	v_cvt_pk_bf16_f32 v18, v24, v21
	v_cvt_pk_bf16_f32 v19, v22, v19
	global_store_dwordx4 v[28:29], v[16:19], off offset:256 sc1
	s_nop 1
	v_cvt_f32_ubyte0_e32 v16, v128
	v_mul_f32_e32 v16, 0x3b808081, v16
	v_mul_f32_e32 v12, v12, v16
	v_cvt_f32_ubyte0_e32 v16, v129
	v_mul_f32_e32 v16, 0x3b808081, v16
	v_mul_f32_e32 v16, v8, v16
	v_cvt_f32_ubyte1_e32 v8, v128
	v_mul_f32_e32 v8, 0x3b808081, v8
	v_mul_f32_e32 v8, v13, v8
	v_cvt_f32_ubyte1_e32 v13, v129
	v_mul_f32_e32 v13, 0x3b808081, v13
	v_mul_f32_e32 v13, v9, v13
	v_cvt_f32_ubyte2_e32 v9, v128
	v_mul_f32_e32 v9, 0x3b808081, v9
	v_mul_f32_e32 v9, v14, v9
	v_cvt_f32_ubyte2_e32 v14, v129
	v_mul_f32_e32 v14, 0x3b808081, v14
	v_mul_f32_e32 v14, v10, v14
	v_cvt_f32_ubyte3_e32 v10, v128
	v_mul_f32_e32 v10, 0x3b808081, v10
	v_mul_f32_e32 v10, v15, v10
	v_cvt_f32_ubyte3_e32 v15, v129
	v_cvt_pk_bf16_f32 v8, v12, v8
	v_cvt_pk_bf16_f32 v9, v9, v10
	v_cvt_pk_bf16_f32 v10, v16, v13
	v_lshlrev_b64 v[12:13], 12, v[162:163]
	v_mul_f32_e32 v15, 0x3b808081, v15
	v_lshl_add_u64 v[12:13], s[8:9], 0, v[12:13]
	v_mul_f32_e32 v11, v11, v15
	v_lshl_add_u64 v[12:13], v[12:13], 0, v[120:121]
	v_cvt_pk_bf16_f32 v11, v14, v11
	global_store_dwordx4 v[12:13], v[8:11], off sc1
	s_nop 1
	v_cvt_f32_ubyte0_e32 v8, v130
	v_mul_f32_e32 v8, 0x3b808081, v8
	v_mul_f32_e32 v4, v4, v8
	v_cvt_f32_ubyte0_e32 v8, v131
	v_mul_f32_e32 v8, 0x3b808081, v8
	v_mul_f32_e32 v8, v0, v8
	v_cvt_f32_ubyte1_e32 v0, v130
	v_mul_f32_e32 v0, 0x3b808081, v0
	v_mul_f32_e32 v0, v5, v0
	v_cvt_f32_ubyte1_e32 v5, v131
	v_mul_f32_e32 v5, 0x3b808081, v5
	v_mul_f32_e32 v5, v1, v5
	v_cvt_f32_ubyte2_e32 v1, v130
	v_mul_f32_e32 v1, 0x3b808081, v1
	v_mul_f32_e32 v1, v6, v1
	v_cvt_f32_ubyte2_e32 v6, v131
	v_mul_f32_e32 v6, 0x3b808081, v6
	v_mul_f32_e32 v6, v2, v6
	v_cvt_f32_ubyte3_e32 v2, v130
	v_mul_f32_e32 v2, 0x3b808081, v2
	v_mul_f32_e32 v2, v7, v2
	v_cvt_f32_ubyte3_e32 v7, v131
	v_mul_f32_e32 v7, 0x3b808081, v7
	v_mul_f32_e32 v3, v3, v7
	v_cvt_pk_bf16_f32 v0, v4, v0
	v_cvt_pk_bf16_f32 v1, v1, v2
	v_cvt_pk_bf16_f32 v2, v8, v5
	v_cvt_pk_bf16_f32 v3, v6, v3
	global_store_dwordx4 v[12:13], v[0:3], off offset:256 sc1
	s_cbranch_vccnz .LBB0_670
	s_andn2_b64 vcc, exec, s[0:1]
	s_cbranch_vccnz .LBB0_669
	s_barrier
	s_branch .LBB0_669

.LBB0_751:
	v_add_u32_e32 v120, s13, v230
	v_add_u32_e32 v148, s29, v230
	ds_read_b128 v[88:91], v120
	ds_read_b128 v[100:103], v120 offset:1024
	ds_read_b128 v[112:115], v120 offset:2048
	ds_read_b128 v[120:123], v120 offset:3072
	ds_read_b128 v[124:127], v148
	ds_read_b128 v[140:143], v148 offset:1024
	ds_read_b128 v[144:147], v148 offset:2048
	ds_read_b128 v[148:151], v148 offset:3072
	s_add_u32 s16, s14, 0xfff80080
	s_addc_u32 s17, s15, -1
	s_cmp_eq_u32 s54, 28
	s_cselect_b32 s19, s7, s17
	s_cselect_b32 s18, s50, s16
	s_cselect_b32 s17, s5, s53
	s_cselect_b32 s16, s51, s52
	v_lshl_add_u64 v[206:207], s[14:15], 0, v[204:205]
	s_add_i32 m0, s34, 0xc000
	ds_read_b128 v[152:155], v232
	ds_read_b128 v[170:173], v232 offset:1024
	ds_read_b128 v[174:177], v232 offset:2048
	ds_read_b128 v[178:181], v232 offset:3072
	ds_read_b128 v[182:185], v232 offset:4096
	ds_read_b128 v[186:189], v232 offset:5120
	ds_read_b128 v[190:193], v232 offset:6144
	ds_read_b128 v[194:197], v232 offset:7168
	global_load_lds_dwordx4 v[206:207], off
	v_lshl_add_u64 v[206:207], s[14:15], 0, v[202:203]
	s_add_i32 m0, s34, 0xe000
	s_nop 0
	global_load_lds_dwordx4 v[206:207], off
	s_waitcnt vmcnt(8)
	s_waitcnt lgkmcnt(0)
	s_barrier
	s_setprio 1
	s_waitcnt lgkmcnt(0)
	v_mfma_f32_16x16x32_bf16 v[166:169], v[88:91], v[152:155], v[166:169]
	v_mfma_f32_16x16x32_bf16 v[156:159], v[112:115], v[152:155], v[156:159]
	v_mfma_f32_16x16x32_bf16 v[128:131], v[88:91], v[174:177], v[128:131]
	v_mfma_f32_16x16x32_bf16 v[116:119], v[112:115], v[174:177], v[116:119]
	v_mfma_f32_16x16x32_bf16 v[96:99], v[88:91], v[182:185], v[96:99]
	v_mfma_f32_16x16x32_bf16 v[92:95], v[112:115], v[182:185], v[92:95]
	v_mfma_f32_16x16x32_bf16 v[76:79], v[88:91], v[190:193], v[76:79]
	v_mfma_f32_16x16x32_bf16 v[72:75], v[112:115], v[190:193], v[72:75]
	v_mfma_f32_16x16x32_bf16 v[166:169], v[100:103], v[170:173], v[166:169]
	v_mfma_f32_16x16x32_bf16 v[156:159], v[120:123], v[170:173], v[156:159]
	v_mfma_f32_16x16x32_bf16 v[128:131], v[100:103], v[178:181], v[128:131]
	v_mfma_f32_16x16x32_bf16 v[116:119], v[120:123], v[178:181], v[116:119]
	v_mfma_f32_16x16x32_bf16 v[96:99], v[100:103], v[186:189], v[96:99]
	v_mfma_f32_16x16x32_bf16 v[92:95], v[120:123], v[186:189], v[92:95]
	v_mfma_f32_16x16x32_bf16 v[76:79], v[100:103], v[194:197], v[76:79]
	v_mfma_f32_16x16x32_bf16 v[72:75], v[120:123], v[194:197], v[72:75]
	s_setprio 0
	s_setprio 1
	v_mfma_f32_16x16x32_bf16 v[136:139], v[124:127], v[152:155], v[136:139]
	v_mfma_f32_16x16x32_bf16 v[132:135], v[144:147], v[152:155], v[132:135]
	v_mfma_f32_16x16x32_bf16 v[108:111], v[124:127], v[174:177], v[108:111]
	v_mfma_f32_16x16x32_bf16 v[104:107], v[144:147], v[174:177], v[104:107]
	v_mfma_f32_16x16x32_bf16 v[84:87], v[124:127], v[182:185], v[84:87]
	v_mfma_f32_16x16x32_bf16 v[80:83], v[144:147], v[182:185], v[80:83]
	v_mfma_f32_16x16x32_bf16 v[68:71], v[124:127], v[190:193], v[68:71]
	v_mfma_f32_16x16x32_bf16 v[64:67], v[144:147], v[190:193], v[64:67]
	v_mfma_f32_16x16x32_bf16 v[136:139], v[140:143], v[170:173], v[136:139]
	v_mfma_f32_16x16x32_bf16 v[132:135], v[148:151], v[170:173], v[132:135]
	v_mfma_f32_16x16x32_bf16 v[108:111], v[140:143], v[178:181], v[108:111]
	v_mfma_f32_16x16x32_bf16 v[104:107], v[148:151], v[178:181], v[104:107]
	v_mfma_f32_16x16x32_bf16 v[84:87], v[140:143], v[186:189], v[84:87]
	v_mfma_f32_16x16x32_bf16 v[80:83], v[148:151], v[186:189], v[80:83]
	v_mfma_f32_16x16x32_bf16 v[68:71], v[140:143], v[194:197], v[68:71]
	v_mfma_f32_16x16x32_bf16 v[64:67], v[148:151], v[194:197], v[64:67]
	s_setprio 0
	s_barrier
	s_mov_b32 m0, s27
	v_lshl_add_u64 v[206:207], s[16:17], 0, v[160:161]
	s_add_u32 s56, s16, 0x80000
	ds_read_b128 v[152:155], v232 offset:16384
	ds_read_b128 v[170:173], v232 offset:17408
	ds_read_b128 v[174:177], v232 offset:18432
	ds_read_b128 v[178:181], v232 offset:19456
	ds_read_b128 v[182:185], v232 offset:20480
	ds_read_b128 v[186:189], v232 offset:21504
	ds_read_b128 v[190:193], v232 offset:22528
	ds_read_b128 v[194:197], v232 offset:23552
	global_load_lds_dwordx4 v[206:207], off
	v_lshl_add_u64 v[208:209], s[16:17], 0, v[200:201]
	s_mov_b32 m0, s28
	s_addc_u32 s57, s17, 0
	global_load_lds_dwordx4 v[208:209], off
	v_lshl_add_u64 v[210:211], s[56:57], 0, v[160:161]
	s_mov_b32 m0, s30
	v_lshl_add_u64 v[212:213], s[18:19], 0, v[198:199]
	global_load_lds_dwordx4 v[210:211], off
	v_lshl_add_u64 v[210:211], s[56:57], 0, v[200:201]
	s_mov_b32 m0, s31
	s_nop 0
	global_load_lds_dwordx4 v[210:211], off
	v_lshl_add_u64 v[210:211], s[18:19], 0, v[162:163]
	s_mov_b32 m0, s34
	s_nop 0
	global_load_lds_dwordx4 v[210:211], off
	s_mov_b32 m0, s35
	s_nop 0
	global_load_lds_dwordx4 v[212:213], off
	s_waitcnt vmcnt(8)
	s_waitcnt lgkmcnt(0)
	s_barrier
	s_setprio 1
	s_waitcnt lgkmcnt(0)
	v_mfma_f32_16x16x32_bf16 v[60:63], v[88:91], v[152:155], v[60:63]
	v_mfma_f32_16x16x32_bf16 v[56:59], v[112:115], v[152:155], v[56:59]
	v_mfma_f32_16x16x32_bf16 v[44:47], v[88:91], v[174:177], v[44:47]
	v_mfma_f32_16x16x32_bf16 v[40:43], v[112:115], v[174:177], v[40:43]
	v_mfma_f32_16x16x32_bf16 v[28:31], v[88:91], v[182:185], v[28:31]
	v_mfma_f32_16x16x32_bf16 v[24:27], v[112:115], v[182:185], v[24:27]
	v_mfma_f32_16x16x32_bf16 v[12:15], v[88:91], v[190:193], v[12:15]
	v_mfma_f32_16x16x32_bf16 v[8:11], v[112:115], v[190:193], v[8:11]
	v_mfma_f32_16x16x32_bf16 v[60:63], v[100:103], v[170:173], v[60:63]
	v_mfma_f32_16x16x32_bf16 v[56:59], v[120:123], v[170:173], v[56:59]
	v_mfma_f32_16x16x32_bf16 v[44:47], v[100:103], v[178:181], v[44:47]
	v_mfma_f32_16x16x32_bf16 v[40:43], v[120:123], v[178:181], v[40:43]
	v_mfma_f32_16x16x32_bf16 v[28:31], v[100:103], v[186:189], v[28:31]
	v_mfma_f32_16x16x32_bf16 v[24:27], v[120:123], v[186:189], v[24:27]
	v_mfma_f32_16x16x32_bf16 v[12:15], v[100:103], v[194:197], v[12:15]
	v_mfma_f32_16x16x32_bf16 v[8:11], v[120:123], v[194:197], v[8:11]
	s_setprio 0
	s_setprio 1
	v_mfma_f32_16x16x32_bf16 v[52:55], v[124:127], v[152:155], v[52:55]
	v_mfma_f32_16x16x32_bf16 v[48:51], v[144:147], v[152:155], v[48:51]
	v_mfma_f32_16x16x32_bf16 v[36:39], v[124:127], v[174:177], v[36:39]
	v_mfma_f32_16x16x32_bf16 v[32:35], v[144:147], v[174:177], v[32:35]
	v_mfma_f32_16x16x32_bf16 v[20:23], v[124:127], v[182:185], v[20:23]
	v_mfma_f32_16x16x32_bf16 v[16:19], v[144:147], v[182:185], v[16:19]
	v_mfma_f32_16x16x32_bf16 v[4:7], v[124:127], v[190:193], v[4:7]
	v_mfma_f32_16x16x32_bf16 v[0:3], v[144:147], v[190:193], v[0:3]
	v_mfma_f32_16x16x32_bf16 v[52:55], v[140:143], v[170:173], v[52:55]
	v_mfma_f32_16x16x32_bf16 v[48:51], v[148:151], v[170:173], v[48:51]
	v_mfma_f32_16x16x32_bf16 v[36:39], v[140:143], v[178:181], v[36:39]
	v_mfma_f32_16x16x32_bf16 v[32:35], v[148:151], v[178:181], v[32:35]
	v_mfma_f32_16x16x32_bf16 v[20:23], v[140:143], v[186:189], v[20:23]
	v_mfma_f32_16x16x32_bf16 v[16:19], v[148:151], v[186:189], v[16:19]
	v_mfma_f32_16x16x32_bf16 v[4:7], v[140:143], v[194:197], v[4:7]
	v_mfma_f32_16x16x32_bf16 v[0:3], v[148:151], v[194:197], v[0:3]
	s_setprio 0
	s_barrier
	v_add_u32_e32 v120, s39, v230
	v_add_u32_e32 v148, s44, v230
	ds_read_b128 v[88:91], v120
	ds_read_b128 v[100:103], v120 offset:1024
	ds_read_b128 v[112:115], v120 offset:2048
	ds_read_b128 v[120:123], v120 offset:3072
	ds_read_b128 v[124:127], v148
	ds_read_b128 v[140:143], v148 offset:1024
	ds_read_b128 v[144:147], v148 offset:2048
	ds_read_b128 v[148:151], v148 offset:3072
	s_add_u32 s18, s18, 0x80000
	s_addc_u32 s19, s19, 0
	s_mov_b32 m0, s36
	v_lshl_add_u64 v[214:215], s[18:19], 0, v[162:163]
	ds_read_b128 v[152:155], v232 offset:32768
	ds_read_b128 v[170:173], v232 offset:33792
	ds_read_b128 v[174:177], v232 offset:34816
	ds_read_b128 v[178:181], v232 offset:35840
	ds_read_b128 v[182:185], v232 offset:36864
	ds_read_b128 v[186:189], v232 offset:37888
	ds_read_b128 v[190:193], v232 offset:38912
	ds_read_b128 v[194:197], v232 offset:39936
	global_load_lds_dwordx4 v[214:215], off
	v_lshl_add_u64 v[214:215], s[18:19], 0, v[198:199]
	s_mov_b32 m0, s37
	s_nop 0
	global_load_lds_dwordx4 v[214:215], off
	s_waitcnt vmcnt(8)
	s_waitcnt lgkmcnt(0)
	s_barrier
	s_setprio 1
	s_waitcnt lgkmcnt(0)
	v_mfma_f32_16x16x32_bf16 v[166:169], v[88:91], v[152:155], v[166:169]
	v_mfma_f32_16x16x32_bf16 v[156:159], v[112:115], v[152:155], v[156:159]
	v_mfma_f32_16x16x32_bf16 v[128:131], v[88:91], v[174:177], v[128:131]
	v_mfma_f32_16x16x32_bf16 v[116:119], v[112:115], v[174:177], v[116:119]
	v_mfma_f32_16x16x32_bf16 v[96:99], v[88:91], v[182:185], v[96:99]
	v_mfma_f32_16x16x32_bf16 v[92:95], v[112:115], v[182:185], v[92:95]
	v_mfma_f32_16x16x32_bf16 v[76:79], v[88:91], v[190:193], v[76:79]
	v_mfma_f32_16x16x32_bf16 v[72:75], v[112:115], v[190:193], v[72:75]
	v_mfma_f32_16x16x32_bf16 v[166:169], v[100:103], v[170:173], v[166:169]
	v_mfma_f32_16x16x32_bf16 v[156:159], v[120:123], v[170:173], v[156:159]
	v_mfma_f32_16x16x32_bf16 v[128:131], v[100:103], v[178:181], v[128:131]
	v_mfma_f32_16x16x32_bf16 v[116:119], v[120:123], v[178:181], v[116:119]
	v_mfma_f32_16x16x32_bf16 v[96:99], v[100:103], v[186:189], v[96:99]
	v_mfma_f32_16x16x32_bf16 v[92:95], v[120:123], v[186:189], v[92:95]
	v_mfma_f32_16x16x32_bf16 v[76:79], v[100:103], v[194:197], v[76:79]
	v_mfma_f32_16x16x32_bf16 v[72:75], v[120:123], v[194:197], v[72:75]
	s_setprio 0
	s_setprio 1
	v_mfma_f32_16x16x32_bf16 v[136:139], v[124:127], v[152:155], v[136:139]
	v_mfma_f32_16x16x32_bf16 v[132:135], v[144:147], v[152:155], v[132:135]
	v_mfma_f32_16x16x32_bf16 v[108:111], v[124:127], v[174:177], v[108:111]
	v_mfma_f32_16x16x32_bf16 v[104:107], v[144:147], v[174:177], v[104:107]
	v_mfma_f32_16x16x32_bf16 v[84:87], v[124:127], v[182:185], v[84:87]
	v_mfma_f32_16x16x32_bf16 v[80:83], v[144:147], v[182:185], v[80:83]
	v_mfma_f32_16x16x32_bf16 v[68:71], v[124:127], v[190:193], v[68:71]
	v_mfma_f32_16x16x32_bf16 v[64:67], v[144:147], v[190:193], v[64:67]
	v_mfma_f32_16x16x32_bf16 v[136:139], v[140:143], v[170:173], v[136:139]
	v_mfma_f32_16x16x32_bf16 v[132:135], v[148:151], v[170:173], v[132:135]
	v_mfma_f32_16x16x32_bf16 v[108:111], v[140:143], v[178:181], v[108:111]
	v_mfma_f32_16x16x32_bf16 v[104:107], v[148:151], v[178:181], v[104:107]
	v_mfma_f32_16x16x32_bf16 v[84:87], v[140:143], v[186:189], v[84:87]
	v_mfma_f32_16x16x32_bf16 v[80:83], v[148:151], v[186:189], v[80:83]
	v_mfma_f32_16x16x32_bf16 v[68:71], v[140:143], v[194:197], v[68:71]
	v_mfma_f32_16x16x32_bf16 v[64:67], v[148:151], v[194:197], v[64:67]
	s_setprio 0
	s_barrier
	s_mov_b32 m0, s40
	v_lshl_add_u64 v[206:207], v[206:207], 0, s[86:87]
	s_add_u32 s16, s16, 0x80080
	ds_read_b128 v[152:155], v232 offset:49152
	ds_read_b128 v[170:173], v232 offset:50176
	ds_read_b128 v[174:177], v232 offset:51200
	ds_read_b128 v[178:181], v232 offset:52224
	ds_read_b128 v[182:185], v232 offset:53248
	ds_read_b128 v[186:189], v232 offset:54272
	ds_read_b128 v[190:193], v232 offset:55296
	ds_read_b128 v[194:197], v232 offset:56320
	global_load_lds_dwordx4 v[206:207], off
	v_lshl_add_u64 v[206:207], v[208:209], 0, s[86:87]
	s_mov_b32 m0, s41
	s_addc_u32 s17, s17, 0
	global_load_lds_dwordx4 v[206:207], off
	v_lshl_add_u64 v[206:207], s[16:17], 0, v[160:161]
	s_mov_b32 m0, s45
	s_nop 0
	global_load_lds_dwordx4 v[206:207], off
	v_lshl_add_u64 v[206:207], s[16:17], 0, v[200:201]
	s_mov_b32 m0, s46
	s_nop 0
	global_load_lds_dwordx4 v[206:207], off
	v_lshl_add_u64 v[206:207], v[210:211], 0, s[86:87]
	s_mov_b32 m0, s42
	s_nop 0
	global_load_lds_dwordx4 v[206:207], off
	v_lshl_add_u64 v[206:207], v[212:213], 0, s[86:87]
	s_mov_b32 m0, s43
	s_nop 0
	global_load_lds_dwordx4 v[206:207], off
	s_waitcnt vmcnt(8)
	s_waitcnt lgkmcnt(0)
	s_barrier
	s_setprio 1
	s_waitcnt lgkmcnt(0)
	v_mfma_f32_16x16x32_bf16 v[60:63], v[88:91], v[152:155], v[60:63]
	v_mfma_f32_16x16x32_bf16 v[56:59], v[112:115], v[152:155], v[56:59]
	v_mfma_f32_16x16x32_bf16 v[44:47], v[88:91], v[174:177], v[44:47]
	v_mfma_f32_16x16x32_bf16 v[40:43], v[112:115], v[174:177], v[40:43]
	v_mfma_f32_16x16x32_bf16 v[28:31], v[88:91], v[182:185], v[28:31]
	v_mfma_f32_16x16x32_bf16 v[24:27], v[112:115], v[182:185], v[24:27]
	v_mfma_f32_16x16x32_bf16 v[12:15], v[88:91], v[190:193], v[12:15]
	v_mfma_f32_16x16x32_bf16 v[8:11], v[112:115], v[190:193], v[8:11]
	v_mfma_f32_16x16x32_bf16 v[60:63], v[100:103], v[170:173], v[60:63]
	v_mfma_f32_16x16x32_bf16 v[56:59], v[120:123], v[170:173], v[56:59]
	v_mfma_f32_16x16x32_bf16 v[44:47], v[100:103], v[178:181], v[44:47]
	v_mfma_f32_16x16x32_bf16 v[40:43], v[120:123], v[178:181], v[40:43]
	v_mfma_f32_16x16x32_bf16 v[28:31], v[100:103], v[186:189], v[28:31]
	v_mfma_f32_16x16x32_bf16 v[24:27], v[120:123], v[186:189], v[24:27]
	v_mfma_f32_16x16x32_bf16 v[12:15], v[100:103], v[194:197], v[12:15]
	v_mfma_f32_16x16x32_bf16 v[8:11], v[120:123], v[194:197], v[8:11]
	s_setprio 0
	s_setprio 1
	v_mfma_f32_16x16x32_bf16 v[52:55], v[124:127], v[152:155], v[52:55]
	v_mfma_f32_16x16x32_bf16 v[48:51], v[144:147], v[152:155], v[48:51]
	v_mfma_f32_16x16x32_bf16 v[36:39], v[124:127], v[174:177], v[36:39]
	v_mfma_f32_16x16x32_bf16 v[32:35], v[144:147], v[174:177], v[32:35]
	v_mfma_f32_16x16x32_bf16 v[20:23], v[124:127], v[182:185], v[20:23]
	v_mfma_f32_16x16x32_bf16 v[16:19], v[144:147], v[182:185], v[16:19]
	v_mfma_f32_16x16x32_bf16 v[4:7], v[124:127], v[190:193], v[4:7]
	v_mfma_f32_16x16x32_bf16 v[0:3], v[144:147], v[190:193], v[0:3]
	v_mfma_f32_16x16x32_bf16 v[52:55], v[140:143], v[170:173], v[52:55]
	v_mfma_f32_16x16x32_bf16 v[48:51], v[148:151], v[170:173], v[48:51]
	v_mfma_f32_16x16x32_bf16 v[36:39], v[140:143], v[178:181], v[36:39]
	v_mfma_f32_16x16x32_bf16 v[32:35], v[148:151], v[178:181], v[32:35]
	v_mfma_f32_16x16x32_bf16 v[20:23], v[140:143], v[186:189], v[20:23]
	v_mfma_f32_16x16x32_bf16 v[16:19], v[148:151], v[186:189], v[16:19]
	v_mfma_f32_16x16x32_bf16 v[4:7], v[140:143], v[194:197], v[4:7]
	v_mfma_f32_16x16x32_bf16 v[0:3], v[148:151], v[194:197], v[0:3]
	s_setprio 0
	s_barrier
	s_add_i32 s54, s54, 2
	s_add_u32 s52, s52, 0x100
	s_addc_u32 s53, s53, 0
	s_add_u32 s14, s14, 0x100
	s_addc_u32 s15, s15, 0
	s_cmp_gt_u32 s54, 29
	s_cbranch_scc0 .LBB0_751
	v_lshl_or_b32 v90, s49, 8, v231
	v_lshl_add_u32 v88, s12, 8, v165
	v_ashrrev_i32_e32 v91, 31, v90
	v_lshlrev_b64 v[206:207], 1, v[90:91]
	v_ashrrev_i32_e32 v89, 31, v88
	v_lshl_add_u64 v[90:91], s[0:1], 0, v[206:207]
	v_lshlrev_b64 v[222:223], 12, v[88:89]
	v_lshl_add_u64 v[100:101], v[90:91], 0, v[222:223]
	global_load_dwordx4 v[194:197], v[100:101], off nt
	global_load_dwordx4 v[190:193], v[100:101], off offset:256 nt
	v_or_b32_e32 v100, 16, v88
	v_ashrrev_i32_e32 v101, 31, v100
	v_lshlrev_b64 v[220:221], 12, v[100:101]
	v_lshl_add_u64 v[100:101], v[90:91], 0, v[220:221]
	global_load_dwordx4 v[186:189], v[100:101], off nt
	global_load_dwordx4 v[182:185], v[100:101], off offset:256 nt
	v_or_b32_e32 v100, 32, v88
	v_ashrrev_i32_e32 v101, 31, v100
	v_lshlrev_b64 v[218:219], 12, v[100:101]
	v_lshl_add_u64 v[100:101], v[90:91], 0, v[218:219]
	global_load_dwordx4 v[178:181], v[100:101], off nt
	global_load_dwordx4 v[174:177], v[100:101], off offset:256 nt
	v_or_b32_e32 v88, 48, v88
	v_ashrrev_i32_e32 v89, 31, v88
	v_lshlrev_b64 v[216:217], 12, v[88:89]
	v_lshl_add_u64 v[88:89], v[90:91], 0, v[216:217]
	global_load_dwordx4 v[170:173], v[88:89], off nt
	global_load_dwordx4 v[152:155], v[88:89], off offset:256 nt
	v_lshl_add_u64 v[214:215], v[222:223], 0, s[58:59]
	v_lshl_add_u64 v[88:89], v[90:91], 0, v[214:215]
	global_load_dwordx4 v[148:151], v[88:89], off nt
	global_load_dwordx4 v[144:147], v[88:89], off offset:256 nt
	s_mov_b64 s[14:15], 0x90000
	v_lshl_add_u64 v[212:213], v[222:223], 0, s[14:15]
	v_lshl_add_u64 v[88:89], v[90:91], 0, v[212:213]
	global_load_dwordx4 v[140:143], v[88:89], off nt
	global_load_dwordx4 v[124:127], v[88:89], off offset:256 nt
	s_mov_b64 s[14:15], 0xa0000
	v_lshl_add_u64 v[210:211], v[222:223], 0, s[14:15]
	v_lshl_add_u64 v[88:89], v[90:91], 0, v[210:211]
	global_load_dwordx4 v[120:123], v[88:89], off nt
	global_load_dwordx4 v[112:115], v[88:89], off offset:256 nt
	s_mov_b64 s[14:15], 0xb0000
	v_lshl_add_u64 v[208:209], v[222:223], 0, s[14:15]
	v_lshl_add_u64 v[88:89], v[90:91], 0, v[208:209]
	global_load_dwordx4 v[100:103], v[88:89], off nt
	s_nop 0
	global_load_dwordx4 v[88:91], v[88:89], off offset:256 nt
	s_and_b64 vcc, exec, s[2:3]
	s_mov_b32 s49, s4
	s_mov_b32 s12, s6
	s_mov_b64 s[14:15], s[10:11]
	s_mov_b64 s[16:17], s[8:9]
	s_waitcnt vmcnt(0)
	v_cvt_f32_f16_e32 v224, v194
	v_cvt_f32_f16_sdwa v225, v194 dst_sel:DWORD dst_unused:UNUSED_PAD src0_sel:WORD_1
	v_pk_add_f32 v[166:167], v[166:167], v[224:225]
	s_nop 0
	v_cvt_pk_f16_f32 v194, v166, v167
	v_cvt_f32_f16_e32 v166, v196
	v_cvt_f32_f16_sdwa v167, v196 dst_sel:DWORD dst_unused:UNUSED_PAD src0_sel:WORD_1
	v_pk_add_f32 v[156:157], v[156:157], v[166:167]
	s_nop 0
	v_cvt_pk_f16_f32 v196, v156, v157
	v_cvt_f32_f16_e32 v156, v195
	v_cvt_f32_f16_sdwa v157, v195 dst_sel:DWORD dst_unused:UNUSED_PAD src0_sel:WORD_1
	v_pk_add_f32 v[156:157], v[168:169], v[156:157]
	s_nop 0
	v_cvt_pk_f16_f32 v195, v156, v157
	v_cvt_f32_f16_e32 v156, v197
	v_cvt_f32_f16_sdwa v157, v197 dst_sel:DWORD dst_unused:UNUSED_PAD src0_sel:WORD_1
	v_pk_add_f32 v[156:157], v[158:159], v[156:157]
	s_nop 0
	v_cvt_pk_f16_f32 v197, v156, v157
	v_lshl_add_u64 v[156:157], s[0:1], 0, v[222:223]
	v_lshl_add_u64 v[166:167], v[156:157], 0, v[206:207]
	v_cvt_f32_f16_e32 v156, v190
	v_cvt_f32_f16_sdwa v157, v190 dst_sel:DWORD dst_unused:UNUSED_PAD src0_sel:WORD_1
	global_store_dwordx4 v[166:167], v[194:197], off sc1
	v_pk_add_f32 v[136:137], v[136:137], v[156:157]
	s_nop 0
	v_cvt_pk_f16_f32 v156, v136, v137
	v_cvt_f32_f16_e32 v136, v192
	v_cvt_f32_f16_sdwa v137, v192 dst_sel:DWORD dst_unused:UNUSED_PAD src0_sel:WORD_1
	v_pk_add_f32 v[132:133], v[132:133], v[136:137]
	s_nop 0
	v_cvt_pk_f16_f32 v158, v132, v133
	v_cvt_f32_f16_e32 v132, v191
	v_cvt_f32_f16_sdwa v133, v191 dst_sel:DWORD dst_unused:UNUSED_PAD src0_sel:WORD_1
	v_pk_add_f32 v[132:133], v[138:139], v[132:133]
	s_nop 0
	v_cvt_pk_f16_f32 v157, v132, v133
	v_cvt_f32_f16_e32 v132, v193
	v_cvt_f32_f16_sdwa v133, v193 dst_sel:DWORD dst_unused:UNUSED_PAD src0_sel:WORD_1
	v_pk_add_f32 v[132:133], v[134:135], v[132:133]
	s_nop 0
	v_cvt_pk_f16_f32 v159, v132, v133
	v_cvt_f32_f16_e32 v132, v186
	v_cvt_f32_f16_sdwa v133, v186 dst_sel:DWORD dst_unused:UNUSED_PAD src0_sel:WORD_1
	global_store_dwordx4 v[166:167], v[156:159], off offset:256 sc1
	v_pk_add_f32 v[128:129], v[128:129], v[132:133]
	s_nop 0
	v_cvt_pk_f16_f32 v132, v128, v129
	v_cvt_f32_f16_e32 v128, v188
	v_cvt_f32_f16_sdwa v129, v188 dst_sel:DWORD dst_unused:UNUSED_PAD src0_sel:WORD_1
	v_pk_add_f32 v[116:117], v[116:117], v[128:129]
	s_nop 0
	v_cvt_pk_f16_f32 v134, v116, v117
	v_cvt_f32_f16_e32 v116, v187
	v_cvt_f32_f16_sdwa v117, v187 dst_sel:DWORD dst_unused:UNUSED_PAD src0_sel:WORD_1
	v_pk_add_f32 v[116:117], v[130:131], v[116:117]
	s_nop 0
	v_cvt_pk_f16_f32 v133, v116, v117
	v_cvt_f32_f16_e32 v116, v189
	v_cvt_f32_f16_sdwa v117, v189 dst_sel:DWORD dst_unused:UNUSED_PAD src0_sel:WORD_1
	v_pk_add_f32 v[116:117], v[118:119], v[116:117]
	s_nop 0
	v_cvt_pk_f16_f32 v135, v116, v117
	v_lshl_add_u64 v[116:117], s[0:1], 0, v[220:221]
	v_lshl_add_u64 v[128:129], v[116:117], 0, v[206:207]
	v_cvt_f32_f16_e32 v116, v182
	v_cvt_f32_f16_sdwa v117, v182 dst_sel:DWORD dst_unused:UNUSED_PAD src0_sel:WORD_1
	global_store_dwordx4 v[128:129], v[132:135], off sc1
	v_pk_add_f32 v[108:109], v[108:109], v[116:117]
	s_nop 0
	v_cvt_pk_f16_f32 v116, v108, v109
	v_cvt_f32_f16_e32 v108, v184
	v_cvt_f32_f16_sdwa v109, v184 dst_sel:DWORD dst_unused:UNUSED_PAD src0_sel:WORD_1
	v_pk_add_f32 v[104:105], v[104:105], v[108:109]
	s_nop 0
	v_cvt_pk_f16_f32 v118, v104, v105
	v_cvt_f32_f16_e32 v104, v183
	v_cvt_f32_f16_sdwa v105, v183 dst_sel:DWORD dst_unused:UNUSED_PAD src0_sel:WORD_1
	v_pk_add_f32 v[104:105], v[110:111], v[104:105]
	s_nop 0
	v_cvt_pk_f16_f32 v117, v104, v105
	v_cvt_f32_f16_e32 v104, v185
	v_cvt_f32_f16_sdwa v105, v185 dst_sel:DWORD dst_unused:UNUSED_PAD src0_sel:WORD_1
	v_pk_add_f32 v[104:105], v[106:107], v[104:105]
	s_nop 0
	v_cvt_pk_f16_f32 v119, v104, v105
	v_cvt_f32_f16_e32 v104, v178
	v_cvt_f32_f16_sdwa v105, v178 dst_sel:DWORD dst_unused:UNUSED_PAD src0_sel:WORD_1
	global_store_dwordx4 v[128:129], v[116:119], off offset:256 sc1
	v_pk_add_f32 v[96:97], v[96:97], v[104:105]
	s_nop 0
	v_cvt_pk_f16_f32 v104, v96, v97
	v_cvt_f32_f16_e32 v96, v180
	v_cvt_f32_f16_sdwa v97, v180 dst_sel:DWORD dst_unused:UNUSED_PAD src0_sel:WORD_1
	v_pk_add_f32 v[92:93], v[92:93], v[96:97]
	s_nop 0
	v_cvt_pk_f16_f32 v106, v92, v93
	v_cvt_f32_f16_e32 v92, v179
	v_cvt_f32_f16_sdwa v93, v179 dst_sel:DWORD dst_unused:UNUSED_PAD src0_sel:WORD_1
	v_pk_add_f32 v[92:93], v[98:99], v[92:93]
	s_nop 0
	v_cvt_pk_f16_f32 v105, v92, v93
	v_cvt_f32_f16_e32 v92, v181
	v_cvt_f32_f16_sdwa v93, v181 dst_sel:DWORD dst_unused:UNUSED_PAD src0_sel:WORD_1
	v_pk_add_f32 v[92:93], v[94:95], v[92:93]
	s_nop 0
	v_cvt_pk_f16_f32 v107, v92, v93
	v_lshl_add_u64 v[92:93], s[0:1], 0, v[218:219]
	v_lshl_add_u64 v[96:97], v[92:93], 0, v[206:207]
	v_cvt_f32_f16_e32 v92, v174
	v_cvt_f32_f16_sdwa v93, v174 dst_sel:DWORD dst_unused:UNUSED_PAD src0_sel:WORD_1
	global_store_dwordx4 v[96:97], v[104:107], off sc1
	v_pk_add_f32 v[84:85], v[84:85], v[92:93]
	s_nop 0
	v_cvt_pk_f16_f32 v92, v84, v85
	v_cvt_f32_f16_e32 v84, v176
	v_cvt_f32_f16_sdwa v85, v176 dst_sel:DWORD dst_unused:UNUSED_PAD src0_sel:WORD_1
	v_pk_add_f32 v[80:81], v[80:81], v[84:85]
	s_nop 0
	v_cvt_pk_f16_f32 v94, v80, v81
	v_cvt_f32_f16_e32 v80, v175
	v_cvt_f32_f16_sdwa v81, v175 dst_sel:DWORD dst_unused:UNUSED_PAD src0_sel:WORD_1
	v_pk_add_f32 v[80:81], v[86:87], v[80:81]
	s_nop 0
	v_cvt_pk_f16_f32 v93, v80, v81
	v_cvt_f32_f16_e32 v80, v177
	v_cvt_f32_f16_sdwa v81, v177 dst_sel:DWORD dst_unused:UNUSED_PAD src0_sel:WORD_1
	v_pk_add_f32 v[80:81], v[82:83], v[80:81]
	s_nop 0
	v_cvt_pk_f16_f32 v95, v80, v81
	v_cvt_f32_f16_e32 v80, v170
	v_cvt_f32_f16_sdwa v81, v170 dst_sel:DWORD dst_unused:UNUSED_PAD src0_sel:WORD_1
	global_store_dwordx4 v[96:97], v[92:95], off offset:256 sc1
	v_pk_add_f32 v[76:77], v[76:77], v[80:81]
	s_nop 0
	v_cvt_pk_f16_f32 v80, v76, v77
	v_cvt_f32_f16_e32 v76, v172
	v_cvt_f32_f16_sdwa v77, v172 dst_sel:DWORD dst_unused:UNUSED_PAD src0_sel:WORD_1
	v_pk_add_f32 v[72:73], v[72:73], v[76:77]
	s_nop 0
	v_cvt_pk_f16_f32 v82, v72, v73
	v_cvt_f32_f16_e32 v72, v171
	v_cvt_f32_f16_sdwa v73, v171 dst_sel:DWORD dst_unused:UNUSED_PAD src0_sel:WORD_1
	v_pk_add_f32 v[72:73], v[78:79], v[72:73]
	s_nop 0
	v_cvt_pk_f16_f32 v81, v72, v73
	v_cvt_f32_f16_e32 v72, v173
	v_cvt_f32_f16_sdwa v73, v173 dst_sel:DWORD dst_unused:UNUSED_PAD src0_sel:WORD_1
	v_pk_add_f32 v[72:73], v[74:75], v[72:73]
	s_nop 0
	v_cvt_pk_f16_f32 v83, v72, v73
	v_lshl_add_u64 v[72:73], s[0:1], 0, v[216:217]
	v_lshl_add_u64 v[76:77], v[72:73], 0, v[206:207]
	v_cvt_f32_f16_e32 v72, v152
	v_cvt_f32_f16_sdwa v73, v152 dst_sel:DWORD dst_unused:UNUSED_PAD src0_sel:WORD_1
	global_store_dwordx4 v[76:77], v[80:83], off sc1
	v_pk_add_f32 v[68:69], v[68:69], v[72:73]
	s_nop 0
	v_cvt_pk_f16_f32 v72, v68, v69
	v_cvt_f32_f16_e32 v68, v154
	v_cvt_f32_f16_sdwa v69, v154 dst_sel:DWORD dst_unused:UNUSED_PAD src0_sel:WORD_1
	v_pk_add_f32 v[64:65], v[64:65], v[68:69]
	s_nop 0
	v_cvt_pk_f16_f32 v74, v64, v65
	v_cvt_f32_f16_e32 v64, v153
	v_cvt_f32_f16_sdwa v65, v153 dst_sel:DWORD dst_unused:UNUSED_PAD src0_sel:WORD_1
	v_pk_add_f32 v[64:65], v[70:71], v[64:65]
	s_nop 0
	v_cvt_pk_f16_f32 v73, v64, v65
	v_cvt_f32_f16_e32 v64, v155
	v_cvt_f32_f16_sdwa v65, v155 dst_sel:DWORD dst_unused:UNUSED_PAD src0_sel:WORD_1
	v_pk_add_f32 v[64:65], v[66:67], v[64:65]
	s_nop 0
	v_cvt_pk_f16_f32 v75, v64, v65
	v_cvt_f32_f16_e32 v64, v148
	v_cvt_f32_f16_sdwa v65, v148 dst_sel:DWORD dst_unused:UNUSED_PAD src0_sel:WORD_1
	global_store_dwordx4 v[76:77], v[72:75], off offset:256 sc1
	v_pk_add_f32 v[60:61], v[60:61], v[64:65]
	s_nop 0
	v_cvt_pk_f16_f32 v64, v60, v61
	v_cvt_f32_f16_e32 v60, v150
	v_cvt_f32_f16_sdwa v61, v150 dst_sel:DWORD dst_unused:UNUSED_PAD src0_sel:WORD_1
	v_pk_add_f32 v[56:57], v[56:57], v[60:61]
	s_nop 0
	v_cvt_pk_f16_f32 v66, v56, v57
	v_cvt_f32_f16_e32 v56, v149
	v_cvt_f32_f16_sdwa v57, v149 dst_sel:DWORD dst_unused:UNUSED_PAD src0_sel:WORD_1
	v_pk_add_f32 v[56:57], v[62:63], v[56:57]
	s_nop 0
	v_cvt_pk_f16_f32 v65, v56, v57
	v_cvt_f32_f16_e32 v56, v151
	v_cvt_f32_f16_sdwa v57, v151 dst_sel:DWORD dst_unused:UNUSED_PAD src0_sel:WORD_1
	v_pk_add_f32 v[56:57], v[58:59], v[56:57]
	s_nop 0
	v_cvt_pk_f16_f32 v67, v56, v57
	v_lshl_add_u64 v[56:57], s[0:1], 0, v[214:215]
	v_lshl_add_u64 v[60:61], v[56:57], 0, v[206:207]
	v_cvt_f32_f16_e32 v56, v144
	v_cvt_f32_f16_sdwa v57, v144 dst_sel:DWORD dst_unused:UNUSED_PAD src0_sel:WORD_1
	global_store_dwordx4 v[60:61], v[64:67], off sc1
	v_pk_add_f32 v[52:53], v[52:53], v[56:57]
	s_nop 0
	v_cvt_pk_f16_f32 v56, v52, v53
	v_cvt_f32_f16_e32 v52, v146
	v_cvt_f32_f16_sdwa v53, v146 dst_sel:DWORD dst_unused:UNUSED_PAD src0_sel:WORD_1
	v_pk_add_f32 v[48:49], v[48:49], v[52:53]
	s_nop 0
	v_cvt_pk_f16_f32 v58, v48, v49
	v_cvt_f32_f16_e32 v48, v145
	v_cvt_f32_f16_sdwa v49, v145 dst_sel:DWORD dst_unused:UNUSED_PAD src0_sel:WORD_1
	v_pk_add_f32 v[48:49], v[54:55], v[48:49]
	s_nop 0
	v_cvt_pk_f16_f32 v57, v48, v49
	v_cvt_f32_f16_e32 v48, v147
	v_cvt_f32_f16_sdwa v49, v147 dst_sel:DWORD dst_unused:UNUSED_PAD src0_sel:WORD_1
	v_pk_add_f32 v[48:49], v[50:51], v[48:49]
	s_nop 0
	v_cvt_pk_f16_f32 v59, v48, v49
	v_cvt_f32_f16_e32 v48, v140
	v_cvt_f32_f16_sdwa v49, v140 dst_sel:DWORD dst_unused:UNUSED_PAD src0_sel:WORD_1
	global_store_dwordx4 v[60:61], v[56:59], off offset:256 sc1
	v_pk_add_f32 v[44:45], v[44:45], v[48:49]
	s_nop 0
	v_cvt_pk_f16_f32 v48, v44, v45
	v_cvt_f32_f16_e32 v44, v142
	v_cvt_f32_f16_sdwa v45, v142 dst_sel:DWORD dst_unused:UNUSED_PAD src0_sel:WORD_1
	v_pk_add_f32 v[40:41], v[40:41], v[44:45]
	s_nop 0
	v_cvt_pk_f16_f32 v50, v40, v41
	v_cvt_f32_f16_e32 v40, v141
	v_cvt_f32_f16_sdwa v41, v141 dst_sel:DWORD dst_unused:UNUSED_PAD src0_sel:WORD_1
	v_pk_add_f32 v[40:41], v[46:47], v[40:41]
	s_nop 0
	v_cvt_pk_f16_f32 v49, v40, v41
	v_cvt_f32_f16_e32 v40, v143
	v_cvt_f32_f16_sdwa v41, v143 dst_sel:DWORD dst_unused:UNUSED_PAD src0_sel:WORD_1
	v_pk_add_f32 v[40:41], v[42:43], v[40:41]
	s_nop 0
	v_cvt_pk_f16_f32 v51, v40, v41
	v_lshl_add_u64 v[40:41], s[0:1], 0, v[212:213]
	v_lshl_add_u64 v[44:45], v[40:41], 0, v[206:207]
	v_cvt_f32_f16_e32 v40, v124
	v_cvt_f32_f16_sdwa v41, v124 dst_sel:DWORD dst_unused:UNUSED_PAD src0_sel:WORD_1
	global_store_dwordx4 v[44:45], v[48:51], off sc1
	v_pk_add_f32 v[36:37], v[36:37], v[40:41]
	s_nop 0
	v_cvt_pk_f16_f32 v40, v36, v37
	v_cvt_f32_f16_e32 v36, v126
	v_cvt_f32_f16_sdwa v37, v126 dst_sel:DWORD dst_unused:UNUSED_PAD src0_sel:WORD_1
	v_pk_add_f32 v[32:33], v[32:33], v[36:37]
	s_nop 0
	v_cvt_pk_f16_f32 v42, v32, v33
	v_cvt_f32_f16_e32 v32, v125
	v_cvt_f32_f16_sdwa v33, v125 dst_sel:DWORD dst_unused:UNUSED_PAD src0_sel:WORD_1
	v_pk_add_f32 v[32:33], v[38:39], v[32:33]
	s_nop 0
	v_cvt_pk_f16_f32 v41, v32, v33
	v_cvt_f32_f16_e32 v32, v127
	v_cvt_f32_f16_sdwa v33, v127 dst_sel:DWORD dst_unused:UNUSED_PAD src0_sel:WORD_1
	v_pk_add_f32 v[32:33], v[34:35], v[32:33]
	s_nop 0
	v_cvt_pk_f16_f32 v43, v32, v33
	v_cvt_f32_f16_e32 v32, v120
	v_cvt_f32_f16_sdwa v33, v120 dst_sel:DWORD dst_unused:UNUSED_PAD src0_sel:WORD_1
	global_store_dwordx4 v[44:45], v[40:43], off offset:256 sc1
	v_pk_add_f32 v[28:29], v[28:29], v[32:33]
	s_nop 0
	v_cvt_pk_f16_f32 v32, v28, v29
	v_cvt_f32_f16_e32 v28, v122
	v_cvt_f32_f16_sdwa v29, v122 dst_sel:DWORD dst_unused:UNUSED_PAD src0_sel:WORD_1
	v_pk_add_f32 v[24:25], v[24:25], v[28:29]
	s_nop 0
	v_cvt_pk_f16_f32 v34, v24, v25
	v_cvt_f32_f16_e32 v24, v121
	v_cvt_f32_f16_sdwa v25, v121 dst_sel:DWORD dst_unused:UNUSED_PAD src0_sel:WORD_1
	v_pk_add_f32 v[24:25], v[30:31], v[24:25]
	s_nop 0
	v_cvt_pk_f16_f32 v33, v24, v25
	v_cvt_f32_f16_e32 v24, v123
	v_cvt_f32_f16_sdwa v25, v123 dst_sel:DWORD dst_unused:UNUSED_PAD src0_sel:WORD_1
	v_pk_add_f32 v[24:25], v[26:27], v[24:25]
	s_nop 0
	v_cvt_pk_f16_f32 v35, v24, v25
	v_lshl_add_u64 v[24:25], s[0:1], 0, v[210:211]
	v_lshl_add_u64 v[28:29], v[24:25], 0, v[206:207]
	v_cvt_f32_f16_e32 v24, v112
	v_cvt_f32_f16_sdwa v25, v112 dst_sel:DWORD dst_unused:UNUSED_PAD src0_sel:WORD_1
	global_store_dwordx4 v[28:29], v[32:35], off sc1
	v_pk_add_f32 v[20:21], v[20:21], v[24:25]
	s_nop 0
	v_cvt_pk_f16_f32 v24, v20, v21
	v_cvt_f32_f16_e32 v20, v114
	v_cvt_f32_f16_sdwa v21, v114 dst_sel:DWORD dst_unused:UNUSED_PAD src0_sel:WORD_1
	v_pk_add_f32 v[16:17], v[16:17], v[20:21]
	s_nop 0
	v_cvt_pk_f16_f32 v26, v16, v17
	v_cvt_f32_f16_e32 v16, v113
	v_cvt_f32_f16_sdwa v17, v113 dst_sel:DWORD dst_unused:UNUSED_PAD src0_sel:WORD_1
	v_pk_add_f32 v[16:17], v[22:23], v[16:17]
	s_nop 0
	v_cvt_pk_f16_f32 v25, v16, v17
	v_cvt_f32_f16_e32 v16, v115
	v_cvt_f32_f16_sdwa v17, v115 dst_sel:DWORD dst_unused:UNUSED_PAD src0_sel:WORD_1
	v_pk_add_f32 v[16:17], v[18:19], v[16:17]
	s_nop 0
	v_cvt_pk_f16_f32 v27, v16, v17
	v_cvt_f32_f16_e32 v16, v100
	v_cvt_f32_f16_sdwa v17, v100 dst_sel:DWORD dst_unused:UNUSED_PAD src0_sel:WORD_1
	global_store_dwordx4 v[28:29], v[24:27], off offset:256 sc1
	v_pk_add_f32 v[12:13], v[12:13], v[16:17]
	s_nop 0
	v_cvt_pk_f16_f32 v16, v12, v13
	v_cvt_f32_f16_e32 v12, v102
	v_cvt_f32_f16_sdwa v13, v102 dst_sel:DWORD dst_unused:UNUSED_PAD src0_sel:WORD_1
	v_pk_add_f32 v[8:9], v[8:9], v[12:13]
	s_nop 0
	v_cvt_pk_f16_f32 v18, v8, v9
	v_cvt_f32_f16_e32 v8, v101
	v_cvt_f32_f16_sdwa v9, v101 dst_sel:DWORD dst_unused:UNUSED_PAD src0_sel:WORD_1
	v_pk_add_f32 v[8:9], v[14:15], v[8:9]
	s_nop 0
	v_cvt_pk_f16_f32 v17, v8, v9
	v_cvt_f32_f16_e32 v8, v103
	v_cvt_f32_f16_sdwa v9, v103 dst_sel:DWORD dst_unused:UNUSED_PAD src0_sel:WORD_1
	v_pk_add_f32 v[8:9], v[10:11], v[8:9]
	s_nop 0
	v_cvt_pk_f16_f32 v19, v8, v9
	v_lshl_add_u64 v[8:9], s[0:1], 0, v[208:209]
	v_lshl_add_u64 v[12:13], v[8:9], 0, v[206:207]
	v_cvt_f32_f16_e32 v8, v88
	v_cvt_f32_f16_sdwa v9, v88 dst_sel:DWORD dst_unused:UNUSED_PAD src0_sel:WORD_1
	global_store_dwordx4 v[12:13], v[16:19], off sc1
	v_pk_add_f32 v[4:5], v[4:5], v[8:9]
	s_nop 0
	v_cvt_pk_f16_f32 v8, v4, v5
	v_cvt_f32_f16_e32 v4, v90
	v_cvt_f32_f16_sdwa v5, v90 dst_sel:DWORD dst_unused:UNUSED_PAD src0_sel:WORD_1
	v_pk_add_f32 v[0:1], v[0:1], v[4:5]
	s_nop 0
	v_cvt_pk_f16_f32 v10, v0, v1
	v_cvt_f32_f16_e32 v0, v89
	v_cvt_f32_f16_sdwa v1, v89 dst_sel:DWORD dst_unused:UNUSED_PAD src0_sel:WORD_1
	v_pk_add_f32 v[0:1], v[6:7], v[0:1]
	s_nop 0
	v_cvt_pk_f16_f32 v9, v0, v1
	v_cvt_f32_f16_e32 v0, v91
	v_cvt_f32_f16_sdwa v1, v91 dst_sel:DWORD dst_unused:UNUSED_PAD src0_sel:WORD_1
	v_pk_add_f32 v[0:1], v[2:3], v[0:1]
	s_nop 0
	v_cvt_pk_f16_f32 v11, v0, v1
	global_store_dwordx4 v[12:13], v[8:11], off offset:256 sc1
	s_cbranch_vccz .LBB0_744
	s_waitcnt vmcnt(0)
	s_cmpk_gt_u32 s21, 0xff
	s_cbranch_scc1 .LBB0_755
	s_barrier

.LBB0_802:
	s_add_u32 s2, s14, s6
	s_addc_u32 s3, s13, s7
	s_add_u32 s4, s14, s10
	v_lshl_add_u64 v[16:17], s[2:3], 0, v[160:161]
	s_addc_u32 s5, s13, s11
	v_add_co_u32_e32 v20, vcc, s20, v16
	v_lshl_add_u64 v[18:19], v[16:17], 0, s[16:17]
	v_lshl_add_u64 v[34:35], s[4:5], 0, v[160:161]
	v_addc_co_u32_e32 v21, vcc, 0, v17, vcc
	global_load_dwordx4 v[22:25], v[18:19], off offset:1024 nt
	global_load_dwordx4 v[26:29], v[18:19], off offset:2048 nt
	global_load_dwordx4 v[30:33], v[20:21], off nt
	v_add_co_u32_e32 v20, vcc, s20, v34
	v_lshl_add_u64 v[44:45], v[34:35], 0, s[16:17]
	s_nop 0
	v_addc_co_u32_e32 v21, vcc, 0, v35, vcc
	global_load_dwordx4 v[40:43], v[44:45], off offset:1024 nt
	global_load_dwordx4 v[64:67], v[44:45], off offset:2048 nt
	global_load_dwordx4 v[68:71], v[18:19], off offset:3072 nt
	global_load_dwordx4 v[72:75], v[44:45], off offset:3072 nt
	global_load_dwordx4 v[76:79], v[20:21], off nt
	v_add_co_u32_e64 v36, s[2:3], s21, v16
	v_lshl_add_u64 v[14:15], v[16:17], 0, s[18:19]
	s_nop 0
	v_addc_co_u32_e64 v37, s[2:3], 0, v17, s[2:3]
	v_add_co_u32_e64 v38, s[2:3], s21, v34
	v_lshl_add_u64 v[16:17], v[34:35], 0, s[18:19]
	s_nop 0
	v_addc_co_u32_e64 v39, s[2:3], 0, v35, s[2:3]
	s_add_i32 s12, s12, s0
	s_add_u32 s14, s14, s8
	s_addc_u32 s13, s13, s9
	s_cmpk_gt_i32 s12, 0x7fff
	s_waitcnt vmcnt(0)
	v_cvt_f32_f16_e32 v84, v22
	v_cvt_f32_f16_sdwa v85, v22 dst_sel:DWORD dst_unused:UNUSED_PAD src0_sel:WORD_1
	v_cvt_f32_f16_e32 v86, v23
	v_cvt_f32_f16_sdwa v87, v23 dst_sel:DWORD dst_unused:UNUSED_PAD src0_sel:WORD_1
	v_cvt_f32_f16_e32 v80, v24
	v_cvt_f32_f16_sdwa v81, v24 dst_sel:DWORD dst_unused:UNUSED_PAD src0_sel:WORD_1
	v_cvt_f32_f16_e32 v82, v25
	v_cvt_f32_f16_sdwa v83, v25 dst_sel:DWORD dst_unused:UNUSED_PAD src0_sel:WORD_1
	v_cvt_f32_f16_e32 v60, v26
	v_cvt_f32_f16_sdwa v61, v26 dst_sel:DWORD dst_unused:UNUSED_PAD src0_sel:WORD_1
	v_cvt_f32_f16_e32 v62, v27
	v_cvt_f32_f16_sdwa v63, v27 dst_sel:DWORD dst_unused:UNUSED_PAD src0_sel:WORD_1
	v_cvt_f32_f16_e32 v56, v28
	v_cvt_f32_f16_sdwa v57, v28 dst_sel:DWORD dst_unused:UNUSED_PAD src0_sel:WORD_1
	v_cvt_f32_f16_e32 v58, v29
	v_cvt_f32_f16_sdwa v59, v29 dst_sel:DWORD dst_unused:UNUSED_PAD src0_sel:WORD_1
	v_cvt_f32_f16_e32 v90, v30
	v_cvt_f32_f16_sdwa v91, v30 dst_sel:DWORD dst_unused:UNUSED_PAD src0_sel:WORD_1
	v_cvt_f32_f16_e32 v92, v31
	v_cvt_f32_f16_sdwa v93, v31 dst_sel:DWORD dst_unused:UNUSED_PAD src0_sel:WORD_1
	v_cvt_f32_f16_e32 v94, v32
	v_cvt_f32_f16_sdwa v95, v32 dst_sel:DWORD dst_unused:UNUSED_PAD src0_sel:WORD_1
	v_cvt_f32_f16_e32 v96, v33
	v_cvt_f32_f16_sdwa v97, v33 dst_sel:DWORD dst_unused:UNUSED_PAD src0_sel:WORD_1
	v_cvt_f32_f16_e32 v48, v40
	v_cvt_f32_f16_sdwa v49, v40 dst_sel:DWORD dst_unused:UNUSED_PAD src0_sel:WORD_1
	v_cvt_f32_f16_e32 v50, v41
	v_cvt_f32_f16_sdwa v51, v41 dst_sel:DWORD dst_unused:UNUSED_PAD src0_sel:WORD_1
	v_cvt_f32_f16_e32 v52, v42
	v_cvt_f32_f16_sdwa v53, v42 dst_sel:DWORD dst_unused:UNUSED_PAD src0_sel:WORD_1
	v_cvt_f32_f16_e32 v54, v43
	v_cvt_f32_f16_sdwa v55, v43 dst_sel:DWORD dst_unused:UNUSED_PAD src0_sel:WORD_1
	v_cvt_f32_f16_e32 v44, v64
	v_cvt_f32_f16_sdwa v45, v64 dst_sel:DWORD dst_unused:UNUSED_PAD src0_sel:WORD_1
	v_cvt_f32_f16_e32 v46, v65
	v_cvt_f32_f16_sdwa v47, v65 dst_sel:DWORD dst_unused:UNUSED_PAD src0_sel:WORD_1
	v_cvt_f32_f16_e32 v40, v66
	v_cvt_f32_f16_sdwa v41, v66 dst_sel:DWORD dst_unused:UNUSED_PAD src0_sel:WORD_1
	v_cvt_f32_f16_e32 v42, v67
	v_cvt_f32_f16_sdwa v43, v67 dst_sel:DWORD dst_unused:UNUSED_PAD src0_sel:WORD_1
	v_cvt_f32_f16_e32 v18, v68
	v_cvt_f32_f16_sdwa v19, v68 dst_sel:DWORD dst_unused:UNUSED_PAD src0_sel:WORD_1
	v_cvt_f32_f16_e32 v20, v69
	v_cvt_f32_f16_sdwa v21, v69 dst_sel:DWORD dst_unused:UNUSED_PAD src0_sel:WORD_1
	v_cvt_f32_f16_e32 v22, v70
	v_cvt_f32_f16_sdwa v23, v70 dst_sel:DWORD dst_unused:UNUSED_PAD src0_sel:WORD_1
	v_cvt_f32_f16_e32 v24, v71
	v_cvt_f32_f16_sdwa v25, v71 dst_sel:DWORD dst_unused:UNUSED_PAD src0_sel:WORD_1
	v_cvt_f32_f16_e32 v26, v72
	v_cvt_f32_f16_sdwa v27, v72 dst_sel:DWORD dst_unused:UNUSED_PAD src0_sel:WORD_1
	v_cvt_f32_f16_e32 v28, v73
	v_cvt_f32_f16_sdwa v29, v73 dst_sel:DWORD dst_unused:UNUSED_PAD src0_sel:WORD_1
	v_cvt_f32_f16_e32 v30, v74
	v_cvt_f32_f16_sdwa v31, v74 dst_sel:DWORD dst_unused:UNUSED_PAD src0_sel:WORD_1
	v_cvt_f32_f16_e32 v32, v75
	v_cvt_f32_f16_sdwa v33, v75 dst_sel:DWORD dst_unused:UNUSED_PAD src0_sel:WORD_1
	v_cvt_f32_f16_e32 v64, v76
	v_cvt_f32_f16_sdwa v65, v76 dst_sel:DWORD dst_unused:UNUSED_PAD src0_sel:WORD_1
	v_cvt_f32_f16_e32 v66, v77
	v_cvt_f32_f16_sdwa v67, v77 dst_sel:DWORD dst_unused:UNUSED_PAD src0_sel:WORD_1
	v_cvt_f32_f16_e32 v68, v78
	v_cvt_f32_f16_sdwa v69, v78 dst_sel:DWORD dst_unused:UNUSED_PAD src0_sel:WORD_1
	v_cvt_f32_f16_e32 v70, v79
	v_cvt_f32_f16_sdwa v71, v79 dst_sel:DWORD dst_unused:UNUSED_PAD src0_sel:WORD_1
	v_pk_mul_f32 v[34:35], v[84:85], v[84:85]
	v_pk_mul_f32 v[72:73], v[86:87], v[86:87]
	v_pk_mul_f32 v[74:75], v[80:81], v[80:81]
	v_pk_mul_f32 v[76:77], v[82:83], v[82:83]
	v_pk_mul_f32 v[78:79], v[60:61], v[60:61]
	v_pk_mul_f32 v[88:89], v[62:63], v[62:63]
	v_pk_mul_f32 v[98:99], v[56:57], v[56:57]
	v_pk_mul_f32 v[100:101], v[58:59], v[58:59]
	v_pk_mul_f32 v[102:103], v[90:91], v[90:91]
	v_pk_mul_f32 v[104:105], v[92:93], v[92:93]
	v_pk_mul_f32 v[106:107], v[94:95], v[94:95]
	v_pk_mul_f32 v[108:109], v[96:97], v[96:97]
	v_add_f32_e32 v122, v72, v73
	v_add_f32_e32 v123, v34, v35
	v_add_f32_e32 v124, v76, v77
	v_add_f32_e32 v125, v74, v75
	v_add_f32_e32 v126, v88, v89
	v_add_f32_e32 v127, v78, v79
	v_add_f32_e32 v128, v100, v101
	v_add_f32_e32 v129, v98, v99
	v_add_f32_e32 v130, v108, v109
	v_add_f32_e32 v131, v106, v107
	v_add_f32_e32 v132, v104, v105
	v_add_f32_e32 v133, v102, v103
	v_pk_mul_f32 v[34:35], v[48:49], v[48:49]
	v_pk_mul_f32 v[72:73], v[50:51], v[50:51]
	v_pk_mul_f32 v[74:75], v[52:53], v[52:53]
	v_pk_mul_f32 v[76:77], v[54:55], v[54:55]
	v_pk_mul_f32 v[78:79], v[44:45], v[44:45]
	v_pk_mul_f32 v[88:89], v[46:47], v[46:47]
	v_pk_mul_f32 v[98:99], v[40:41], v[40:41]
	v_pk_mul_f32 v[100:101], v[42:43], v[42:43]
	v_pk_mul_f32 v[114:115], v[26:27], v[26:27]
	v_pk_mul_f32 v[116:117], v[28:29], v[28:29]
	v_add_f32_e32 v134, v123, v122
	v_add_f32_e32 v135, v125, v124
	v_add_f32_e32 v126, v127, v126
	v_add_f32_e32 v127, v129, v128
	v_pk_mul_f32 v[102:103], v[30:31], v[30:31]
	v_pk_mul_f32 v[104:105], v[32:33], v[32:33]
	v_pk_mul_f32 v[106:107], v[64:65], v[64:65]
	v_pk_mul_f32 v[108:109], v[66:67], v[66:67]
	v_pk_mul_f32 v[122:123], v[68:69], v[68:69]
	v_pk_mul_f32 v[124:125], v[70:71], v[70:71]
	v_add_f32_e32 v128, v131, v130
	v_add_f32_e32 v129, v133, v132
	v_add_f32_e32 v72, v72, v73
	v_add_f32_e32 v34, v34, v35
	v_add_f32_e32 v35, v76, v77
	v_add_f32_e32 v73, v74, v75
	v_add_f32_e32 v74, v88, v89
	v_add_f32_e32 v75, v78, v79
	v_add_f32_e32 v76, v100, v101
	v_add_f32_e32 v77, v98, v99
	v_add_f32_e32 v78, v116, v117
	v_add_f32_e32 v79, v114, v115
	v_add_f32_e32 v88, v104, v105
	v_add_f32_e32 v89, v102, v103
	v_add_f32_e32 v98, v129, v128
	v_add_f32_e32 v101, v124, v125
	v_add_f32_e32 v102, v122, v123
	v_add_f32_e32 v103, v108, v109
	v_add_f32_e32 v104, v106, v107
	v_add_f32_e32 v34, v34, v72
	v_add_f32_e32 v35, v73, v35
	v_add_f32_e32 v72, v75, v74
	v_add_f32_e32 v73, v77, v76
	v_add_f32_e32 v74, v79, v78
	v_add_f32_e32 v76, v98, v134
	v_add_f32_e32 v77, v102, v101
	v_add_f32_e32 v78, v104, v103
	v_pk_mul_f32 v[110:111], v[18:19], v[18:19]
	v_pk_mul_f32 v[112:113], v[20:21], v[20:21]
	v_add_f32_e32 v76, v135, v76
	v_add_f32_e32 v77, v78, v77
	v_pk_mul_f32 v[118:119], v[22:23], v[22:23]
	v_pk_mul_f32 v[120:121], v[24:25], v[24:25]
	v_add_f32_e32 v112, v112, v113
	v_add_f32_e32 v110, v110, v111
	v_add_f32_e32 v76, v76, v126
	v_add_f32_e32 v34, v77, v34
	v_add_f32_e32 v111, v120, v121
	v_add_f32_e32 v113, v118, v119
	v_add_f32_e32 v99, v110, v112
	v_add_f32_e32 v76, v127, v76
	v_add_f32_e32 v34, v35, v34
	v_add_f32_e32 v100, v113, v111
	v_add_f32_e32 v35, v76, v99
	v_add_f32_e32 v34, v34, v72
	v_add_f32_e32 v35, v100, v35
	v_add_f32_e32 v34, v73, v34
	v_add_f32_e32 v75, v89, v88
	v_add_f32_e32 v34, v34, v74
	ds_swizzle_b32 v72, v35 offset:swizzle(SWAP,1)
	v_add_f32_e32 v34, v75, v34
	ds_swizzle_b32 v73, v34 offset:swizzle(SWAP,1)
	s_waitcnt lgkmcnt(1)
	v_add_f32_e32 v35, v35, v72
	ds_swizzle_b32 v72, v35 offset:swizzle(SWAP,2)
	s_waitcnt lgkmcnt(1)
	v_add_f32_e32 v34, v34, v73
	ds_swizzle_b32 v73, v34 offset:swizzle(SWAP,2)
	s_waitcnt lgkmcnt(1)
	v_add_f32_e32 v35, v35, v72
	ds_swizzle_b32 v72, v35 offset:swizzle(SWAP,4)
	s_waitcnt lgkmcnt(1)
	v_add_f32_e32 v34, v34, v73
	ds_swizzle_b32 v73, v34 offset:swizzle(SWAP,4)
	s_waitcnt lgkmcnt(1)
	v_add_f32_e32 v35, v35, v72
	ds_swizzle_b32 v72, v35 offset:swizzle(SWAP,8)
	s_waitcnt lgkmcnt(1)
	v_add_f32_e32 v34, v34, v73
	ds_swizzle_b32 v73, v34 offset:swizzle(SWAP,8)
	s_waitcnt lgkmcnt(1)
	v_add_f32_e32 v35, v35, v72
	ds_swizzle_b32 v72, v35 offset:swizzle(SWAP,16)
	s_waitcnt lgkmcnt(1)
	v_add_f32_e32 v34, v34, v73
	ds_swizzle_b32 v73, v34 offset:swizzle(SWAP,16)
	s_waitcnt lgkmcnt(1)
	v_add_f32_e32 v35, v35, v72
	v_mov_b32_e32 v72, v35
	s_waitcnt lgkmcnt(0)
	v_add_f32_e32 v34, v34, v73
	v_permlane32_swap_b32_e32 v35, v72
	v_add_f32_e32 v35, v35, v72
	v_mov_b32_e32 v72, v34
	s_nop 1
	v_permlane32_swap_b32_e32 v34, v72
	v_fmamk_f32 v35, v35, 0x3a000000, v254
	v_add_f32_e32 v34, v34, v72
	v_mul_f32_e32 v72, 0x4f800000, v35
	v_cmp_gt_f32_e32 vcc, s76, v35
	v_fmamk_f32 v34, v34, 0x3a000000, v254
	v_mul_f32_e32 v73, 0x4f800000, v34
	v_cndmask_b32_e32 v35, v35, v72, vcc
	v_sqrt_f32_e32 v72, v35
	v_cmp_gt_f32_e64 s[2:3], s76, v34
	v_add_u32_e32 v74, -1, v72
	s_nop 0
	v_cndmask_b32_e64 v34, v34, v73, s[2:3]
	v_sqrt_f32_e32 v73, v34
	v_add_u32_e32 v75, 1, v72
	v_fma_f32 v76, -v74, v72, v35
	v_fma_f32 v77, -v75, v72, v35
	v_cmp_ge_f32_e64 s[4:5], 0, v76
	v_add_u32_e32 v76, 1, v73
	s_nop 0
	v_cndmask_b32_e64 v72, v72, v74, s[4:5]
	v_add_u32_e32 v74, -1, v73
	v_cmp_lt_f32_e64 s[4:5], 0, v77
	v_fma_f32 v77, -v76, v73, v34
	s_nop 0
	v_cndmask_b32_e64 v72, v72, v75, s[4:5]
	v_fma_f32 v75, -v74, v73, v34
	v_cmp_ge_f32_e64 s[4:5], 0, v75
	v_mul_f32_e32 v78, 0x37800000, v72
	v_cndmask_b32_e32 v72, v72, v78, vcc
	v_cndmask_b32_e64 v73, v73, v74, s[4:5]
	v_cmp_lt_f32_e64 s[4:5], 0, v77
	v_cmp_class_f32_e32 vcc, v35, v229
	s_nop 0
	v_cndmask_b32_e64 v73, v73, v76, s[4:5]
	v_cndmask_b32_e32 v72, v72, v35, vcc
	v_mul_f32_e32 v35, 0x37800000, v73
	v_div_scale_f32 v74, s[4:5], v72, v72, 1.0
	v_cndmask_b32_e64 v35, v73, v35, s[2:3]
	v_cmp_class_f32_e64 s[2:3], v34, v229
	v_rcp_f32_e32 v73, v74
	v_div_scale_f32 v75, vcc, 1.0, v72, 1.0
	v_cndmask_b32_e64 v35, v35, v34, s[2:3]
	v_div_scale_f32 v76, s[2:3], v35, v35, 1.0
	v_rcp_f32_e32 v78, v76
	v_fma_f32 v34, -v74, v73, 1.0
	v_fmac_f32_e32 v73, v34, v73
	v_mul_f32_e32 v34, v75, v73
	v_fma_f32 v79, -v76, v78, 1.0
	v_div_scale_f32 v77, s[2:3], 1.0, v35, 1.0
	v_fma_f32 v88, -v74, v34, v75
	v_fmac_f32_e32 v78, v79, v78
	v_fmac_f32_e32 v34, v88, v73
	v_mul_f32_e32 v79, v77, v78
	v_fma_f32 v74, -v74, v34, v75
	v_fma_f32 v75, -v76, v79, v77
	v_div_fmas_f32 v34, v74, v73, v34
	v_fmac_f32_e32 v79, v75, v78
	v_div_fixup_f32 v34, v34, v72, 1.0
	v_fma_f32 v72, -v76, v79, v77
	s_mov_b64 vcc, s[2:3]
	v_div_fmas_f32 v88, v72, v78, v79
	v_pk_mul_f32 v[72:73], v[90:91], v[34:35] op_sel_hi:[1,0]
	v_pk_mul_f32 v[76:77], v[92:93], v[34:35] op_sel_hi:[1,0]
	v_pk_mul_f32 v[74:75], v[94:95], v[34:35] op_sel_hi:[1,0]
	v_pk_mul_f32 v[78:79], v[96:97], v[34:35] op_sel_hi:[1,0]
	v_pk_mul_f32 v[90:91], v[56:57], v[34:35] op_sel_hi:[1,0]
	v_div_fixup_f32 v56, v88, v35, 1.0
	v_pk_mul_f32 v[76:77], v[142:143], v[76:77]
	v_pk_mul_f32 v[72:73], v[140:141], v[72:73]
	v_pk_mul_f32 v[74:75], v[136:137], v[74:75]
	v_pk_mul_f32 v[84:85], v[84:85], v[34:35] op_sel_hi:[1,0]
	v_pk_mul_f32 v[86:87], v[86:87], v[34:35] op_sel_hi:[1,0]
	v_pk_mul_f32 v[80:81], v[80:81], v[34:35] op_sel_hi:[1,0]
	v_pk_mul_f32 v[82:83], v[82:83], v[34:35] op_sel_hi:[1,0]
	v_pk_mul_f32 v[60:61], v[60:61], v[34:35] op_sel_hi:[1,0]
	v_pk_mul_f32 v[62:63], v[62:63], v[34:35] op_sel_hi:[1,0]
	v_pk_mul_f32 v[58:59], v[58:59], v[34:35] op_sel_hi:[1,0]
	v_pk_mul_f32 v[78:79], v[138:139], v[78:79]
	v_pk_mul_f32 v[64:65], v[64:65], v[56:57] op_sel_hi:[1,0]
	v_pk_mul_f32 v[66:67], v[66:67], v[56:57] op_sel_hi:[1,0]
	v_pk_mul_f32 v[68:69], v[68:69], v[56:57] op_sel_hi:[1,0]
	v_pk_mul_f32 v[70:71], v[70:71], v[56:57] op_sel_hi:[1,0]
	v_bfe_u32 v35, v72, 16, 1
	v_bfe_u32 v57, v73, 16, 1
	v_bfe_u32 v94, v76, 16, 1
	v_bfe_u32 v96, v74, 16, 1
	v_bfe_u32 v95, v77, 16, 1
	v_bfe_u32 v97, v75, 16, 1
	v_bfe_u32 v98, v78, 16, 1
	v_pk_mul_f32 v[88:89], v[44:45], v[56:57] op_sel_hi:[1,0]
	v_pk_mul_f32 v[92:93], v[46:47], v[56:57] op_sel_hi:[1,0]
	v_pk_mul_f32 v[44:45], v[40:41], v[56:57] op_sel_hi:[1,0]
	v_pk_mul_f32 v[46:47], v[42:43], v[56:57] op_sel_hi:[1,0]
	v_pk_mul_f32 v[6:7], v[142:143], v[66:67]
	v_pk_mul_f32 v[4:5], v[140:141], v[64:65]
	v_pk_mul_f32 v[40:41], v[138:139], v[70:71]
	v_pk_mul_f32 v[42:43], v[136:137], v[68:69]
	v_add3_u32 v0, v72, v35, s75
	v_add3_u32 v2, v76, v94, s75
	v_add3_u32 v35, v74, v96, s75
	v_bfe_u32 v99, v79, 16, 1
	v_pk_mul_f32 v[48:49], v[48:49], v[56:57] op_sel_hi:[1,0]
	v_pk_mul_f32 v[50:51], v[50:51], v[56:57] op_sel_hi:[1,0]
	v_pk_mul_f32 v[52:53], v[52:53], v[56:57] op_sel_hi:[1,0]
	v_pk_mul_f32 v[54:55], v[54:55], v[56:57] op_sel_hi:[1,0]
	v_add3_u32 v1, v73, v57, s75
	v_add3_u32 v3, v77, v95, s75
	v_add3_u32 v57, v75, v97, s75
	v_add3_u32 v64, v78, v98, s75
	v_lshrrev_b32_e32 v0, 16, v0
	v_lshrrev_b32_e32 v2, 16, v2
	v_lshrrev_b32_e32 v35, 16, v35
	v_bfe_u32 v66, v4, 16, 1
	v_bfe_u32 v68, v6, 16, 1
	v_bfe_u32 v70, v42, 16, 1
	v_bfe_u32 v72, v40, 16, 1
	v_add3_u32 v65, v79, v99, s75
	v_lshrrev_b32_e32 v64, 16, v64
	v_bfe_u32 v67, v5, 16, 1
	v_bfe_u32 v69, v7, 16, 1
	v_bfe_u32 v71, v43, 16, 1
	v_bfe_u32 v73, v41, 16, 1
	v_and_or_b32 v0, v1, s15, v0
	v_and_or_b32 v1, v3, s15, v2
	v_and_or_b32 v2, v57, s15, v35
	v_add3_u32 v4, v4, v66, s75
	v_add3_u32 v6, v6, v68, s75
	v_add3_u32 v35, v42, v70, s75
	v_add3_u32 v40, v40, v72, s75
	v_and_or_b32 v3, v65, s15, v64
	v_add3_u32 v5, v5, v67, s75
	v_add3_u32 v7, v7, v69, s75
	v_add3_u32 v42, v43, v71, s75
	v_add3_u32 v41, v41, v73, s75
	v_lshrrev_b32_e32 v4, 16, v4
	v_lshrrev_b32_e32 v6, 16, v6
	v_lshrrev_b32_e32 v35, 16, v35
	v_lshrrev_b32_e32 v40, 16, v40
	global_store_dwordx4 v[36:37], v[0:3], off sc1
	s_nop 1
	v_and_or_b32 v0, v5, s15, v4
	v_and_or_b32 v1, v7, s15, v6
	v_and_or_b32 v2, v42, s15, v35
	v_and_or_b32 v3, v41, s15, v40
	global_store_dwordx4 v[38:39], v[0:3], off sc1
	s_nop 0
	v_pk_mul_f32 v[36:37], v[146:147], v[86:87]
	v_pk_mul_f32 v[38:39], v[144:145], v[84:85]
	v_pk_mul_f32 v[40:41], v[150:151], v[82:83]
	v_pk_mul_f32 v[42:43], v[148:149], v[80:81]
	v_pk_mul_f32 v[2:3], v[146:147], v[50:51]
	v_pk_mul_f32 v[0:1], v[144:145], v[48:49]
	v_pk_mul_f32 v[6:7], v[150:151], v[54:55]
	v_pk_mul_f32 v[4:5], v[148:149], v[52:53]
	v_bfe_u32 v35, v38, 16, 1
	v_bfe_u32 v48, v39, 16, 1
	v_bfe_u32 v49, v36, 16, 1
	v_bfe_u32 v51, v42, 16, 1
	v_bfe_u32 v53, v40, 16, 1
	v_bfe_u32 v50, v37, 16, 1
	v_bfe_u32 v52, v43, 16, 1
	v_bfe_u32 v54, v41, 16, 1
	v_bfe_u32 v55, v0, 16, 1
	v_bfe_u32 v57, v1, 16, 1
	v_bfe_u32 v64, v2, 16, 1
	v_bfe_u32 v65, v3, 16, 1
	v_bfe_u32 v66, v4, 16, 1
	v_bfe_u32 v67, v5, 16, 1
	v_bfe_u32 v68, v6, 16, 1
	v_add3_u32 v35, v38, v35, s75
	v_add3_u32 v38, v39, v48, s75
	v_add3_u32 v36, v36, v49, s75
	v_add3_u32 v39, v42, v51, s75
	v_add3_u32 v40, v40, v53, s75
	v_bfe_u32 v69, v7, 16, 1
	v_add3_u32 v37, v37, v50, s75
	v_add3_u32 v42, v43, v52, s75
	v_add3_u32 v41, v41, v54, s75
	v_add3_u32 v0, v0, v55, s75
	v_add3_u32 v43, v1, v57, s75
	v_add3_u32 v1, v2, v64, s75
	v_add3_u32 v48, v3, v65, s75
	v_add3_u32 v2, v4, v66, s75
	v_add3_u32 v49, v5, v67, s75
	v_add3_u32 v3, v6, v68, s75
	v_lshrrev_b32_e32 v4, 16, v35
	v_lshrrev_b32_e32 v5, 16, v36
	v_lshrrev_b32_e32 v6, 16, v39
	v_lshrrev_b32_e32 v35, 16, v40
	v_add3_u32 v7, v7, v69, s75
	v_lshrrev_b32_e32 v36, 16, v0
	v_lshrrev_b32_e32 v39, 16, v1
	v_lshrrev_b32_e32 v40, 16, v2
	v_lshrrev_b32_e32 v50, 16, v3
	v_and_or_b32 v0, v38, s15, v4
	v_and_or_b32 v1, v37, s15, v5
	v_and_or_b32 v2, v42, s15, v6
	v_and_or_b32 v3, v41, s15, v35
	v_and_or_b32 v4, v43, s15, v36
	v_and_or_b32 v5, v48, s15, v39
	v_and_or_b32 v6, v49, s15, v40
	v_and_or_b32 v7, v7, s15, v50
	global_store_dwordx4 v[14:15], v[0:3], off offset:1024 sc1
	global_store_dwordx4 v[16:17], v[4:7], off offset:1024 sc1
	s_nop 0
	v_pk_mul_f32 v[38:39], v[154:155], v[62:63]
	v_pk_mul_f32 v[42:43], v[152:153], v[60:61]
	v_pk_mul_f32 v[6:7], v[58:59], v[158:159]
	v_pk_mul_f32 v[40:41], v[90:91], v[156:157]
	v_pk_mul_f32 v[4:5], v[154:155], v[92:93]
	v_pk_mul_f32 v[36:37], v[152:153], v[88:89]
	v_pk_mul_f32 v[2:3], v[158:159], v[46:47]
	v_pk_mul_f32 v[0:1], v[156:157], v[44:45]
	v_bfe_u32 v35, v42, 16, 1
	v_bfe_u32 v45, v38, 16, 1
	v_bfe_u32 v47, v40, 16, 1
	v_bfe_u32 v49, v6, 16, 1
	v_bfe_u32 v44, v43, 16, 1
	v_bfe_u32 v46, v39, 16, 1
	v_bfe_u32 v48, v41, 16, 1
	v_bfe_u32 v50, v7, 16, 1
	v_bfe_u32 v51, v36, 16, 1
	v_bfe_u32 v53, v4, 16, 1
	v_bfe_u32 v55, v0, 16, 1
	v_bfe_u32 v57, v1, 16, 1
	v_bfe_u32 v58, v2, 16, 1
	v_bfe_u32 v59, v3, 16, 1
	v_add3_u32 v35, v42, v35, s75
	v_add3_u32 v38, v38, v45, s75
	v_add3_u32 v40, v40, v47, s75
	v_add3_u32 v6, v6, v49, s75
	v_bfe_u32 v52, v37, 16, 1
	v_bfe_u32 v54, v5, 16, 1
	v_add3_u32 v42, v43, v44, s75
	v_add3_u32 v39, v39, v46, s75
	v_add3_u32 v41, v41, v48, s75
	v_add3_u32 v7, v7, v50, s75
	v_add3_u32 v36, v36, v51, s75
	v_add3_u32 v4, v4, v53, s75
	v_add3_u32 v0, v0, v55, s75
	v_add3_u32 v43, v1, v57, s75
	v_add3_u32 v1, v2, v58, s75
	v_add3_u32 v44, v3, v59, s75
	v_lshrrev_b32_e32 v2, 16, v35
	v_lshrrev_b32_e32 v3, 16, v38
	v_lshrrev_b32_e32 v35, 16, v40
	v_lshrrev_b32_e32 v6, 16, v6
	v_add3_u32 v37, v37, v52, s75
	v_add3_u32 v5, v5, v54, s75
	v_lshrrev_b32_e32 v36, 16, v36
	v_lshrrev_b32_e32 v38, 16, v4
	v_lshrrev_b32_e32 v40, 16, v0
	v_lshrrev_b32_e32 v45, 16, v1
	v_and_or_b32 v0, v42, s15, v2
	v_and_or_b32 v1, v39, s15, v3
	v_and_or_b32 v2, v41, s15, v35
	v_and_or_b32 v3, v7, s15, v6
	v_and_or_b32 v4, v37, s15, v36
	v_and_or_b32 v5, v5, s15, v38
	v_and_or_b32 v6, v43, s15, v40
	v_and_or_b32 v7, v44, s15, v45
	global_store_dwordx4 v[14:15], v[0:3], off offset:2048 sc1
	global_store_dwordx4 v[16:17], v[4:7], off offset:2048 sc1
	s_nop 0
	v_pk_mul_f32 v[18:19], v[18:19], v[34:35] op_sel_hi:[1,0]
	v_pk_mul_f32 v[20:21], v[20:21], v[34:35] op_sel_hi:[1,0]
	v_pk_mul_f32 v[22:23], v[22:23], v[34:35] op_sel_hi:[1,0]
	v_pk_mul_f32 v[24:25], v[24:25], v[34:35] op_sel_hi:[1,0]
	v_pk_mul_f32 v[26:27], v[26:27], v[56:57] op_sel_hi:[1,0]
	v_pk_mul_f32 v[28:29], v[28:29], v[56:57] op_sel_hi:[1,0]
	v_pk_mul_f32 v[30:31], v[30:31], v[56:57] op_sel_hi:[1,0]
	v_pk_mul_f32 v[32:33], v[32:33], v[56:57] op_sel_hi:[1,0]
	v_pk_mul_f32 v[20:21], v[20:21], v[166:167]
	v_pk_mul_f32 v[18:19], v[18:19], v[164:165]
	v_pk_mul_f32 v[24:25], v[24:25], v[170:171]
	v_pk_mul_f32 v[22:23], v[22:23], v[168:169]
	v_pk_mul_f32 v[6:7], v[28:29], v[166:167]
	v_pk_mul_f32 v[4:5], v[26:27], v[164:165]
	v_pk_mul_f32 v[2:3], v[32:33], v[170:171]
	v_pk_mul_f32 v[0:1], v[30:31], v[168:169]
	v_bfe_u32 v26, v18, 16, 1
	v_bfe_u32 v28, v20, 16, 1
	v_bfe_u32 v30, v22, 16, 1
	v_bfe_u32 v32, v24, 16, 1
	v_bfe_u32 v27, v19, 16, 1
	v_bfe_u32 v29, v21, 16, 1
	v_bfe_u32 v31, v23, 16, 1
	v_bfe_u32 v33, v25, 16, 1
	v_bfe_u32 v34, v4, 16, 1
	v_bfe_u32 v36, v6, 16, 1
	v_bfe_u32 v38, v0, 16, 1
	v_bfe_u32 v39, v1, 16, 1
	v_bfe_u32 v40, v2, 16, 1
	v_bfe_u32 v41, v3, 16, 1
	v_add3_u32 v18, v18, v26, s75
	v_add3_u32 v20, v20, v28, s75
	v_add3_u32 v22, v22, v30, s75
	v_add3_u32 v24, v24, v32, s75
	v_bfe_u32 v35, v5, 16, 1
	v_bfe_u32 v37, v7, 16, 1
	v_add3_u32 v19, v19, v27, s75
	v_add3_u32 v21, v21, v29, s75
	v_add3_u32 v23, v23, v31, s75
	v_add3_u32 v25, v25, v33, s75
	v_add3_u32 v4, v4, v34, s75
	v_add3_u32 v6, v6, v36, s75
	v_add3_u32 v0, v0, v38, s75
	v_add3_u32 v26, v1, v39, s75
	v_add3_u32 v1, v2, v40, s75
	v_add3_u32 v27, v3, v41, s75
	v_lshrrev_b32_e32 v2, 16, v18
	v_lshrrev_b32_e32 v3, 16, v20
	v_lshrrev_b32_e32 v18, 16, v22
	v_lshrrev_b32_e32 v20, 16, v24
	v_add3_u32 v5, v5, v35, s75
	v_add3_u32 v7, v7, v37, s75
	v_lshrrev_b32_e32 v4, 16, v4
	v_lshrrev_b32_e32 v6, 16, v6
	v_lshrrev_b32_e32 v22, 16, v0
	v_lshrrev_b32_e32 v24, 16, v1
	v_and_or_b32 v0, v19, s15, v2
	v_and_or_b32 v1, v21, s15, v3
	v_and_or_b32 v2, v23, s15, v18
	v_and_or_b32 v3, v25, s15, v20
	v_and_or_b32 v4, v5, s15, v4
	v_and_or_b32 v5, v7, s15, v6
	v_and_or_b32 v6, v26, s15, v22
	v_and_or_b32 v7, v27, s15, v24
	global_store_dwordx4 v[14:15], v[0:3], off offset:3072 sc1
	global_store_dwordx4 v[16:17], v[4:7], off offset:3072 sc1
	s_cbranch_scc0 .LBB0_802

.LBB0_927:
	v_add_u32_e32 v120, s23, v230
	v_add_u32_e32 v148, s26, v230
	ds_read_b128 v[88:91], v120
	ds_read_b128 v[100:103], v120 offset:1024
	ds_read_b128 v[112:115], v120 offset:2048
	ds_read_b128 v[120:123], v120 offset:3072
	ds_read_b128 v[124:127], v148
	ds_read_b128 v[140:143], v148 offset:1024
	ds_read_b128 v[144:147], v148 offset:2048
	ds_read_b128 v[148:151], v148 offset:3072
	s_add_u32 s10, s8, 0x100
	s_addc_u32 s11, s9, 0
	s_cmpk_eq_i32 s52, 0x54
	s_cselect_b32 s15, s5, s11
	s_cselect_b32 s14, s4, s10
	s_cselect_b32 s13, s7, s51
	s_cselect_b32 s12, s6, s50
	v_lshl_add_u64 v[206:207], s[8:9], 0, v[204:205]
	s_add_i32 m0, s29, 0xc000
	ds_read_b128 v[152:155], v232
	ds_read_b128 v[170:173], v232 offset:1024
	ds_read_b128 v[174:177], v232 offset:2048
	ds_read_b128 v[178:181], v232 offset:3072
	ds_read_b128 v[182:185], v232 offset:4096
	ds_read_b128 v[186:189], v232 offset:5120
	ds_read_b128 v[190:193], v232 offset:6144
	ds_read_b128 v[194:197], v232 offset:7168
	global_load_lds_dwordx4 v[206:207], off
	v_lshl_add_u64 v[206:207], s[8:9], 0, v[202:203]
	s_add_i32 m0, s29, 0xe000
	s_nop 0
	global_load_lds_dwordx4 v[206:207], off
	s_waitcnt vmcnt(8)
	s_waitcnt lgkmcnt(0)
	s_barrier
	s_setprio 1
	s_waitcnt lgkmcnt(0)
	v_mfma_f32_16x16x32_bf16 v[166:169], v[88:91], v[152:155], v[166:169]
	v_mfma_f32_16x16x32_bf16 v[156:159], v[112:115], v[152:155], v[156:159]
	v_mfma_f32_16x16x32_bf16 v[128:131], v[88:91], v[174:177], v[128:131]
	v_mfma_f32_16x16x32_bf16 v[116:119], v[112:115], v[174:177], v[116:119]
	v_mfma_f32_16x16x32_bf16 v[96:99], v[88:91], v[182:185], v[96:99]
	v_mfma_f32_16x16x32_bf16 v[92:95], v[112:115], v[182:185], v[92:95]
	v_mfma_f32_16x16x32_bf16 v[76:79], v[88:91], v[190:193], v[76:79]
	v_mfma_f32_16x16x32_bf16 v[72:75], v[112:115], v[190:193], v[72:75]
	v_mfma_f32_16x16x32_bf16 v[166:169], v[100:103], v[170:173], v[166:169]
	v_mfma_f32_16x16x32_bf16 v[156:159], v[120:123], v[170:173], v[156:159]
	v_mfma_f32_16x16x32_bf16 v[128:131], v[100:103], v[178:181], v[128:131]
	v_mfma_f32_16x16x32_bf16 v[116:119], v[120:123], v[178:181], v[116:119]
	v_mfma_f32_16x16x32_bf16 v[96:99], v[100:103], v[186:189], v[96:99]
	v_mfma_f32_16x16x32_bf16 v[92:95], v[120:123], v[186:189], v[92:95]
	v_mfma_f32_16x16x32_bf16 v[76:79], v[100:103], v[194:197], v[76:79]
	v_mfma_f32_16x16x32_bf16 v[72:75], v[120:123], v[194:197], v[72:75]
	s_setprio 0
	s_setprio 1
	v_mfma_f32_16x16x32_bf16 v[136:139], v[124:127], v[152:155], v[136:139]
	v_mfma_f32_16x16x32_bf16 v[132:135], v[144:147], v[152:155], v[132:135]
	v_mfma_f32_16x16x32_bf16 v[108:111], v[124:127], v[174:177], v[108:111]
	v_mfma_f32_16x16x32_bf16 v[104:107], v[144:147], v[174:177], v[104:107]
	v_mfma_f32_16x16x32_bf16 v[84:87], v[124:127], v[182:185], v[84:87]
	v_mfma_f32_16x16x32_bf16 v[80:83], v[144:147], v[182:185], v[80:83]
	v_mfma_f32_16x16x32_bf16 v[68:71], v[124:127], v[190:193], v[68:71]
	v_mfma_f32_16x16x32_bf16 v[64:67], v[144:147], v[190:193], v[64:67]
	v_mfma_f32_16x16x32_bf16 v[136:139], v[140:143], v[170:173], v[136:139]
	v_mfma_f32_16x16x32_bf16 v[132:135], v[148:151], v[170:173], v[132:135]
	v_mfma_f32_16x16x32_bf16 v[108:111], v[140:143], v[178:181], v[108:111]
	v_mfma_f32_16x16x32_bf16 v[104:107], v[148:151], v[178:181], v[104:107]
	v_mfma_f32_16x16x32_bf16 v[84:87], v[140:143], v[186:189], v[84:87]
	v_mfma_f32_16x16x32_bf16 v[80:83], v[148:151], v[186:189], v[80:83]
	v_mfma_f32_16x16x32_bf16 v[68:71], v[140:143], v[194:197], v[68:71]
	v_mfma_f32_16x16x32_bf16 v[64:67], v[148:151], v[194:197], v[64:67]
	s_setprio 0
	s_barrier
	s_mov_b32 m0, s24
	v_lshl_add_u64 v[206:207], s[12:13], 0, v[160:161]
	s_add_u32 s8, s12, 0x160000
	ds_read_b128 v[152:155], v232 offset:16384
	ds_read_b128 v[170:173], v232 offset:17408
	ds_read_b128 v[174:177], v232 offset:18432
	ds_read_b128 v[178:181], v232 offset:19456
	ds_read_b128 v[182:185], v232 offset:20480
	ds_read_b128 v[186:189], v232 offset:21504
	ds_read_b128 v[190:193], v232 offset:22528
	ds_read_b128 v[194:197], v232 offset:23552
	global_load_lds_dwordx4 v[206:207], off
	v_lshl_add_u64 v[208:209], s[12:13], 0, v[200:201]
	s_mov_b32 m0, s25
	s_addc_u32 s9, s13, 0
	global_load_lds_dwordx4 v[208:209], off
	v_lshl_add_u64 v[210:211], s[8:9], 0, v[160:161]
	s_mov_b32 m0, s27
	v_lshl_add_u64 v[212:213], s[14:15], 0, v[198:199]
	global_load_lds_dwordx4 v[210:211], off
	v_lshl_add_u64 v[210:211], s[8:9], 0, v[200:201]
	s_mov_b32 m0, s28
	s_nop 0
	global_load_lds_dwordx4 v[210:211], off
	v_lshl_add_u64 v[210:211], s[14:15], 0, v[162:163]
	s_mov_b32 m0, s29
	s_nop 0
	global_load_lds_dwordx4 v[210:211], off
	s_mov_b32 m0, s30
	s_nop 0
	global_load_lds_dwordx4 v[212:213], off
	s_waitcnt vmcnt(8)
	s_waitcnt lgkmcnt(0)
	s_barrier
	s_setprio 1
	s_waitcnt lgkmcnt(0)
	v_mfma_f32_16x16x32_bf16 v[60:63], v[88:91], v[152:155], v[60:63]
	v_mfma_f32_16x16x32_bf16 v[56:59], v[112:115], v[152:155], v[56:59]
	v_mfma_f32_16x16x32_bf16 v[44:47], v[88:91], v[174:177], v[44:47]
	v_mfma_f32_16x16x32_bf16 v[40:43], v[112:115], v[174:177], v[40:43]
	v_mfma_f32_16x16x32_bf16 v[28:31], v[88:91], v[182:185], v[28:31]
	v_mfma_f32_16x16x32_bf16 v[24:27], v[112:115], v[182:185], v[24:27]
	v_mfma_f32_16x16x32_bf16 v[12:15], v[88:91], v[190:193], v[12:15]
	v_mfma_f32_16x16x32_bf16 v[8:11], v[112:115], v[190:193], v[8:11]
	v_mfma_f32_16x16x32_bf16 v[60:63], v[100:103], v[170:173], v[60:63]
	v_mfma_f32_16x16x32_bf16 v[56:59], v[120:123], v[170:173], v[56:59]
	v_mfma_f32_16x16x32_bf16 v[44:47], v[100:103], v[178:181], v[44:47]
	v_mfma_f32_16x16x32_bf16 v[40:43], v[120:123], v[178:181], v[40:43]
	v_mfma_f32_16x16x32_bf16 v[28:31], v[100:103], v[186:189], v[28:31]
	v_mfma_f32_16x16x32_bf16 v[24:27], v[120:123], v[186:189], v[24:27]
	v_mfma_f32_16x16x32_bf16 v[12:15], v[100:103], v[194:197], v[12:15]
	v_mfma_f32_16x16x32_bf16 v[8:11], v[120:123], v[194:197], v[8:11]
	s_setprio 0
	s_setprio 1
	v_mfma_f32_16x16x32_bf16 v[52:55], v[124:127], v[152:155], v[52:55]
	v_mfma_f32_16x16x32_bf16 v[48:51], v[144:147], v[152:155], v[48:51]
	v_mfma_f32_16x16x32_bf16 v[36:39], v[124:127], v[174:177], v[36:39]
	v_mfma_f32_16x16x32_bf16 v[32:35], v[144:147], v[174:177], v[32:35]
	v_mfma_f32_16x16x32_bf16 v[20:23], v[124:127], v[182:185], v[20:23]
	v_mfma_f32_16x16x32_bf16 v[16:19], v[144:147], v[182:185], v[16:19]
	v_mfma_f32_16x16x32_bf16 v[4:7], v[124:127], v[190:193], v[4:7]
	v_mfma_f32_16x16x32_bf16 v[0:3], v[144:147], v[190:193], v[0:3]
	v_mfma_f32_16x16x32_bf16 v[52:55], v[140:143], v[170:173], v[52:55]
	v_mfma_f32_16x16x32_bf16 v[48:51], v[148:151], v[170:173], v[48:51]
	v_mfma_f32_16x16x32_bf16 v[36:39], v[140:143], v[178:181], v[36:39]
	v_mfma_f32_16x16x32_bf16 v[32:35], v[148:151], v[178:181], v[32:35]
	v_mfma_f32_16x16x32_bf16 v[20:23], v[140:143], v[186:189], v[20:23]
	v_mfma_f32_16x16x32_bf16 v[16:19], v[148:151], v[186:189], v[16:19]
	v_mfma_f32_16x16x32_bf16 v[4:7], v[140:143], v[194:197], v[4:7]
	v_mfma_f32_16x16x32_bf16 v[0:3], v[148:151], v[194:197], v[0:3]
	s_setprio 0
	s_barrier
	v_add_u32_e32 v120, s36, v230
	v_add_u32_e32 v148, s41, v230
	ds_read_b128 v[88:91], v120
	ds_read_b128 v[100:103], v120 offset:1024
	ds_read_b128 v[112:115], v120 offset:2048
	ds_read_b128 v[120:123], v120 offset:3072
	ds_read_b128 v[124:127], v148
	ds_read_b128 v[140:143], v148 offset:1024
	ds_read_b128 v[144:147], v148 offset:2048
	ds_read_b128 v[148:151], v148 offset:3072
	s_add_u32 s8, s14, 0x160000
	s_addc_u32 s9, s15, 0
	s_mov_b32 m0, s31
	v_lshl_add_u64 v[214:215], s[8:9], 0, v[162:163]
	ds_read_b128 v[152:155], v232 offset:32768
	ds_read_b128 v[170:173], v232 offset:33792
	ds_read_b128 v[174:177], v232 offset:34816
	ds_read_b128 v[178:181], v232 offset:35840
	ds_read_b128 v[182:185], v232 offset:36864
	ds_read_b128 v[186:189], v232 offset:37888
	ds_read_b128 v[190:193], v232 offset:38912
	ds_read_b128 v[194:197], v232 offset:39936
	global_load_lds_dwordx4 v[214:215], off
	v_lshl_add_u64 v[214:215], s[8:9], 0, v[198:199]
	s_mov_b32 m0, s34
	s_nop 0
	global_load_lds_dwordx4 v[214:215], off
	s_waitcnt vmcnt(8)
	s_waitcnt lgkmcnt(0)
	s_barrier
	s_setprio 1
	s_waitcnt lgkmcnt(0)
	v_mfma_f32_16x16x32_bf16 v[166:169], v[88:91], v[152:155], v[166:169]
	v_mfma_f32_16x16x32_bf16 v[156:159], v[112:115], v[152:155], v[156:159]
	v_mfma_f32_16x16x32_bf16 v[128:131], v[88:91], v[174:177], v[128:131]
	v_mfma_f32_16x16x32_bf16 v[116:119], v[112:115], v[174:177], v[116:119]
	v_mfma_f32_16x16x32_bf16 v[96:99], v[88:91], v[182:185], v[96:99]
	v_mfma_f32_16x16x32_bf16 v[92:95], v[112:115], v[182:185], v[92:95]
	v_mfma_f32_16x16x32_bf16 v[76:79], v[88:91], v[190:193], v[76:79]
	v_mfma_f32_16x16x32_bf16 v[72:75], v[112:115], v[190:193], v[72:75]
	v_mfma_f32_16x16x32_bf16 v[166:169], v[100:103], v[170:173], v[166:169]
	v_mfma_f32_16x16x32_bf16 v[156:159], v[120:123], v[170:173], v[156:159]
	v_mfma_f32_16x16x32_bf16 v[128:131], v[100:103], v[178:181], v[128:131]
	v_mfma_f32_16x16x32_bf16 v[116:119], v[120:123], v[178:181], v[116:119]
	v_mfma_f32_16x16x32_bf16 v[96:99], v[100:103], v[186:189], v[96:99]
	v_mfma_f32_16x16x32_bf16 v[92:95], v[120:123], v[186:189], v[92:95]
	v_mfma_f32_16x16x32_bf16 v[76:79], v[100:103], v[194:197], v[76:79]
	v_mfma_f32_16x16x32_bf16 v[72:75], v[120:123], v[194:197], v[72:75]
	s_setprio 0
	s_setprio 1
	v_mfma_f32_16x16x32_bf16 v[136:139], v[124:127], v[152:155], v[136:139]
	v_mfma_f32_16x16x32_bf16 v[132:135], v[144:147], v[152:155], v[132:135]
	v_mfma_f32_16x16x32_bf16 v[108:111], v[124:127], v[174:177], v[108:111]
	v_mfma_f32_16x16x32_bf16 v[104:107], v[144:147], v[174:177], v[104:107]
	v_mfma_f32_16x16x32_bf16 v[84:87], v[124:127], v[182:185], v[84:87]
	v_mfma_f32_16x16x32_bf16 v[80:83], v[144:147], v[182:185], v[80:83]
	v_mfma_f32_16x16x32_bf16 v[68:71], v[124:127], v[190:193], v[68:71]
	v_mfma_f32_16x16x32_bf16 v[64:67], v[144:147], v[190:193], v[64:67]
	v_mfma_f32_16x16x32_bf16 v[136:139], v[140:143], v[170:173], v[136:139]
	v_mfma_f32_16x16x32_bf16 v[132:135], v[148:151], v[170:173], v[132:135]
	v_mfma_f32_16x16x32_bf16 v[108:111], v[140:143], v[178:181], v[108:111]
	v_mfma_f32_16x16x32_bf16 v[104:107], v[148:151], v[178:181], v[104:107]
	v_mfma_f32_16x16x32_bf16 v[84:87], v[140:143], v[186:189], v[84:87]
	v_mfma_f32_16x16x32_bf16 v[80:83], v[148:151], v[186:189], v[80:83]
	v_mfma_f32_16x16x32_bf16 v[68:71], v[140:143], v[194:197], v[68:71]
	v_mfma_f32_16x16x32_bf16 v[64:67], v[148:151], v[194:197], v[64:67]
	s_setprio 0
	s_barrier
	s_mov_b32 m0, s37
	v_lshl_add_u64 v[206:207], v[206:207], 0, s[86:87]
	s_add_u32 s8, s12, 0x160080
	ds_read_b128 v[152:155], v232 offset:49152
	ds_read_b128 v[170:173], v232 offset:50176
	ds_read_b128 v[174:177], v232 offset:51200
	ds_read_b128 v[178:181], v232 offset:52224
	ds_read_b128 v[182:185], v232 offset:53248
	ds_read_b128 v[186:189], v232 offset:54272
	ds_read_b128 v[190:193], v232 offset:55296
	ds_read_b128 v[194:197], v232 offset:56320
	global_load_lds_dwordx4 v[206:207], off
	v_lshl_add_u64 v[206:207], v[208:209], 0, s[86:87]
	s_mov_b32 m0, s38
	s_addc_u32 s9, s13, 0
	global_load_lds_dwordx4 v[206:207], off
	v_lshl_add_u64 v[206:207], s[8:9], 0, v[160:161]
	s_mov_b32 m0, s42
	s_nop 0
	global_load_lds_dwordx4 v[206:207], off
	v_lshl_add_u64 v[206:207], s[8:9], 0, v[200:201]
	s_mov_b32 m0, s43
	s_nop 0
	global_load_lds_dwordx4 v[206:207], off
	v_lshl_add_u64 v[206:207], v[210:211], 0, s[86:87]
	s_mov_b32 m0, s39
	s_nop 0
	global_load_lds_dwordx4 v[206:207], off
	v_lshl_add_u64 v[206:207], v[212:213], 0, s[86:87]
	s_mov_b32 m0, s40
	s_nop 0
	global_load_lds_dwordx4 v[206:207], off
	s_waitcnt vmcnt(8)
	s_waitcnt lgkmcnt(0)
	s_barrier
	s_setprio 1
	s_waitcnt lgkmcnt(0)
	v_mfma_f32_16x16x32_bf16 v[60:63], v[88:91], v[152:155], v[60:63]
	v_mfma_f32_16x16x32_bf16 v[56:59], v[112:115], v[152:155], v[56:59]
	v_mfma_f32_16x16x32_bf16 v[44:47], v[88:91], v[174:177], v[44:47]
	v_mfma_f32_16x16x32_bf16 v[40:43], v[112:115], v[174:177], v[40:43]
	v_mfma_f32_16x16x32_bf16 v[28:31], v[88:91], v[182:185], v[28:31]
	v_mfma_f32_16x16x32_bf16 v[24:27], v[112:115], v[182:185], v[24:27]
	v_mfma_f32_16x16x32_bf16 v[12:15], v[88:91], v[190:193], v[12:15]
	v_mfma_f32_16x16x32_bf16 v[8:11], v[112:115], v[190:193], v[8:11]
	v_mfma_f32_16x16x32_bf16 v[60:63], v[100:103], v[170:173], v[60:63]
	v_mfma_f32_16x16x32_bf16 v[56:59], v[120:123], v[170:173], v[56:59]
	v_mfma_f32_16x16x32_bf16 v[44:47], v[100:103], v[178:181], v[44:47]
	v_mfma_f32_16x16x32_bf16 v[40:43], v[120:123], v[178:181], v[40:43]
	v_mfma_f32_16x16x32_bf16 v[28:31], v[100:103], v[186:189], v[28:31]
	v_mfma_f32_16x16x32_bf16 v[24:27], v[120:123], v[186:189], v[24:27]
	v_mfma_f32_16x16x32_bf16 v[12:15], v[100:103], v[194:197], v[12:15]
	v_mfma_f32_16x16x32_bf16 v[8:11], v[120:123], v[194:197], v[8:11]
	s_setprio 0
	s_setprio 1
	v_mfma_f32_16x16x32_bf16 v[52:55], v[124:127], v[152:155], v[52:55]
	v_mfma_f32_16x16x32_bf16 v[48:51], v[144:147], v[152:155], v[48:51]
	v_mfma_f32_16x16x32_bf16 v[36:39], v[124:127], v[174:177], v[36:39]
	v_mfma_f32_16x16x32_bf16 v[32:35], v[144:147], v[174:177], v[32:35]
	v_mfma_f32_16x16x32_bf16 v[20:23], v[124:127], v[182:185], v[20:23]
	v_mfma_f32_16x16x32_bf16 v[16:19], v[144:147], v[182:185], v[16:19]
	v_mfma_f32_16x16x32_bf16 v[4:7], v[124:127], v[190:193], v[4:7]
	v_mfma_f32_16x16x32_bf16 v[0:3], v[144:147], v[190:193], v[0:3]
	v_mfma_f32_16x16x32_bf16 v[52:55], v[140:143], v[170:173], v[52:55]
	v_mfma_f32_16x16x32_bf16 v[48:51], v[148:151], v[170:173], v[48:51]
	v_mfma_f32_16x16x32_bf16 v[36:39], v[140:143], v[178:181], v[36:39]
	v_mfma_f32_16x16x32_bf16 v[32:35], v[148:151], v[178:181], v[32:35]
	v_mfma_f32_16x16x32_bf16 v[20:23], v[140:143], v[186:189], v[20:23]
	v_mfma_f32_16x16x32_bf16 v[16:19], v[148:151], v[186:189], v[16:19]
	v_mfma_f32_16x16x32_bf16 v[4:7], v[140:143], v[194:197], v[4:7]
	v_mfma_f32_16x16x32_bf16 v[0:3], v[148:151], v[194:197], v[0:3]
	s_setprio 0
	s_barrier
	s_add_i32 s52, s52, 2
	s_add_u32 s50, s50, 0x100
	s_addc_u32 s51, s51, 0
	s_cmpk_gt_u32 s52, 0x55
	s_mov_b64 s[8:9], s[10:11]
	s_cbranch_scc0 .LBB0_927
	v_lshl_or_b32 v90, s49, 8, v231
	v_lshl_add_u32 v88, s48, 8, v165
	v_ashrrev_i32_e32 v91, 31, v90
	v_lshlrev_b64 v[206:207], 1, v[90:91]
	v_ashrrev_i32_e32 v89, 31, v88
	v_lshl_add_u64 v[90:91], s[0:1], 0, v[206:207]
	v_lshlrev_b64 v[222:223], 12, v[88:89]
	v_lshl_add_u64 v[100:101], v[90:91], 0, v[222:223]
	global_load_dwordx4 v[194:197], v[100:101], off nt
	global_load_dwordx4 v[190:193], v[100:101], off offset:256 nt
	v_or_b32_e32 v100, 16, v88
	v_ashrrev_i32_e32 v101, 31, v100
	v_lshlrev_b64 v[220:221], 12, v[100:101]
	v_lshl_add_u64 v[100:101], v[90:91], 0, v[220:221]
	global_load_dwordx4 v[186:189], v[100:101], off nt
	global_load_dwordx4 v[182:185], v[100:101], off offset:256 nt
	v_or_b32_e32 v100, 32, v88
	v_ashrrev_i32_e32 v101, 31, v100
	v_lshlrev_b64 v[218:219], 12, v[100:101]
	v_lshl_add_u64 v[100:101], v[90:91], 0, v[218:219]
	global_load_dwordx4 v[178:181], v[100:101], off nt
	global_load_dwordx4 v[174:177], v[100:101], off offset:256 nt
	v_or_b32_e32 v88, 48, v88
	v_ashrrev_i32_e32 v89, 31, v88
	v_lshlrev_b64 v[216:217], 12, v[88:89]
	v_lshl_add_u64 v[88:89], v[90:91], 0, v[216:217]
	global_load_dwordx4 v[170:173], v[88:89], off nt
	global_load_dwordx4 v[152:155], v[88:89], off offset:256 nt
	v_lshl_add_u64 v[214:215], v[222:223], 0, s[54:55]
	v_lshl_add_u64 v[88:89], v[90:91], 0, v[214:215]
	global_load_dwordx4 v[148:151], v[88:89], off nt
	global_load_dwordx4 v[144:147], v[88:89], off offset:256 nt
	s_mov_b64 s[8:9], 0x90000
	v_lshl_add_u64 v[212:213], v[222:223], 0, s[8:9]
	v_lshl_add_u64 v[88:89], v[90:91], 0, v[212:213]
	global_load_dwordx4 v[140:143], v[88:89], off nt
	global_load_dwordx4 v[124:127], v[88:89], off offset:256 nt
	s_mov_b64 s[8:9], 0xa0000
	v_lshl_add_u64 v[210:211], v[222:223], 0, s[8:9]
	v_lshl_add_u64 v[88:89], v[90:91], 0, v[210:211]
	global_load_dwordx4 v[120:123], v[88:89], off nt
	global_load_dwordx4 v[112:115], v[88:89], off offset:256 nt
	s_mov_b64 s[8:9], 0xb0000
	v_lshl_add_u64 v[208:209], v[222:223], 0, s[8:9]
	v_lshl_add_u64 v[88:89], v[90:91], 0, v[208:209]
	global_load_dwordx4 v[100:103], v[88:89], off nt
	s_nop 0
	global_load_dwordx4 v[88:91], v[88:89], off offset:256 nt
	s_and_b64 vcc, exec, s[2:3]
	s_mov_b32 s49, s46
	s_mov_b32 s48, s47
	s_mov_b64 s[10:11], s[6:7]
	s_mov_b64 s[8:9], s[4:5]
	s_waitcnt vmcnt(0)
	v_cvt_f32_f16_e32 v224, v194
	v_cvt_f32_f16_sdwa v225, v194 dst_sel:DWORD dst_unused:UNUSED_PAD src0_sel:WORD_1
	v_pk_add_f32 v[166:167], v[166:167], v[224:225]
	s_nop 0
	v_cvt_pk_f16_f32 v194, v166, v167
	v_cvt_f32_f16_e32 v166, v196
	v_cvt_f32_f16_sdwa v167, v196 dst_sel:DWORD dst_unused:UNUSED_PAD src0_sel:WORD_1
	v_pk_add_f32 v[156:157], v[156:157], v[166:167]
	s_nop 0
	v_cvt_pk_f16_f32 v196, v156, v157
	v_cvt_f32_f16_e32 v156, v195
	v_cvt_f32_f16_sdwa v157, v195 dst_sel:DWORD dst_unused:UNUSED_PAD src0_sel:WORD_1
	v_pk_add_f32 v[156:157], v[168:169], v[156:157]
	s_nop 0
	v_cvt_pk_f16_f32 v195, v156, v157
	v_cvt_f32_f16_e32 v156, v197
	v_cvt_f32_f16_sdwa v157, v197 dst_sel:DWORD dst_unused:UNUSED_PAD src0_sel:WORD_1
	v_pk_add_f32 v[156:157], v[158:159], v[156:157]
	s_nop 0
	v_cvt_pk_f16_f32 v197, v156, v157
	v_lshl_add_u64 v[156:157], s[0:1], 0, v[222:223]
	v_lshl_add_u64 v[166:167], v[156:157], 0, v[206:207]
	v_cvt_f32_f16_e32 v156, v190
	v_cvt_f32_f16_sdwa v157, v190 dst_sel:DWORD dst_unused:UNUSED_PAD src0_sel:WORD_1
	global_store_dwordx4 v[166:167], v[194:197], off sc1
	v_pk_add_f32 v[136:137], v[136:137], v[156:157]
	s_nop 0
	v_cvt_pk_f16_f32 v156, v136, v137
	v_cvt_f32_f16_e32 v136, v192
	v_cvt_f32_f16_sdwa v137, v192 dst_sel:DWORD dst_unused:UNUSED_PAD src0_sel:WORD_1
	v_pk_add_f32 v[132:133], v[132:133], v[136:137]
	s_nop 0
	v_cvt_pk_f16_f32 v158, v132, v133
	v_cvt_f32_f16_e32 v132, v191
	v_cvt_f32_f16_sdwa v133, v191 dst_sel:DWORD dst_unused:UNUSED_PAD src0_sel:WORD_1
	v_pk_add_f32 v[132:133], v[138:139], v[132:133]
	s_nop 0
	v_cvt_pk_f16_f32 v157, v132, v133
	v_cvt_f32_f16_e32 v132, v193
	v_cvt_f32_f16_sdwa v133, v193 dst_sel:DWORD dst_unused:UNUSED_PAD src0_sel:WORD_1
	v_pk_add_f32 v[132:133], v[134:135], v[132:133]
	s_nop 0
	v_cvt_pk_f16_f32 v159, v132, v133
	v_cvt_f32_f16_e32 v132, v186
	v_cvt_f32_f16_sdwa v133, v186 dst_sel:DWORD dst_unused:UNUSED_PAD src0_sel:WORD_1
	global_store_dwordx4 v[166:167], v[156:159], off offset:256 sc1
	v_pk_add_f32 v[128:129], v[128:129], v[132:133]
	s_nop 0
	v_cvt_pk_f16_f32 v132, v128, v129
	v_cvt_f32_f16_e32 v128, v188
	v_cvt_f32_f16_sdwa v129, v188 dst_sel:DWORD dst_unused:UNUSED_PAD src0_sel:WORD_1
	v_pk_add_f32 v[116:117], v[116:117], v[128:129]
	s_nop 0
	v_cvt_pk_f16_f32 v134, v116, v117
	v_cvt_f32_f16_e32 v116, v187
	v_cvt_f32_f16_sdwa v117, v187 dst_sel:DWORD dst_unused:UNUSED_PAD src0_sel:WORD_1
	v_pk_add_f32 v[116:117], v[130:131], v[116:117]
	s_nop 0
	v_cvt_pk_f16_f32 v133, v116, v117
	v_cvt_f32_f16_e32 v116, v189
	v_cvt_f32_f16_sdwa v117, v189 dst_sel:DWORD dst_unused:UNUSED_PAD src0_sel:WORD_1
	v_pk_add_f32 v[116:117], v[118:119], v[116:117]
	s_nop 0
	v_cvt_pk_f16_f32 v135, v116, v117
	v_lshl_add_u64 v[116:117], s[0:1], 0, v[220:221]
	v_lshl_add_u64 v[128:129], v[116:117], 0, v[206:207]
	v_cvt_f32_f16_e32 v116, v182
	v_cvt_f32_f16_sdwa v117, v182 dst_sel:DWORD dst_unused:UNUSED_PAD src0_sel:WORD_1
	global_store_dwordx4 v[128:129], v[132:135], off sc1
	v_pk_add_f32 v[108:109], v[108:109], v[116:117]
	s_nop 0
	v_cvt_pk_f16_f32 v116, v108, v109
	v_cvt_f32_f16_e32 v108, v184
	v_cvt_f32_f16_sdwa v109, v184 dst_sel:DWORD dst_unused:UNUSED_PAD src0_sel:WORD_1
	v_pk_add_f32 v[104:105], v[104:105], v[108:109]
	s_nop 0
	v_cvt_pk_f16_f32 v118, v104, v105
	v_cvt_f32_f16_e32 v104, v183
	v_cvt_f32_f16_sdwa v105, v183 dst_sel:DWORD dst_unused:UNUSED_PAD src0_sel:WORD_1
	v_pk_add_f32 v[104:105], v[110:111], v[104:105]
	s_nop 0
	v_cvt_pk_f16_f32 v117, v104, v105
	v_cvt_f32_f16_e32 v104, v185
	v_cvt_f32_f16_sdwa v105, v185 dst_sel:DWORD dst_unused:UNUSED_PAD src0_sel:WORD_1
	v_pk_add_f32 v[104:105], v[106:107], v[104:105]
	s_nop 0
	v_cvt_pk_f16_f32 v119, v104, v105
	v_cvt_f32_f16_e32 v104, v178
	v_cvt_f32_f16_sdwa v105, v178 dst_sel:DWORD dst_unused:UNUSED_PAD src0_sel:WORD_1
	global_store_dwordx4 v[128:129], v[116:119], off offset:256 sc1
	v_pk_add_f32 v[96:97], v[96:97], v[104:105]
	s_nop 0
	v_cvt_pk_f16_f32 v104, v96, v97
	v_cvt_f32_f16_e32 v96, v180
	v_cvt_f32_f16_sdwa v97, v180 dst_sel:DWORD dst_unused:UNUSED_PAD src0_sel:WORD_1
	v_pk_add_f32 v[92:93], v[92:93], v[96:97]
	s_nop 0
	v_cvt_pk_f16_f32 v106, v92, v93
	v_cvt_f32_f16_e32 v92, v179
	v_cvt_f32_f16_sdwa v93, v179 dst_sel:DWORD dst_unused:UNUSED_PAD src0_sel:WORD_1
	v_pk_add_f32 v[92:93], v[98:99], v[92:93]
	s_nop 0
	v_cvt_pk_f16_f32 v105, v92, v93
	v_cvt_f32_f16_e32 v92, v181
	v_cvt_f32_f16_sdwa v93, v181 dst_sel:DWORD dst_unused:UNUSED_PAD src0_sel:WORD_1
	v_pk_add_f32 v[92:93], v[94:95], v[92:93]
	s_nop 0
	v_cvt_pk_f16_f32 v107, v92, v93
	v_lshl_add_u64 v[92:93], s[0:1], 0, v[218:219]
	v_lshl_add_u64 v[96:97], v[92:93], 0, v[206:207]
	v_cvt_f32_f16_e32 v92, v174
	v_cvt_f32_f16_sdwa v93, v174 dst_sel:DWORD dst_unused:UNUSED_PAD src0_sel:WORD_1
	global_store_dwordx4 v[96:97], v[104:107], off sc1
	v_pk_add_f32 v[84:85], v[84:85], v[92:93]
	s_nop 0
	v_cvt_pk_f16_f32 v92, v84, v85
	v_cvt_f32_f16_e32 v84, v176
	v_cvt_f32_f16_sdwa v85, v176 dst_sel:DWORD dst_unused:UNUSED_PAD src0_sel:WORD_1
	v_pk_add_f32 v[80:81], v[80:81], v[84:85]
	s_nop 0
	v_cvt_pk_f16_f32 v94, v80, v81
	v_cvt_f32_f16_e32 v80, v175
	v_cvt_f32_f16_sdwa v81, v175 dst_sel:DWORD dst_unused:UNUSED_PAD src0_sel:WORD_1
	v_pk_add_f32 v[80:81], v[86:87], v[80:81]
	s_nop 0
	v_cvt_pk_f16_f32 v93, v80, v81
	v_cvt_f32_f16_e32 v80, v177
	v_cvt_f32_f16_sdwa v81, v177 dst_sel:DWORD dst_unused:UNUSED_PAD src0_sel:WORD_1
	v_pk_add_f32 v[80:81], v[82:83], v[80:81]
	s_nop 0
	v_cvt_pk_f16_f32 v95, v80, v81
	v_cvt_f32_f16_e32 v80, v170
	v_cvt_f32_f16_sdwa v81, v170 dst_sel:DWORD dst_unused:UNUSED_PAD src0_sel:WORD_1
	global_store_dwordx4 v[96:97], v[92:95], off offset:256 sc1
	v_pk_add_f32 v[76:77], v[76:77], v[80:81]
	s_nop 0
	v_cvt_pk_f16_f32 v80, v76, v77
	v_cvt_f32_f16_e32 v76, v172
	v_cvt_f32_f16_sdwa v77, v172 dst_sel:DWORD dst_unused:UNUSED_PAD src0_sel:WORD_1
	v_pk_add_f32 v[72:73], v[72:73], v[76:77]
	s_nop 0
	v_cvt_pk_f16_f32 v82, v72, v73
	v_cvt_f32_f16_e32 v72, v171
	v_cvt_f32_f16_sdwa v73, v171 dst_sel:DWORD dst_unused:UNUSED_PAD src0_sel:WORD_1
	v_pk_add_f32 v[72:73], v[78:79], v[72:73]
	s_nop 0
	v_cvt_pk_f16_f32 v81, v72, v73
	v_cvt_f32_f16_e32 v72, v173
	v_cvt_f32_f16_sdwa v73, v173 dst_sel:DWORD dst_unused:UNUSED_PAD src0_sel:WORD_1
	v_pk_add_f32 v[72:73], v[74:75], v[72:73]
	s_nop 0
	v_cvt_pk_f16_f32 v83, v72, v73
	v_lshl_add_u64 v[72:73], s[0:1], 0, v[216:217]
	v_lshl_add_u64 v[76:77], v[72:73], 0, v[206:207]
	v_cvt_f32_f16_e32 v72, v152
	v_cvt_f32_f16_sdwa v73, v152 dst_sel:DWORD dst_unused:UNUSED_PAD src0_sel:WORD_1
	global_store_dwordx4 v[76:77], v[80:83], off sc1
	v_pk_add_f32 v[68:69], v[68:69], v[72:73]
	s_nop 0
	v_cvt_pk_f16_f32 v72, v68, v69
	v_cvt_f32_f16_e32 v68, v154
	v_cvt_f32_f16_sdwa v69, v154 dst_sel:DWORD dst_unused:UNUSED_PAD src0_sel:WORD_1
	v_pk_add_f32 v[64:65], v[64:65], v[68:69]
	s_nop 0
	v_cvt_pk_f16_f32 v74, v64, v65
	v_cvt_f32_f16_e32 v64, v153
	v_cvt_f32_f16_sdwa v65, v153 dst_sel:DWORD dst_unused:UNUSED_PAD src0_sel:WORD_1
	v_pk_add_f32 v[64:65], v[70:71], v[64:65]
	s_nop 0
	v_cvt_pk_f16_f32 v73, v64, v65
	v_cvt_f32_f16_e32 v64, v155
	v_cvt_f32_f16_sdwa v65, v155 dst_sel:DWORD dst_unused:UNUSED_PAD src0_sel:WORD_1
	v_pk_add_f32 v[64:65], v[66:67], v[64:65]
	s_nop 0
	v_cvt_pk_f16_f32 v75, v64, v65
	v_cvt_f32_f16_e32 v64, v148
	v_cvt_f32_f16_sdwa v65, v148 dst_sel:DWORD dst_unused:UNUSED_PAD src0_sel:WORD_1
	global_store_dwordx4 v[76:77], v[72:75], off offset:256 sc1
	v_pk_add_f32 v[60:61], v[60:61], v[64:65]
	s_nop 0
	v_cvt_pk_f16_f32 v64, v60, v61
	v_cvt_f32_f16_e32 v60, v150
	v_cvt_f32_f16_sdwa v61, v150 dst_sel:DWORD dst_unused:UNUSED_PAD src0_sel:WORD_1
	v_pk_add_f32 v[56:57], v[56:57], v[60:61]
	s_nop 0
	v_cvt_pk_f16_f32 v66, v56, v57
	v_cvt_f32_f16_e32 v56, v149
	v_cvt_f32_f16_sdwa v57, v149 dst_sel:DWORD dst_unused:UNUSED_PAD src0_sel:WORD_1
	v_pk_add_f32 v[56:57], v[62:63], v[56:57]
	s_nop 0
	v_cvt_pk_f16_f32 v65, v56, v57
	v_cvt_f32_f16_e32 v56, v151
	v_cvt_f32_f16_sdwa v57, v151 dst_sel:DWORD dst_unused:UNUSED_PAD src0_sel:WORD_1
	v_pk_add_f32 v[56:57], v[58:59], v[56:57]
	s_nop 0
	v_cvt_pk_f16_f32 v67, v56, v57
	v_lshl_add_u64 v[56:57], s[0:1], 0, v[214:215]
	v_lshl_add_u64 v[60:61], v[56:57], 0, v[206:207]
	v_cvt_f32_f16_e32 v56, v144
	v_cvt_f32_f16_sdwa v57, v144 dst_sel:DWORD dst_unused:UNUSED_PAD src0_sel:WORD_1
	global_store_dwordx4 v[60:61], v[64:67], off sc1
	v_pk_add_f32 v[52:53], v[52:53], v[56:57]
	s_nop 0
	v_cvt_pk_f16_f32 v56, v52, v53
	v_cvt_f32_f16_e32 v52, v146
	v_cvt_f32_f16_sdwa v53, v146 dst_sel:DWORD dst_unused:UNUSED_PAD src0_sel:WORD_1
	v_pk_add_f32 v[48:49], v[48:49], v[52:53]
	s_nop 0
	v_cvt_pk_f16_f32 v58, v48, v49
	v_cvt_f32_f16_e32 v48, v145
	v_cvt_f32_f16_sdwa v49, v145 dst_sel:DWORD dst_unused:UNUSED_PAD src0_sel:WORD_1
	v_pk_add_f32 v[48:49], v[54:55], v[48:49]
	s_nop 0
	v_cvt_pk_f16_f32 v57, v48, v49
	v_cvt_f32_f16_e32 v48, v147
	v_cvt_f32_f16_sdwa v49, v147 dst_sel:DWORD dst_unused:UNUSED_PAD src0_sel:WORD_1
	v_pk_add_f32 v[48:49], v[50:51], v[48:49]
	s_nop 0
	v_cvt_pk_f16_f32 v59, v48, v49
	v_cvt_f32_f16_e32 v48, v140
	v_cvt_f32_f16_sdwa v49, v140 dst_sel:DWORD dst_unused:UNUSED_PAD src0_sel:WORD_1
	global_store_dwordx4 v[60:61], v[56:59], off offset:256 sc1
	v_pk_add_f32 v[44:45], v[44:45], v[48:49]
	s_nop 0
	v_cvt_pk_f16_f32 v48, v44, v45
	v_cvt_f32_f16_e32 v44, v142
	v_cvt_f32_f16_sdwa v45, v142 dst_sel:DWORD dst_unused:UNUSED_PAD src0_sel:WORD_1
	v_pk_add_f32 v[40:41], v[40:41], v[44:45]
	s_nop 0
	v_cvt_pk_f16_f32 v50, v40, v41
	v_cvt_f32_f16_e32 v40, v141
	v_cvt_f32_f16_sdwa v41, v141 dst_sel:DWORD dst_unused:UNUSED_PAD src0_sel:WORD_1
	v_pk_add_f32 v[40:41], v[46:47], v[40:41]
	s_nop 0
	v_cvt_pk_f16_f32 v49, v40, v41
	v_cvt_f32_f16_e32 v40, v143
	v_cvt_f32_f16_sdwa v41, v143 dst_sel:DWORD dst_unused:UNUSED_PAD src0_sel:WORD_1
	v_pk_add_f32 v[40:41], v[42:43], v[40:41]
	s_nop 0
	v_cvt_pk_f16_f32 v51, v40, v41
	v_lshl_add_u64 v[40:41], s[0:1], 0, v[212:213]
	v_lshl_add_u64 v[44:45], v[40:41], 0, v[206:207]
	v_cvt_f32_f16_e32 v40, v124
	v_cvt_f32_f16_sdwa v41, v124 dst_sel:DWORD dst_unused:UNUSED_PAD src0_sel:WORD_1
	global_store_dwordx4 v[44:45], v[48:51], off sc1
	v_pk_add_f32 v[36:37], v[36:37], v[40:41]
	s_nop 0
	v_cvt_pk_f16_f32 v40, v36, v37
	v_cvt_f32_f16_e32 v36, v126
	v_cvt_f32_f16_sdwa v37, v126 dst_sel:DWORD dst_unused:UNUSED_PAD src0_sel:WORD_1
	v_pk_add_f32 v[32:33], v[32:33], v[36:37]
	s_nop 0
	v_cvt_pk_f16_f32 v42, v32, v33
	v_cvt_f32_f16_e32 v32, v125
	v_cvt_f32_f16_sdwa v33, v125 dst_sel:DWORD dst_unused:UNUSED_PAD src0_sel:WORD_1
	v_pk_add_f32 v[32:33], v[38:39], v[32:33]
	s_nop 0
	v_cvt_pk_f16_f32 v41, v32, v33
	v_cvt_f32_f16_e32 v32, v127
	v_cvt_f32_f16_sdwa v33, v127 dst_sel:DWORD dst_unused:UNUSED_PAD src0_sel:WORD_1
	v_pk_add_f32 v[32:33], v[34:35], v[32:33]
	s_nop 0
	v_cvt_pk_f16_f32 v43, v32, v33
	v_cvt_f32_f16_e32 v32, v120
	v_cvt_f32_f16_sdwa v33, v120 dst_sel:DWORD dst_unused:UNUSED_PAD src0_sel:WORD_1
	global_store_dwordx4 v[44:45], v[40:43], off offset:256 sc1
	v_pk_add_f32 v[28:29], v[28:29], v[32:33]
	s_nop 0
	v_cvt_pk_f16_f32 v32, v28, v29
	v_cvt_f32_f16_e32 v28, v122
	v_cvt_f32_f16_sdwa v29, v122 dst_sel:DWORD dst_unused:UNUSED_PAD src0_sel:WORD_1
	v_pk_add_f32 v[24:25], v[24:25], v[28:29]
	s_nop 0
	v_cvt_pk_f16_f32 v34, v24, v25
	v_cvt_f32_f16_e32 v24, v121
	v_cvt_f32_f16_sdwa v25, v121 dst_sel:DWORD dst_unused:UNUSED_PAD src0_sel:WORD_1
	v_pk_add_f32 v[24:25], v[30:31], v[24:25]
	s_nop 0
	v_cvt_pk_f16_f32 v33, v24, v25
	v_cvt_f32_f16_e32 v24, v123
	v_cvt_f32_f16_sdwa v25, v123 dst_sel:DWORD dst_unused:UNUSED_PAD src0_sel:WORD_1
	v_pk_add_f32 v[24:25], v[26:27], v[24:25]
	s_nop 0
	v_cvt_pk_f16_f32 v35, v24, v25
	v_lshl_add_u64 v[24:25], s[0:1], 0, v[210:211]
	v_lshl_add_u64 v[28:29], v[24:25], 0, v[206:207]
	v_cvt_f32_f16_e32 v24, v112
	v_cvt_f32_f16_sdwa v25, v112 dst_sel:DWORD dst_unused:UNUSED_PAD src0_sel:WORD_1
	global_store_dwordx4 v[28:29], v[32:35], off sc1
	v_pk_add_f32 v[20:21], v[20:21], v[24:25]
	s_nop 0
	v_cvt_pk_f16_f32 v24, v20, v21
	v_cvt_f32_f16_e32 v20, v114
	v_cvt_f32_f16_sdwa v21, v114 dst_sel:DWORD dst_unused:UNUSED_PAD src0_sel:WORD_1
	v_pk_add_f32 v[16:17], v[16:17], v[20:21]
	s_nop 0
	v_cvt_pk_f16_f32 v26, v16, v17
	v_cvt_f32_f16_e32 v16, v113
	v_cvt_f32_f16_sdwa v17, v113 dst_sel:DWORD dst_unused:UNUSED_PAD src0_sel:WORD_1
	v_pk_add_f32 v[16:17], v[22:23], v[16:17]
	s_nop 0
	v_cvt_pk_f16_f32 v25, v16, v17
	v_cvt_f32_f16_e32 v16, v115
	v_cvt_f32_f16_sdwa v17, v115 dst_sel:DWORD dst_unused:UNUSED_PAD src0_sel:WORD_1
	v_pk_add_f32 v[16:17], v[18:19], v[16:17]
	s_nop 0
	v_cvt_pk_f16_f32 v27, v16, v17
	v_cvt_f32_f16_e32 v16, v100
	v_cvt_f32_f16_sdwa v17, v100 dst_sel:DWORD dst_unused:UNUSED_PAD src0_sel:WORD_1
	global_store_dwordx4 v[28:29], v[24:27], off offset:256 sc1
	v_pk_add_f32 v[12:13], v[12:13], v[16:17]
	s_nop 0
	v_cvt_pk_f16_f32 v16, v12, v13
	v_cvt_f32_f16_e32 v12, v102
	v_cvt_f32_f16_sdwa v13, v102 dst_sel:DWORD dst_unused:UNUSED_PAD src0_sel:WORD_1
	v_pk_add_f32 v[8:9], v[8:9], v[12:13]
	s_nop 0
	v_cvt_pk_f16_f32 v18, v8, v9
	v_cvt_f32_f16_e32 v8, v101
	v_cvt_f32_f16_sdwa v9, v101 dst_sel:DWORD dst_unused:UNUSED_PAD src0_sel:WORD_1
	v_pk_add_f32 v[8:9], v[14:15], v[8:9]
	s_nop 0
	v_cvt_pk_f16_f32 v17, v8, v9
	v_cvt_f32_f16_e32 v8, v103
	v_cvt_f32_f16_sdwa v9, v103 dst_sel:DWORD dst_unused:UNUSED_PAD src0_sel:WORD_1
	v_pk_add_f32 v[8:9], v[10:11], v[8:9]
	s_nop 0
	v_cvt_pk_f16_f32 v19, v8, v9
	v_lshl_add_u64 v[8:9], s[0:1], 0, v[208:209]
	v_lshl_add_u64 v[12:13], v[8:9], 0, v[206:207]
	v_cvt_f32_f16_e32 v8, v88
	v_cvt_f32_f16_sdwa v9, v88 dst_sel:DWORD dst_unused:UNUSED_PAD src0_sel:WORD_1
	global_store_dwordx4 v[12:13], v[16:19], off sc1
	v_pk_add_f32 v[4:5], v[4:5], v[8:9]
	s_nop 0
	v_cvt_pk_f16_f32 v8, v4, v5
	v_cvt_f32_f16_e32 v4, v90
	v_cvt_f32_f16_sdwa v5, v90 dst_sel:DWORD dst_unused:UNUSED_PAD src0_sel:WORD_1
	v_pk_add_f32 v[0:1], v[0:1], v[4:5]
	s_nop 0
	v_cvt_pk_f16_f32 v10, v0, v1
	v_cvt_f32_f16_e32 v0, v89
	v_cvt_f32_f16_sdwa v1, v89 dst_sel:DWORD dst_unused:UNUSED_PAD src0_sel:WORD_1
	v_pk_add_f32 v[0:1], v[6:7], v[0:1]
	s_nop 0
	v_cvt_pk_f16_f32 v9, v0, v1
	v_cvt_f32_f16_e32 v0, v91
	v_cvt_f32_f16_sdwa v1, v91 dst_sel:DWORD dst_unused:UNUSED_PAD src0_sel:WORD_1
	v_pk_add_f32 v[0:1], v[2:3], v[0:1]
	s_nop 0
	v_cvt_pk_f16_f32 v11, v0, v1
	global_store_dwordx4 v[12:13], v[8:11], off offset:256 sc1
	s_cbranch_vccz .LBB0_916
	s_waitcnt vmcnt(0)
	s_cmpk_gt_u32 s17, 0xff
	s_cbranch_scc1 .LBB0_931
	s_barrier
